# v43 + the 241 copy instructions in front of LDS-DMA loads removed (source register used directly)
# baseline (speedup 1.0000x reference)
; #define LAS __attribute__((address_space(3)))
; template <class Desc, class Epi>
; __device__ __forceinline__ void gemm_phase(const int wv_, LAS unsigned char* lds, const Desc& d, const Epi& E) {
;     ...
; #pragma unroll
;     for (int i = 0; i < 2; ++i) { int R, C; stage_rc(tid * 16 + i * 8192, R, C); const int Rb = (R & ~31) + perm32(R & 31); Rr[i] = R; Cc[i] = C;
;         voffA[i] = (unsigned)(R * d.lda + C) * 2u; voffA1[i] = voffA[i] + (unsigned)hstepA; voffB[i] = (unsigned)(Rb * d.ldb + C) * 2u; }
;     unsigned voffAn[2] = {0u, 0u}, voffAn1[2] = {0u, 0u};
;     LAS unsigned short* const tix = (LAS unsigned short*)(lds + STAGE_BYTES + 16384);
;     ...
;     const unsigned ldsw = (unsigned)wid * 1024u;
;     const int aoff = lds_byte(wr * 64 + fr, fq * 8), boff = lds_byte(wc * 32 + fr, fq * 8);
;     ...
;     GU cur, nxt; int ui = 0;
;     if (bid < 0 || bid >= d.nunits) return;
;     LAS float* const rsc = (LAS float*)(lds + STAGE_BYTES);
;     if constexpr (Epi::STAGED || Desc::GATHER) {
;         const int nmy = (d.nunits - bid + nblk - 1) / nblk;
;         for (int idx = tid; idx < nmy * 256; idx += NTHREADS) { GU su; d.unit(bid + (idx >> 8) * nblk, su);
;             if constexpr (Epi::STAGED) rsc[idx] = E.rowscale(su, idx & 255);
;             if constexpr (Desc::GATHER) tix[idx] = (unsigned short)d.tokidx(su, idx & 255); }
;         asm volatile("s_waitcnt vmcnt(0) lgkmcnt(0)" ::: "memory"); __builtin_amdgcn_s_barrier(); asm volatile("" ::: "memory");
;     }
;     d.unit(bid, cur);
;     if constexpr (Desc::GATHER) PG8_AOFF(0, cur, voffA, voffA1);
;     f32x4 acc[2][2][4][2];
; #pragma unroll
;     for (int a = 0; a < 2; ++a)
; #pragma unroll
;         for (int b = 0; b < 2; ++b)
; #pragma unroll
;             for (int m = 0; m < 4; ++m)
; #pragma unroll
;                 for (int n = 0; n < 2; ++n) acc[a][b][m][n] = (f32x4){0.f, 0.f, 0.f, 0.f};
;     bf16x8 At[4][2], B0[2][2], B1[2][2];
;     const char* cA = (const char*)cur.a; const char* cB = (const char*)cur.b;
;     PG8_STAGE(PG8_SB(0, 0), cB, voffB); PG8_STAGE(PG8_SB(0, 1), cB + hstepB, voffB); PG8_STAGE(PG8_SA(0, 0), cA, voffA); PG8_STAGE(PG8_SA(0, 1), cA, voffA1);
;     if (wr == 1) PG8_BAR;
;     PG8_WAIT_V(2); PG8_BAR;
;     PG8_STAGE(PG8_SB(1, 0), cB + kstep, voffB); PG8_STAGE(PG8_SA(1, 0), cA + kstep, voffA); PG8_STAGE(PG8_SB(1, 1), cB + hstepB + kstep, voffB);
;     PG8_WAIT_V(6); PG8_BAR;
.LBB0_654:
	s_or_b64 exec, exec, s[2:3]
	v_ashrrev_i32_e32 v3, 31, v1
	v_lshrrev_b32_e32 v3, 26, v3
	v_lshlrev_b32_e32 v2, 4, v1
	v_add_u32_e32 v3, v1, v3
	v_bfe_i32 v1, v1, 27, 1
	v_lshrrev_b32_e32 v1, 22, v1
	v_add_u32_e32 v1, v2, v1
	v_and_b32_e32 v1, 0xfffffc00, v1
	v_sub_u32_e32 v1, v2, v1
	v_lshrrev_b32_e32 v4, 4, v1
	v_bitop3_b32 v1, v4, v1, 32 bitop3:0x6c
	v_ashrrev_i32_e32 v5, 31, v1
	v_ashrrev_i32_e32 v3, 6, v3
	v_lshrrev_b32_e32 v5, 26, v5
	v_lshlrev_b32_e32 v4, 3, v3
	v_add_u32_e32 v5, v1, v5
	v_and_b32_e32 v4, -16, v4
	v_ashrrev_i32_e32 v6, 6, v5
	v_and_b32_e32 v5, 0xc0, v5
	v_add_u32_e32 v4, v6, v4
	v_sub_u32_e32 v1, v1, v5
	v_mov_b32_e32 v5, 1
	v_lshlrev_b32_e32 v3, 5, v3
	v_ashrrev_i16_sdwa v1, v5, sext(v1) dst_sel:DWORD dst_unused:UNUSED_PAD src0_sel:DWORD src1_sel:BYTE_0
	v_lshlrev_b32_e32 v7, 1, v4
	v_lshrrev_b32_e32 v8, 2, v4
	v_and_b32_e32 v6, 3, v6
	s_mov_b32 s2, 0x1fffe0
	v_and_b32_e32 v3, 32, v3
	v_bfe_i32 v1, v1, 0, 16
	v_and_b32_e32 v7, 24, v7
	v_and_b32_e32 v8, 4, v8
	v_and_or_b32 v6, v4, s2, v6
	v_or3_b32 v6, v6, v8, v7
	v_add_lshl_u32 v1, v3, v1, 1
	v_lshl_add_u32 v132, v4, 11, v1
	v_lshl_add_u32 v134, v6, 11, v1
	v_add_u32_e32 v1, 0x2000, v2
	v_ashrrev_i32_e32 v2, 31, v1
	v_lshrrev_b32_e32 v2, 22, v2
	v_add_u32_e32 v2, v1, v2
	v_ashrrev_i32_e32 v2, 10, v2
	v_mul_i32_i24_e32 v3, 0x400, v2
	v_sub_u32_e32 v1, v1, v3
	v_lshrrev_b32_e32 v3, 4, v1
	s_add_u32 s29, s0, 0x38200000
	v_bitop3_b32 v1, v3, v1, 32 bitop3:0x6c
	s_addc_u32 s30, s1, 0
	v_ashrrev_i32_e32 v4, 31, v1
	s_add_u32 s31, s0, 0x1e00000
	v_lshrrev_b32_e32 v4, 26, v4
	s_addc_u32 s33, s1, 0
	v_lshlrev_b32_e32 v3, 3, v2
	v_add_u32_e32 v4, v1, v4
	s_add_u32 s34, s0, 0x2600000
	v_and_b32_e32 v3, -16, v3
	v_ashrrev_i32_e32 v6, 6, v4
	s_addc_u32 s35, s1, 0
	v_add_u32_e32 v3, v6, v3
	v_and_b32_e32 v6, 3, v6
	s_ashr_i32 s8, s14, 6
	s_ashr_i32 s15, s14, 8
	v_and_b32_e32 v4, 0xc0, v4
	v_and_or_b32 v6, v3, s2, v6
	s_lshl_b32 s16, s8, 10
	s_and_b32 s55, s20, 3
	s_lshl_b32 s2, s20, 16
	v_sub_u32_e32 v1, v1, v4
	s_cmpk_lt_u32 s20, 0x80
	v_lshlrev_b32_e32 v2, 5, v2
	v_ashrrev_i16_sdwa v1, v5, sext(v1) dst_sel:DWORD dst_unused:UNUSED_PAD src0_sel:DWORD src1_sel:BYTE_0
	v_lshlrev_b32_e32 v4, 1, v3
	v_lshrrev_b32_e32 v5, 2, v3
	s_cselect_b32 s3, s33, s35
	s_cselect_b32 s4, s31, s34
	s_and_b32 s2, s2, 0x600000
	s_lshl_b32 s5, s55, 19
	v_and_b32_e32 v2, 32, v2
	v_bfe_i32 v1, v1, 0, 16
	v_and_b32_e32 v4, 24, v4
	v_and_b32_e32 v5, 4, v5
	s_or_b32 s2, s2, s5
	v_or3_b32 v4, v6, v5, v4
	v_add_lshl_u32 v1, v2, v1, 1
	s_add_u32 s2, s4, s2
	v_lshl_add_u32 v135, v3, 11, v1
	v_lshl_add_u32 v137, v4, 11, v1
	s_addc_u32 s3, s3, 0
	s_add_i32 s36, s16, 0
	s_waitcnt vmcnt(0) lgkmcnt(0)
	s_barrier
	s_add_i32 m0, s36, 0x10000
	v_add_u32_e32 v133, 0x40000, v132
	global_load_lds_dwordx4 v134, s[2:3]
	s_add_i32 m0, s36, 0x12000
	s_add_u32 s4, s2, 0x40000
	global_load_lds_dwordx4 v137, s[2:3]
	s_addc_u32 s5, s3, 0
	s_add_i32 m0, s36, 0x14000
	v_add_u32_e32 v136, 0x40000, v135
	global_load_lds_dwordx4 v134, s[4:5]
	s_add_i32 m0, s36, 0x16000
	s_mov_b32 s56, 0
	global_load_lds_dwordx4 v137, s[4:5]
	s_lshl_b32 s4, s20, 17
	s_and_b32 s4, s4, 0xf80000
	s_add_u32 s26, s29, s4
	s_addc_u32 s27, s30, 0
	s_mov_b32 m0, s36
	s_add_i32 s37, s36, 0x2000
	global_load_lds_dwordx4 v132, s[26:27]
	s_mov_b32 m0, s37
	s_add_i32 s38, s36, 0x4000
	global_load_lds_dwordx4 v135, s[26:27]
	s_mov_b32 m0, s38
	s_add_i32 s39, s36, 0x6000
	global_load_lds_dwordx4 v133, s[26:27]
	v_mov_b32_e32 v1, v136
	s_mov_b32 m0, s39
	s_cmp_eq_u32 s15, 1
	global_load_lds_dwordx4 v1, s[26:27]
	s_cselect_b64 s[4:5], -1, 0
	s_and_b64 vcc, exec, s[4:5]
	s_cbranch_vccz .LBB0_656
	s_barrier
.LBB0_656:
	s_lshr_b32 s57, s20, 2
	s_add_u32 s6, s0, 0x39200000
	v_mov_b32_e32 v128, v134
	v_mov_b32_e32 v129, 0
	s_addc_u32 s7, s1, 0
	s_lshl_b32 s0, s8, 5
	s_waitcnt vmcnt(2)
	s_barrier
	s_mov_b64 s[8:9], 0x80
	v_lshl_add_u64 v[2:3], s[2:3], 0, v[128:129]
	s_add_i32 m0, s36, 0x18000
	v_lshl_add_u64 v[2:3], v[2:3], 0, s[8:9]
	v_mov_b32_e32 v128, v137
	global_load_lds_dwordx4 v[2:3], off
	s_add_i32 m0, s36, 0x1a000
	v_lshl_add_u64 v[2:3], s[2:3], 0, v[128:129]
	v_lshl_add_u64 v[2:3], v[2:3], 0, s[8:9]
	v_mov_b32_e32 v128, v132
	global_load_lds_dwordx4 v[2:3], off
	s_add_i32 s40, s36, 0x8000
	v_lshl_add_u64 v[2:3], s[26:27], 0, v[128:129]
	s_and_b32 s22, s0, 0x60
	v_lshl_add_u64 v[2:3], v[2:3], 0, s[8:9]
	s_mov_b32 m0, s40
	v_mov_b32_e32 v128, v135
	s_lshl_b32 s17, s15, 13
	s_lshl_b32 s23, s22, 7
	global_load_lds_dwordx4 v[2:3], off
	s_add_i32 s41, s36, 0xa000
	v_lshl_add_u64 v[2:3], s[26:27], 0, v[128:129]
	v_lshl_add_u64 v[2:3], v[2:3], 0, s[8:9]
	s_mov_b32 m0, s41
	s_add_u32 s0, s2, 0x40080
	global_load_lds_dwordx4 v[2:3], off
	s_addc_u32 s1, s3, 0
	s_add_i32 m0, s36, 0x1c000
	v_lshrrev_b32_e32 v2, 1, v0
	global_load_lds_dwordx4 v134, s[0:1]
	s_add_i32 m0, s36, 0x1e000
	v_and_b32_e32 v2, 24, v2
	global_load_lds_dwordx4 v137, s[0:1]
	v_and_b32_e32 v1, 15, v0
	v_lshl_or_b32 v138, s15, 6, v1
	v_lshlrev_b32_e32 v3, 1, v2
	v_lshlrev_b32_e32 v0, 2, v0
	v_lshl_or_b32 v1, v1, 6, v3
	v_lshlrev_b32_e32 v3, 2, v138
	v_and_b32_e32 v0, 32, v0
	s_cmpk_lt_u32 s14, 0x100
	v_and_b32_e32 v4, 32, v3
	v_bitop3_b32 v0, v1, s23, v0 bitop3:0xde
	s_waitcnt vmcnt(6)
	s_cselect_b64 s[14:15], -1, 0
	s_add_i32 s44, 0, 0x10000
	s_add_i32 s46, 0, 0x14000
	s_add_i32 s48, 0, 0x18000
	s_add_i32 s50, 0, 0x1c000
	v_bitop3_b32 v4, v1, s17, v4 bitop3:0xde
	s_add_i32 s0, 0, 0x20000
	v_add_u32_e32 v148, s44, v0
	v_add_u32_e32 v149, s46, v0
	s_add_i32 s44, s44, s16
	s_add_i32 s46, s46, s16
	v_add_u32_e32 v151, s48, v0
	v_add_u32_e32 v152, s50, v0
	s_add_i32 s48, s48, s16
	s_add_i32 s50, s50, s16
	v_or_b32_e32 v139, 16, v138
	v_or_b32_e32 v140, 32, v138
	v_or_b32_e32 v141, 48, v138
	v_add_u32_e32 v142, 0x80, v138
	v_add_u32_e32 v143, 0x90, v138
	v_add_u32_e32 v144, 0xa0, v138
	v_add_u32_e32 v145, 0xb0, v138
	v_or_b32_e32 v146, s22, v2
	v_add_u32_e32 v147, s0, v3
	v_add_u32_e32 v150, 0, v4
	s_add_i32 s42, s36, 0xc000
	s_add_i32 s43, s36, 0xe000
	s_add_i32 s45, s44, 0x2000
	s_add_i32 s47, s46, 0x2000
	s_add_i32 s49, s48, 0x2000
	s_add_i32 s51, s50, 0x2000
	s_mov_b64 s[22:23], s[2:3]
	s_mov_b64 s[16:17], s[26:27]
	s_barrier
	s_branch .LBB0_659

; #define PG8_STAGE(bufoff, gbase, voff) do { _Pragma("unroll") for (int _i = 0; _i < 2; ++_i) \
;         __builtin_amdgcn_global_load_lds((const __attribute__((address_space(1))) unsigned*)((const __attribute__((address_space(1))) char*)(gbase) + (unsigned)lnd_v((int)(voff)[_i])), (LAS unsigned*)(lds + (bufoff) + ldsw + _i * 8192), 16, 0, 0); } while (0)
; #define PG8_LDA(dst, b, h) do { _Pragma("unroll") for (int m = 0; m < 4; ++m) _Pragma("unroll") for (int k = 0; k < 2; ++k) dst[m][k] = *(const LAS bf16x8*)(lds + PG8_SA(b, h) + aoff + m * 2048 + k * 1024); } while (0)
; #define PG8_LDB(dst, b, h) do { _Pragma("unroll") for (int n = 0; n < 2; ++n) _Pragma("unroll") for (int k = 0; k < 2; ++k) dst[n][k] = *(const LAS bf16x8*)(lds + PG8_SB(b, h) + boff + n * 2048 + k * 1024); } while (0)
; #define PG8_WAIT_V(n) asm volatile("s_waitcnt vmcnt(" #n ")" ::: "memory")
; #define PG8_WAIT_L(n) asm volatile("s_waitcnt lgkmcnt(" #n ")" ::: "memory")
; #define PG8_BAR __builtin_amdgcn_s_barrier()
; template <class Desc, class Epi>
; __device__ __forceinline__ void gemm_phase(const int wv_, LAS unsigned char* lds, const Desc& d, const Epi& E) {
;     ...
;         for (int t = 0; t < nt; t += 2) {
;             const bool last = (t == nt - 2);
;             unsigned sA0[2], sA1[2];
;             if constexpr (Desc::GATHER) { sA0[0] = last ? voffAn[0] : voffA[0]; sA0[1] = last ? voffAn[1] : voffA[1]; sA1[0] = last ? voffAn1[0] : voffA1[0]; sA1[1] = last ? voffAn1[1] : voffA1[1]; }
;             else { sA0[0] = voffA[0]; sA0[1] = voffA[1]; sA1[0] = voffA1[0]; sA1[1] = voffA1[1]; }
;             const char* a1 = cA + (size_t)(t + 1) * kstep;
;             const char* a2 = last ? nA : cA + (size_t)(t + 2) * kstep; const char* b2 = last ? nB : cB + (size_t)(t + 2) * kstep;
;             const char* a3 = a2 + kstep; const char* b3 = b2 + kstep;
;             PG8_LDB(B0, 0, 0); PG8_LDB(B1, 0, 1); PG8_SCHED; PG8_LDA(At, 0, 0); PG8_STAGE(PG8_SA(1, 1), a1, voffA1);
;             PG8_WAIT_V(8); PG8_WAIT_L(0); PG8_BAR; PG8_MMA(0, 0, At, B0); PG8_MMA(0, 1, At, B1); PG8_BAR; PG8_SCHED;
;             PG8_LDA(At, 0, 1); PG8_STAGE(PG8_SB(0, 0), b2, voffB); PG8_STAGE(PG8_SB(0, 1), b2 + hstepB, voffB); PG8_STAGE(PG8_SA(0, 0), a2, sA0);
;             PG8_WAIT_V(8); PG8_WAIT_L(0); PG8_BAR; PG8_MMA(1, 0, At, B0); PG8_MMA(1, 1, At, B1); PG8_BAR; PG8_SCHED;
.LBB0_662:
	ds_read_b128 v[154:157], v148
	ds_read_b128 v[158:161], v148 offset:1024
	ds_read_b128 v[162:165], v148 offset:2048
	ds_read_b128 v[166:169], v148 offset:3072
	ds_read_b128 v[170:173], v149
	ds_read_b128 v[174:177], v149 offset:1024
	ds_read_b128 v[178:181], v149 offset:2048
	ds_read_b128 v[182:185], v149 offset:3072
	s_add_u32 s2, s0, 0x80
	s_addc_u32 s3, s1, 0
	s_cmp_eq_u32 s60, 12
	s_cselect_b32 s3, s17, s3
	s_cselect_b32 s2, s16, s2
	s_cselect_b32 s27, s23, s59
	s_cselect_b32 s26, s22, s58
	s_mov_b32 m0, s42
	ds_read_b128 v[186:189], v150
	ds_read_b128 v[190:193], v150 offset:1024
	ds_read_b128 v[194:197], v150 offset:2048
	ds_read_b128 v[198:201], v150 offset:3072
	ds_read_b128 v[202:205], v150 offset:4096
	ds_read_b128 v[206:209], v150 offset:5120
	ds_read_b128 v[210:213], v150 offset:6144
	ds_read_b128 v[214:217], v150 offset:7168
	s_nop 0
	global_load_lds_dwordx4 v133, s[0:1]
	s_mov_b32 m0, s43
	s_nop 0
	global_load_lds_dwordx4 v136, s[0:1]
	s_waitcnt vmcnt(8)
	s_waitcnt lgkmcnt(0)
	s_barrier
	s_waitcnt lgkmcnt(0)
	v_mfma_f32_16x16x32_bf16 v[124:127], v[154:157], v[186:189], v[124:127]
	v_mfma_f32_16x16x32_bf16 v[120:123], v[162:165], v[186:189], v[120:123]
	v_mfma_f32_16x16x32_bf16 v[108:111], v[154:157], v[194:197], v[108:111]
	v_mfma_f32_16x16x32_bf16 v[104:107], v[162:165], v[194:197], v[104:107]
	v_mfma_f32_16x16x32_bf16 v[92:95], v[154:157], v[202:205], v[92:95]
	v_mfma_f32_16x16x32_bf16 v[88:91], v[162:165], v[202:205], v[88:91]
	v_mfma_f32_16x16x32_bf16 v[76:79], v[154:157], v[210:213], v[76:79]
	v_mfma_f32_16x16x32_bf16 v[72:75], v[162:165], v[210:213], v[72:75]
	v_mfma_f32_16x16x32_bf16 v[124:127], v[158:161], v[190:193], v[124:127]
	v_mfma_f32_16x16x32_bf16 v[120:123], v[166:169], v[190:193], v[120:123]
	v_mfma_f32_16x16x32_bf16 v[108:111], v[158:161], v[198:201], v[108:111]
	v_mfma_f32_16x16x32_bf16 v[104:107], v[166:169], v[198:201], v[104:107]
	v_mfma_f32_16x16x32_bf16 v[92:95], v[158:161], v[206:209], v[92:95]
	v_mfma_f32_16x16x32_bf16 v[88:91], v[166:169], v[206:209], v[88:91]
	v_mfma_f32_16x16x32_bf16 v[76:79], v[158:161], v[214:217], v[76:79]
	v_mfma_f32_16x16x32_bf16 v[72:75], v[166:169], v[214:217], v[72:75]
	v_mfma_f32_16x16x32_bf16 v[116:119], v[170:173], v[186:189], v[116:119]
	v_mfma_f32_16x16x32_bf16 v[112:115], v[178:181], v[186:189], v[112:115]
	v_mfma_f32_16x16x32_bf16 v[100:103], v[170:173], v[194:197], v[100:103]
	v_mfma_f32_16x16x32_bf16 v[96:99], v[178:181], v[194:197], v[96:99]
	v_mfma_f32_16x16x32_bf16 v[84:87], v[170:173], v[202:205], v[84:87]
	v_mfma_f32_16x16x32_bf16 v[80:83], v[178:181], v[202:205], v[80:83]
	v_mfma_f32_16x16x32_bf16 v[68:71], v[170:173], v[210:213], v[68:71]
	v_mfma_f32_16x16x32_bf16 v[64:67], v[178:181], v[210:213], v[64:67]
	v_mfma_f32_16x16x32_bf16 v[116:119], v[174:177], v[190:193], v[116:119]
	v_mfma_f32_16x16x32_bf16 v[112:115], v[182:185], v[190:193], v[112:115]
	v_mfma_f32_16x16x32_bf16 v[100:103], v[174:177], v[198:201], v[100:103]
	v_mfma_f32_16x16x32_bf16 v[96:99], v[182:185], v[198:201], v[96:99]
	v_mfma_f32_16x16x32_bf16 v[84:87], v[174:177], v[206:209], v[84:87]
	v_mfma_f32_16x16x32_bf16 v[80:83], v[182:185], v[206:209], v[80:83]
	v_mfma_f32_16x16x32_bf16 v[68:71], v[174:177], v[214:217], v[68:71]
	v_mfma_f32_16x16x32_bf16 v[64:67], v[182:185], v[214:217], v[64:67]
	s_barrier
	s_mov_b32 m0, s44
	ds_read_b128 v[186:189], v150 offset:16384
	ds_read_b128 v[190:193], v150 offset:17408
	ds_read_b128 v[194:197], v150 offset:18432
	ds_read_b128 v[198:201], v150 offset:19456
	ds_read_b128 v[202:205], v150 offset:20480
	ds_read_b128 v[206:209], v150 offset:21504
	ds_read_b128 v[210:213], v150 offset:22528
	ds_read_b128 v[214:217], v150 offset:23552
	s_add_u32 s62, s26, 0x40000
	global_load_lds_dwordx4 v134, s[26:27]
	s_mov_b32 m0, s45
	s_addc_u32 s63, s27, 0
	global_load_lds_dwordx4 v137, s[26:27]
	s_mov_b32 m0, s46
	s_nop 0
	global_load_lds_dwordx4 v134, s[62:63]
	s_mov_b32 m0, s47
	s_nop 0
	global_load_lds_dwordx4 v137, s[62:63]
	s_mov_b32 m0, s36
	s_nop 0
	global_load_lds_dwordx4 v132, s[2:3]
	s_mov_b32 m0, s37
	s_nop 0
	global_load_lds_dwordx4 v135, s[2:3]
	s_waitcnt vmcnt(8)
	s_waitcnt lgkmcnt(0)
	s_barrier
	s_waitcnt lgkmcnt(0)
	v_mfma_f32_16x16x32_bf16 v[60:63], v[154:157], v[186:189], v[60:63]
	v_mfma_f32_16x16x32_bf16 v[56:59], v[162:165], v[186:189], v[56:59]
	v_mfma_f32_16x16x32_bf16 v[44:47], v[154:157], v[194:197], v[44:47]
	v_mfma_f32_16x16x32_bf16 v[32:35], v[162:165], v[194:197], v[32:35]
	v_mfma_f32_16x16x32_bf16 v[16:19], v[154:157], v[202:205], v[16:19]
	v_mfma_f32_16x16x32_bf16 v[8:11], v[162:165], v[202:205], v[8:11]
	v_mfma_f32_16x16x32_bf16 v[4:7], v[154:157], v[210:213], v[4:7]
	v_mfma_f32_16x16x32_bf16 v[0:3], v[162:165], v[210:213], v[0:3]
	v_mfma_f32_16x16x32_bf16 v[60:63], v[158:161], v[190:193], v[60:63]
	v_mfma_f32_16x16x32_bf16 v[56:59], v[166:169], v[190:193], v[56:59]
	v_mfma_f32_16x16x32_bf16 v[44:47], v[158:161], v[198:201], v[44:47]
	v_mfma_f32_16x16x32_bf16 v[32:35], v[166:169], v[198:201], v[32:35]
	v_mfma_f32_16x16x32_bf16 v[16:19], v[158:161], v[206:209], v[16:19]
	v_mfma_f32_16x16x32_bf16 v[8:11], v[166:169], v[206:209], v[8:11]
	v_mfma_f32_16x16x32_bf16 v[4:7], v[158:161], v[214:217], v[4:7]
	v_mfma_f32_16x16x32_bf16 v[0:3], v[166:169], v[214:217], v[0:3]
	v_mfma_f32_16x16x32_bf16 v[52:55], v[170:173], v[186:189], v[52:55]
	v_mfma_f32_16x16x32_bf16 v[48:51], v[178:181], v[186:189], v[48:51]
	v_mfma_f32_16x16x32_bf16 v[28:31], v[170:173], v[194:197], v[28:31]
	v_mfma_f32_16x16x32_bf16 v[12:15], v[178:181], v[194:197], v[12:15]
	v_mfma_f32_16x16x32_bf16 v[36:39], v[170:173], v[202:205], v[36:39]
	v_mfma_f32_16x16x32_bf16 v[40:43], v[178:181], v[202:205], v[40:43]
	v_mfma_f32_16x16x32_bf16 v[20:23], v[170:173], v[210:213], v[20:23]
	v_mfma_f32_16x16x32_bf16 v[24:27], v[178:181], v[210:213], v[24:27]
	v_mfma_f32_16x16x32_bf16 v[52:55], v[174:177], v[190:193], v[52:55]
	v_mfma_f32_16x16x32_bf16 v[48:51], v[182:185], v[190:193], v[48:51]
	v_mfma_f32_16x16x32_bf16 v[28:31], v[174:177], v[198:201], v[28:31]
	v_mfma_f32_16x16x32_bf16 v[12:15], v[182:185], v[198:201], v[12:15]
	v_mfma_f32_16x16x32_bf16 v[36:39], v[174:177], v[206:209], v[36:39]
	v_mfma_f32_16x16x32_bf16 v[40:43], v[182:185], v[206:209], v[40:43]
	v_mfma_f32_16x16x32_bf16 v[20:23], v[174:177], v[214:217], v[20:23]
	v_mfma_f32_16x16x32_bf16 v[24:27], v[182:185], v[214:217], v[24:27]
	s_barrier
; #define PG8_STAGE(bufoff, gbase, voff) do { _Pragma("unroll") for (int _i = 0; _i < 2; ++_i) \
;         __builtin_amdgcn_global_load_lds((const __attribute__((address_space(1))) unsigned*)((const __attribute__((address_space(1))) char*)(gbase) + (unsigned)lnd_v((int)(voff)[_i])), (LAS unsigned*)(lds + (bufoff) + ldsw + _i * 8192), 16, 0, 0); } while (0)
; #define PG8_LDA(dst, b, h) do { _Pragma("unroll") for (int m = 0; m < 4; ++m) _Pragma("unroll") for (int k = 0; k < 2; ++k) dst[m][k] = *(const LAS bf16x8*)(lds + PG8_SA(b, h) + aoff + m * 2048 + k * 1024); } while (0)
; #define PG8_LDB(dst, b, h) do { _Pragma("unroll") for (int n = 0; n < 2; ++n) _Pragma("unroll") for (int k = 0; k < 2; ++k) dst[n][k] = *(const LAS bf16x8*)(lds + PG8_SB(b, h) + boff + n * 2048 + k * 1024); } while (0)
; #define PG8_MMA(ai, bj, At, Bt) do { __builtin_amdgcn_s_setprio(1); _Pragma("unroll") for (int m = 0; m < 4; ++m) _Pragma("unroll") for (int n = 0; n < 2; ++n) _Pragma("unroll") for (int k = 0; k < 2; ++k) \
;         acc[ai][bj][m][n] = __builtin_amdgcn_mfma_f32_16x16x32_bf16(Bt[n][k], At[m][k], acc[ai][bj][m][n], 0, 0, 0); __builtin_amdgcn_s_setprio(0); } while (0)
; #define PG8_WAIT_V(n) asm volatile("s_waitcnt vmcnt(" #n ")" ::: "memory")
; #define PG8_WAIT_L(n) asm volatile("s_waitcnt lgkmcnt(" #n ")" ::: "memory")
; #define PG8_BAR __builtin_amdgcn_s_barrier()
; #define PG8_SCHED __builtin_amdgcn_sched_barrier(0)
; template <class Desc, class Epi>
; __device__ __forceinline__ void gemm_phase(const int wv_, LAS unsigned char* lds, const Desc& d, const Epi& E) {
;     ...
;             PG8_LDB(B0, 1, 0); PG8_LDB(B1, 1, 1); PG8_SCHED; PG8_LDA(At, 1, 0); PG8_STAGE(PG8_SA(0, 1), a2, sA1);
;             PG8_WAIT_V(8); PG8_WAIT_L(0); PG8_BAR; PG8_MMA(0, 0, At, B0); PG8_MMA(0, 1, At, B1); PG8_BAR; PG8_SCHED;
;             PG8_LDA(At, 1, 1); PG8_STAGE(PG8_SB(1, 0), b3, voffB); PG8_STAGE(PG8_SB(1, 1), b3 + hstepB, voffB); PG8_STAGE(PG8_SA(1, 0), a3, sA0);
;             PG8_WAIT_V(8); PG8_WAIT_L(0); PG8_BAR; PG8_MMA(1, 0, At, B0); PG8_MMA(1, 1, At, B1); PG8_BAR; PG8_SCHED;
;         }
;         if (wr == 0) PG8_BAR;
	ds_read_b128 v[154:157], v151
	ds_read_b128 v[158:161], v151 offset:1024
	ds_read_b128 v[162:165], v151 offset:2048
	ds_read_b128 v[166:169], v151 offset:3072
	ds_read_b128 v[170:173], v152
	ds_read_b128 v[174:177], v152 offset:1024
	ds_read_b128 v[178:181], v152 offset:2048
	ds_read_b128 v[182:185], v152 offset:3072
	s_mov_b32 m0, s38
	ds_read_b128 v[186:189], v150 offset:32768
	ds_read_b128 v[190:193], v150 offset:33792
	ds_read_b128 v[194:197], v150 offset:34816
	ds_read_b128 v[198:201], v150 offset:35840
	ds_read_b128 v[202:205], v150 offset:36864
	ds_read_b128 v[206:209], v150 offset:37888
	ds_read_b128 v[210:213], v150 offset:38912
	ds_read_b128 v[214:217], v150 offset:39936
	s_nop 0
	global_load_lds_dwordx4 v133, s[2:3]
	s_mov_b32 m0, s39
	s_nop 0
	global_load_lds_dwordx4 v136, s[2:3]
	s_waitcnt vmcnt(8)
	s_waitcnt lgkmcnt(0)
	s_barrier
	s_waitcnt lgkmcnt(0)
	v_mfma_f32_16x16x32_bf16 v[124:127], v[154:157], v[186:189], v[124:127]
	v_mfma_f32_16x16x32_bf16 v[120:123], v[162:165], v[186:189], v[120:123]
	v_mfma_f32_16x16x32_bf16 v[108:111], v[154:157], v[194:197], v[108:111]
	v_mfma_f32_16x16x32_bf16 v[104:107], v[162:165], v[194:197], v[104:107]
	v_mfma_f32_16x16x32_bf16 v[92:95], v[154:157], v[202:205], v[92:95]
	v_mfma_f32_16x16x32_bf16 v[88:91], v[162:165], v[202:205], v[88:91]
	v_mfma_f32_16x16x32_bf16 v[76:79], v[154:157], v[210:213], v[76:79]
	v_mfma_f32_16x16x32_bf16 v[72:75], v[162:165], v[210:213], v[72:75]
	v_mfma_f32_16x16x32_bf16 v[124:127], v[158:161], v[190:193], v[124:127]
	v_mfma_f32_16x16x32_bf16 v[120:123], v[166:169], v[190:193], v[120:123]
	v_mfma_f32_16x16x32_bf16 v[108:111], v[158:161], v[198:201], v[108:111]
	v_mfma_f32_16x16x32_bf16 v[104:107], v[166:169], v[198:201], v[104:107]
	v_mfma_f32_16x16x32_bf16 v[92:95], v[158:161], v[206:209], v[92:95]
	v_mfma_f32_16x16x32_bf16 v[88:91], v[166:169], v[206:209], v[88:91]
	v_mfma_f32_16x16x32_bf16 v[76:79], v[158:161], v[214:217], v[76:79]
	v_mfma_f32_16x16x32_bf16 v[72:75], v[166:169], v[214:217], v[72:75]
	v_mfma_f32_16x16x32_bf16 v[116:119], v[170:173], v[186:189], v[116:119]
	v_mfma_f32_16x16x32_bf16 v[112:115], v[178:181], v[186:189], v[112:115]
	v_mfma_f32_16x16x32_bf16 v[100:103], v[170:173], v[194:197], v[100:103]
	v_mfma_f32_16x16x32_bf16 v[96:99], v[178:181], v[194:197], v[96:99]
	v_mfma_f32_16x16x32_bf16 v[84:87], v[170:173], v[202:205], v[84:87]
	v_mfma_f32_16x16x32_bf16 v[80:83], v[178:181], v[202:205], v[80:83]
	v_mfma_f32_16x16x32_bf16 v[68:71], v[170:173], v[210:213], v[68:71]
	v_mfma_f32_16x16x32_bf16 v[64:67], v[178:181], v[210:213], v[64:67]
	v_mfma_f32_16x16x32_bf16 v[116:119], v[174:177], v[190:193], v[116:119]
	v_mfma_f32_16x16x32_bf16 v[112:115], v[182:185], v[190:193], v[112:115]
	v_mfma_f32_16x16x32_bf16 v[100:103], v[174:177], v[198:201], v[100:103]
	v_mfma_f32_16x16x32_bf16 v[96:99], v[182:185], v[198:201], v[96:99]
	v_mfma_f32_16x16x32_bf16 v[84:87], v[174:177], v[206:209], v[84:87]
	v_mfma_f32_16x16x32_bf16 v[80:83], v[182:185], v[206:209], v[80:83]
	v_mfma_f32_16x16x32_bf16 v[68:71], v[174:177], v[214:217], v[68:71]
	v_mfma_f32_16x16x32_bf16 v[64:67], v[182:185], v[214:217], v[64:67]
	s_barrier
	v_mov_b32_e32 v128, v134
	ds_read_b128 v[186:189], v150 offset:49152
	ds_read_b128 v[190:193], v150 offset:50176
	ds_read_b128 v[194:197], v150 offset:51200
	ds_read_b128 v[198:201], v150 offset:52224
	ds_read_b128 v[202:205], v150 offset:53248
	ds_read_b128 v[206:209], v150 offset:54272
	ds_read_b128 v[210:213], v150 offset:55296
	ds_read_b128 v[214:217], v150 offset:56320
	s_mov_b32 m0, s48
	v_lshl_add_u64 v[130:131], s[26:27], 0, v[128:129]
	v_lshl_add_u64 v[130:131], v[130:131], 0, s[8:9]
	v_mov_b32_e32 v128, v137
	global_load_lds_dwordx4 v[130:131], off
	s_mov_b32 m0, s49
	v_lshl_add_u64 v[130:131], s[26:27], 0, v[128:129]
	v_lshl_add_u64 v[130:131], v[130:131], 0, s[8:9]
	s_add_u32 s26, s26, 0x40080
	global_load_lds_dwordx4 v[130:131], off
	s_addc_u32 s27, s27, 0
	s_mov_b32 m0, s50
	s_nop 0
	global_load_lds_dwordx4 v134, s[26:27]
	s_mov_b32 m0, s51
	s_nop 0
	global_load_lds_dwordx4 v137, s[26:27]
	v_mov_b32_e32 v128, v132
	s_mov_b32 m0, s40
	v_lshl_add_u64 v[130:131], s[2:3], 0, v[128:129]
	v_lshl_add_u64 v[130:131], v[130:131], 0, s[8:9]
	v_mov_b32_e32 v128, v135
	global_load_lds_dwordx4 v[130:131], off
	s_mov_b32 m0, s41
	v_lshl_add_u64 v[130:131], s[2:3], 0, v[128:129]
	v_lshl_add_u64 v[130:131], v[130:131], 0, s[8:9]
	global_load_lds_dwordx4 v[130:131], off
	s_waitcnt vmcnt(8)
	s_waitcnt lgkmcnt(0)
	s_barrier
	s_waitcnt lgkmcnt(0)
	v_mfma_f32_16x16x32_bf16 v[60:63], v[154:157], v[186:189], v[60:63]
	v_mfma_f32_16x16x32_bf16 v[56:59], v[162:165], v[186:189], v[56:59]
	v_mfma_f32_16x16x32_bf16 v[44:47], v[154:157], v[194:197], v[44:47]
	v_mfma_f32_16x16x32_bf16 v[32:35], v[162:165], v[194:197], v[32:35]
	v_mfma_f32_16x16x32_bf16 v[16:19], v[154:157], v[202:205], v[16:19]
	v_mfma_f32_16x16x32_bf16 v[8:11], v[162:165], v[202:205], v[8:11]
	v_mfma_f32_16x16x32_bf16 v[4:7], v[154:157], v[210:213], v[4:7]
	v_mfma_f32_16x16x32_bf16 v[0:3], v[162:165], v[210:213], v[0:3]
	v_mfma_f32_16x16x32_bf16 v[60:63], v[158:161], v[190:193], v[60:63]
	v_mfma_f32_16x16x32_bf16 v[56:59], v[166:169], v[190:193], v[56:59]
	v_mfma_f32_16x16x32_bf16 v[44:47], v[158:161], v[198:201], v[44:47]
	v_mfma_f32_16x16x32_bf16 v[32:35], v[166:169], v[198:201], v[32:35]
	v_mfma_f32_16x16x32_bf16 v[16:19], v[158:161], v[206:209], v[16:19]
	v_mfma_f32_16x16x32_bf16 v[8:11], v[166:169], v[206:209], v[8:11]
	v_mfma_f32_16x16x32_bf16 v[4:7], v[158:161], v[214:217], v[4:7]
	v_mfma_f32_16x16x32_bf16 v[0:3], v[166:169], v[214:217], v[0:3]
	v_mfma_f32_16x16x32_bf16 v[52:55], v[170:173], v[186:189], v[52:55]
	v_mfma_f32_16x16x32_bf16 v[48:51], v[178:181], v[186:189], v[48:51]
	v_mfma_f32_16x16x32_bf16 v[28:31], v[170:173], v[194:197], v[28:31]
	v_mfma_f32_16x16x32_bf16 v[12:15], v[178:181], v[194:197], v[12:15]
	v_mfma_f32_16x16x32_bf16 v[36:39], v[170:173], v[202:205], v[36:39]
	v_mfma_f32_16x16x32_bf16 v[40:43], v[178:181], v[202:205], v[40:43]
	v_mfma_f32_16x16x32_bf16 v[20:23], v[170:173], v[210:213], v[20:23]
	v_mfma_f32_16x16x32_bf16 v[24:27], v[178:181], v[210:213], v[24:27]
	v_mfma_f32_16x16x32_bf16 v[52:55], v[174:177], v[190:193], v[52:55]
	v_mfma_f32_16x16x32_bf16 v[48:51], v[182:185], v[190:193], v[48:51]
	v_mfma_f32_16x16x32_bf16 v[28:31], v[174:177], v[198:201], v[28:31]
	v_mfma_f32_16x16x32_bf16 v[12:15], v[182:185], v[198:201], v[12:15]
	v_mfma_f32_16x16x32_bf16 v[36:39], v[174:177], v[206:209], v[36:39]
	v_mfma_f32_16x16x32_bf16 v[40:43], v[182:185], v[206:209], v[40:43]
	v_mfma_f32_16x16x32_bf16 v[20:23], v[174:177], v[214:217], v[20:23]
	v_mfma_f32_16x16x32_bf16 v[24:27], v[182:185], v[214:217], v[24:27]
	s_barrier
	s_add_i32 s60, s60, 2
	s_add_u32 s0, s0, 0x100
	s_addc_u32 s1, s1, 0
	s_add_u32 s58, s58, 0x100
	s_addc_u32 s59, s59, 0
	s_cmp_gt_u32 s60, 13
	s_cbranch_scc0 .LBB0_662
	s_and_b64 vcc, exec, s[14:15]
	s_cbranch_vccz .LBB0_665
	s_barrier

; #define LAS __attribute__((address_space(3)))
; template <class Desc, class Epi>
; __device__ __forceinline__ void gemm_phase(const int wv_, LAS unsigned char* lds, const Desc& d, const Epi& E) {
;     ...
; #pragma unroll
;     for (int i = 0; i < 2; ++i) { int R, C; stage_rc(tid * 16 + i * 8192, R, C); const int Rb = (R & ~31) + perm32(R & 31); Rr[i] = R; Cc[i] = C;
;         voffA[i] = (unsigned)(R * d.lda + C) * 2u; voffA1[i] = voffA[i] + (unsigned)hstepA; voffB[i] = (unsigned)(Rb * d.ldb + C) * 2u; }
;     unsigned voffAn[2] = {0u, 0u}, voffAn1[2] = {0u, 0u};
;     LAS unsigned short* const tix = (LAS unsigned short*)(lds + STAGE_BYTES + 16384);
;     ...
;     const unsigned ldsw = (unsigned)wid * 1024u;
;     const int aoff = lds_byte(wr * 64 + fr, fq * 8), boff = lds_byte(wc * 32 + fr, fq * 8);
;     ...
;     GU cur, nxt; int ui = 0;
;     if (bid < 0 || bid >= d.nunits) return;
;     LAS float* const rsc = (LAS float*)(lds + STAGE_BYTES);
;     if constexpr (Epi::STAGED || Desc::GATHER) {
;         const int nmy = (d.nunits - bid + nblk - 1) / nblk;
;         for (int idx = tid; idx < nmy * 256; idx += NTHREADS) { GU su; d.unit(bid + (idx >> 8) * nblk, su);
;             if constexpr (Epi::STAGED) rsc[idx] = E.rowscale(su, idx & 255);
;             if constexpr (Desc::GATHER) tix[idx] = (unsigned short)d.tokidx(su, idx & 255); }
;         asm volatile("s_waitcnt vmcnt(0) lgkmcnt(0)" ::: "memory"); __builtin_amdgcn_s_barrier(); asm volatile("" ::: "memory");
;     }
;     d.unit(bid, cur);
;     if constexpr (Desc::GATHER) PG8_AOFF(0, cur, voffA, voffA1);
;     f32x4 acc[2][2][4][2];
; #pragma unroll
;     for (int a = 0; a < 2; ++a)
; #pragma unroll
;         for (int b = 0; b < 2; ++b)
; #pragma unroll
;             for (int m = 0; m < 4; ++m)
; #pragma unroll
;                 for (int n = 0; n < 2; ++n) acc[a][b][m][n] = (f32x4){0.f, 0.f, 0.f, 0.f};
;     bf16x8 At[4][2], B0[2][2], B1[2][2];
;     const char* cA = (const char*)cur.a; const char* cB = (const char*)cur.b;
;     PG8_STAGE(PG8_SB(0, 0), cB, voffB); PG8_STAGE(PG8_SB(0, 1), cB + hstepB, voffB); PG8_STAGE(PG8_SA(0, 0), cA, voffA); PG8_STAGE(PG8_SA(0, 1), cA, voffA1);
;     if (wr == 1) PG8_BAR;
;     PG8_WAIT_V(2); PG8_BAR;
;     PG8_STAGE(PG8_SB(1, 0), cB + kstep, voffB); PG8_STAGE(PG8_SA(1, 0), cA + kstep, voffA); PG8_STAGE(PG8_SB(1, 1), cB + hstepB + kstep, voffB);
;     PG8_WAIT_V(6); PG8_BAR;
.LBB0_739:
	s_or_b64 exec, exec, s[4:5]
	v_ashrrev_i32_e32 v2, 31, v0
	v_lshrrev_b32_e32 v2, 26, v2
	v_lshlrev_b32_e32 v1, 4, v0
	v_add_u32_e32 v2, v0, v2
	v_bfe_i32 v0, v0, 27, 1
	v_lshrrev_b32_e32 v0, 22, v0
	v_add_u32_e32 v0, v1, v0
	v_and_b32_e32 v0, 0xfffffc00, v0
	v_sub_u32_e32 v0, v1, v0
	v_lshrrev_b32_e32 v3, 4, v0
	v_bitop3_b32 v0, v3, v0, 32 bitop3:0x6c
	v_ashrrev_i32_e32 v5, 31, v0
	s_add_u32 s22, s29, 0x33600000
	v_readlane_b32 s0, v254, 57
	v_ashrrev_i32_e32 v2, 6, v2
	v_lshrrev_b32_e32 v5, 26, v5
	s_addc_u32 s23, s3, 0
	s_lshl_b32 s0, s0, 21
	v_lshlrev_b32_e32 v3, 3, v2
	v_add_u32_e32 v5, v0, v5
	v_readlane_b32 s1, v254, 58
	s_add_u32 s0, s29, s0
	v_and_b32_e32 v3, -16, v3
	v_ashrrev_i32_e32 v6, 6, v5
	v_and_b32_e32 v5, 0xc0, v5
	s_addc_u32 s1, s3, 0
	v_add_u32_e32 v3, v6, v3
	v_sub_u32_e32 v0, v0, v5
	s_add_u32 s24, s0, 0x100000
	v_lshlrev_b32_e32 v2, 5, v2
	v_ashrrev_i16_sdwa v0, v216, sext(v0) dst_sel:DWORD dst_unused:UNUSED_PAD src0_sel:DWORD src1_sel:BYTE_0
	v_lshlrev_b32_e32 v5, 1, v3
	v_lshrrev_b32_e32 v7, 2, v3
	v_and_b32_e32 v6, 3, v6
	s_mov_b32 s0, 0x1fffe0
	v_and_b32_e32 v2, 32, v2
	v_bfe_i32 v0, v0, 0, 16
	v_and_b32_e32 v5, 24, v5
	v_and_b32_e32 v7, 4, v7
	v_and_or_b32 v6, v3, s0, v6
	v_or3_b32 v5, v6, v7, v5
	v_add_lshl_u32 v0, v2, v0, 1
	v_lshl_add_u32 v132, v3, 11, v0
	v_lshl_add_u32 v134, v5, 11, v0
	v_add_u32_e32 v0, 0x2000, v1
	v_ashrrev_i32_e32 v1, 31, v0
	v_lshrrev_b32_e32 v1, 22, v1
	v_add_u32_e32 v1, v0, v1
	v_ashrrev_i32_e32 v1, 10, v1
	v_mul_i32_i24_e32 v2, 0x400, v1
	v_sub_u32_e32 v0, v0, v2
	v_lshrrev_b32_e32 v2, 4, v0
	v_bitop3_b32 v0, v2, v0, 32 bitop3:0x6c
	v_ashrrev_i32_e32 v3, 31, v0
	v_lshrrev_b32_e32 v3, 26, v3
	v_lshlrev_b32_e32 v2, 3, v1
	v_add_u32_e32 v3, v0, v3
	v_and_b32_e32 v2, -16, v2
	v_ashrrev_i32_e32 v5, 6, v3
	s_addc_u32 s25, s1, 0
	v_add_u32_e32 v2, v5, v2
	v_and_b32_e32 v5, 3, v5
	s_lshl_b32 s1, s52, 5
	v_and_b32_e32 v3, 0xc0, v3
	v_and_or_b32 v5, v2, s0, v5
	s_and_b32 s0, s52, 0x100
	s_and_b32 s1, s1, 0xe0
	s_lshr_b32 s4, s52, 3
	v_sub_u32_e32 v0, v0, v3
	s_and_b32 s4, s4, 28
	s_or_b32 s0, s1, s0
	v_lshlrev_b32_e32 v1, 5, v1
	v_ashrrev_i16_sdwa v0, v216, sext(v0) dst_sel:DWORD dst_unused:UNUSED_PAD src0_sel:DWORD src1_sel:BYTE_0
	v_lshlrev_b32_e32 v3, 1, v2
	v_lshrrev_b32_e32 v6, 2, v2
	s_ashr_i32 s41, s2, 6
	s_or_b32 s1, s0, s4
	s_bfe_u32 s0, s52, 0x20003
	s_ashr_i32 s40, s2, 8
	v_and_b32_e32 v1, 32, v1
	v_bfe_i32 v0, v0, 0, 16
	v_and_b32_e32 v3, 24, v3
	v_and_b32_e32 v6, 4, v6
	s_lshl_b32 s54, s41, 10
	s_lshl_b32 s4, s0, 19
	v_or3_b32 v3, v5, v6, v3
	v_add_lshl_u32 v0, v1, v0, 1
	s_add_u32 s4, s24, s4
	v_lshl_add_u32 v135, v2, 11, v0
	v_lshl_add_u32 v137, v3, 11, v0
	s_addc_u32 s5, s25, 0
	s_add_i32 s55, s54, 0
	s_waitcnt vmcnt(0) lgkmcnt(0)
	s_barrier
	s_add_i32 m0, s55, 0x10000
	v_add_u32_e32 v133, 0x40000, v132
	global_load_lds_dwordx4 v134, s[4:5]
	s_add_i32 m0, s55, 0x12000
	s_add_u32 s20, s4, 0x40000
	global_load_lds_dwordx4 v137, s[4:5]
	s_addc_u32 s21, s5, 0
	s_add_i32 m0, s55, 0x14000
	v_add_u32_e32 v136, 0x40000, v135
	global_load_lds_dwordx4 v134, s[20:21]
	s_add_i32 m0, s55, 0x16000
	s_nop 0
	global_load_lds_dwordx4 v137, s[20:21]
	s_lshl_b32 s20, s1, 17
	s_add_u32 s20, s22, s20
	s_addc_u32 s21, s23, 0
	s_mov_b32 m0, s55
	s_add_i32 s56, s55, 0x2000
	global_load_lds_dwordx4 v132, s[20:21]
	s_mov_b32 m0, s56
	s_add_i32 s57, s55, 0x4000
	global_load_lds_dwordx4 v135, s[20:21]
	s_mov_b32 m0, s57
	s_add_i32 s58, s55, 0x6000
	global_load_lds_dwordx4 v133, s[20:21]
	v_mov_b32_e32 v0, v136
	s_mov_b32 m0, s58
	s_cmp_eq_u32 s40, 1
	global_load_lds_dwordx4 v0, s[20:21]
	s_cselect_b64 s[36:37], -1, 0
	s_and_b64 vcc, exec, s[36:37]
	s_cbranch_vccz .LBB0_741
	s_barrier
.LBB0_741:
	s_lshr_b32 s1, s1, 2
	v_mov_b32_e32 v96, v134
	s_add_u32 s38, s29, 0x43200000
	s_waitcnt vmcnt(2)
	s_barrier
	s_addc_u32 s39, s3, 0
	v_lshl_add_u64 v[0:1], s[4:5], 0, v[96:97]
	s_add_i32 m0, s55, 0x18000
	v_lshl_add_u64 v[0:1], v[0:1], 0, s[30:31]
	v_mov_b32_e32 v96, v137
	global_load_lds_dwordx4 v[0:1], off
	s_add_i32 m0, s55, 0x1a000
	v_lshl_add_u64 v[0:1], s[4:5], 0, v[96:97]
	v_lshl_add_u64 v[0:1], v[0:1], 0, s[30:31]
	v_mov_b32_e32 v96, v132
	global_load_lds_dwordx4 v[0:1], off
	s_add_i32 s59, s55, 0x8000
	v_lshl_add_u64 v[0:1], s[20:21], 0, v[96:97]
	s_lshl_b32 s29, s41, 5
	v_lshl_add_u64 v[0:1], v[0:1], 0, s[30:31]
	s_mov_b32 m0, s59
	v_mov_b32_e32 v96, v135
	s_and_b32 s29, s29, 0x60
	global_load_lds_dwordx4 v[0:1], off
	s_add_i32 s60, s55, 0xa000
	v_lshl_add_u64 v[0:1], s[20:21], 0, v[96:97]
	s_lshl_b32 s3, s40, 13
	s_lshl_b32 s41, s29, 7
	v_lshl_add_u64 v[0:1], v[0:1], 0, s[30:31]
	s_mov_b32 m0, s60
	s_add_u32 s42, s4, 0x40080
	global_load_lds_dwordx4 v[0:1], off
	s_addc_u32 s43, s5, 0
	s_add_i32 m0, s55, 0x1c000
	v_lshrrev_b32_e32 v1, 1, v4
	global_load_lds_dwordx4 v134, s[42:43]
	s_add_i32 m0, s55, 0x1e000
	v_and_b32_e32 v1, 24, v1
	global_load_lds_dwordx4 v137, s[42:43]
	v_and_b32_e32 v0, 15, v4
	v_lshl_or_b32 v138, s40, 6, v0
	v_lshlrev_b32_e32 v2, 1, v1
	v_lshl_or_b32 v0, v0, 6, v2
	v_lshlrev_b32_e32 v2, 2, v138
	v_lshlrev_b32_e32 v4, 2, v4
	v_and_b32_e32 v3, 32, v2
	v_and_b32_e32 v4, 32, v4
	s_waitcnt vmcnt(6)
	s_cmpk_lt_u32 s2, 0x100
	v_bitop3_b32 v3, v0, s3, v3 bitop3:0xde
	v_bitop3_b32 v139, v0, s41, v4 bitop3:0xde
	s_cselect_b64 s[40:41], -1, 0
	s_add_i32 s2, 0, 0x20000
	v_or_b32_e32 v140, 16, v138
	v_or_b32_e32 v141, 32, v138
	v_or_b32_e32 v142, 48, v138
	v_add_u32_e32 v143, 0x80, v138
	v_add_u32_e32 v144, 0x90, v138
	v_add_u32_e32 v145, 0xa0, v138
	v_add_u32_e32 v146, 0xb0, v138
	v_or_b32_e32 v147, s29, v1
	v_add_u32_e32 v148, s2, v2
	s_mov_b32 s62, 0
	v_add_u32_e32 v149, 0, v3
	s_mov_b64 s[48:49], s[4:5]
	s_mov_b64 s[46:47], s[20:21]
	s_barrier
	s_waitcnt vmcnt(0)
	s_branch .LBB0_744

; #define PG8_STAGE(bufoff, gbase, voff) do { _Pragma("unroll") for (int _i = 0; _i < 2; ++_i) \
;         __builtin_amdgcn_global_load_lds((const __attribute__((address_space(1))) unsigned*)((const __attribute__((address_space(1))) char*)(gbase) + (unsigned)lnd_v((int)(voff)[_i])), (LAS unsigned*)(lds + (bufoff) + ldsw + _i * 8192), 16, 0, 0); } while (0)
; #define PG8_LDA(dst, b, h) do { _Pragma("unroll") for (int m = 0; m < 4; ++m) _Pragma("unroll") for (int k = 0; k < 2; ++k) dst[m][k] = *(const LAS bf16x8*)(lds + PG8_SA(b, h) + aoff + m * 2048 + k * 1024); } while (0)
; #define PG8_LDB(dst, b, h) do { _Pragma("unroll") for (int n = 0; n < 2; ++n) _Pragma("unroll") for (int k = 0; k < 2; ++k) dst[n][k] = *(const LAS bf16x8*)(lds + PG8_SB(b, h) + boff + n * 2048 + k * 1024); } while (0)
; #define PG8_WAIT_V(n) asm volatile("s_waitcnt vmcnt(" #n ")" ::: "memory")
; #define PG8_WAIT_L(n) asm volatile("s_waitcnt lgkmcnt(" #n ")" ::: "memory")
; #define PG8_BAR __builtin_amdgcn_s_barrier()
; template <class Desc, class Epi>
; __device__ __forceinline__ void gemm_phase(const int wv_, LAS unsigned char* lds, const Desc& d, const Epi& E) {
;     ...
;         for (int t = 0; t < nt; t += 2) {
;             const bool last = (t == nt - 2);
;             unsigned sA0[2], sA1[2];
;             if constexpr (Desc::GATHER) { sA0[0] = last ? voffAn[0] : voffA[0]; sA0[1] = last ? voffAn[1] : voffA[1]; sA1[0] = last ? voffAn1[0] : voffA1[0]; sA1[1] = last ? voffAn1[1] : voffA1[1]; }
;             else { sA0[0] = voffA[0]; sA0[1] = voffA[1]; sA1[0] = voffA1[0]; sA1[1] = voffA1[1]; }
;             const char* a1 = cA + (size_t)(t + 1) * kstep;
;             const char* a2 = last ? nA : cA + (size_t)(t + 2) * kstep; const char* b2 = last ? nB : cB + (size_t)(t + 2) * kstep;
;             const char* a3 = a2 + kstep; const char* b3 = b2 + kstep;
;             PG8_LDB(B0, 0, 0); PG8_LDB(B1, 0, 1); PG8_SCHED; PG8_LDA(At, 0, 0); PG8_STAGE(PG8_SA(1, 1), a1, voffA1);
;             PG8_WAIT_V(8); PG8_WAIT_L(0); PG8_BAR; PG8_MMA(0, 0, At, B0); PG8_MMA(0, 1, At, B1); PG8_BAR; PG8_SCHED;
;             PG8_LDA(At, 0, 1); PG8_STAGE(PG8_SB(0, 0), b2, voffB); PG8_STAGE(PG8_SB(0, 1), b2 + hstepB, voffB); PG8_STAGE(PG8_SA(0, 0), a2, sA0);
;             PG8_WAIT_V(8); PG8_WAIT_L(0); PG8_BAR; PG8_MMA(1, 0, At, B0); PG8_MMA(1, 1, At, B1); PG8_BAR; PG8_SCHED;
.LBB0_747:
	s_add_u32 s4, s2, 0x80
	s_addc_u32 s5, s3, 0
	s_add_i32 s63, 0, 0x10000
	s_cmp_eq_u32 s45, 12
	s_cselect_b32 s5, s47, s5
	s_cselect_b32 s4, s46, s4
	v_add_u32_e32 v96, s63, v139
	s_cselect_b32 s21, s49, s43
	s_cselect_b32 s20, s48, s29
	s_add_i32 s66, 0, 0x14000
	ds_read_b128 v[150:153], v96
	ds_read_b128 v[154:157], v96 offset:1024
	ds_read_b128 v[158:161], v96 offset:2048
	ds_read_b128 v[162:165], v96 offset:3072
	v_add_u32_e32 v96, s66, v139
	ds_read_b128 v[166:169], v96
	ds_read_b128 v[170:173], v96 offset:1024
	ds_read_b128 v[174:177], v96 offset:2048
	ds_read_b128 v[178:181], v96 offset:3072
	ds_read_b128 v[182:185], v149
	ds_read_b128 v[186:189], v149 offset:1024
	ds_read_b128 v[190:193], v149 offset:2048
	ds_read_b128 v[194:197], v149 offset:3072
	ds_read_b128 v[198:201], v149 offset:4096
	ds_read_b128 v[202:205], v149 offset:5120
	ds_read_b128 v[206:209], v149 offset:6144
	ds_read_b128 v[210:213], v149 offset:7168
	s_add_i32 m0, s55, 0xc000
	s_nop 0
	global_load_lds_dwordx4 v133, s[2:3]
	s_add_i32 m0, s55, 0xe000
	s_nop 0
	global_load_lds_dwordx4 v136, s[2:3]
	s_waitcnt vmcnt(8)
	s_waitcnt lgkmcnt(0)
	s_barrier
	s_waitcnt lgkmcnt(0)
	v_mfma_f32_16x16x32_bf16 v[126:129], v[150:153], v[182:185], v[126:129]
	v_mfma_f32_16x16x32_bf16 v[122:125], v[158:161], v[182:185], v[122:125]
	v_mfma_f32_16x16x32_bf16 v[110:113], v[150:153], v[190:193], v[110:113]
	v_mfma_f32_16x16x32_bf16 v[106:109], v[158:161], v[190:193], v[106:109]
	v_mfma_f32_16x16x32_bf16 v[92:95], v[150:153], v[198:201], v[92:95]
	v_mfma_f32_16x16x32_bf16 v[88:91], v[158:161], v[198:201], v[88:91]
	v_mfma_f32_16x16x32_bf16 v[76:79], v[150:153], v[206:209], v[76:79]
	v_mfma_f32_16x16x32_bf16 v[72:75], v[158:161], v[206:209], v[72:75]
	v_mfma_f32_16x16x32_bf16 v[126:129], v[154:157], v[186:189], v[126:129]
	v_mfma_f32_16x16x32_bf16 v[122:125], v[162:165], v[186:189], v[122:125]
	v_mfma_f32_16x16x32_bf16 v[110:113], v[154:157], v[194:197], v[110:113]
	v_mfma_f32_16x16x32_bf16 v[106:109], v[162:165], v[194:197], v[106:109]
	v_mfma_f32_16x16x32_bf16 v[92:95], v[154:157], v[202:205], v[92:95]
	v_mfma_f32_16x16x32_bf16 v[88:91], v[162:165], v[202:205], v[88:91]
	v_mfma_f32_16x16x32_bf16 v[76:79], v[154:157], v[210:213], v[76:79]
	v_mfma_f32_16x16x32_bf16 v[72:75], v[162:165], v[210:213], v[72:75]
	v_mfma_f32_16x16x32_bf16 v[118:121], v[166:169], v[182:185], v[118:121]
	v_mfma_f32_16x16x32_bf16 v[114:117], v[174:177], v[182:185], v[114:117]
	v_mfma_f32_16x16x32_bf16 v[102:105], v[166:169], v[190:193], v[102:105]
	v_mfma_f32_16x16x32_bf16 v[98:101], v[174:177], v[190:193], v[98:101]
	v_mfma_f32_16x16x32_bf16 v[84:87], v[166:169], v[198:201], v[84:87]
	v_mfma_f32_16x16x32_bf16 v[80:83], v[174:177], v[198:201], v[80:83]
	v_mfma_f32_16x16x32_bf16 v[68:71], v[166:169], v[206:209], v[68:71]
	v_mfma_f32_16x16x32_bf16 v[64:67], v[174:177], v[206:209], v[64:67]
	v_mfma_f32_16x16x32_bf16 v[118:121], v[170:173], v[186:189], v[118:121]
	v_mfma_f32_16x16x32_bf16 v[114:117], v[178:181], v[186:189], v[114:117]
	v_mfma_f32_16x16x32_bf16 v[102:105], v[170:173], v[194:197], v[102:105]
	v_mfma_f32_16x16x32_bf16 v[98:101], v[178:181], v[194:197], v[98:101]
	v_mfma_f32_16x16x32_bf16 v[84:87], v[170:173], v[202:205], v[84:87]
	v_mfma_f32_16x16x32_bf16 v[80:83], v[178:181], v[202:205], v[80:83]
	v_mfma_f32_16x16x32_bf16 v[68:71], v[170:173], v[210:213], v[68:71]
	v_mfma_f32_16x16x32_bf16 v[64:67], v[178:181], v[210:213], v[64:67]
	s_barrier
	s_add_i32 s63, s63, s54
	ds_read_b128 v[182:185], v149 offset:16384
	ds_read_b128 v[186:189], v149 offset:17408
	ds_read_b128 v[190:193], v149 offset:18432
	ds_read_b128 v[194:197], v149 offset:19456
	ds_read_b128 v[198:201], v149 offset:20480
	ds_read_b128 v[202:205], v149 offset:21504
	ds_read_b128 v[206:209], v149 offset:22528
	ds_read_b128 v[210:213], v149 offset:23552
	s_mov_b32 m0, s63
	s_nop 0
	global_load_lds_dwordx4 v134, s[20:21]
	s_add_i32 m0, s63, 0x2000
	s_add_u32 s64, s20, 0x40000
	global_load_lds_dwordx4 v137, s[20:21]
	s_addc_u32 s65, s21, 0
	s_add_i32 s63, s66, s54
	s_mov_b32 m0, s63
	s_nop 0
	global_load_lds_dwordx4 v134, s[64:65]
	s_add_i32 m0, s63, 0x2000
	s_nop 0
	global_load_lds_dwordx4 v137, s[64:65]
	s_mov_b32 m0, s55
	s_nop 0
	global_load_lds_dwordx4 v132, s[4:5]
	s_mov_b32 m0, s56
	s_nop 0
	global_load_lds_dwordx4 v135, s[4:5]
	s_waitcnt vmcnt(8)
	s_waitcnt lgkmcnt(0)
	s_barrier
	s_waitcnt lgkmcnt(0)
	v_mfma_f32_16x16x32_bf16 v[60:63], v[150:153], v[182:185], v[60:63]
	v_mfma_f32_16x16x32_bf16 v[56:59], v[158:161], v[182:185], v[56:59]
	v_mfma_f32_16x16x32_bf16 v[44:47], v[150:153], v[190:193], v[44:47]
	v_mfma_f32_16x16x32_bf16 v[32:35], v[158:161], v[190:193], v[32:35]
	v_mfma_f32_16x16x32_bf16 v[16:19], v[150:153], v[198:201], v[16:19]
	v_mfma_f32_16x16x32_bf16 v[8:11], v[158:161], v[198:201], v[8:11]
	v_mfma_f32_16x16x32_bf16 v[4:7], v[150:153], v[206:209], v[4:7]
	v_mfma_f32_16x16x32_bf16 v[0:3], v[158:161], v[206:209], v[0:3]
	v_mfma_f32_16x16x32_bf16 v[60:63], v[154:157], v[186:189], v[60:63]
	v_mfma_f32_16x16x32_bf16 v[56:59], v[162:165], v[186:189], v[56:59]
	v_mfma_f32_16x16x32_bf16 v[44:47], v[154:157], v[194:197], v[44:47]
	v_mfma_f32_16x16x32_bf16 v[32:35], v[162:165], v[194:197], v[32:35]
	v_mfma_f32_16x16x32_bf16 v[16:19], v[154:157], v[202:205], v[16:19]
	v_mfma_f32_16x16x32_bf16 v[8:11], v[162:165], v[202:205], v[8:11]
	v_mfma_f32_16x16x32_bf16 v[4:7], v[154:157], v[210:213], v[4:7]
	v_mfma_f32_16x16x32_bf16 v[0:3], v[162:165], v[210:213], v[0:3]
	v_mfma_f32_16x16x32_bf16 v[52:55], v[166:169], v[182:185], v[52:55]
	v_mfma_f32_16x16x32_bf16 v[48:51], v[174:177], v[182:185], v[48:51]
	v_mfma_f32_16x16x32_bf16 v[28:31], v[166:169], v[190:193], v[28:31]
	v_mfma_f32_16x16x32_bf16 v[12:15], v[174:177], v[190:193], v[12:15]
	v_mfma_f32_16x16x32_bf16 v[36:39], v[166:169], v[198:201], v[36:39]
	v_mfma_f32_16x16x32_bf16 v[40:43], v[174:177], v[198:201], v[40:43]
	v_mfma_f32_16x16x32_bf16 v[20:23], v[166:169], v[206:209], v[20:23]
	v_mfma_f32_16x16x32_bf16 v[24:27], v[174:177], v[206:209], v[24:27]
	v_mfma_f32_16x16x32_bf16 v[52:55], v[170:173], v[186:189], v[52:55]
	v_mfma_f32_16x16x32_bf16 v[48:51], v[178:181], v[186:189], v[48:51]
	v_mfma_f32_16x16x32_bf16 v[28:31], v[170:173], v[194:197], v[28:31]
	v_mfma_f32_16x16x32_bf16 v[12:15], v[178:181], v[194:197], v[12:15]
	v_mfma_f32_16x16x32_bf16 v[36:39], v[170:173], v[202:205], v[36:39]
	v_mfma_f32_16x16x32_bf16 v[40:43], v[178:181], v[202:205], v[40:43]
	v_mfma_f32_16x16x32_bf16 v[20:23], v[170:173], v[210:213], v[20:23]
	v_mfma_f32_16x16x32_bf16 v[24:27], v[178:181], v[210:213], v[24:27]
	s_barrier
; #define PG8_STAGE(bufoff, gbase, voff) do { _Pragma("unroll") for (int _i = 0; _i < 2; ++_i) \
;         __builtin_amdgcn_global_load_lds((const __attribute__((address_space(1))) unsigned*)((const __attribute__((address_space(1))) char*)(gbase) + (unsigned)lnd_v((int)(voff)[_i])), (LAS unsigned*)(lds + (bufoff) + ldsw + _i * 8192), 16, 0, 0); } while (0)
; #define PG8_LDA(dst, b, h) do { _Pragma("unroll") for (int m = 0; m < 4; ++m) _Pragma("unroll") for (int k = 0; k < 2; ++k) dst[m][k] = *(const LAS bf16x8*)(lds + PG8_SA(b, h) + aoff + m * 2048 + k * 1024); } while (0)
; #define PG8_LDB(dst, b, h) do { _Pragma("unroll") for (int n = 0; n < 2; ++n) _Pragma("unroll") for (int k = 0; k < 2; ++k) dst[n][k] = *(const LAS bf16x8*)(lds + PG8_SB(b, h) + boff + n * 2048 + k * 1024); } while (0)
; #define PG8_MMA(ai, bj, At, Bt) do { __builtin_amdgcn_s_setprio(1); _Pragma("unroll") for (int m = 0; m < 4; ++m) _Pragma("unroll") for (int n = 0; n < 2; ++n) _Pragma("unroll") for (int k = 0; k < 2; ++k) \
;         acc[ai][bj][m][n] = __builtin_amdgcn_mfma_f32_16x16x32_bf16(Bt[n][k], At[m][k], acc[ai][bj][m][n], 0, 0, 0); __builtin_amdgcn_s_setprio(0); } while (0)
; #define PG8_WAIT_V(n) asm volatile("s_waitcnt vmcnt(" #n ")" ::: "memory")
; #define PG8_WAIT_L(n) asm volatile("s_waitcnt lgkmcnt(" #n ")" ::: "memory")
; #define PG8_BAR __builtin_amdgcn_s_barrier()
; #define PG8_SCHED __builtin_amdgcn_sched_barrier(0)
; template <class Desc, class Epi>
; __device__ __forceinline__ void gemm_phase(const int wv_, LAS unsigned char* lds, const Desc& d, const Epi& E) {
;     ...
;             PG8_LDB(B0, 1, 0); PG8_LDB(B1, 1, 1); PG8_SCHED; PG8_LDA(At, 1, 0); PG8_STAGE(PG8_SA(0, 1), a2, sA1);
;             PG8_WAIT_V(8); PG8_WAIT_L(0); PG8_BAR; PG8_MMA(0, 0, At, B0); PG8_MMA(0, 1, At, B1); PG8_BAR; PG8_SCHED;
	s_add_i32 s63, 0, 0x18000
	v_add_u32_e32 v96, s63, v139
	s_add_i32 s64, 0, 0x1c000
	ds_read_b128 v[150:153], v96
	ds_read_b128 v[154:157], v96 offset:1024
	ds_read_b128 v[158:161], v96 offset:2048
	ds_read_b128 v[162:165], v96 offset:3072
	v_add_u32_e32 v96, s64, v139
	ds_read_b128 v[166:169], v96
	ds_read_b128 v[170:173], v96 offset:1024
	ds_read_b128 v[174:177], v96 offset:2048
	ds_read_b128 v[178:181], v96 offset:3072
	s_mov_b32 m0, s57
	ds_read_b128 v[182:185], v149 offset:32768
	ds_read_b128 v[186:189], v149 offset:33792
	ds_read_b128 v[190:193], v149 offset:34816
	ds_read_b128 v[194:197], v149 offset:35840
	ds_read_b128 v[198:201], v149 offset:36864
	ds_read_b128 v[202:205], v149 offset:37888
	ds_read_b128 v[206:209], v149 offset:38912
	ds_read_b128 v[210:213], v149 offset:39936
	s_nop 0
	global_load_lds_dwordx4 v133, s[4:5]
	s_mov_b32 m0, s58
	s_nop 0
	global_load_lds_dwordx4 v136, s[4:5]
	s_waitcnt vmcnt(8)
	s_waitcnt lgkmcnt(0)
	s_barrier
	s_waitcnt lgkmcnt(0)
	v_mfma_f32_16x16x32_bf16 v[126:129], v[150:153], v[182:185], v[126:129]
	v_mfma_f32_16x16x32_bf16 v[122:125], v[158:161], v[182:185], v[122:125]
	v_mfma_f32_16x16x32_bf16 v[110:113], v[150:153], v[190:193], v[110:113]
	v_mfma_f32_16x16x32_bf16 v[106:109], v[158:161], v[190:193], v[106:109]
	v_mfma_f32_16x16x32_bf16 v[92:95], v[150:153], v[198:201], v[92:95]
	v_mfma_f32_16x16x32_bf16 v[88:91], v[158:161], v[198:201], v[88:91]
	v_mfma_f32_16x16x32_bf16 v[76:79], v[150:153], v[206:209], v[76:79]
	v_mfma_f32_16x16x32_bf16 v[72:75], v[158:161], v[206:209], v[72:75]
	v_mfma_f32_16x16x32_bf16 v[126:129], v[154:157], v[186:189], v[126:129]
	v_mfma_f32_16x16x32_bf16 v[122:125], v[162:165], v[186:189], v[122:125]
	v_mfma_f32_16x16x32_bf16 v[110:113], v[154:157], v[194:197], v[110:113]
	v_mfma_f32_16x16x32_bf16 v[106:109], v[162:165], v[194:197], v[106:109]
	v_mfma_f32_16x16x32_bf16 v[92:95], v[154:157], v[202:205], v[92:95]
	v_mfma_f32_16x16x32_bf16 v[88:91], v[162:165], v[202:205], v[88:91]
	v_mfma_f32_16x16x32_bf16 v[76:79], v[154:157], v[210:213], v[76:79]
	v_mfma_f32_16x16x32_bf16 v[72:75], v[162:165], v[210:213], v[72:75]
	v_mfma_f32_16x16x32_bf16 v[118:121], v[166:169], v[182:185], v[118:121]
	v_mfma_f32_16x16x32_bf16 v[114:117], v[174:177], v[182:185], v[114:117]
	v_mfma_f32_16x16x32_bf16 v[102:105], v[166:169], v[190:193], v[102:105]
	v_mfma_f32_16x16x32_bf16 v[98:101], v[174:177], v[190:193], v[98:101]
	v_mfma_f32_16x16x32_bf16 v[84:87], v[166:169], v[198:201], v[84:87]
	v_mfma_f32_16x16x32_bf16 v[80:83], v[174:177], v[198:201], v[80:83]
	v_mfma_f32_16x16x32_bf16 v[68:71], v[166:169], v[206:209], v[68:71]
	v_mfma_f32_16x16x32_bf16 v[64:67], v[174:177], v[206:209], v[64:67]
	v_mfma_f32_16x16x32_bf16 v[118:121], v[170:173], v[186:189], v[118:121]
	v_mfma_f32_16x16x32_bf16 v[114:117], v[178:181], v[186:189], v[114:117]
	v_mfma_f32_16x16x32_bf16 v[102:105], v[170:173], v[194:197], v[102:105]
	v_mfma_f32_16x16x32_bf16 v[98:101], v[178:181], v[194:197], v[98:101]
	v_mfma_f32_16x16x32_bf16 v[84:87], v[170:173], v[202:205], v[84:87]
	v_mfma_f32_16x16x32_bf16 v[80:83], v[178:181], v[202:205], v[80:83]
	v_mfma_f32_16x16x32_bf16 v[68:71], v[170:173], v[210:213], v[68:71]
	v_mfma_f32_16x16x32_bf16 v[64:67], v[178:181], v[210:213], v[64:67]
	s_barrier
; #define PG8_STAGE(bufoff, gbase, voff) do { _Pragma("unroll") for (int _i = 0; _i < 2; ++_i) \
;         __builtin_amdgcn_global_load_lds((const __attribute__((address_space(1))) unsigned*)((const __attribute__((address_space(1))) char*)(gbase) + (unsigned)lnd_v((int)(voff)[_i])), (LAS unsigned*)(lds + (bufoff) + ldsw + _i * 8192), 16, 0, 0); } while (0)
; #define PG8_LDA(dst, b, h) do { _Pragma("unroll") for (int m = 0; m < 4; ++m) _Pragma("unroll") for (int k = 0; k < 2; ++k) dst[m][k] = *(const LAS bf16x8*)(lds + PG8_SA(b, h) + aoff + m * 2048 + k * 1024); } while (0)
; #define PG8_MMA(ai, bj, At, Bt) do { __builtin_amdgcn_s_setprio(1); _Pragma("unroll") for (int m = 0; m < 4; ++m) _Pragma("unroll") for (int n = 0; n < 2; ++n) _Pragma("unroll") for (int k = 0; k < 2; ++k) \
;         acc[ai][bj][m][n] = __builtin_amdgcn_mfma_f32_16x16x32_bf16(Bt[n][k], At[m][k], acc[ai][bj][m][n], 0, 0, 0); __builtin_amdgcn_s_setprio(0); } while (0)
; #define PG8_WAIT_V(n) asm volatile("s_waitcnt vmcnt(" #n ")" ::: "memory")
; #define PG8_WAIT_L(n) asm volatile("s_waitcnt lgkmcnt(" #n ")" ::: "memory")
; #define PG8_BAR __builtin_amdgcn_s_barrier()
; #define PG8_SCHED __builtin_amdgcn_sched_barrier(0)
; template <class Desc, class Epi>
; __device__ __forceinline__ void gemm_phase(const int wv_, LAS unsigned char* lds, const Desc& d, const Epi& E) {
;     ...
;             PG8_LDA(At, 1, 1); PG8_STAGE(PG8_SB(1, 0), b3, voffB); PG8_STAGE(PG8_SB(1, 1), b3 + hstepB, voffB); PG8_STAGE(PG8_SA(1, 0), a3, sA0);
;             PG8_WAIT_V(8); PG8_WAIT_L(0); PG8_BAR; PG8_MMA(1, 0, At, B0); PG8_MMA(1, 1, At, B1); PG8_BAR; PG8_SCHED;
;         }
;         if (wr == 0) PG8_BAR;
	v_mov_b32_e32 v96, v134
	ds_read_b128 v[182:185], v149 offset:49152
	ds_read_b128 v[186:189], v149 offset:50176
	ds_read_b128 v[190:193], v149 offset:51200
	ds_read_b128 v[194:197], v149 offset:52224
	ds_read_b128 v[198:201], v149 offset:53248
	ds_read_b128 v[202:205], v149 offset:54272
	ds_read_b128 v[206:209], v149 offset:55296
	ds_read_b128 v[210:213], v149 offset:56320
	s_add_i32 s63, s63, s54
	v_lshl_add_u64 v[130:131], s[20:21], 0, v[96:97]
	v_lshl_add_u64 v[130:131], v[130:131], 0, s[30:31]
	s_mov_b32 m0, s63
	v_mov_b32_e32 v96, v137
	global_load_lds_dwordx4 v[130:131], off
	s_add_i32 m0, s63, 0x2000
	s_nop 0
	v_lshl_add_u64 v[130:131], s[20:21], 0, v[96:97]
	s_add_u32 s20, s20, 0x40080
	v_lshl_add_u64 v[130:131], v[130:131], 0, s[30:31]
	s_addc_u32 s21, s21, 0
	s_add_i32 s63, s64, s54
	global_load_lds_dwordx4 v[130:131], off
	s_mov_b32 m0, s63
	s_nop 0
	global_load_lds_dwordx4 v134, s[20:21]
	s_add_i32 m0, s63, 0x2000
	s_nop 0
	global_load_lds_dwordx4 v137, s[20:21]
	v_mov_b32_e32 v96, v132
	s_mov_b32 m0, s59
	v_lshl_add_u64 v[130:131], s[4:5], 0, v[96:97]
	v_lshl_add_u64 v[130:131], v[130:131], 0, s[30:31]
	v_mov_b32_e32 v96, v135
	global_load_lds_dwordx4 v[130:131], off
	s_mov_b32 m0, s60
	v_lshl_add_u64 v[130:131], s[4:5], 0, v[96:97]
	v_lshl_add_u64 v[130:131], v[130:131], 0, s[30:31]
	global_load_lds_dwordx4 v[130:131], off
	s_waitcnt vmcnt(8)
	s_waitcnt lgkmcnt(0)
	s_barrier
	s_waitcnt lgkmcnt(0)
	v_mfma_f32_16x16x32_bf16 v[60:63], v[150:153], v[182:185], v[60:63]
	v_mfma_f32_16x16x32_bf16 v[56:59], v[158:161], v[182:185], v[56:59]
	v_mfma_f32_16x16x32_bf16 v[44:47], v[150:153], v[190:193], v[44:47]
	v_mfma_f32_16x16x32_bf16 v[32:35], v[158:161], v[190:193], v[32:35]
	v_mfma_f32_16x16x32_bf16 v[16:19], v[150:153], v[198:201], v[16:19]
	v_mfma_f32_16x16x32_bf16 v[8:11], v[158:161], v[198:201], v[8:11]
	v_mfma_f32_16x16x32_bf16 v[4:7], v[150:153], v[206:209], v[4:7]
	v_mfma_f32_16x16x32_bf16 v[0:3], v[158:161], v[206:209], v[0:3]
	v_mfma_f32_16x16x32_bf16 v[60:63], v[154:157], v[186:189], v[60:63]
	v_mfma_f32_16x16x32_bf16 v[56:59], v[162:165], v[186:189], v[56:59]
	v_mfma_f32_16x16x32_bf16 v[44:47], v[154:157], v[194:197], v[44:47]
	v_mfma_f32_16x16x32_bf16 v[32:35], v[162:165], v[194:197], v[32:35]
	v_mfma_f32_16x16x32_bf16 v[16:19], v[154:157], v[202:205], v[16:19]
	v_mfma_f32_16x16x32_bf16 v[8:11], v[162:165], v[202:205], v[8:11]
	v_mfma_f32_16x16x32_bf16 v[4:7], v[154:157], v[210:213], v[4:7]
	v_mfma_f32_16x16x32_bf16 v[0:3], v[162:165], v[210:213], v[0:3]
	v_mfma_f32_16x16x32_bf16 v[52:55], v[166:169], v[182:185], v[52:55]
	v_mfma_f32_16x16x32_bf16 v[48:51], v[174:177], v[182:185], v[48:51]
	v_mfma_f32_16x16x32_bf16 v[28:31], v[166:169], v[190:193], v[28:31]
	v_mfma_f32_16x16x32_bf16 v[12:15], v[174:177], v[190:193], v[12:15]
	v_mfma_f32_16x16x32_bf16 v[36:39], v[166:169], v[198:201], v[36:39]
	v_mfma_f32_16x16x32_bf16 v[40:43], v[174:177], v[198:201], v[40:43]
	v_mfma_f32_16x16x32_bf16 v[20:23], v[166:169], v[206:209], v[20:23]
	v_mfma_f32_16x16x32_bf16 v[24:27], v[174:177], v[206:209], v[24:27]
	v_mfma_f32_16x16x32_bf16 v[52:55], v[170:173], v[186:189], v[52:55]
	v_mfma_f32_16x16x32_bf16 v[48:51], v[178:181], v[186:189], v[48:51]
	v_mfma_f32_16x16x32_bf16 v[28:31], v[170:173], v[194:197], v[28:31]
	v_mfma_f32_16x16x32_bf16 v[12:15], v[178:181], v[194:197], v[12:15]
	v_mfma_f32_16x16x32_bf16 v[36:39], v[170:173], v[202:205], v[36:39]
	v_mfma_f32_16x16x32_bf16 v[40:43], v[178:181], v[202:205], v[40:43]
	v_mfma_f32_16x16x32_bf16 v[20:23], v[170:173], v[210:213], v[20:23]
	v_mfma_f32_16x16x32_bf16 v[24:27], v[178:181], v[210:213], v[24:27]
	s_barrier
	s_add_i32 s45, s45, 2
	s_add_u32 s2, s2, 0x100
	s_addc_u32 s3, s3, 0
	s_add_u32 s29, s29, 0x100
	s_addc_u32 s43, s43, 0
	s_cmp_gt_u32 s45, 13
	s_cbranch_scc0 .LBB0_747
	s_and_b64 vcc, exec, s[40:41]
	s_cbranch_vccz .LBB0_750
	s_barrier

; #define LAS __attribute__((address_space(3)))
; template <class Desc, class Epi>
; __device__ __forceinline__ void gemm_phase(const int wv_, LAS unsigned char* lds, const Desc& d, const Epi& E) {
;     ...
; #pragma unroll
;     for (int i = 0; i < 2; ++i) { int R, C; stage_rc(tid * 16 + i * 8192, R, C); const int Rb = (R & ~31) + perm32(R & 31); Rr[i] = R; Cc[i] = C;
;         voffA[i] = (unsigned)(R * d.lda + C) * 2u; voffA1[i] = voffA[i] + (unsigned)hstepA; voffB[i] = (unsigned)(Rb * d.ldb + C) * 2u; }
;     unsigned voffAn[2] = {0u, 0u}, voffAn1[2] = {0u, 0u};
;     LAS unsigned short* const tix = (LAS unsigned short*)(lds + STAGE_BYTES + 16384);
;     ...
;     const unsigned ldsw = (unsigned)wid * 1024u;
;     const int aoff = lds_byte(wr * 64 + fr, fq * 8), boff = lds_byte(wc * 32 + fr, fq * 8);
;     ...
;     GU cur, nxt; int ui = 0;
;     if (bid < 0 || bid >= d.nunits) return;
;     LAS float* const rsc = (LAS float*)(lds + STAGE_BYTES);
;     if constexpr (Epi::STAGED || Desc::GATHER) {
;         const int nmy = (d.nunits - bid + nblk - 1) / nblk;
;         for (int idx = tid; idx < nmy * 256; idx += NTHREADS) { GU su; d.unit(bid + (idx >> 8) * nblk, su);
;             if constexpr (Epi::STAGED) rsc[idx] = E.rowscale(su, idx & 255);
;             if constexpr (Desc::GATHER) tix[idx] = (unsigned short)d.tokidx(su, idx & 255); }
;         asm volatile("s_waitcnt vmcnt(0) lgkmcnt(0)" ::: "memory"); __builtin_amdgcn_s_barrier(); asm volatile("" ::: "memory");
;     }
;     d.unit(bid, cur);
;     if constexpr (Desc::GATHER) PG8_AOFF(0, cur, voffA, voffA1);
;     f32x4 acc[2][2][4][2];
; #pragma unroll
;     for (int a = 0; a < 2; ++a)
; #pragma unroll
;         for (int b = 0; b < 2; ++b)
; #pragma unroll
;             for (int m = 0; m < 4; ++m)
; #pragma unroll
;                 for (int n = 0; n < 2; ++n) acc[a][b][m][n] = (f32x4){0.f, 0.f, 0.f, 0.f};
;     bf16x8 At[4][2], B0[2][2], B1[2][2];
;     const char* cA = (const char*)cur.a; const char* cB = (const char*)cur.b;
;     PG8_STAGE(PG8_SB(0, 0), cB, voffB); PG8_STAGE(PG8_SB(0, 1), cB + hstepB, voffB); PG8_STAGE(PG8_SA(0, 0), cA, voffA); PG8_STAGE(PG8_SA(0, 1), cA, voffA1);
;     if (wr == 1) PG8_BAR;
;     PG8_WAIT_V(2); PG8_BAR;
;     PG8_STAGE(PG8_SB(1, 0), cB + kstep, voffB); PG8_STAGE(PG8_SA(1, 0), cA + kstep, voffA); PG8_STAGE(PG8_SB(1, 1), cB + hstepB + kstep, voffB);
;     PG8_WAIT_V(6); PG8_BAR;
.LBB0_882:
	s_or_b64 exec, exec, s[2:3]
	v_ashrrev_i32_e32 v2, 31, v0
	v_lshrrev_b32_e32 v2, 26, v2
	v_lshlrev_b32_e32 v1, 4, v0
	v_add_u32_e32 v2, v0, v2
	v_bfe_i32 v0, v0, 27, 1
	v_lshrrev_b32_e32 v0, 22, v0
	v_add_u32_e32 v0, v1, v0
	v_and_b32_e32 v0, 0xfffffc00, v0
	v_sub_u32_e32 v0, v1, v0
	v_lshrrev_b32_e32 v3, 4, v0
	v_bitop3_b32 v0, v3, v0, 32 bitop3:0x6c
	v_readlane_b32 s0, v254, 57
	v_ashrrev_i32_e32 v5, 31, v0
	v_readlane_b32 s1, v254, 58
	s_mul_i32 s26, s0, 0x30000
	s_add_u32 s65, s38, 0x43200400
	v_ashrrev_i32_e32 v2, 6, v2
	v_lshrrev_b32_e32 v5, 26, v5
	s_addc_u32 s66, s39, 0
	s_lshl_b64 s[0:1], s[26:27], 1
	v_lshlrev_b32_e32 v3, 3, v2
	v_add_u32_e32 v5, v0, v5
	s_add_u32 s0, s38, s0
	v_and_b32_e32 v3, -16, v3
	v_ashrrev_i32_e32 v6, 6, v5
	v_and_b32_e32 v5, 0xc0, v5
	s_addc_u32 s1, s39, s1
	v_add_u32_e32 v3, v6, v3
	v_sub_u32_e32 v0, v0, v5
	s_add_u32 s26, s0, 0x900000
	v_lshlrev_b32_e32 v2, 5, v2
	v_ashrrev_i16_sdwa v0, v216, sext(v0) dst_sel:DWORD dst_unused:UNUSED_PAD src0_sel:DWORD src1_sel:BYTE_0
	v_lshlrev_b32_e32 v5, 1, v3
	v_lshrrev_b32_e32 v7, 2, v3
	v_and_b32_e32 v6, 3, v6
	s_mov_b32 s0, 0x7fffe0
	v_and_b32_e32 v2, 32, v2
	v_bfe_i32 v0, v0, 0, 16
	v_and_b32_e32 v5, 24, v5
	v_and_b32_e32 v7, 4, v7
	v_and_or_b32 v6, v3, s0, v6
	v_or3_b32 v5, v6, v7, v5
	v_add_lshl_u32 v0, v2, v0, 1
	v_lshl_add_u32 v187, v3, 11, v0
	v_lshl_add_u32 v205, v5, 9, v0
	v_add_u32_e32 v0, 0x2000, v1
	v_ashrrev_i32_e32 v1, 31, v0
	v_lshrrev_b32_e32 v1, 22, v1
	v_add_u32_e32 v1, v0, v1
	v_ashrrev_i32_e32 v1, 10, v1
	v_mul_i32_i24_e32 v2, 0x400, v1
	v_sub_u32_e32 v0, v0, v2
	v_lshrrev_b32_e32 v2, 4, v0
	v_bitop3_b32 v0, v2, v0, 32 bitop3:0x6c
	v_ashrrev_i32_e32 v3, 31, v0
	v_lshrrev_b32_e32 v3, 26, v3
	v_lshlrev_b32_e32 v2, 3, v1
	v_add_u32_e32 v3, v0, v3
	v_and_b32_e32 v2, -16, v2
	v_ashrrev_i32_e32 v5, 6, v3
	v_add_u32_e32 v2, v5, v2
	v_and_b32_e32 v5, 3, v5
	s_addc_u32 s67, s1, 0
	v_and_or_b32 v5, v2, s0, v5
	s_lshl_b32 s0, s63, 5
	s_ashr_i32 s3, s44, 6
	s_and_b32 s0, s0, 0xe0
	s_bfe_u32 s1, s63, 0x50003
	s_ashr_i32 s2, s44, 8
	s_lshl_b32 s68, s3, 10
	s_or_b32 s0, s1, s0
	s_cmpk_lt_u32 s63, 0x100
	s_cselect_b32 s1, s0, s63
	s_mul_i32 s5, s1, 0xaaab
	s_lshr_b32 s0, s5, 17
	v_and_b32_e32 v3, 0xc0, v3
	s_mul_i32 s4, s0, 3
	v_sub_u32_e32 v0, v0, v3
	s_sub_i32 s4, s1, s4
	v_lshlrev_b32_e32 v1, 5, v1
	v_ashrrev_i16_sdwa v0, v216, sext(v0) dst_sel:DWORD dst_unused:UNUSED_PAD src0_sel:DWORD src1_sel:BYTE_0
	v_lshlrev_b32_e32 v3, 1, v2
	v_lshrrev_b32_e32 v6, 2, v2
	s_lshl_b32 s1, s4, 17
	v_and_b32_e32 v1, 32, v1
	v_bfe_i32 v0, v0, 0, 16
	v_and_b32_e32 v3, 24, v3
	v_and_b32_e32 v6, 4, v6
	s_and_b32 s1, s1, 0x1fe0000
	v_or3_b32 v3, v5, v6, v3
	v_add_lshl_u32 v0, v1, v0, 1
	s_add_u32 s56, s26, s1
	v_lshl_add_u32 v206, v2, 11, v0
	v_lshl_add_u32 v208, v3, 9, v0
	s_addc_u32 s57, s67, 0
	s_add_i32 s69, s68, 0
	s_waitcnt vmcnt(0) lgkmcnt(0)
	s_barrier
	s_add_i32 m0, s69, 0x10000
	v_add_u32_e32 v204, 0x40000, v187
	global_load_lds_dwordx4 v205, s[56:57]
	s_add_i32 m0, s69, 0x12000
	s_add_u32 s20, s56, 0x10000
	global_load_lds_dwordx4 v208, s[56:57]
	s_addc_u32 s21, s57, 0
	s_add_i32 m0, s69, 0x14000
	s_lshl_b32 s1, s5, 2
	global_load_lds_dwordx4 v205, s[20:21]
	s_add_i32 m0, s69, 0x16000
	s_and_b32 s1, s1, 0x7f80000
	global_load_lds_dwordx4 v208, s[20:21]
	s_add_u32 s58, s65, s1
	s_addc_u32 s59, s66, 0
	s_mov_b32 m0, s69
	s_add_i32 s70, s69, 0x2000
	global_load_lds_dwordx4 v187, s[58:59]
	s_mov_b32 m0, s70
	s_add_i32 s71, s69, 0x4000
	global_load_lds_dwordx4 v206, s[58:59]
	v_add_u32_e32 v207, 0x40000, v206
	s_mov_b32 m0, s71
	s_add_i32 s72, s69, 0x6000
	global_load_lds_dwordx4 v204, s[58:59]
	v_mov_b32_e32 v0, v207
	s_mov_b32 m0, s72
	s_cmp_eq_u32 s2, 1
	global_load_lds_dwordx4 v0, s[58:59]
	s_cselect_b64 s[36:37], -1, 0
	s_and_b64 vcc, exec, s[36:37]
	s_cbranch_vccz .LBB0_884
	s_barrier
.LBB0_884:
	s_and_b32 s1, 0xffff, s0
	s_and_b32 s0, 0xffff, s4
	s_add_u32 s40, s38, 0x49400000
	s_addc_u32 s41, s39, 0
	v_mov_b32_e32 v96, v205
	s_add_u32 s42, s38, 0x37a00000
	s_waitcnt vmcnt(2)
	s_barrier
	s_addc_u32 s43, s39, 0
	v_lshl_add_u64 v[0:1], s[56:57], 0, v[96:97]
	s_add_i32 m0, s69, 0x18000
	v_lshl_add_u64 v[0:1], v[0:1], 0, s[30:31]
	v_mov_b32_e32 v96, v208
	global_load_lds_dwordx4 v[0:1], off
	s_add_i32 m0, s69, 0x1a000
	v_lshl_add_u64 v[0:1], s[56:57], 0, v[96:97]
	v_lshl_add_u64 v[0:1], v[0:1], 0, s[30:31]
	v_mov_b32_e32 v96, v187
	global_load_lds_dwordx4 v[0:1], off
	s_add_i32 s74, s69, 0x8000
	v_lshl_add_u64 v[0:1], s[58:59], 0, v[96:97]
	s_lshl_b32 s3, s3, 5
	v_lshl_add_u64 v[0:1], v[0:1], 0, s[30:31]
	s_mov_b32 m0, s74
	v_mov_b32_e32 v96, v206
	s_and_b32 s73, s3, 0x60
	global_load_lds_dwordx4 v[0:1], off
	s_add_i32 s75, s69, 0xa000
	v_lshl_add_u64 v[0:1], s[58:59], 0, v[96:97]
	s_lshl_b32 s20, s2, 13
	s_lshl_b32 s3, s73, 7
	v_lshl_add_u64 v[0:1], v[0:1], 0, s[30:31]
	s_mov_b32 m0, s75
	s_add_u32 s4, s56, 0x10080
	global_load_lds_dwordx4 v[0:1], off
	s_addc_u32 s5, s57, 0
	s_add_i32 m0, s69, 0x1c000
	v_lshrrev_b32_e32 v1, 1, v4
	global_load_lds_dwordx4 v205, s[4:5]
	s_add_i32 m0, s69, 0x1e000
	v_and_b32_e32 v186, 24, v1
	global_load_lds_dwordx4 v208, s[4:5]
	v_and_b32_e32 v0, 15, v4
	v_lshlrev_b32_e32 v1, 1, v186
	v_lshl_or_b32 v209, s2, 6, v0
	v_lshl_or_b32 v0, v0, 6, v1
	v_lshlrev_b32_e32 v1, 2, v4
	v_and_b32_e32 v1, 32, v1
	s_waitcnt vmcnt(6)
	v_bitop3_b32 v2, v0, s20, v1 bitop3:0xde
	s_cmpk_lt_u32 s44, 0x100
	v_bitop3_b32 v210, v0, s3, v1 bitop3:0xde
	s_cselect_b64 s[44:45], -1, 0
	v_or_b32_e32 v211, 0xffffff80, v186
	v_or_b32_e32 v212, 16, v209
	v_or_b32_e32 v213, 32, v209
	v_or_b32_e32 v214, 48, v209
	v_add_u32_e32 v215, 0x80, v209
	v_add_u32_e32 v219, 0x90, v209
	v_add_u32_e32 v220, 0xa0, v209
	v_add_u32_e32 v221, 0xb0, v209
	s_mov_b32 s77, 0
	v_add_u32_e32 v222, 0, v2
	s_mov_b64 s[52:53], s[56:57]
	s_mov_b64 s[50:51], s[58:59]
	s_barrier
	s_waitcnt vmcnt(0)
	s_branch .LBB0_887

; #define PG8_STAGE(bufoff, gbase, voff) do { _Pragma("unroll") for (int _i = 0; _i < 2; ++_i) \
;         __builtin_amdgcn_global_load_lds((const __attribute__((address_space(1))) unsigned*)((const __attribute__((address_space(1))) char*)(gbase) + (unsigned)lnd_v((int)(voff)[_i])), (LAS unsigned*)(lds + (bufoff) + ldsw + _i * 8192), 16, 0, 0); } while (0)
; #define PG8_LDA(dst, b, h) do { _Pragma("unroll") for (int m = 0; m < 4; ++m) _Pragma("unroll") for (int k = 0; k < 2; ++k) dst[m][k] = *(const LAS bf16x8*)(lds + PG8_SA(b, h) + aoff + m * 2048 + k * 1024); } while (0)
; #define PG8_LDB(dst, b, h) do { _Pragma("unroll") for (int n = 0; n < 2; ++n) _Pragma("unroll") for (int k = 0; k < 2; ++k) dst[n][k] = *(const LAS bf16x8*)(lds + PG8_SB(b, h) + boff + n * 2048 + k * 1024); } while (0)
; #define PG8_WAIT_V(n) asm volatile("s_waitcnt vmcnt(" #n ")" ::: "memory")
; #define PG8_WAIT_L(n) asm volatile("s_waitcnt lgkmcnt(" #n ")" ::: "memory")
; #define PG8_BAR __builtin_amdgcn_s_barrier()
; #define PG8_SCHED __builtin_amdgcn_sched_barrier(0)
; template <class Desc, class Epi>
; __device__ __forceinline__ void gemm_phase(const int wv_, LAS unsigned char* lds, const Desc& d, const Epi& E) {
;     ...
;         for (int t = 0; t < nt; t += 2) {
;             const bool last = (t == nt - 2);
;             unsigned sA0[2], sA1[2];
;             if constexpr (Desc::GATHER) { sA0[0] = last ? voffAn[0] : voffA[0]; sA0[1] = last ? voffAn[1] : voffA[1]; sA1[0] = last ? voffAn1[0] : voffA1[0]; sA1[1] = last ? voffAn1[1] : voffA1[1]; }
;             else { sA0[0] = voffA[0]; sA0[1] = voffA[1]; sA1[0] = voffA1[0]; sA1[1] = voffA1[1]; }
;             const char* a1 = cA + (size_t)(t + 1) * kstep;
;             const char* a2 = last ? nA : cA + (size_t)(t + 2) * kstep; const char* b2 = last ? nB : cB + (size_t)(t + 2) * kstep;
;             const char* a3 = a2 + kstep; const char* b3 = b2 + kstep;
;             PG8_LDB(B0, 0, 0); PG8_LDB(B1, 0, 1); PG8_SCHED; PG8_LDA(At, 0, 0); PG8_STAGE(PG8_SA(1, 1), a1, voffA1);
;             PG8_WAIT_V(8); PG8_WAIT_L(0); PG8_BAR; PG8_MMA(0, 0, At, B0); PG8_MMA(0, 1, At, B1); PG8_BAR; PG8_SCHED;
;             PG8_LDA(At, 0, 1); PG8_STAGE(PG8_SB(0, 0), b2, voffB); PG8_STAGE(PG8_SB(0, 1), b2 + hstepB, voffB); PG8_STAGE(PG8_SA(0, 0), a2, sA0);
.LBB0_890:
	s_add_u32 s60, s58, s22
	s_addc_u32 s61, s59, 0
	s_add_u32 s23, s60, 0x100
	s_addc_u32 s24, s61, 0
	s_and_b64 s[4:5], s[20:21], exec
	s_cselect_b32 s4, s50, s23
	s_cselect_b32 s5, s51, s24
	s_add_u32 s22, s56, s22
	s_addc_u32 s23, s57, 0
	s_add_u32 s22, s22, 0x100
	s_addc_u32 s23, s23, 0
	s_add_i32 s82, 0, 0x10000
	s_and_b64 s[20:21], s[20:21], exec
	s_cselect_b32 s21, s53, s23
	s_cselect_b32 s20, s52, s22
	s_add_i32 s23, 0, 0x14000
	v_add_u32_e32 v96, s82, v210
	s_add_i32 s84, s82, s68
	ds_read_b128 v[130:133], v96
	ds_read_b128 v[134:137], v96 offset:1024
	ds_read_b128 v[138:141], v96 offset:2048
	ds_read_b128 v[142:145], v96 offset:3072
	v_add_u32_e32 v96, s23, v210
	s_add_i32 m0, s69, 0xc000
	s_add_i32 s85, s69, 0xe000
	s_add_i32 s80, s84, 0x2000
	ds_read_b128 v[146:149], v96
	ds_read_b128 v[150:153], v96 offset:1024
	ds_read_b128 v[154:157], v96 offset:2048
	ds_read_b128 v[158:161], v96 offset:3072
	s_add_u32 s24, s20, 0x10000
	s_addc_u32 s25, s21, 0
	s_add_i32 s78, 0, 0x18000
	s_add_i32 s81, s23, s68
	s_add_i32 s47, s78, s68
	s_add_i32 s79, s81, 0x2000
	s_add_i32 s49, 0, 0x1c000
	s_add_i32 s29, s47, 0x2000
	s_add_u32 s22, s20, 0x10080
	s_addc_u32 s23, s21, 0
	s_add_i32 s83, s49, s68
	s_add_i32 s82, s83, 0x2000
	v_mov_b32_e32 v96, v204
	ds_read_b128 v[162:165], v222
	ds_read_b128 v[166:169], v222 offset:1024
	ds_read_b128 v[170:173], v222 offset:2048
	ds_read_b128 v[174:177], v222 offset:3072
	ds_read_b128 v[178:181], v222 offset:4096
	ds_read_b128 v[182:185], v222 offset:5120
	ds_read_b128 v[188:191], v222 offset:6144
	ds_read_b128 v[192:195], v222 offset:7168
	s_nop 0
	v_lshl_add_u64 v[196:197], s[60:61], 0, v[96:97]
	v_lshl_add_u64 v[196:197], v[196:197], 0, s[30:31]
	v_mov_b32_e32 v96, v207
	global_load_lds_dwordx4 v[196:197], off
	s_mov_b32 m0, s85
	v_lshl_add_u64 v[196:197], s[60:61], 0, v[96:97]
	v_lshl_add_u64 v[196:197], v[196:197], 0, s[30:31]
	global_load_lds_dwordx4 v[196:197], off
	s_waitcnt vmcnt(8)
	s_waitcnt lgkmcnt(0)
	s_barrier
	s_waitcnt lgkmcnt(0)
	v_mfma_f32_16x16x32_bf16 v[126:129], v[130:133], v[162:165], v[126:129]
	v_mfma_f32_16x16x32_bf16 v[122:125], v[138:141], v[162:165], v[122:125]
	v_mfma_f32_16x16x32_bf16 v[118:121], v[130:133], v[170:173], v[118:121]
	v_mfma_f32_16x16x32_bf16 v[114:117], v[138:141], v[170:173], v[114:117]
	v_mfma_f32_16x16x32_bf16 v[110:113], v[130:133], v[178:181], v[110:113]
	v_mfma_f32_16x16x32_bf16 v[106:109], v[138:141], v[178:181], v[106:109]
	v_mfma_f32_16x16x32_bf16 v[102:105], v[130:133], v[188:191], v[102:105]
	v_mfma_f32_16x16x32_bf16 v[98:101], v[138:141], v[188:191], v[98:101]
	v_mfma_f32_16x16x32_bf16 v[126:129], v[134:137], v[166:169], v[126:129]
	v_mfma_f32_16x16x32_bf16 v[122:125], v[142:145], v[166:169], v[122:125]
	v_mfma_f32_16x16x32_bf16 v[118:121], v[134:137], v[174:177], v[118:121]
	v_mfma_f32_16x16x32_bf16 v[114:117], v[142:145], v[174:177], v[114:117]
	v_mfma_f32_16x16x32_bf16 v[110:113], v[134:137], v[182:185], v[110:113]
	v_mfma_f32_16x16x32_bf16 v[106:109], v[142:145], v[182:185], v[106:109]
	v_mfma_f32_16x16x32_bf16 v[102:105], v[134:137], v[192:195], v[102:105]
	v_mfma_f32_16x16x32_bf16 v[98:101], v[142:145], v[192:195], v[98:101]
	v_mfma_f32_16x16x32_bf16 v[60:63], v[146:149], v[162:165], v[60:63]
	v_mfma_f32_16x16x32_bf16 v[56:59], v[154:157], v[162:165], v[56:59]
	v_mfma_f32_16x16x32_bf16 v[52:55], v[146:149], v[170:173], v[52:55]
	v_mfma_f32_16x16x32_bf16 v[48:51], v[154:157], v[170:173], v[48:51]
	v_mfma_f32_16x16x32_bf16 v[44:47], v[146:149], v[178:181], v[44:47]
	v_mfma_f32_16x16x32_bf16 v[40:43], v[154:157], v[178:181], v[40:43]
	v_mfma_f32_16x16x32_bf16 v[36:39], v[146:149], v[188:191], v[36:39]
	v_mfma_f32_16x16x32_bf16 v[32:35], v[154:157], v[188:191], v[32:35]
	v_mfma_f32_16x16x32_bf16 v[60:63], v[150:153], v[166:169], v[60:63]
	v_mfma_f32_16x16x32_bf16 v[56:59], v[158:161], v[166:169], v[56:59]
	v_mfma_f32_16x16x32_bf16 v[52:55], v[150:153], v[174:177], v[52:55]
	v_mfma_f32_16x16x32_bf16 v[48:51], v[158:161], v[174:177], v[48:51]
	v_mfma_f32_16x16x32_bf16 v[44:47], v[150:153], v[182:185], v[44:47]
	v_mfma_f32_16x16x32_bf16 v[40:43], v[158:161], v[182:185], v[40:43]
	v_mfma_f32_16x16x32_bf16 v[36:39], v[150:153], v[192:195], v[36:39]
	v_mfma_f32_16x16x32_bf16 v[32:35], v[158:161], v[192:195], v[32:35]
	s_barrier
	s_mov_b32 m0, s84
	ds_read_b128 v[162:165], v222 offset:16384
	ds_read_b128 v[166:169], v222 offset:17408
	ds_read_b128 v[170:173], v222 offset:18432
	ds_read_b128 v[174:177], v222 offset:19456
	ds_read_b128 v[178:181], v222 offset:20480
	ds_read_b128 v[182:185], v222 offset:21504
	ds_read_b128 v[188:191], v222 offset:22528
	ds_read_b128 v[192:195], v222 offset:23552
	s_nop 0
	global_load_lds_dwordx4 v205, s[20:21]
	s_mov_b32 m0, s80
	s_nop 0
	global_load_lds_dwordx4 v208, s[20:21]
	s_mov_b32 m0, s81
	s_nop 0
	global_load_lds_dwordx4 v205, s[24:25]
	s_mov_b32 m0, s79
	s_nop 0
	global_load_lds_dwordx4 v208, s[24:25]
	s_mov_b32 m0, s69
	s_nop 0
	global_load_lds_dwordx4 v187, s[4:5]
	s_mov_b32 m0, s70
	s_nop 0
	global_load_lds_dwordx4 v206, s[4:5]
	s_waitcnt vmcnt(8)
	s_waitcnt lgkmcnt(0)
	s_barrier
; #define PG8_STAGE(bufoff, gbase, voff) do { _Pragma("unroll") for (int _i = 0; _i < 2; ++_i) \
;         __builtin_amdgcn_global_load_lds((const __attribute__((address_space(1))) unsigned*)((const __attribute__((address_space(1))) char*)(gbase) + (unsigned)lnd_v((int)(voff)[_i])), (LAS unsigned*)(lds + (bufoff) + ldsw + _i * 8192), 16, 0, 0); } while (0)
; #define PG8_LDA(dst, b, h) do { _Pragma("unroll") for (int m = 0; m < 4; ++m) _Pragma("unroll") for (int k = 0; k < 2; ++k) dst[m][k] = *(const LAS bf16x8*)(lds + PG8_SA(b, h) + aoff + m * 2048 + k * 1024); } while (0)
; #define PG8_LDB(dst, b, h) do { _Pragma("unroll") for (int n = 0; n < 2; ++n) _Pragma("unroll") for (int k = 0; k < 2; ++k) dst[n][k] = *(const LAS bf16x8*)(lds + PG8_SB(b, h) + boff + n * 2048 + k * 1024); } while (0)
; #define PG8_MMA(ai, bj, At, Bt) do { __builtin_amdgcn_s_setprio(1); _Pragma("unroll") for (int m = 0; m < 4; ++m) _Pragma("unroll") for (int n = 0; n < 2; ++n) _Pragma("unroll") for (int k = 0; k < 2; ++k) \
;         acc[ai][bj][m][n] = __builtin_amdgcn_mfma_f32_16x16x32_bf16(Bt[n][k], At[m][k], acc[ai][bj][m][n], 0, 0, 0); __builtin_amdgcn_s_setprio(0); } while (0)
; #define PG8_WAIT_V(n) asm volatile("s_waitcnt vmcnt(" #n ")" ::: "memory")
; #define PG8_WAIT_L(n) asm volatile("s_waitcnt lgkmcnt(" #n ")" ::: "memory")
; #define PG8_BAR __builtin_amdgcn_s_barrier()
; #define PG8_SCHED __builtin_amdgcn_sched_barrier(0)
; template <class Desc, class Epi>
; __device__ __forceinline__ void gemm_phase(const int wv_, LAS unsigned char* lds, const Desc& d, const Epi& E) {
;     ...
;             PG8_WAIT_V(8); PG8_WAIT_L(0); PG8_BAR; PG8_MMA(1, 0, At, B0); PG8_MMA(1, 1, At, B1); PG8_BAR; PG8_SCHED;
;             PG8_LDB(B0, 1, 0); PG8_LDB(B1, 1, 1); PG8_SCHED; PG8_LDA(At, 1, 0); PG8_STAGE(PG8_SA(0, 1), a2, sA1);
;             PG8_WAIT_V(8); PG8_WAIT_L(0); PG8_BAR; PG8_MMA(0, 0, At, B0); PG8_MMA(0, 1, At, B1); PG8_BAR; PG8_SCHED;
	s_waitcnt lgkmcnt(0)
	v_mfma_f32_16x16x32_bf16 v[92:95], v[130:133], v[162:165], v[92:95]
	v_mfma_f32_16x16x32_bf16 v[88:91], v[138:141], v[162:165], v[88:91]
	v_mfma_f32_16x16x32_bf16 v[84:87], v[130:133], v[170:173], v[84:87]
	v_mfma_f32_16x16x32_bf16 v[80:83], v[138:141], v[170:173], v[80:83]
	v_mfma_f32_16x16x32_bf16 v[76:79], v[130:133], v[178:181], v[76:79]
	v_mfma_f32_16x16x32_bf16 v[72:75], v[138:141], v[178:181], v[72:75]
	v_mfma_f32_16x16x32_bf16 v[68:71], v[130:133], v[188:191], v[68:71]
	v_mfma_f32_16x16x32_bf16 v[64:67], v[138:141], v[188:191], v[64:67]
	v_mfma_f32_16x16x32_bf16 v[92:95], v[134:137], v[166:169], v[92:95]
	v_mfma_f32_16x16x32_bf16 v[88:91], v[142:145], v[166:169], v[88:91]
	v_mfma_f32_16x16x32_bf16 v[84:87], v[134:137], v[174:177], v[84:87]
	v_mfma_f32_16x16x32_bf16 v[80:83], v[142:145], v[174:177], v[80:83]
	v_mfma_f32_16x16x32_bf16 v[76:79], v[134:137], v[182:185], v[76:79]
	v_mfma_f32_16x16x32_bf16 v[72:75], v[142:145], v[182:185], v[72:75]
	v_mfma_f32_16x16x32_bf16 v[68:71], v[134:137], v[192:195], v[68:71]
	v_mfma_f32_16x16x32_bf16 v[64:67], v[142:145], v[192:195], v[64:67]
	v_mfma_f32_16x16x32_bf16 v[28:31], v[146:149], v[162:165], v[28:31]
	v_mfma_f32_16x16x32_bf16 v[24:27], v[154:157], v[162:165], v[24:27]
	v_mfma_f32_16x16x32_bf16 v[12:15], v[146:149], v[170:173], v[12:15]
	v_mfma_f32_16x16x32_bf16 v[8:11], v[154:157], v[170:173], v[8:11]
	v_mfma_f32_16x16x32_bf16 v[20:23], v[146:149], v[178:181], v[20:23]
	v_mfma_f32_16x16x32_bf16 v[16:19], v[154:157], v[178:181], v[16:19]
	v_mfma_f32_16x16x32_bf16 v[4:7], v[146:149], v[188:191], v[4:7]
	v_mfma_f32_16x16x32_bf16 v[0:3], v[154:157], v[188:191], v[0:3]
	v_mfma_f32_16x16x32_bf16 v[28:31], v[150:153], v[166:169], v[28:31]
	v_mfma_f32_16x16x32_bf16 v[24:27], v[158:161], v[166:169], v[24:27]
	v_mfma_f32_16x16x32_bf16 v[12:15], v[150:153], v[174:177], v[12:15]
	v_mfma_f32_16x16x32_bf16 v[8:11], v[158:161], v[174:177], v[8:11]
	v_mfma_f32_16x16x32_bf16 v[20:23], v[150:153], v[182:185], v[20:23]
	v_mfma_f32_16x16x32_bf16 v[16:19], v[158:161], v[182:185], v[16:19]
	v_mfma_f32_16x16x32_bf16 v[4:7], v[150:153], v[192:195], v[4:7]
	v_mfma_f32_16x16x32_bf16 v[0:3], v[158:161], v[192:195], v[0:3]
	s_barrier
	v_add_u32_e32 v96, s78, v210
	ds_read_b128 v[130:133], v96
	ds_read_b128 v[134:137], v96 offset:1024
	ds_read_b128 v[138:141], v96 offset:2048
	ds_read_b128 v[142:145], v96 offset:3072
	v_add_u32_e32 v96, s49, v210
	ds_read_b128 v[146:149], v96
	ds_read_b128 v[150:153], v96 offset:1024
	ds_read_b128 v[154:157], v96 offset:2048
	ds_read_b128 v[158:161], v96 offset:3072
	s_mov_b32 m0, s71
	ds_read_b128 v[162:165], v222 offset:32768
	ds_read_b128 v[166:169], v222 offset:33792
	ds_read_b128 v[170:173], v222 offset:34816
	ds_read_b128 v[174:177], v222 offset:35840
	ds_read_b128 v[178:181], v222 offset:36864
	ds_read_b128 v[182:185], v222 offset:37888
	ds_read_b128 v[188:191], v222 offset:38912
	ds_read_b128 v[192:195], v222 offset:39936
	s_nop 0
	global_load_lds_dwordx4 v204, s[4:5]
	s_mov_b32 m0, s72
	s_nop 0
	global_load_lds_dwordx4 v207, s[4:5]
	s_waitcnt vmcnt(8)
	s_waitcnt lgkmcnt(0)
	s_barrier
	s_waitcnt lgkmcnt(0)
	v_mfma_f32_16x16x32_bf16 v[126:129], v[130:133], v[162:165], v[126:129]
	v_mfma_f32_16x16x32_bf16 v[122:125], v[138:141], v[162:165], v[122:125]
	v_mfma_f32_16x16x32_bf16 v[118:121], v[130:133], v[170:173], v[118:121]
	v_mfma_f32_16x16x32_bf16 v[114:117], v[138:141], v[170:173], v[114:117]
	v_mfma_f32_16x16x32_bf16 v[110:113], v[130:133], v[178:181], v[110:113]
	v_mfma_f32_16x16x32_bf16 v[106:109], v[138:141], v[178:181], v[106:109]
	v_mfma_f32_16x16x32_bf16 v[102:105], v[130:133], v[188:191], v[102:105]
	v_mfma_f32_16x16x32_bf16 v[98:101], v[138:141], v[188:191], v[98:101]
	v_mfma_f32_16x16x32_bf16 v[126:129], v[134:137], v[166:169], v[126:129]
	v_mfma_f32_16x16x32_bf16 v[122:125], v[142:145], v[166:169], v[122:125]
	v_mfma_f32_16x16x32_bf16 v[118:121], v[134:137], v[174:177], v[118:121]
	v_mfma_f32_16x16x32_bf16 v[114:117], v[142:145], v[174:177], v[114:117]
	v_mfma_f32_16x16x32_bf16 v[110:113], v[134:137], v[182:185], v[110:113]
	v_mfma_f32_16x16x32_bf16 v[106:109], v[142:145], v[182:185], v[106:109]
	v_mfma_f32_16x16x32_bf16 v[102:105], v[134:137], v[192:195], v[102:105]
	v_mfma_f32_16x16x32_bf16 v[98:101], v[142:145], v[192:195], v[98:101]
	v_mfma_f32_16x16x32_bf16 v[60:63], v[146:149], v[162:165], v[60:63]
	v_mfma_f32_16x16x32_bf16 v[56:59], v[154:157], v[162:165], v[56:59]
	v_mfma_f32_16x16x32_bf16 v[52:55], v[146:149], v[170:173], v[52:55]
	v_mfma_f32_16x16x32_bf16 v[48:51], v[154:157], v[170:173], v[48:51]
	v_mfma_f32_16x16x32_bf16 v[44:47], v[146:149], v[178:181], v[44:47]
	v_mfma_f32_16x16x32_bf16 v[40:43], v[154:157], v[178:181], v[40:43]
	v_mfma_f32_16x16x32_bf16 v[36:39], v[146:149], v[188:191], v[36:39]
	v_mfma_f32_16x16x32_bf16 v[32:35], v[154:157], v[188:191], v[32:35]
	v_mfma_f32_16x16x32_bf16 v[60:63], v[150:153], v[166:169], v[60:63]
	v_mfma_f32_16x16x32_bf16 v[56:59], v[158:161], v[166:169], v[56:59]
	v_mfma_f32_16x16x32_bf16 v[52:55], v[150:153], v[174:177], v[52:55]
	v_mfma_f32_16x16x32_bf16 v[48:51], v[158:161], v[174:177], v[48:51]
	v_mfma_f32_16x16x32_bf16 v[44:47], v[150:153], v[182:185], v[44:47]
	v_mfma_f32_16x16x32_bf16 v[40:43], v[158:161], v[182:185], v[40:43]
	v_mfma_f32_16x16x32_bf16 v[36:39], v[150:153], v[192:195], v[36:39]
	v_mfma_f32_16x16x32_bf16 v[32:35], v[158:161], v[192:195], v[32:35]
	s_barrier
; #define PG8_STAGE(bufoff, gbase, voff) do { _Pragma("unroll") for (int _i = 0; _i < 2; ++_i) \
;         __builtin_amdgcn_global_load_lds((const __attribute__((address_space(1))) unsigned*)((const __attribute__((address_space(1))) char*)(gbase) + (unsigned)lnd_v((int)(voff)[_i])), (LAS unsigned*)(lds + (bufoff) + ldsw + _i * 8192), 16, 0, 0); } while (0)
; #define PG8_LDA(dst, b, h) do { _Pragma("unroll") for (int m = 0; m < 4; ++m) _Pragma("unroll") for (int k = 0; k < 2; ++k) dst[m][k] = *(const LAS bf16x8*)(lds + PG8_SA(b, h) + aoff + m * 2048 + k * 1024); } while (0)
; #define PG8_MMA(ai, bj, At, Bt) do { __builtin_amdgcn_s_setprio(1); _Pragma("unroll") for (int m = 0; m < 4; ++m) _Pragma("unroll") for (int n = 0; n < 2; ++n) _Pragma("unroll") for (int k = 0; k < 2; ++k) \
;         acc[ai][bj][m][n] = __builtin_amdgcn_mfma_f32_16x16x32_bf16(Bt[n][k], At[m][k], acc[ai][bj][m][n], 0, 0, 0); __builtin_amdgcn_s_setprio(0); } while (0)
; #define PG8_WAIT_V(n) asm volatile("s_waitcnt vmcnt(" #n ")" ::: "memory")
; #define PG8_WAIT_L(n) asm volatile("s_waitcnt lgkmcnt(" #n ")" ::: "memory")
; #define PG8_BAR __builtin_amdgcn_s_barrier()
; #define PG8_SCHED __builtin_amdgcn_sched_barrier(0)
; template <class Desc, class Epi>
; __device__ __forceinline__ void gemm_phase(const int wv_, LAS unsigned char* lds, const Desc& d, const Epi& E) {
;     ...
;             PG8_LDA(At, 1, 1); PG8_STAGE(PG8_SB(1, 0), b3, voffB); PG8_STAGE(PG8_SB(1, 1), b3 + hstepB, voffB); PG8_STAGE(PG8_SA(1, 0), a3, sA0);
;             PG8_WAIT_V(8); PG8_WAIT_L(0); PG8_BAR; PG8_MMA(1, 0, At, B0); PG8_MMA(1, 1, At, B1); PG8_BAR; PG8_SCHED;
;         }
;         if (wr == 0) PG8_BAR;
	v_mov_b32_e32 v96, v205
	ds_read_b128 v[162:165], v222 offset:49152
	ds_read_b128 v[166:169], v222 offset:50176
	ds_read_b128 v[170:173], v222 offset:51200
	ds_read_b128 v[174:177], v222 offset:52224
	ds_read_b128 v[178:181], v222 offset:53248
	ds_read_b128 v[182:185], v222 offset:54272
	ds_read_b128 v[188:191], v222 offset:55296
	ds_read_b128 v[192:195], v222 offset:56320
	s_mov_b32 m0, s47
	v_lshl_add_u64 v[196:197], s[20:21], 0, v[96:97]
	v_lshl_add_u64 v[196:197], v[196:197], 0, s[30:31]
	v_mov_b32_e32 v96, v208
	global_load_lds_dwordx4 v[196:197], off
	s_mov_b32 m0, s29
	v_lshl_add_u64 v[196:197], s[20:21], 0, v[96:97]
	v_lshl_add_u64 v[196:197], v[196:197], 0, s[30:31]
	global_load_lds_dwordx4 v[196:197], off
	s_mov_b32 m0, s83
	s_nop 0
	global_load_lds_dwordx4 v205, s[22:23]
	s_mov_b32 m0, s82
	s_nop 0
	global_load_lds_dwordx4 v208, s[22:23]
	v_mov_b32_e32 v96, v187
	s_mov_b32 m0, s74
	v_lshl_add_u64 v[196:197], s[4:5], 0, v[96:97]
	v_lshl_add_u64 v[196:197], v[196:197], 0, s[30:31]
	v_mov_b32_e32 v96, v206
	global_load_lds_dwordx4 v[196:197], off
	s_mov_b32 m0, s75
	v_lshl_add_u64 v[196:197], s[4:5], 0, v[96:97]
	v_lshl_add_u64 v[196:197], v[196:197], 0, s[30:31]
	global_load_lds_dwordx4 v[196:197], off
	s_waitcnt vmcnt(8)
	s_waitcnt lgkmcnt(0)
	s_barrier
	s_waitcnt lgkmcnt(0)
	v_mfma_f32_16x16x32_bf16 v[92:95], v[130:133], v[162:165], v[92:95]
	v_mfma_f32_16x16x32_bf16 v[88:91], v[138:141], v[162:165], v[88:91]
	v_mfma_f32_16x16x32_bf16 v[84:87], v[130:133], v[170:173], v[84:87]
	v_mfma_f32_16x16x32_bf16 v[80:83], v[138:141], v[170:173], v[80:83]
	v_mfma_f32_16x16x32_bf16 v[76:79], v[130:133], v[178:181], v[76:79]
	v_mfma_f32_16x16x32_bf16 v[72:75], v[138:141], v[178:181], v[72:75]
	v_mfma_f32_16x16x32_bf16 v[68:71], v[130:133], v[188:191], v[68:71]
	v_mfma_f32_16x16x32_bf16 v[64:67], v[138:141], v[188:191], v[64:67]
	v_mfma_f32_16x16x32_bf16 v[92:95], v[134:137], v[166:169], v[92:95]
	v_mfma_f32_16x16x32_bf16 v[88:91], v[142:145], v[166:169], v[88:91]
	v_mfma_f32_16x16x32_bf16 v[84:87], v[134:137], v[174:177], v[84:87]
	v_mfma_f32_16x16x32_bf16 v[80:83], v[142:145], v[174:177], v[80:83]
	v_mfma_f32_16x16x32_bf16 v[76:79], v[134:137], v[182:185], v[76:79]
	v_mfma_f32_16x16x32_bf16 v[72:75], v[142:145], v[182:185], v[72:75]
	v_mfma_f32_16x16x32_bf16 v[68:71], v[134:137], v[192:195], v[68:71]
	v_mfma_f32_16x16x32_bf16 v[64:67], v[142:145], v[192:195], v[64:67]
	v_mfma_f32_16x16x32_bf16 v[28:31], v[146:149], v[162:165], v[28:31]
	v_mfma_f32_16x16x32_bf16 v[24:27], v[154:157], v[162:165], v[24:27]
	v_mfma_f32_16x16x32_bf16 v[12:15], v[146:149], v[170:173], v[12:15]
	v_mfma_f32_16x16x32_bf16 v[8:11], v[154:157], v[170:173], v[8:11]
	v_mfma_f32_16x16x32_bf16 v[20:23], v[146:149], v[178:181], v[20:23]
	v_mfma_f32_16x16x32_bf16 v[16:19], v[154:157], v[178:181], v[16:19]
	v_mfma_f32_16x16x32_bf16 v[4:7], v[146:149], v[188:191], v[4:7]
	v_mfma_f32_16x16x32_bf16 v[0:3], v[154:157], v[188:191], v[0:3]
	v_mfma_f32_16x16x32_bf16 v[28:31], v[150:153], v[166:169], v[28:31]
	v_mfma_f32_16x16x32_bf16 v[24:27], v[158:161], v[166:169], v[24:27]
	v_mfma_f32_16x16x32_bf16 v[12:15], v[150:153], v[174:177], v[12:15]
	v_mfma_f32_16x16x32_bf16 v[8:11], v[158:161], v[174:177], v[8:11]
	v_mfma_f32_16x16x32_bf16 v[20:23], v[150:153], v[182:185], v[20:23]
	v_mfma_f32_16x16x32_bf16 v[16:19], v[158:161], v[182:185], v[16:19]
	v_mfma_f32_16x16x32_bf16 v[4:7], v[150:153], v[192:195], v[4:7]
	v_mfma_f32_16x16x32_bf16 v[0:3], v[158:161], v[192:195], v[0:3]
	s_barrier
	s_movk_i32 s22, 0x100
	s_andn2_b64 vcc, exec, s[2:3]
	s_mov_b64 s[20:21], -1
	s_mov_b64 s[2:3], 0
	s_cbranch_vccz .LBB0_890
	s_and_b64 vcc, exec, s[44:45]
	s_cbranch_vccz .LBB0_893
	s_barrier

; #define PG8_STAGE(bufoff, gbase, voff) do { _Pragma("unroll") for (int _i = 0; _i < 2; ++_i) \
;         __builtin_amdgcn_global_load_lds((const __attribute__((address_space(1))) unsigned*)((const __attribute__((address_space(1))) char*)(gbase) + (unsigned)lnd_v((int)(voff)[_i])), (LAS unsigned*)(lds + (bufoff) + ldsw + _i * 8192), 16, 0, 0); } while (0)
; #define PG8_WAIT_V(n) asm volatile("s_waitcnt vmcnt(" #n ")" ::: "memory")
; #define PG8_BAR __builtin_amdgcn_s_barrier()
; template <class Desc, class Epi>
; __device__ __forceinline__ void gemm_phase(const int wv_, LAS unsigned char* lds, const Desc& d, const Epi& E) {
;     ...
; #pragma unroll
;     for (int i = 0; i < 2; ++i) { int R, C; stage_rc(tid * 16 + i * 8192, R, C); const int Rb = (R & ~31) + perm32(R & 31); Rr[i] = R; Cc[i] = C;
;         voffA[i] = (unsigned)(R * d.lda + C) * 2u; voffA1[i] = voffA[i] + (unsigned)hstepA; voffB[i] = (unsigned)(Rb * d.ldb + C) * 2u; }
;     ...
;     PG8_STAGE(PG8_SB(0, 0), cB, voffB); PG8_STAGE(PG8_SB(0, 1), cB + hstepB, voffB); PG8_STAGE(PG8_SA(0, 0), cA, voffA); PG8_STAGE(PG8_SA(0, 1), cA, voffA1);
;     if (wr == 1) PG8_BAR;
;     PG8_WAIT_V(2); PG8_BAR;
;     PG8_STAGE(PG8_SB(1, 0), cB + kstep, voffB); PG8_STAGE(PG8_SA(1, 0), cA + kstep, voffA); PG8_STAGE(PG8_SB(1, 1), cB + hstepB + kstep, voffB);
;     PG8_WAIT_V(6); PG8_BAR;
.LBB0_909:
	s_or_b64 exec, exec, s[2:3]
	v_ashrrev_i32_e32 v3, 31, v1
	v_lshrrev_b32_e32 v3, 26, v3
	v_lshlrev_b32_e32 v2, 4, v1
	v_add_u32_e32 v3, v1, v3
	v_bfe_i32 v1, v1, 27, 1
	v_lshrrev_b32_e32 v1, 22, v1
	v_add_u32_e32 v1, v2, v1
	v_and_b32_e32 v1, 0xfffffc00, v1
	v_sub_u32_e32 v1, v2, v1
	v_lshrrev_b32_e32 v4, 4, v1
	v_bitop3_b32 v1, v4, v1, 32 bitop3:0x6c
	v_ashrrev_i32_e32 v5, 31, v1
	v_ashrrev_i32_e32 v3, 6, v3
	v_lshrrev_b32_e32 v5, 26, v5
	v_lshlrev_b32_e32 v4, 3, v3
	v_add_u32_e32 v5, v1, v5
	v_and_b32_e32 v4, -16, v4
	v_ashrrev_i32_e32 v6, 6, v5
	v_and_b32_e32 v5, 0xc0, v5
	v_add_u32_e32 v4, v6, v4
	v_sub_u32_e32 v1, v1, v5
	v_lshlrev_b32_e32 v3, 5, v3
	v_ashrrev_i16_sdwa v1, v216, sext(v1) dst_sel:DWORD dst_unused:UNUSED_PAD src0_sel:DWORD src1_sel:BYTE_0
	v_lshlrev_b32_e32 v5, 1, v4
	v_lshrrev_b32_e32 v7, 2, v4
	v_and_b32_e32 v6, 3, v6
	s_mov_b32 s0, 0x1fffe0
	v_and_b32_e32 v3, 32, v3
	v_bfe_i32 v1, v1, 0, 16
	v_and_b32_e32 v5, 24, v5
	v_and_b32_e32 v7, 4, v7
	v_and_or_b32 v6, v4, s0, v6
	v_or3_b32 v5, v6, v7, v5
	v_add_lshl_u32 v1, v3, v1, 1
	v_lshl_add_u32 v132, v4, 11, v1
	v_lshl_add_u32 v134, v5, 11, v1
	v_add_u32_e32 v1, 0x2000, v2
	v_ashrrev_i32_e32 v2, 31, v1
	v_lshrrev_b32_e32 v2, 22, v2
	v_add_u32_e32 v2, v1, v2
	v_ashrrev_i32_e32 v2, 10, v2
	v_mul_i32_i24_e32 v3, 0x400, v2
	v_sub_u32_e32 v1, v1, v3
	v_lshrrev_b32_e32 v3, 4, v1
	v_bitop3_b32 v1, v3, v1, 32 bitop3:0x6c
	v_ashrrev_i32_e32 v4, 31, v1
	v_lshrrev_b32_e32 v4, 26, v4
	v_lshlrev_b32_e32 v3, 3, v2
	v_add_u32_e32 v4, v1, v4
	v_and_b32_e32 v3, -16, v3
	v_ashrrev_i32_e32 v5, 6, v4
	s_add_u32 s56, s38, 0x39200000
	v_add_u32_e32 v3, v5, v3
	v_and_b32_e32 v5, 3, v5
	s_addc_u32 s57, s39, 0
	v_and_or_b32 v5, v3, s0, v5
	v_readlane_b32 s0, v254, 57
	s_add_u32 s58, s38, 0x1600000
	v_readlane_b32 s1, v254, 58
	s_mov_b32 s20, s0
	s_addc_u32 s59, s39, 0
	s_ashr_i32 s3, s4, 6
	s_mov_b32 s1, s27
	v_writelane_b32 v254, s20, 57
	s_ashr_i32 s2, s4, 8
	s_lshl_b32 s60, s3, 10
	s_lshl_b64 s[22:23], s[0:1], 22
	v_writelane_b32 v254, s21, 58
	s_lshl_b64 s[24:25], s[0:1], 21
	s_bfe_u32 s20, s5, 0x30004
	s_bfe_u32 s1, s5, 0x20002
	s_and_b32 s0, s5, 3
	s_add_u32 s21, s56, s22
	s_addc_u32 s22, s57, s23
	s_add_u32 s23, s58, s24
	s_addc_u32 s24, s59, s25
	s_lshl_b32 s25, s0, 19
	v_and_b32_e32 v4, 0xc0, v4
	s_add_u32 s23, s23, s25
	v_sub_u32_e32 v1, v1, v4
	s_addc_u32 s24, s24, 0
	s_lshl_b32 s25, s20, 19
	v_lshlrev_b32_e32 v2, 5, v2
	v_ashrrev_i16_sdwa v1, v216, sext(v1) dst_sel:DWORD dst_unused:UNUSED_PAD src0_sel:DWORD src1_sel:BYTE_0
	v_lshlrev_b32_e32 v4, 1, v3
	v_lshrrev_b32_e32 v6, 2, v3
	s_add_u32 s21, s21, s25
	v_and_b32_e32 v2, 32, v2
	v_bfe_i32 v1, v1, 0, 16
	v_and_b32_e32 v4, 24, v4
	v_and_b32_e32 v6, 4, v6
	s_addc_u32 s25, s22, 0
	s_lshl_b32 s29, s1, 9
	v_or3_b32 v4, v5, v6, v4
	v_add_lshl_u32 v1, v2, v1, 1
	s_add_u32 s50, s23, s29
	v_lshl_add_u32 v135, v3, 11, v1
	v_lshl_add_u32 v137, v4, 11, v1
	s_addc_u32 s51, s24, 0
	s_add_i32 s61, s60, 0
	s_waitcnt vmcnt(0) lgkmcnt(0)
	s_barrier
	s_add_i32 m0, s61, 0x10000
	v_add_u32_e32 v133, 0x40000, v132
	global_load_lds_dwordx4 v134, s[50:51]
	s_add_i32 m0, s61, 0x12000
	s_add_u32 s22, s50, 0x40000
	global_load_lds_dwordx4 v137, s[50:51]
	s_addc_u32 s23, s51, 0
	s_add_i32 m0, s61, 0x14000
	v_add_u32_e32 v136, 0x40000, v135
	global_load_lds_dwordx4 v134, s[22:23]
	s_add_i32 m0, s61, 0x16000
	s_add_u32 s52, s21, s29
	global_load_lds_dwordx4 v137, s[22:23]
	s_addc_u32 s53, s25, 0
	s_mov_b32 m0, s61
	s_add_i32 s63, s61, 0x2000
	global_load_lds_dwordx4 v132, s[52:53]
	s_mov_b32 m0, s63
	s_add_i32 s64, s61, 0x4000
	global_load_lds_dwordx4 v135, s[52:53]
	s_mov_b32 m0, s64
	s_add_i32 s65, s61, 0x6000
	global_load_lds_dwordx4 v133, s[52:53]
	v_mov_b32_e32 v1, v136
	s_mov_b32 m0, s65
	s_cmp_eq_u32 s2, 1
	global_load_lds_dwordx4 v1, s[52:53]
	s_cselect_b64 s[36:37], -1, 0
	s_and_b64 vcc, exec, s[36:37]
	s_cbranch_vccz .LBB0_911
	s_barrier
.LBB0_911:
	v_readlane_b32 s22, v254, 57
	s_lshl_b32 s21, s22, 5
	s_lshl_b32 s20, s20, 2
	s_or_b32 s20, s20, s21
	s_or_b32 s1, s20, s1
	v_mov_b32_e32 v96, v134
	s_add_u32 s40, s38, 0x3b200000
	s_waitcnt vmcnt(2)
	s_barrier
	s_addc_u32 s41, s39, 0
	v_lshl_add_u64 v[2:3], s[50:51], 0, v[96:97]
	s_add_i32 m0, s61, 0x18000
	v_lshl_add_u64 v[2:3], v[2:3], 0, s[30:31]
	v_mov_b32_e32 v96, v137
	global_load_lds_dwordx4 v[2:3], off
	s_add_i32 m0, s61, 0x1a000
	v_lshl_add_u64 v[2:3], s[50:51], 0, v[96:97]
	v_lshl_add_u64 v[2:3], v[2:3], 0, s[30:31]
	v_mov_b32_e32 v96, v132
	s_lshl_b32 s3, s3, 5
	global_load_lds_dwordx4 v[2:3], off
	s_add_i32 s68, s61, 0x8000
	v_lshl_add_u64 v[2:3], s[52:53], 0, v[96:97]
	s_mov_b32 s24, s22
	s_and_b32 s3, s3, 0x60
	v_lshl_add_u64 v[2:3], v[2:3], 0, s[30:31]
	s_mov_b32 m0, s68
	v_mov_b32_e32 v96, v135
	s_add_i32 s66, s5, 0xffffff80
	s_lshl_b32 s5, s2, 13
	s_lshl_b32 s22, s3, 7
	s_lshl_b32 s67, s24, 7
	global_load_lds_dwordx4 v[2:3], off
	s_add_i32 s69, s61, 0xa000
	v_lshl_add_u64 v[2:3], s[52:53], 0, v[96:97]
	v_lshl_add_u64 v[2:3], v[2:3], 0, s[30:31]
	s_mov_b32 m0, s69
	s_add_u32 s20, s50, 0x40080
	global_load_lds_dwordx4 v[2:3], off
	s_addc_u32 s21, s51, 0
	s_add_i32 m0, s61, 0x1c000
	v_lshrrev_b32_e32 v2, 1, v0
	global_load_lds_dwordx4 v134, s[20:21]
	s_add_i32 m0, s61, 0x1e000
	v_and_b32_e32 v2, 24, v2
	global_load_lds_dwordx4 v137, s[20:21]
	v_and_b32_e32 v1, 15, v0
	v_lshl_or_b32 v138, s2, 6, v1
	v_lshlrev_b32_e32 v3, 1, v2
	v_lshl_or_b32 v1, v1, 6, v3
	v_lshlrev_b32_e32 v3, 2, v138
	v_and_b32_e32 v4, 32, v3
	v_lshlrev_b32_e32 v0, 2, v0
	s_waitcnt vmcnt(6)
	s_cmpk_lt_u32 s4, 0x100
	v_bitop3_b32 v4, v1, s5, v4 bitop3:0xde
	v_and_b32_e32 v0, 32, v0
	s_cselect_b64 s[42:43], -1, 0
	s_add_i32 s2, 0, 0x20000
	v_bitop3_b32 v139, v1, s22, v0 bitop3:0xde
	v_or_b32_e32 v140, 16, v138
	v_or_b32_e32 v141, 32, v138
	v_or_b32_e32 v142, 48, v138
	v_add_u32_e32 v143, 0x80, v138
	v_add_u32_e32 v144, 0x90, v138
	v_add_u32_e32 v145, 0xa0, v138
	v_add_u32_e32 v146, 0xb0, v138
	v_or_b32_e32 v147, s3, v2
	v_add_u32_e32 v148, s2, v3
	s_mov_b32 s73, 0
	v_add_u32_e32 v149, 0, v4
	s_mov_b64 s[46:47], s[50:51]
	s_mov_b64 s[44:45], s[52:53]
	v_readlane_b32 s23, v254, 58
	s_barrier
	s_waitcnt vmcnt(0)
	s_branch .LBB0_914

; #define PG8_STAGE(bufoff, gbase, voff) do { _Pragma("unroll") for (int _i = 0; _i < 2; ++_i) \
;         __builtin_amdgcn_global_load_lds((const __attribute__((address_space(1))) unsigned*)((const __attribute__((address_space(1))) char*)(gbase) + (unsigned)lnd_v((int)(voff)[_i])), (LAS unsigned*)(lds + (bufoff) + ldsw + _i * 8192), 16, 0, 0); } while (0)
; #define PG8_LDA(dst, b, h) do { _Pragma("unroll") for (int m = 0; m < 4; ++m) _Pragma("unroll") for (int k = 0; k < 2; ++k) dst[m][k] = *(const LAS bf16x8*)(lds + PG8_SA(b, h) + aoff + m * 2048 + k * 1024); } while (0)
; #define PG8_LDB(dst, b, h) do { _Pragma("unroll") for (int n = 0; n < 2; ++n) _Pragma("unroll") for (int k = 0; k < 2; ++k) dst[n][k] = *(const LAS bf16x8*)(lds + PG8_SB(b, h) + boff + n * 2048 + k * 1024); } while (0)
; #define PG8_WAIT_V(n) asm volatile("s_waitcnt vmcnt(" #n ")" ::: "memory")
; #define PG8_WAIT_L(n) asm volatile("s_waitcnt lgkmcnt(" #n ")" ::: "memory")
; #define PG8_BAR __builtin_amdgcn_s_barrier()
; #define PG8_SCHED __builtin_amdgcn_sched_barrier(0)
; template <class Desc, class Epi>
; __device__ __forceinline__ void gemm_phase(const int wv_, LAS unsigned char* lds, const Desc& d, const Epi& E) {
;     ...
;         for (int t = 0; t < nt; t += 2) {
;             const bool last = (t == nt - 2);
;             unsigned sA0[2], sA1[2];
;             if constexpr (Desc::GATHER) { sA0[0] = last ? voffAn[0] : voffA[0]; sA0[1] = last ? voffAn[1] : voffA[1]; sA1[0] = last ? voffAn1[0] : voffA1[0]; sA1[1] = last ? voffAn1[1] : voffA1[1]; }
;             else { sA0[0] = voffA[0]; sA0[1] = voffA[1]; sA1[0] = voffA1[0]; sA1[1] = voffA1[1]; }
;             const char* a1 = cA + (size_t)(t + 1) * kstep;
;             const char* a2 = last ? nA : cA + (size_t)(t + 2) * kstep; const char* b2 = last ? nB : cB + (size_t)(t + 2) * kstep;
;             const char* a3 = a2 + kstep; const char* b3 = b2 + kstep;
;             PG8_LDB(B0, 0, 0); PG8_LDB(B1, 0, 1); PG8_SCHED; PG8_LDA(At, 0, 0); PG8_STAGE(PG8_SA(1, 1), a1, voffA1);
;             PG8_WAIT_V(8); PG8_WAIT_L(0); PG8_BAR; PG8_MMA(0, 0, At, B0); PG8_MMA(0, 1, At, B1); PG8_BAR; PG8_SCHED;
;             PG8_LDA(At, 0, 1); PG8_STAGE(PG8_SB(0, 0), b2, voffB); PG8_STAGE(PG8_SB(0, 1), b2 + hstepB, voffB); PG8_STAGE(PG8_SA(0, 0), a2, sA0);
.LBB0_917:
	s_add_u32 s54, s52, s22
	s_addc_u32 s55, s53, 0
	s_add_u32 s23, s54, 0x100
	s_addc_u32 s24, s55, 0
	s_and_b64 s[4:5], s[20:21], exec
	s_cselect_b32 s4, s44, s23
	s_cselect_b32 s5, s45, s24
	s_add_u32 s22, s50, s22
	s_addc_u32 s23, s51, 0
	s_add_u32 s22, s22, 0x100
	s_addc_u32 s23, s23, 0
	s_add_i32 s80, 0, 0x10000
	s_and_b64 s[20:21], s[20:21], exec
	s_cselect_b32 s21, s47, s23
	s_cselect_b32 s20, s46, s22
	s_add_i32 s23, 0, 0x14000
	v_add_u32_e32 v96, s80, v139
	s_add_i32 s82, s80, s60
	ds_read_b128 v[150:153], v96
	ds_read_b128 v[154:157], v96 offset:1024
	ds_read_b128 v[158:161], v96 offset:2048
	ds_read_b128 v[162:165], v96 offset:3072
	v_add_u32_e32 v96, s23, v139
	s_add_i32 m0, s61, 0xc000
	s_add_i32 s83, s61, 0xe000
	s_add_i32 s78, s82, 0x2000
	ds_read_b128 v[166:169], v96
	ds_read_b128 v[170:173], v96 offset:1024
	ds_read_b128 v[174:177], v96 offset:2048
	ds_read_b128 v[178:181], v96 offset:3072
	s_add_u32 s24, s20, 0x40000
	s_addc_u32 s25, s21, 0
	s_add_i32 s76, 0, 0x18000
	s_add_i32 s79, s23, s60
	s_add_i32 s74, s76, s60
	s_add_i32 s77, s79, 0x2000
	s_add_i32 s75, 0, 0x1c000
	s_add_i32 s29, s74, 0x2000
	s_add_u32 s22, s20, 0x40080
	s_addc_u32 s23, s21, 0
	s_add_i32 s81, s75, s60
	s_add_i32 s80, s81, 0x2000
	v_mov_b32_e32 v96, v133
	ds_read_b128 v[182:185], v149
	ds_read_b128 v[186:189], v149 offset:1024
	ds_read_b128 v[190:193], v149 offset:2048
	ds_read_b128 v[194:197], v149 offset:3072
	ds_read_b128 v[198:201], v149 offset:4096
	ds_read_b128 v[202:205], v149 offset:5120
	ds_read_b128 v[206:209], v149 offset:6144
	ds_read_b128 v[210:213], v149 offset:7168
	s_nop 0
	v_lshl_add_u64 v[130:131], s[54:55], 0, v[96:97]
	v_lshl_add_u64 v[130:131], v[130:131], 0, s[30:31]
	v_mov_b32_e32 v96, v136
	global_load_lds_dwordx4 v[130:131], off
	s_mov_b32 m0, s83
	v_lshl_add_u64 v[130:131], s[54:55], 0, v[96:97]
	v_lshl_add_u64 v[130:131], v[130:131], 0, s[30:31]
	global_load_lds_dwordx4 v[130:131], off
	s_waitcnt vmcnt(8)
	s_waitcnt lgkmcnt(0)
	s_barrier
	s_waitcnt lgkmcnt(0)
	v_mfma_f32_16x16x32_bf16 v[126:129], v[150:153], v[182:185], v[126:129]
	v_mfma_f32_16x16x32_bf16 v[122:125], v[158:161], v[182:185], v[122:125]
	v_mfma_f32_16x16x32_bf16 v[110:113], v[150:153], v[190:193], v[110:113]
	v_mfma_f32_16x16x32_bf16 v[106:109], v[158:161], v[190:193], v[106:109]
	v_mfma_f32_16x16x32_bf16 v[92:95], v[150:153], v[198:201], v[92:95]
	v_mfma_f32_16x16x32_bf16 v[88:91], v[158:161], v[198:201], v[88:91]
	v_mfma_f32_16x16x32_bf16 v[76:79], v[150:153], v[206:209], v[76:79]
	v_mfma_f32_16x16x32_bf16 v[72:75], v[158:161], v[206:209], v[72:75]
	v_mfma_f32_16x16x32_bf16 v[126:129], v[154:157], v[186:189], v[126:129]
	v_mfma_f32_16x16x32_bf16 v[122:125], v[162:165], v[186:189], v[122:125]
	v_mfma_f32_16x16x32_bf16 v[110:113], v[154:157], v[194:197], v[110:113]
	v_mfma_f32_16x16x32_bf16 v[106:109], v[162:165], v[194:197], v[106:109]
	v_mfma_f32_16x16x32_bf16 v[92:95], v[154:157], v[202:205], v[92:95]
	v_mfma_f32_16x16x32_bf16 v[88:91], v[162:165], v[202:205], v[88:91]
	v_mfma_f32_16x16x32_bf16 v[76:79], v[154:157], v[210:213], v[76:79]
	v_mfma_f32_16x16x32_bf16 v[72:75], v[162:165], v[210:213], v[72:75]
	v_mfma_f32_16x16x32_bf16 v[118:121], v[166:169], v[182:185], v[118:121]
	v_mfma_f32_16x16x32_bf16 v[114:117], v[174:177], v[182:185], v[114:117]
	v_mfma_f32_16x16x32_bf16 v[102:105], v[166:169], v[190:193], v[102:105]
	v_mfma_f32_16x16x32_bf16 v[98:101], v[174:177], v[190:193], v[98:101]
	v_mfma_f32_16x16x32_bf16 v[84:87], v[166:169], v[198:201], v[84:87]
	v_mfma_f32_16x16x32_bf16 v[80:83], v[174:177], v[198:201], v[80:83]
	v_mfma_f32_16x16x32_bf16 v[68:71], v[166:169], v[206:209], v[68:71]
	v_mfma_f32_16x16x32_bf16 v[64:67], v[174:177], v[206:209], v[64:67]
	v_mfma_f32_16x16x32_bf16 v[118:121], v[170:173], v[186:189], v[118:121]
	v_mfma_f32_16x16x32_bf16 v[114:117], v[178:181], v[186:189], v[114:117]
	v_mfma_f32_16x16x32_bf16 v[102:105], v[170:173], v[194:197], v[102:105]
	v_mfma_f32_16x16x32_bf16 v[98:101], v[178:181], v[194:197], v[98:101]
	v_mfma_f32_16x16x32_bf16 v[84:87], v[170:173], v[202:205], v[84:87]
	v_mfma_f32_16x16x32_bf16 v[80:83], v[178:181], v[202:205], v[80:83]
	v_mfma_f32_16x16x32_bf16 v[68:71], v[170:173], v[210:213], v[68:71]
	v_mfma_f32_16x16x32_bf16 v[64:67], v[178:181], v[210:213], v[64:67]
	s_barrier
	s_mov_b32 m0, s82
	ds_read_b128 v[182:185], v149 offset:16384
	ds_read_b128 v[186:189], v149 offset:17408
	ds_read_b128 v[190:193], v149 offset:18432
	ds_read_b128 v[194:197], v149 offset:19456
	ds_read_b128 v[198:201], v149 offset:20480
	ds_read_b128 v[202:205], v149 offset:21504
	ds_read_b128 v[206:209], v149 offset:22528
	ds_read_b128 v[210:213], v149 offset:23552
	s_nop 0
	global_load_lds_dwordx4 v134, s[20:21]
	s_mov_b32 m0, s78
	s_nop 0
	global_load_lds_dwordx4 v137, s[20:21]
	s_mov_b32 m0, s79
	s_nop 0
	global_load_lds_dwordx4 v134, s[24:25]
	s_mov_b32 m0, s77
	s_nop 0
	global_load_lds_dwordx4 v137, s[24:25]
	s_mov_b32 m0, s61
	s_nop 0
	global_load_lds_dwordx4 v132, s[4:5]
	s_mov_b32 m0, s63
	s_nop 0
	global_load_lds_dwordx4 v135, s[4:5]
	s_waitcnt vmcnt(8)
	s_waitcnt lgkmcnt(0)
	s_barrier
; #define PG8_STAGE(bufoff, gbase, voff) do { _Pragma("unroll") for (int _i = 0; _i < 2; ++_i) \
;         __builtin_amdgcn_global_load_lds((const __attribute__((address_space(1))) unsigned*)((const __attribute__((address_space(1))) char*)(gbase) + (unsigned)lnd_v((int)(voff)[_i])), (LAS unsigned*)(lds + (bufoff) + ldsw + _i * 8192), 16, 0, 0); } while (0)
; #define PG8_LDA(dst, b, h) do { _Pragma("unroll") for (int m = 0; m < 4; ++m) _Pragma("unroll") for (int k = 0; k < 2; ++k) dst[m][k] = *(const LAS bf16x8*)(lds + PG8_SA(b, h) + aoff + m * 2048 + k * 1024); } while (0)
; #define PG8_LDB(dst, b, h) do { _Pragma("unroll") for (int n = 0; n < 2; ++n) _Pragma("unroll") for (int k = 0; k < 2; ++k) dst[n][k] = *(const LAS bf16x8*)(lds + PG8_SB(b, h) + boff + n * 2048 + k * 1024); } while (0)
; #define PG8_MMA(ai, bj, At, Bt) do { __builtin_amdgcn_s_setprio(1); _Pragma("unroll") for (int m = 0; m < 4; ++m) _Pragma("unroll") for (int n = 0; n < 2; ++n) _Pragma("unroll") for (int k = 0; k < 2; ++k) \
;         acc[ai][bj][m][n] = __builtin_amdgcn_mfma_f32_16x16x32_bf16(Bt[n][k], At[m][k], acc[ai][bj][m][n], 0, 0, 0); __builtin_amdgcn_s_setprio(0); } while (0)
; #define PG8_WAIT_V(n) asm volatile("s_waitcnt vmcnt(" #n ")" ::: "memory")
; #define PG8_WAIT_L(n) asm volatile("s_waitcnt lgkmcnt(" #n ")" ::: "memory")
; #define PG8_BAR __builtin_amdgcn_s_barrier()
; #define PG8_SCHED __builtin_amdgcn_sched_barrier(0)
; template <class Desc, class Epi>
; __device__ __forceinline__ void gemm_phase(const int wv_, LAS unsigned char* lds, const Desc& d, const Epi& E) {
;     ...
;             PG8_WAIT_V(8); PG8_WAIT_L(0); PG8_BAR; PG8_MMA(1, 0, At, B0); PG8_MMA(1, 1, At, B1); PG8_BAR; PG8_SCHED;
;             PG8_LDB(B0, 1, 0); PG8_LDB(B1, 1, 1); PG8_SCHED; PG8_LDA(At, 1, 0); PG8_STAGE(PG8_SA(0, 1), a2, sA1);
;             PG8_WAIT_V(8); PG8_WAIT_L(0); PG8_BAR; PG8_MMA(0, 0, At, B0); PG8_MMA(0, 1, At, B1); PG8_BAR; PG8_SCHED;
	s_waitcnt lgkmcnt(0)
	v_mfma_f32_16x16x32_bf16 v[60:63], v[150:153], v[182:185], v[60:63]
	v_mfma_f32_16x16x32_bf16 v[56:59], v[158:161], v[182:185], v[56:59]
	v_mfma_f32_16x16x32_bf16 v[44:47], v[150:153], v[190:193], v[44:47]
	v_mfma_f32_16x16x32_bf16 v[32:35], v[158:161], v[190:193], v[32:35]
	v_mfma_f32_16x16x32_bf16 v[16:19], v[150:153], v[198:201], v[16:19]
	v_mfma_f32_16x16x32_bf16 v[8:11], v[158:161], v[198:201], v[8:11]
	v_mfma_f32_16x16x32_bf16 v[4:7], v[150:153], v[206:209], v[4:7]
	v_mfma_f32_16x16x32_bf16 v[0:3], v[158:161], v[206:209], v[0:3]
	v_mfma_f32_16x16x32_bf16 v[60:63], v[154:157], v[186:189], v[60:63]
	v_mfma_f32_16x16x32_bf16 v[56:59], v[162:165], v[186:189], v[56:59]
	v_mfma_f32_16x16x32_bf16 v[44:47], v[154:157], v[194:197], v[44:47]
	v_mfma_f32_16x16x32_bf16 v[32:35], v[162:165], v[194:197], v[32:35]
	v_mfma_f32_16x16x32_bf16 v[16:19], v[154:157], v[202:205], v[16:19]
	v_mfma_f32_16x16x32_bf16 v[8:11], v[162:165], v[202:205], v[8:11]
	v_mfma_f32_16x16x32_bf16 v[4:7], v[154:157], v[210:213], v[4:7]
	v_mfma_f32_16x16x32_bf16 v[0:3], v[162:165], v[210:213], v[0:3]
	v_mfma_f32_16x16x32_bf16 v[52:55], v[166:169], v[182:185], v[52:55]
	v_mfma_f32_16x16x32_bf16 v[48:51], v[174:177], v[182:185], v[48:51]
	v_mfma_f32_16x16x32_bf16 v[28:31], v[166:169], v[190:193], v[28:31]
	v_mfma_f32_16x16x32_bf16 v[12:15], v[174:177], v[190:193], v[12:15]
	v_mfma_f32_16x16x32_bf16 v[36:39], v[166:169], v[198:201], v[36:39]
	v_mfma_f32_16x16x32_bf16 v[40:43], v[174:177], v[198:201], v[40:43]
	v_mfma_f32_16x16x32_bf16 v[20:23], v[166:169], v[206:209], v[20:23]
	v_mfma_f32_16x16x32_bf16 v[24:27], v[174:177], v[206:209], v[24:27]
	v_mfma_f32_16x16x32_bf16 v[52:55], v[170:173], v[186:189], v[52:55]
	v_mfma_f32_16x16x32_bf16 v[48:51], v[178:181], v[186:189], v[48:51]
	v_mfma_f32_16x16x32_bf16 v[28:31], v[170:173], v[194:197], v[28:31]
	v_mfma_f32_16x16x32_bf16 v[12:15], v[178:181], v[194:197], v[12:15]
	v_mfma_f32_16x16x32_bf16 v[36:39], v[170:173], v[202:205], v[36:39]
	v_mfma_f32_16x16x32_bf16 v[40:43], v[178:181], v[202:205], v[40:43]
	v_mfma_f32_16x16x32_bf16 v[20:23], v[170:173], v[210:213], v[20:23]
	v_mfma_f32_16x16x32_bf16 v[24:27], v[178:181], v[210:213], v[24:27]
	s_barrier
	v_add_u32_e32 v96, s76, v139
	ds_read_b128 v[150:153], v96
	ds_read_b128 v[154:157], v96 offset:1024
	ds_read_b128 v[158:161], v96 offset:2048
	ds_read_b128 v[162:165], v96 offset:3072
	v_add_u32_e32 v96, s75, v139
	ds_read_b128 v[166:169], v96
	ds_read_b128 v[170:173], v96 offset:1024
	ds_read_b128 v[174:177], v96 offset:2048
	ds_read_b128 v[178:181], v96 offset:3072
	s_mov_b32 m0, s64
	ds_read_b128 v[182:185], v149 offset:32768
	ds_read_b128 v[186:189], v149 offset:33792
	ds_read_b128 v[190:193], v149 offset:34816
	ds_read_b128 v[194:197], v149 offset:35840
	ds_read_b128 v[198:201], v149 offset:36864
	ds_read_b128 v[202:205], v149 offset:37888
	ds_read_b128 v[206:209], v149 offset:38912
	ds_read_b128 v[210:213], v149 offset:39936
	s_nop 0
	global_load_lds_dwordx4 v133, s[4:5]
	s_mov_b32 m0, s65
	s_nop 0
	global_load_lds_dwordx4 v136, s[4:5]
	s_waitcnt vmcnt(8)
	s_waitcnt lgkmcnt(0)
	s_barrier
	s_waitcnt lgkmcnt(0)
	v_mfma_f32_16x16x32_bf16 v[126:129], v[150:153], v[182:185], v[126:129]
	v_mfma_f32_16x16x32_bf16 v[122:125], v[158:161], v[182:185], v[122:125]
	v_mfma_f32_16x16x32_bf16 v[110:113], v[150:153], v[190:193], v[110:113]
	v_mfma_f32_16x16x32_bf16 v[106:109], v[158:161], v[190:193], v[106:109]
	v_mfma_f32_16x16x32_bf16 v[92:95], v[150:153], v[198:201], v[92:95]
	v_mfma_f32_16x16x32_bf16 v[88:91], v[158:161], v[198:201], v[88:91]
	v_mfma_f32_16x16x32_bf16 v[76:79], v[150:153], v[206:209], v[76:79]
	v_mfma_f32_16x16x32_bf16 v[72:75], v[158:161], v[206:209], v[72:75]
	v_mfma_f32_16x16x32_bf16 v[126:129], v[154:157], v[186:189], v[126:129]
	v_mfma_f32_16x16x32_bf16 v[122:125], v[162:165], v[186:189], v[122:125]
	v_mfma_f32_16x16x32_bf16 v[110:113], v[154:157], v[194:197], v[110:113]
	v_mfma_f32_16x16x32_bf16 v[106:109], v[162:165], v[194:197], v[106:109]
	v_mfma_f32_16x16x32_bf16 v[92:95], v[154:157], v[202:205], v[92:95]
	v_mfma_f32_16x16x32_bf16 v[88:91], v[162:165], v[202:205], v[88:91]
	v_mfma_f32_16x16x32_bf16 v[76:79], v[154:157], v[210:213], v[76:79]
	v_mfma_f32_16x16x32_bf16 v[72:75], v[162:165], v[210:213], v[72:75]
	v_mfma_f32_16x16x32_bf16 v[118:121], v[166:169], v[182:185], v[118:121]
	v_mfma_f32_16x16x32_bf16 v[114:117], v[174:177], v[182:185], v[114:117]
	v_mfma_f32_16x16x32_bf16 v[102:105], v[166:169], v[190:193], v[102:105]
	v_mfma_f32_16x16x32_bf16 v[98:101], v[174:177], v[190:193], v[98:101]
	v_mfma_f32_16x16x32_bf16 v[84:87], v[166:169], v[198:201], v[84:87]
	v_mfma_f32_16x16x32_bf16 v[80:83], v[174:177], v[198:201], v[80:83]
	v_mfma_f32_16x16x32_bf16 v[68:71], v[166:169], v[206:209], v[68:71]
	v_mfma_f32_16x16x32_bf16 v[64:67], v[174:177], v[206:209], v[64:67]
	v_mfma_f32_16x16x32_bf16 v[118:121], v[170:173], v[186:189], v[118:121]
	v_mfma_f32_16x16x32_bf16 v[114:117], v[178:181], v[186:189], v[114:117]
	v_mfma_f32_16x16x32_bf16 v[102:105], v[170:173], v[194:197], v[102:105]
	v_mfma_f32_16x16x32_bf16 v[98:101], v[178:181], v[194:197], v[98:101]
	v_mfma_f32_16x16x32_bf16 v[84:87], v[170:173], v[202:205], v[84:87]
	v_mfma_f32_16x16x32_bf16 v[80:83], v[178:181], v[202:205], v[80:83]
	v_mfma_f32_16x16x32_bf16 v[68:71], v[170:173], v[210:213], v[68:71]
	v_mfma_f32_16x16x32_bf16 v[64:67], v[178:181], v[210:213], v[64:67]
	s_barrier
; #define PG8_STAGE(bufoff, gbase, voff) do { _Pragma("unroll") for (int _i = 0; _i < 2; ++_i) \
;         __builtin_amdgcn_global_load_lds((const __attribute__((address_space(1))) unsigned*)((const __attribute__((address_space(1))) char*)(gbase) + (unsigned)lnd_v((int)(voff)[_i])), (LAS unsigned*)(lds + (bufoff) + ldsw + _i * 8192), 16, 0, 0); } while (0)
; #define PG8_LDA(dst, b, h) do { _Pragma("unroll") for (int m = 0; m < 4; ++m) _Pragma("unroll") for (int k = 0; k < 2; ++k) dst[m][k] = *(const LAS bf16x8*)(lds + PG8_SA(b, h) + aoff + m * 2048 + k * 1024); } while (0)
; #define PG8_MMA(ai, bj, At, Bt) do { __builtin_amdgcn_s_setprio(1); _Pragma("unroll") for (int m = 0; m < 4; ++m) _Pragma("unroll") for (int n = 0; n < 2; ++n) _Pragma("unroll") for (int k = 0; k < 2; ++k) \
;         acc[ai][bj][m][n] = __builtin_amdgcn_mfma_f32_16x16x32_bf16(Bt[n][k], At[m][k], acc[ai][bj][m][n], 0, 0, 0); __builtin_amdgcn_s_setprio(0); } while (0)
; #define PG8_WAIT_V(n) asm volatile("s_waitcnt vmcnt(" #n ")" ::: "memory")
; #define PG8_WAIT_L(n) asm volatile("s_waitcnt lgkmcnt(" #n ")" ::: "memory")
; #define PG8_BAR __builtin_amdgcn_s_barrier()
; #define PG8_SCHED __builtin_amdgcn_sched_barrier(0)
; template <class Desc, class Epi>
; __device__ __forceinline__ void gemm_phase(const int wv_, LAS unsigned char* lds, const Desc& d, const Epi& E) {
;     ...
;             PG8_LDA(At, 1, 1); PG8_STAGE(PG8_SB(1, 0), b3, voffB); PG8_STAGE(PG8_SB(1, 1), b3 + hstepB, voffB); PG8_STAGE(PG8_SA(1, 0), a3, sA0);
;             PG8_WAIT_V(8); PG8_WAIT_L(0); PG8_BAR; PG8_MMA(1, 0, At, B0); PG8_MMA(1, 1, At, B1); PG8_BAR; PG8_SCHED;
;         }
;         if (wr == 0) PG8_BAR;
	v_mov_b32_e32 v96, v134
	ds_read_b128 v[182:185], v149 offset:49152
	ds_read_b128 v[186:189], v149 offset:50176
	ds_read_b128 v[190:193], v149 offset:51200
	ds_read_b128 v[194:197], v149 offset:52224
	ds_read_b128 v[198:201], v149 offset:53248
	ds_read_b128 v[202:205], v149 offset:54272
	ds_read_b128 v[206:209], v149 offset:55296
	ds_read_b128 v[210:213], v149 offset:56320
	s_mov_b32 m0, s74
	v_lshl_add_u64 v[130:131], s[20:21], 0, v[96:97]
	v_lshl_add_u64 v[130:131], v[130:131], 0, s[30:31]
	v_mov_b32_e32 v96, v137
	global_load_lds_dwordx4 v[130:131], off
	s_mov_b32 m0, s29
	v_lshl_add_u64 v[130:131], s[20:21], 0, v[96:97]
	v_lshl_add_u64 v[130:131], v[130:131], 0, s[30:31]
	global_load_lds_dwordx4 v[130:131], off
	s_mov_b32 m0, s81
	s_nop 0
	global_load_lds_dwordx4 v134, s[22:23]
	s_mov_b32 m0, s80
	s_nop 0
	global_load_lds_dwordx4 v137, s[22:23]
	v_mov_b32_e32 v96, v132
	s_mov_b32 m0, s68
	v_lshl_add_u64 v[130:131], s[4:5], 0, v[96:97]
	v_lshl_add_u64 v[130:131], v[130:131], 0, s[30:31]
	v_mov_b32_e32 v96, v135
	global_load_lds_dwordx4 v[130:131], off
	s_mov_b32 m0, s69
	v_lshl_add_u64 v[130:131], s[4:5], 0, v[96:97]
	v_lshl_add_u64 v[130:131], v[130:131], 0, s[30:31]
	global_load_lds_dwordx4 v[130:131], off
	s_waitcnt vmcnt(8)
	s_waitcnt lgkmcnt(0)
	s_barrier
	s_waitcnt lgkmcnt(0)
	v_mfma_f32_16x16x32_bf16 v[60:63], v[150:153], v[182:185], v[60:63]
	v_mfma_f32_16x16x32_bf16 v[56:59], v[158:161], v[182:185], v[56:59]
	v_mfma_f32_16x16x32_bf16 v[44:47], v[150:153], v[190:193], v[44:47]
	v_mfma_f32_16x16x32_bf16 v[32:35], v[158:161], v[190:193], v[32:35]
	v_mfma_f32_16x16x32_bf16 v[16:19], v[150:153], v[198:201], v[16:19]
	v_mfma_f32_16x16x32_bf16 v[8:11], v[158:161], v[198:201], v[8:11]
	v_mfma_f32_16x16x32_bf16 v[4:7], v[150:153], v[206:209], v[4:7]
	v_mfma_f32_16x16x32_bf16 v[0:3], v[158:161], v[206:209], v[0:3]
	v_mfma_f32_16x16x32_bf16 v[60:63], v[154:157], v[186:189], v[60:63]
	v_mfma_f32_16x16x32_bf16 v[56:59], v[162:165], v[186:189], v[56:59]
	v_mfma_f32_16x16x32_bf16 v[44:47], v[154:157], v[194:197], v[44:47]
	v_mfma_f32_16x16x32_bf16 v[32:35], v[162:165], v[194:197], v[32:35]
	v_mfma_f32_16x16x32_bf16 v[16:19], v[154:157], v[202:205], v[16:19]
	v_mfma_f32_16x16x32_bf16 v[8:11], v[162:165], v[202:205], v[8:11]
	v_mfma_f32_16x16x32_bf16 v[4:7], v[154:157], v[210:213], v[4:7]
	v_mfma_f32_16x16x32_bf16 v[0:3], v[162:165], v[210:213], v[0:3]
	v_mfma_f32_16x16x32_bf16 v[52:55], v[166:169], v[182:185], v[52:55]
	v_mfma_f32_16x16x32_bf16 v[48:51], v[174:177], v[182:185], v[48:51]
	v_mfma_f32_16x16x32_bf16 v[28:31], v[166:169], v[190:193], v[28:31]
	v_mfma_f32_16x16x32_bf16 v[12:15], v[174:177], v[190:193], v[12:15]
	v_mfma_f32_16x16x32_bf16 v[36:39], v[166:169], v[198:201], v[36:39]
	v_mfma_f32_16x16x32_bf16 v[40:43], v[174:177], v[198:201], v[40:43]
	v_mfma_f32_16x16x32_bf16 v[20:23], v[166:169], v[206:209], v[20:23]
	v_mfma_f32_16x16x32_bf16 v[24:27], v[174:177], v[206:209], v[24:27]
	v_mfma_f32_16x16x32_bf16 v[52:55], v[170:173], v[186:189], v[52:55]
	v_mfma_f32_16x16x32_bf16 v[48:51], v[178:181], v[186:189], v[48:51]
	v_mfma_f32_16x16x32_bf16 v[28:31], v[170:173], v[194:197], v[28:31]
	v_mfma_f32_16x16x32_bf16 v[12:15], v[178:181], v[194:197], v[12:15]
	v_mfma_f32_16x16x32_bf16 v[36:39], v[170:173], v[202:205], v[36:39]
	v_mfma_f32_16x16x32_bf16 v[40:43], v[178:181], v[202:205], v[40:43]
	v_mfma_f32_16x16x32_bf16 v[20:23], v[170:173], v[210:213], v[20:23]
	v_mfma_f32_16x16x32_bf16 v[24:27], v[178:181], v[210:213], v[24:27]
	s_barrier
	s_movk_i32 s22, 0x100
	s_andn2_b64 vcc, exec, s[2:3]
	s_mov_b64 s[20:21], -1
	s_mov_b64 s[2:3], 0
	s_cbranch_vccz .LBB0_917
	s_and_b64 vcc, exec, s[42:43]
	s_cbranch_vccz .LBB0_920
	s_barrier

; #define PG8_STAGE(bufoff, gbase, voff) do { _Pragma("unroll") for (int _i = 0; _i < 2; ++_i) \
;         __builtin_amdgcn_global_load_lds((const __attribute__((address_space(1))) unsigned*)((const __attribute__((address_space(1))) char*)(gbase) + (unsigned)lnd_v((int)(voff)[_i])), (LAS unsigned*)(lds + (bufoff) + ldsw + _i * 8192), 16, 0, 0); } while (0)
; #define PG8_WAIT_V(n) asm volatile("s_waitcnt vmcnt(" #n ")" ::: "memory")
; #define PG8_BAR __builtin_amdgcn_s_barrier()
; template <class Desc, class Epi>
; __device__ __forceinline__ void gemm_phase(const int wv_, LAS unsigned char* lds, const Desc& d, const Epi& E) {
;     ...
; #pragma unroll
;     for (int i = 0; i < 2; ++i) { int R, C; stage_rc(tid * 16 + i * 8192, R, C); const int Rb = (R & ~31) + perm32(R & 31); Rr[i] = R; Cc[i] = C;
;         voffA[i] = (unsigned)(R * d.lda + C) * 2u; voffA1[i] = voffA[i] + (unsigned)hstepA; voffB[i] = (unsigned)(Rb * d.ldb + C) * 2u; }
;     ...
;     PG8_STAGE(PG8_SB(0, 0), cB, voffB); PG8_STAGE(PG8_SB(0, 1), cB + hstepB, voffB); PG8_STAGE(PG8_SA(0, 0), cA, voffA); PG8_STAGE(PG8_SA(0, 1), cA, voffA1);
;     if (wr == 1) PG8_BAR;
;     PG8_WAIT_V(2); PG8_BAR;
;     PG8_STAGE(PG8_SB(1, 0), cB + kstep, voffB); PG8_STAGE(PG8_SA(1, 0), cA + kstep, voffA); PG8_STAGE(PG8_SB(1, 1), cB + hstepB + kstep, voffB);
;     PG8_WAIT_V(6); PG8_BAR;
.LBB0_929:
	s_or_b64 exec, exec, s[2:3]
	v_ashrrev_i32_e32 v3, 31, v1
	v_lshrrev_b32_e32 v3, 26, v3
	v_lshlrev_b32_e32 v2, 4, v1
	v_add_u32_e32 v3, v1, v3
	v_bfe_i32 v1, v1, 27, 1
	v_lshrrev_b32_e32 v1, 22, v1
	v_add_u32_e32 v1, v2, v1
	v_and_b32_e32 v1, 0xfffffc00, v1
	v_sub_u32_e32 v1, v2, v1
	v_lshrrev_b32_e32 v4, 4, v1
	v_bitop3_b32 v1, v4, v1, 32 bitop3:0x6c
	v_ashrrev_i32_e32 v5, 31, v1
	v_ashrrev_i32_e32 v3, 6, v3
	v_lshrrev_b32_e32 v5, 26, v5
	v_lshlrev_b32_e32 v4, 3, v3
	v_add_u32_e32 v5, v1, v5
	v_and_b32_e32 v4, -16, v4
	v_ashrrev_i32_e32 v6, 6, v5
	v_and_b32_e32 v5, 0xc0, v5
	v_add_u32_e32 v4, v6, v4
	v_sub_u32_e32 v1, v1, v5
	v_lshlrev_b32_e32 v3, 5, v3
	v_ashrrev_i16_sdwa v1, v216, sext(v1) dst_sel:DWORD dst_unused:UNUSED_PAD src0_sel:DWORD src1_sel:BYTE_0
	v_lshlrev_b32_e32 v5, 1, v4
	v_lshrrev_b32_e32 v7, 2, v4
	v_and_b32_e32 v6, 3, v6
	s_mov_b32 s0, 0x1fffe0
	v_and_b32_e32 v3, 32, v3
	v_bfe_i32 v1, v1, 0, 16
	v_and_b32_e32 v5, 24, v5
	v_and_b32_e32 v7, 4, v7
	v_and_or_b32 v6, v4, s0, v6
	v_or3_b32 v5, v6, v7, v5
	v_add_lshl_u32 v1, v3, v1, 1
	v_lshl_add_u32 v132, v4, 11, v1
	v_lshl_add_u32 v134, v5, 11, v1
	v_add_u32_e32 v1, 0x2000, v2
	v_ashrrev_i32_e32 v2, 31, v1
	v_lshrrev_b32_e32 v2, 22, v2
	v_add_u32_e32 v2, v1, v2
	v_ashrrev_i32_e32 v2, 10, v2
	v_mul_i32_i24_e32 v3, 0x400, v2
	v_sub_u32_e32 v1, v1, v3
	v_lshrrev_b32_e32 v3, 4, v1
	v_bitop3_b32 v1, v3, v1, 32 bitop3:0x6c
	v_ashrrev_i32_e32 v4, 31, v1
	s_add_u32 s55, s38, 0x2e00000
	v_lshrrev_b32_e32 v4, 26, v4
	s_addc_u32 s56, s39, 0
	v_lshlrev_b32_e32 v3, 3, v2
	v_add_u32_e32 v4, v1, v4
	s_add_u32 s57, s38, 0x3a200000
	v_and_b32_e32 v3, -16, v3
	v_ashrrev_i32_e32 v5, 6, v4
	s_addc_u32 s58, s39, 0
	v_add_u32_e32 v3, v5, v3
	v_and_b32_e32 v5, 3, v5
	s_ashr_i32 s3, s4, 6
	s_lshr_b32 s1, s26, 4
	s_ashr_i32 s2, s4, 8
	v_and_or_b32 v5, v3, s0, v5
	s_lshl_b32 s59, s3, 10
	s_bfe_u32 s0, s26, 0x20002
	s_and_b32 s5, s26, 3
	s_lshl_b32 s20, s1, 19
	v_and_b32_e32 v4, 0xc0, v4
	s_add_u32 s20, s57, s20
	v_sub_u32_e32 v1, v1, v4
	s_addc_u32 s21, s58, 0
	s_lshl_b32 s22, s5, 19
	v_lshlrev_b32_e32 v2, 5, v2
	v_ashrrev_i16_sdwa v1, v216, sext(v1) dst_sel:DWORD dst_unused:UNUSED_PAD src0_sel:DWORD src1_sel:BYTE_0
	v_lshlrev_b32_e32 v4, 1, v3
	v_lshrrev_b32_e32 v6, 2, v3
	s_add_u32 s22, s55, s22
	v_and_b32_e32 v2, 32, v2
	v_bfe_i32 v1, v1, 0, 16
	v_and_b32_e32 v4, 24, v4
	v_and_b32_e32 v6, 4, v6
	s_addc_u32 s23, s56, 0
	s_lshl_b32 s24, s0, 9
	v_or3_b32 v4, v5, v6, v4
	v_add_lshl_u32 v1, v2, v1, 1
	s_add_u32 s48, s20, s24
	v_lshl_add_u32 v135, v3, 11, v1
	v_lshl_add_u32 v137, v4, 11, v1
	s_addc_u32 s49, s21, 0
	s_add_i32 s60, s59, 0
	s_waitcnt vmcnt(0) lgkmcnt(0)
	s_barrier
	s_add_i32 m0, s60, 0x10000
	v_add_u32_e32 v133, 0x40000, v132
	global_load_lds_dwordx4 v134, s[48:49]
	s_add_i32 m0, s60, 0x12000
	s_add_u32 s20, s48, 0x40000
	global_load_lds_dwordx4 v137, s[48:49]
	s_addc_u32 s21, s49, 0
	s_add_i32 m0, s60, 0x14000
	v_add_u32_e32 v136, 0x40000, v135
	global_load_lds_dwordx4 v134, s[20:21]
	s_add_i32 m0, s60, 0x16000
	s_add_u32 s50, s22, s24
	global_load_lds_dwordx4 v137, s[20:21]
	s_addc_u32 s51, s23, 0
	s_mov_b32 m0, s60
	s_add_i32 s61, s60, 0x2000
	global_load_lds_dwordx4 v132, s[50:51]
	s_mov_b32 m0, s61
	s_add_i32 s63, s60, 0x4000
	global_load_lds_dwordx4 v135, s[50:51]
	s_mov_b32 m0, s63
	s_add_i32 s64, s60, 0x6000
	global_load_lds_dwordx4 v133, s[50:51]
	v_mov_b32_e32 v1, v136
	s_mov_b32 m0, s64
	s_cmp_eq_u32 s2, 1
	global_load_lds_dwordx4 v1, s[50:51]
	s_cselect_b64 s[36:37], -1, 0
	s_and_b64 vcc, exec, s[36:37]
	s_cbranch_vccz .LBB0_931
	s_barrier
.LBB0_931:
	s_lshl_b32 s1, s1, 2
	s_or_b32 s1, s1, s5
	v_mov_b32_e32 v96, v134
	s_add_u32 s38, s38, 0x3f200000
	s_waitcnt vmcnt(2)
	s_barrier
	s_addc_u32 s39, s39, 0
	v_lshl_add_u64 v[2:3], s[48:49], 0, v[96:97]
	s_add_i32 m0, s60, 0x18000
	v_lshl_add_u64 v[2:3], v[2:3], 0, s[30:31]
	v_mov_b32_e32 v96, v137
	global_load_lds_dwordx4 v[2:3], off
	s_add_i32 m0, s60, 0x1a000
	v_lshl_add_u64 v[2:3], s[48:49], 0, v[96:97]
	v_lshl_add_u64 v[2:3], v[2:3], 0, s[30:31]
	v_mov_b32_e32 v96, v132
	s_lshl_b32 s3, s3, 5
	global_load_lds_dwordx4 v[2:3], off
	s_add_i32 s65, s60, 0x8000
	v_lshl_add_u64 v[2:3], s[50:51], 0, v[96:97]
	s_and_b32 s3, s3, 0x60
	v_lshl_add_u64 v[2:3], v[2:3], 0, s[30:31]
	s_mov_b32 m0, s65
	v_mov_b32_e32 v96, v135
	s_lshl_b32 s5, s2, 13
	s_lshl_b32 s22, s3, 7
	global_load_lds_dwordx4 v[2:3], off
	s_add_i32 s66, s60, 0xa000
	v_lshl_add_u64 v[2:3], s[50:51], 0, v[96:97]
	v_lshl_add_u64 v[2:3], v[2:3], 0, s[30:31]
	s_mov_b32 m0, s66
	s_add_u32 s20, s48, 0x40080
	global_load_lds_dwordx4 v[2:3], off
	s_addc_u32 s21, s49, 0
	s_add_i32 m0, s60, 0x1c000
	v_lshrrev_b32_e32 v2, 1, v0
	global_load_lds_dwordx4 v134, s[20:21]
	s_add_i32 m0, s60, 0x1e000
	v_and_b32_e32 v2, 24, v2
	global_load_lds_dwordx4 v137, s[20:21]
	v_and_b32_e32 v1, 15, v0
	v_lshl_or_b32 v138, s2, 6, v1
	v_lshlrev_b32_e32 v3, 1, v2
	v_lshl_or_b32 v1, v1, 6, v3
	v_lshlrev_b32_e32 v3, 2, v138
	v_and_b32_e32 v4, 32, v3
	v_lshlrev_b32_e32 v0, 2, v0
	s_waitcnt vmcnt(6)
	s_cmpk_lt_u32 s4, 0x100
	v_bitop3_b32 v4, v1, s5, v4 bitop3:0xde
	v_and_b32_e32 v0, 32, v0
	s_cselect_b64 s[40:41], -1, 0
	s_add_i32 s2, 0, 0x20000
	v_bitop3_b32 v139, v1, s22, v0 bitop3:0xde
	v_or_b32_e32 v140, 16, v138
	v_or_b32_e32 v141, 32, v138
	v_or_b32_e32 v142, 48, v138
	v_add_u32_e32 v143, 0x80, v138
	v_add_u32_e32 v144, 0x90, v138
	v_add_u32_e32 v145, 0xa0, v138
	v_add_u32_e32 v146, 0xb0, v138
	v_or_b32_e32 v147, s3, v2
	v_add_u32_e32 v148, s2, v3
	s_mov_b32 s70, 0
	v_add_u32_e32 v149, 0, v4
	s_mov_b64 s[44:45], s[48:49]
	s_mov_b64 s[42:43], s[50:51]
	s_barrier
	s_waitcnt vmcnt(0)
	s_branch .LBB0_934

; #define PG8_STAGE(bufoff, gbase, voff) do { _Pragma("unroll") for (int _i = 0; _i < 2; ++_i) \
;         __builtin_amdgcn_global_load_lds((const __attribute__((address_space(1))) unsigned*)((const __attribute__((address_space(1))) char*)(gbase) + (unsigned)lnd_v((int)(voff)[_i])), (LAS unsigned*)(lds + (bufoff) + ldsw + _i * 8192), 16, 0, 0); } while (0)
; #define PG8_LDA(dst, b, h) do { _Pragma("unroll") for (int m = 0; m < 4; ++m) _Pragma("unroll") for (int k = 0; k < 2; ++k) dst[m][k] = *(const LAS bf16x8*)(lds + PG8_SA(b, h) + aoff + m * 2048 + k * 1024); } while (0)
; #define PG8_LDB(dst, b, h) do { _Pragma("unroll") for (int n = 0; n < 2; ++n) _Pragma("unroll") for (int k = 0; k < 2; ++k) dst[n][k] = *(const LAS bf16x8*)(lds + PG8_SB(b, h) + boff + n * 2048 + k * 1024); } while (0)
; #define PG8_WAIT_V(n) asm volatile("s_waitcnt vmcnt(" #n ")" ::: "memory")
; #define PG8_WAIT_L(n) asm volatile("s_waitcnt lgkmcnt(" #n ")" ::: "memory")
; #define PG8_BAR __builtin_amdgcn_s_barrier()
; #define PG8_SCHED __builtin_amdgcn_sched_barrier(0)
; template <class Desc, class Epi>
; __device__ __forceinline__ void gemm_phase(const int wv_, LAS unsigned char* lds, const Desc& d, const Epi& E) {
;     ...
;         for (int t = 0; t < nt; t += 2) {
;             const bool last = (t == nt - 2);
;             unsigned sA0[2], sA1[2];
;             if constexpr (Desc::GATHER) { sA0[0] = last ? voffAn[0] : voffA[0]; sA0[1] = last ? voffAn[1] : voffA[1]; sA1[0] = last ? voffAn1[0] : voffA1[0]; sA1[1] = last ? voffAn1[1] : voffA1[1]; }
;             else { sA0[0] = voffA[0]; sA0[1] = voffA[1]; sA1[0] = voffA1[0]; sA1[1] = voffA1[1]; }
;             const char* a1 = cA + (size_t)(t + 1) * kstep;
;             const char* a2 = last ? nA : cA + (size_t)(t + 2) * kstep; const char* b2 = last ? nB : cB + (size_t)(t + 2) * kstep;
;             const char* a3 = a2 + kstep; const char* b3 = b2 + kstep;
;             PG8_LDB(B0, 0, 0); PG8_LDB(B1, 0, 1); PG8_SCHED; PG8_LDA(At, 0, 0); PG8_STAGE(PG8_SA(1, 1), a1, voffA1);
;             PG8_WAIT_V(8); PG8_WAIT_L(0); PG8_BAR; PG8_MMA(0, 0, At, B0); PG8_MMA(0, 1, At, B1); PG8_BAR; PG8_SCHED;
;             PG8_LDA(At, 0, 1); PG8_STAGE(PG8_SB(0, 0), b2, voffB); PG8_STAGE(PG8_SB(0, 1), b2 + hstepB, voffB); PG8_STAGE(PG8_SA(0, 0), a2, sA0);
.LBB0_937:
	s_add_u32 s52, s50, s22
	s_addc_u32 s53, s51, 0
	s_add_u32 s23, s52, 0x100
	s_addc_u32 s24, s53, 0
	s_and_b64 s[4:5], s[20:21], exec
	s_cselect_b32 s4, s42, s23
	s_cselect_b32 s5, s43, s24
	s_add_u32 s22, s48, s22
	s_addc_u32 s23, s49, 0
	s_add_u32 s22, s22, 0x100
	s_addc_u32 s23, s23, 0
	s_add_i32 s77, 0, 0x10000
	s_and_b64 s[20:21], s[20:21], exec
	s_cselect_b32 s21, s45, s23
	s_cselect_b32 s20, s44, s22
	s_add_i32 s23, 0, 0x14000
	v_add_u32_e32 v96, s77, v139
	s_add_i32 s79, s77, s59
	ds_read_b128 v[150:153], v96
	ds_read_b128 v[154:157], v96 offset:1024
	ds_read_b128 v[158:161], v96 offset:2048
	ds_read_b128 v[162:165], v96 offset:3072
	v_add_u32_e32 v96, s23, v139
	s_add_i32 m0, s60, 0xc000
	s_add_i32 s80, s60, 0xe000
	s_add_i32 s75, s79, 0x2000
	ds_read_b128 v[166:169], v96
	ds_read_b128 v[170:173], v96 offset:1024
	ds_read_b128 v[174:177], v96 offset:2048
	ds_read_b128 v[178:181], v96 offset:3072
	s_add_u32 s24, s20, 0x40000
	s_addc_u32 s25, s21, 0
	s_add_i32 s73, 0, 0x18000
	s_add_i32 s76, s23, s59
	s_add_i32 s71, s73, s59
	s_add_i32 s74, s76, 0x2000
	s_add_i32 s72, 0, 0x1c000
	s_add_i32 s29, s71, 0x2000
	s_add_u32 s22, s20, 0x40080
	s_addc_u32 s23, s21, 0
	s_add_i32 s78, s72, s59
	s_add_i32 s77, s78, 0x2000
	v_mov_b32_e32 v96, v133
	ds_read_b128 v[182:185], v149
	ds_read_b128 v[186:189], v149 offset:1024
	ds_read_b128 v[190:193], v149 offset:2048
	ds_read_b128 v[194:197], v149 offset:3072
	ds_read_b128 v[198:201], v149 offset:4096
	ds_read_b128 v[202:205], v149 offset:5120
	ds_read_b128 v[206:209], v149 offset:6144
	ds_read_b128 v[210:213], v149 offset:7168
	s_nop 0
	v_lshl_add_u64 v[130:131], s[52:53], 0, v[96:97]
	v_lshl_add_u64 v[130:131], v[130:131], 0, s[30:31]
	v_mov_b32_e32 v96, v136
	global_load_lds_dwordx4 v[130:131], off
	s_mov_b32 m0, s80
	v_lshl_add_u64 v[130:131], s[52:53], 0, v[96:97]
	v_lshl_add_u64 v[130:131], v[130:131], 0, s[30:31]
	global_load_lds_dwordx4 v[130:131], off
	s_waitcnt vmcnt(8)
	s_waitcnt lgkmcnt(0)
	s_barrier
	s_waitcnt lgkmcnt(0)
	v_mfma_f32_16x16x32_bf16 v[126:129], v[150:153], v[182:185], v[126:129]
	v_mfma_f32_16x16x32_bf16 v[122:125], v[158:161], v[182:185], v[122:125]
	v_mfma_f32_16x16x32_bf16 v[110:113], v[150:153], v[190:193], v[110:113]
	v_mfma_f32_16x16x32_bf16 v[106:109], v[158:161], v[190:193], v[106:109]
	v_mfma_f32_16x16x32_bf16 v[92:95], v[150:153], v[198:201], v[92:95]
	v_mfma_f32_16x16x32_bf16 v[88:91], v[158:161], v[198:201], v[88:91]
	v_mfma_f32_16x16x32_bf16 v[76:79], v[150:153], v[206:209], v[76:79]
	v_mfma_f32_16x16x32_bf16 v[72:75], v[158:161], v[206:209], v[72:75]
	v_mfma_f32_16x16x32_bf16 v[126:129], v[154:157], v[186:189], v[126:129]
	v_mfma_f32_16x16x32_bf16 v[122:125], v[162:165], v[186:189], v[122:125]
	v_mfma_f32_16x16x32_bf16 v[110:113], v[154:157], v[194:197], v[110:113]
	v_mfma_f32_16x16x32_bf16 v[106:109], v[162:165], v[194:197], v[106:109]
	v_mfma_f32_16x16x32_bf16 v[92:95], v[154:157], v[202:205], v[92:95]
	v_mfma_f32_16x16x32_bf16 v[88:91], v[162:165], v[202:205], v[88:91]
	v_mfma_f32_16x16x32_bf16 v[76:79], v[154:157], v[210:213], v[76:79]
	v_mfma_f32_16x16x32_bf16 v[72:75], v[162:165], v[210:213], v[72:75]
	v_mfma_f32_16x16x32_bf16 v[118:121], v[166:169], v[182:185], v[118:121]
	v_mfma_f32_16x16x32_bf16 v[114:117], v[174:177], v[182:185], v[114:117]
	v_mfma_f32_16x16x32_bf16 v[102:105], v[166:169], v[190:193], v[102:105]
	v_mfma_f32_16x16x32_bf16 v[98:101], v[174:177], v[190:193], v[98:101]
	v_mfma_f32_16x16x32_bf16 v[84:87], v[166:169], v[198:201], v[84:87]
	v_mfma_f32_16x16x32_bf16 v[80:83], v[174:177], v[198:201], v[80:83]
	v_mfma_f32_16x16x32_bf16 v[68:71], v[166:169], v[206:209], v[68:71]
	v_mfma_f32_16x16x32_bf16 v[64:67], v[174:177], v[206:209], v[64:67]
	v_mfma_f32_16x16x32_bf16 v[118:121], v[170:173], v[186:189], v[118:121]
	v_mfma_f32_16x16x32_bf16 v[114:117], v[178:181], v[186:189], v[114:117]
	v_mfma_f32_16x16x32_bf16 v[102:105], v[170:173], v[194:197], v[102:105]
	v_mfma_f32_16x16x32_bf16 v[98:101], v[178:181], v[194:197], v[98:101]
	v_mfma_f32_16x16x32_bf16 v[84:87], v[170:173], v[202:205], v[84:87]
	v_mfma_f32_16x16x32_bf16 v[80:83], v[178:181], v[202:205], v[80:83]
	v_mfma_f32_16x16x32_bf16 v[68:71], v[170:173], v[210:213], v[68:71]
	v_mfma_f32_16x16x32_bf16 v[64:67], v[178:181], v[210:213], v[64:67]
	s_barrier
	s_mov_b32 m0, s79
	ds_read_b128 v[182:185], v149 offset:16384
	ds_read_b128 v[186:189], v149 offset:17408
	ds_read_b128 v[190:193], v149 offset:18432
	ds_read_b128 v[194:197], v149 offset:19456
	ds_read_b128 v[198:201], v149 offset:20480
	ds_read_b128 v[202:205], v149 offset:21504
	ds_read_b128 v[206:209], v149 offset:22528
	ds_read_b128 v[210:213], v149 offset:23552
	s_nop 0
	global_load_lds_dwordx4 v134, s[20:21]
	s_mov_b32 m0, s75
	s_nop 0
	global_load_lds_dwordx4 v137, s[20:21]
	s_mov_b32 m0, s76
	s_nop 0
	global_load_lds_dwordx4 v134, s[24:25]
	s_mov_b32 m0, s74
	s_nop 0
	global_load_lds_dwordx4 v137, s[24:25]
	s_mov_b32 m0, s60
	s_nop 0
	global_load_lds_dwordx4 v132, s[4:5]
	s_mov_b32 m0, s61
	s_nop 0
	global_load_lds_dwordx4 v135, s[4:5]
	s_waitcnt vmcnt(8)
	s_waitcnt lgkmcnt(0)
	s_barrier
; #define PG8_STAGE(bufoff, gbase, voff) do { _Pragma("unroll") for (int _i = 0; _i < 2; ++_i) \
;         __builtin_amdgcn_global_load_lds((const __attribute__((address_space(1))) unsigned*)((const __attribute__((address_space(1))) char*)(gbase) + (unsigned)lnd_v((int)(voff)[_i])), (LAS unsigned*)(lds + (bufoff) + ldsw + _i * 8192), 16, 0, 0); } while (0)
; #define PG8_LDA(dst, b, h) do { _Pragma("unroll") for (int m = 0; m < 4; ++m) _Pragma("unroll") for (int k = 0; k < 2; ++k) dst[m][k] = *(const LAS bf16x8*)(lds + PG8_SA(b, h) + aoff + m * 2048 + k * 1024); } while (0)
; #define PG8_LDB(dst, b, h) do { _Pragma("unroll") for (int n = 0; n < 2; ++n) _Pragma("unroll") for (int k = 0; k < 2; ++k) dst[n][k] = *(const LAS bf16x8*)(lds + PG8_SB(b, h) + boff + n * 2048 + k * 1024); } while (0)
; #define PG8_MMA(ai, bj, At, Bt) do { __builtin_amdgcn_s_setprio(1); _Pragma("unroll") for (int m = 0; m < 4; ++m) _Pragma("unroll") for (int n = 0; n < 2; ++n) _Pragma("unroll") for (int k = 0; k < 2; ++k) \
;         acc[ai][bj][m][n] = __builtin_amdgcn_mfma_f32_16x16x32_bf16(Bt[n][k], At[m][k], acc[ai][bj][m][n], 0, 0, 0); __builtin_amdgcn_s_setprio(0); } while (0)
; #define PG8_WAIT_V(n) asm volatile("s_waitcnt vmcnt(" #n ")" ::: "memory")
; #define PG8_WAIT_L(n) asm volatile("s_waitcnt lgkmcnt(" #n ")" ::: "memory")
; #define PG8_BAR __builtin_amdgcn_s_barrier()
; #define PG8_SCHED __builtin_amdgcn_sched_barrier(0)
; template <class Desc, class Epi>
; __device__ __forceinline__ void gemm_phase(const int wv_, LAS unsigned char* lds, const Desc& d, const Epi& E) {
;     ...
;             PG8_WAIT_V(8); PG8_WAIT_L(0); PG8_BAR; PG8_MMA(1, 0, At, B0); PG8_MMA(1, 1, At, B1); PG8_BAR; PG8_SCHED;
;             PG8_LDB(B0, 1, 0); PG8_LDB(B1, 1, 1); PG8_SCHED; PG8_LDA(At, 1, 0); PG8_STAGE(PG8_SA(0, 1), a2, sA1);
;             PG8_WAIT_V(8); PG8_WAIT_L(0); PG8_BAR; PG8_MMA(0, 0, At, B0); PG8_MMA(0, 1, At, B1); PG8_BAR; PG8_SCHED;
	s_waitcnt lgkmcnt(0)
	v_mfma_f32_16x16x32_bf16 v[60:63], v[150:153], v[182:185], v[60:63]
	v_mfma_f32_16x16x32_bf16 v[56:59], v[158:161], v[182:185], v[56:59]
	v_mfma_f32_16x16x32_bf16 v[44:47], v[150:153], v[190:193], v[44:47]
	v_mfma_f32_16x16x32_bf16 v[32:35], v[158:161], v[190:193], v[32:35]
	v_mfma_f32_16x16x32_bf16 v[16:19], v[150:153], v[198:201], v[16:19]
	v_mfma_f32_16x16x32_bf16 v[8:11], v[158:161], v[198:201], v[8:11]
	v_mfma_f32_16x16x32_bf16 v[4:7], v[150:153], v[206:209], v[4:7]
	v_mfma_f32_16x16x32_bf16 v[0:3], v[158:161], v[206:209], v[0:3]
	v_mfma_f32_16x16x32_bf16 v[60:63], v[154:157], v[186:189], v[60:63]
	v_mfma_f32_16x16x32_bf16 v[56:59], v[162:165], v[186:189], v[56:59]
	v_mfma_f32_16x16x32_bf16 v[44:47], v[154:157], v[194:197], v[44:47]
	v_mfma_f32_16x16x32_bf16 v[32:35], v[162:165], v[194:197], v[32:35]
	v_mfma_f32_16x16x32_bf16 v[16:19], v[154:157], v[202:205], v[16:19]
	v_mfma_f32_16x16x32_bf16 v[8:11], v[162:165], v[202:205], v[8:11]
	v_mfma_f32_16x16x32_bf16 v[4:7], v[154:157], v[210:213], v[4:7]
	v_mfma_f32_16x16x32_bf16 v[0:3], v[162:165], v[210:213], v[0:3]
	v_mfma_f32_16x16x32_bf16 v[52:55], v[166:169], v[182:185], v[52:55]
	v_mfma_f32_16x16x32_bf16 v[48:51], v[174:177], v[182:185], v[48:51]
	v_mfma_f32_16x16x32_bf16 v[28:31], v[166:169], v[190:193], v[28:31]
	v_mfma_f32_16x16x32_bf16 v[12:15], v[174:177], v[190:193], v[12:15]
	v_mfma_f32_16x16x32_bf16 v[36:39], v[166:169], v[198:201], v[36:39]
	v_mfma_f32_16x16x32_bf16 v[40:43], v[174:177], v[198:201], v[40:43]
	v_mfma_f32_16x16x32_bf16 v[20:23], v[166:169], v[206:209], v[20:23]
	v_mfma_f32_16x16x32_bf16 v[24:27], v[174:177], v[206:209], v[24:27]
	v_mfma_f32_16x16x32_bf16 v[52:55], v[170:173], v[186:189], v[52:55]
	v_mfma_f32_16x16x32_bf16 v[48:51], v[178:181], v[186:189], v[48:51]
	v_mfma_f32_16x16x32_bf16 v[28:31], v[170:173], v[194:197], v[28:31]
	v_mfma_f32_16x16x32_bf16 v[12:15], v[178:181], v[194:197], v[12:15]
	v_mfma_f32_16x16x32_bf16 v[36:39], v[170:173], v[202:205], v[36:39]
	v_mfma_f32_16x16x32_bf16 v[40:43], v[178:181], v[202:205], v[40:43]
	v_mfma_f32_16x16x32_bf16 v[20:23], v[170:173], v[210:213], v[20:23]
	v_mfma_f32_16x16x32_bf16 v[24:27], v[178:181], v[210:213], v[24:27]
	s_barrier
	v_add_u32_e32 v96, s73, v139
	ds_read_b128 v[150:153], v96
	ds_read_b128 v[154:157], v96 offset:1024
	ds_read_b128 v[158:161], v96 offset:2048
	ds_read_b128 v[162:165], v96 offset:3072
	v_add_u32_e32 v96, s72, v139
	ds_read_b128 v[166:169], v96
	ds_read_b128 v[170:173], v96 offset:1024
	ds_read_b128 v[174:177], v96 offset:2048
	ds_read_b128 v[178:181], v96 offset:3072
	s_mov_b32 m0, s63
	ds_read_b128 v[182:185], v149 offset:32768
	ds_read_b128 v[186:189], v149 offset:33792
	ds_read_b128 v[190:193], v149 offset:34816
	ds_read_b128 v[194:197], v149 offset:35840
	ds_read_b128 v[198:201], v149 offset:36864
	ds_read_b128 v[202:205], v149 offset:37888
	ds_read_b128 v[206:209], v149 offset:38912
	ds_read_b128 v[210:213], v149 offset:39936
	s_nop 0
	global_load_lds_dwordx4 v133, s[4:5]
	s_mov_b32 m0, s64
	s_nop 0
	global_load_lds_dwordx4 v136, s[4:5]
	s_waitcnt vmcnt(8)
	s_waitcnt lgkmcnt(0)
	s_barrier
	s_waitcnt lgkmcnt(0)
	v_mfma_f32_16x16x32_bf16 v[126:129], v[150:153], v[182:185], v[126:129]
	v_mfma_f32_16x16x32_bf16 v[122:125], v[158:161], v[182:185], v[122:125]
	v_mfma_f32_16x16x32_bf16 v[110:113], v[150:153], v[190:193], v[110:113]
	v_mfma_f32_16x16x32_bf16 v[106:109], v[158:161], v[190:193], v[106:109]
	v_mfma_f32_16x16x32_bf16 v[92:95], v[150:153], v[198:201], v[92:95]
	v_mfma_f32_16x16x32_bf16 v[88:91], v[158:161], v[198:201], v[88:91]
	v_mfma_f32_16x16x32_bf16 v[76:79], v[150:153], v[206:209], v[76:79]
	v_mfma_f32_16x16x32_bf16 v[72:75], v[158:161], v[206:209], v[72:75]
	v_mfma_f32_16x16x32_bf16 v[126:129], v[154:157], v[186:189], v[126:129]
	v_mfma_f32_16x16x32_bf16 v[122:125], v[162:165], v[186:189], v[122:125]
	v_mfma_f32_16x16x32_bf16 v[110:113], v[154:157], v[194:197], v[110:113]
	v_mfma_f32_16x16x32_bf16 v[106:109], v[162:165], v[194:197], v[106:109]
	v_mfma_f32_16x16x32_bf16 v[92:95], v[154:157], v[202:205], v[92:95]
	v_mfma_f32_16x16x32_bf16 v[88:91], v[162:165], v[202:205], v[88:91]
	v_mfma_f32_16x16x32_bf16 v[76:79], v[154:157], v[210:213], v[76:79]
	v_mfma_f32_16x16x32_bf16 v[72:75], v[162:165], v[210:213], v[72:75]
	v_mfma_f32_16x16x32_bf16 v[118:121], v[166:169], v[182:185], v[118:121]
	v_mfma_f32_16x16x32_bf16 v[114:117], v[174:177], v[182:185], v[114:117]
	v_mfma_f32_16x16x32_bf16 v[102:105], v[166:169], v[190:193], v[102:105]
	v_mfma_f32_16x16x32_bf16 v[98:101], v[174:177], v[190:193], v[98:101]
	v_mfma_f32_16x16x32_bf16 v[84:87], v[166:169], v[198:201], v[84:87]
	v_mfma_f32_16x16x32_bf16 v[80:83], v[174:177], v[198:201], v[80:83]
	v_mfma_f32_16x16x32_bf16 v[68:71], v[166:169], v[206:209], v[68:71]
	v_mfma_f32_16x16x32_bf16 v[64:67], v[174:177], v[206:209], v[64:67]
	v_mfma_f32_16x16x32_bf16 v[118:121], v[170:173], v[186:189], v[118:121]
	v_mfma_f32_16x16x32_bf16 v[114:117], v[178:181], v[186:189], v[114:117]
	v_mfma_f32_16x16x32_bf16 v[102:105], v[170:173], v[194:197], v[102:105]
	v_mfma_f32_16x16x32_bf16 v[98:101], v[178:181], v[194:197], v[98:101]
	v_mfma_f32_16x16x32_bf16 v[84:87], v[170:173], v[202:205], v[84:87]
	v_mfma_f32_16x16x32_bf16 v[80:83], v[178:181], v[202:205], v[80:83]
	v_mfma_f32_16x16x32_bf16 v[68:71], v[170:173], v[210:213], v[68:71]
	v_mfma_f32_16x16x32_bf16 v[64:67], v[178:181], v[210:213], v[64:67]
	s_barrier
; #define PG8_STAGE(bufoff, gbase, voff) do { _Pragma("unroll") for (int _i = 0; _i < 2; ++_i) \
;         __builtin_amdgcn_global_load_lds((const __attribute__((address_space(1))) unsigned*)((const __attribute__((address_space(1))) char*)(gbase) + (unsigned)lnd_v((int)(voff)[_i])), (LAS unsigned*)(lds + (bufoff) + ldsw + _i * 8192), 16, 0, 0); } while (0)
; #define PG8_LDA(dst, b, h) do { _Pragma("unroll") for (int m = 0; m < 4; ++m) _Pragma("unroll") for (int k = 0; k < 2; ++k) dst[m][k] = *(const LAS bf16x8*)(lds + PG8_SA(b, h) + aoff + m * 2048 + k * 1024); } while (0)
; #define PG8_MMA(ai, bj, At, Bt) do { __builtin_amdgcn_s_setprio(1); _Pragma("unroll") for (int m = 0; m < 4; ++m) _Pragma("unroll") for (int n = 0; n < 2; ++n) _Pragma("unroll") for (int k = 0; k < 2; ++k) \
;         acc[ai][bj][m][n] = __builtin_amdgcn_mfma_f32_16x16x32_bf16(Bt[n][k], At[m][k], acc[ai][bj][m][n], 0, 0, 0); __builtin_amdgcn_s_setprio(0); } while (0)
; #define PG8_WAIT_V(n) asm volatile("s_waitcnt vmcnt(" #n ")" ::: "memory")
; #define PG8_WAIT_L(n) asm volatile("s_waitcnt lgkmcnt(" #n ")" ::: "memory")
; #define PG8_BAR __builtin_amdgcn_s_barrier()
; #define PG8_SCHED __builtin_amdgcn_sched_barrier(0)
; template <class Desc, class Epi>
; __device__ __forceinline__ void gemm_phase(const int wv_, LAS unsigned char* lds, const Desc& d, const Epi& E) {
;     ...
;             PG8_LDA(At, 1, 1); PG8_STAGE(PG8_SB(1, 0), b3, voffB); PG8_STAGE(PG8_SB(1, 1), b3 + hstepB, voffB); PG8_STAGE(PG8_SA(1, 0), a3, sA0);
;             PG8_WAIT_V(8); PG8_WAIT_L(0); PG8_BAR; PG8_MMA(1, 0, At, B0); PG8_MMA(1, 1, At, B1); PG8_BAR; PG8_SCHED;
;         }
;         if (wr == 0) PG8_BAR;
	v_mov_b32_e32 v96, v134
	ds_read_b128 v[182:185], v149 offset:49152
	ds_read_b128 v[186:189], v149 offset:50176
	ds_read_b128 v[190:193], v149 offset:51200
	ds_read_b128 v[194:197], v149 offset:52224
	ds_read_b128 v[198:201], v149 offset:53248
	ds_read_b128 v[202:205], v149 offset:54272
	ds_read_b128 v[206:209], v149 offset:55296
	ds_read_b128 v[210:213], v149 offset:56320
	s_mov_b32 m0, s71
	v_lshl_add_u64 v[130:131], s[20:21], 0, v[96:97]
	v_lshl_add_u64 v[130:131], v[130:131], 0, s[30:31]
	v_mov_b32_e32 v96, v137
	global_load_lds_dwordx4 v[130:131], off
	s_mov_b32 m0, s29
	v_lshl_add_u64 v[130:131], s[20:21], 0, v[96:97]
	v_lshl_add_u64 v[130:131], v[130:131], 0, s[30:31]
	global_load_lds_dwordx4 v[130:131], off
	s_mov_b32 m0, s78
	s_nop 0
	global_load_lds_dwordx4 v134, s[22:23]
	s_mov_b32 m0, s77
	s_nop 0
	global_load_lds_dwordx4 v137, s[22:23]
	v_mov_b32_e32 v96, v132
	s_mov_b32 m0, s65
	v_lshl_add_u64 v[130:131], s[4:5], 0, v[96:97]
	v_lshl_add_u64 v[130:131], v[130:131], 0, s[30:31]
	v_mov_b32_e32 v96, v135
	global_load_lds_dwordx4 v[130:131], off
	s_mov_b32 m0, s66
	v_lshl_add_u64 v[130:131], s[4:5], 0, v[96:97]
	v_lshl_add_u64 v[130:131], v[130:131], 0, s[30:31]
	global_load_lds_dwordx4 v[130:131], off
	s_waitcnt vmcnt(8)
	s_waitcnt lgkmcnt(0)
	s_barrier
	s_waitcnt lgkmcnt(0)
	v_mfma_f32_16x16x32_bf16 v[60:63], v[150:153], v[182:185], v[60:63]
	v_mfma_f32_16x16x32_bf16 v[56:59], v[158:161], v[182:185], v[56:59]
	v_mfma_f32_16x16x32_bf16 v[44:47], v[150:153], v[190:193], v[44:47]
	v_mfma_f32_16x16x32_bf16 v[32:35], v[158:161], v[190:193], v[32:35]
	v_mfma_f32_16x16x32_bf16 v[16:19], v[150:153], v[198:201], v[16:19]
	v_mfma_f32_16x16x32_bf16 v[8:11], v[158:161], v[198:201], v[8:11]
	v_mfma_f32_16x16x32_bf16 v[4:7], v[150:153], v[206:209], v[4:7]
	v_mfma_f32_16x16x32_bf16 v[0:3], v[158:161], v[206:209], v[0:3]
	v_mfma_f32_16x16x32_bf16 v[60:63], v[154:157], v[186:189], v[60:63]
	v_mfma_f32_16x16x32_bf16 v[56:59], v[162:165], v[186:189], v[56:59]
	v_mfma_f32_16x16x32_bf16 v[44:47], v[154:157], v[194:197], v[44:47]
	v_mfma_f32_16x16x32_bf16 v[32:35], v[162:165], v[194:197], v[32:35]
	v_mfma_f32_16x16x32_bf16 v[16:19], v[154:157], v[202:205], v[16:19]
	v_mfma_f32_16x16x32_bf16 v[8:11], v[162:165], v[202:205], v[8:11]
	v_mfma_f32_16x16x32_bf16 v[4:7], v[154:157], v[210:213], v[4:7]
	v_mfma_f32_16x16x32_bf16 v[0:3], v[162:165], v[210:213], v[0:3]
	v_mfma_f32_16x16x32_bf16 v[52:55], v[166:169], v[182:185], v[52:55]
	v_mfma_f32_16x16x32_bf16 v[48:51], v[174:177], v[182:185], v[48:51]
	v_mfma_f32_16x16x32_bf16 v[28:31], v[166:169], v[190:193], v[28:31]
	v_mfma_f32_16x16x32_bf16 v[12:15], v[174:177], v[190:193], v[12:15]
	v_mfma_f32_16x16x32_bf16 v[36:39], v[166:169], v[198:201], v[36:39]
	v_mfma_f32_16x16x32_bf16 v[40:43], v[174:177], v[198:201], v[40:43]
	v_mfma_f32_16x16x32_bf16 v[20:23], v[166:169], v[206:209], v[20:23]
	v_mfma_f32_16x16x32_bf16 v[24:27], v[174:177], v[206:209], v[24:27]
	v_mfma_f32_16x16x32_bf16 v[52:55], v[170:173], v[186:189], v[52:55]
	v_mfma_f32_16x16x32_bf16 v[48:51], v[178:181], v[186:189], v[48:51]
	v_mfma_f32_16x16x32_bf16 v[28:31], v[170:173], v[194:197], v[28:31]
	v_mfma_f32_16x16x32_bf16 v[12:15], v[178:181], v[194:197], v[12:15]
	v_mfma_f32_16x16x32_bf16 v[36:39], v[170:173], v[202:205], v[36:39]
	v_mfma_f32_16x16x32_bf16 v[40:43], v[178:181], v[202:205], v[40:43]
	v_mfma_f32_16x16x32_bf16 v[20:23], v[170:173], v[210:213], v[20:23]
	v_mfma_f32_16x16x32_bf16 v[24:27], v[178:181], v[210:213], v[24:27]
	s_barrier
	s_movk_i32 s22, 0x100
	s_andn2_b64 vcc, exec, s[2:3]
	s_mov_b64 s[20:21], -1
	s_mov_b64 s[2:3], 0
	s_cbranch_vccz .LBB0_937
	s_and_b64 vcc, exec, s[40:41]
	s_cbranch_vccz .LBB0_940
	s_barrier

; #define PG8_STAGE(bufoff, gbase, voff) do { _Pragma("unroll") for (int _i = 0; _i < 2; ++_i) \
;         __builtin_amdgcn_global_load_lds((const __attribute__((address_space(1))) unsigned*)((const __attribute__((address_space(1))) char*)(gbase) + (unsigned)lnd_v((int)(voff)[_i])), (LAS unsigned*)(lds + (bufoff) + ldsw + _i * 8192), 16, 0, 0); } while (0)
; #define PG8_WAIT_V(n) asm volatile("s_waitcnt vmcnt(" #n ")" ::: "memory")
; #define PG8_BAR __builtin_amdgcn_s_barrier()
; template <class Desc, class Epi>
; __device__ __forceinline__ void gemm_phase(const int wv_, LAS unsigned char* lds, const Desc& d, const Epi& E) {
;     ...
; #pragma unroll
;     for (int i = 0; i < 2; ++i) { int R, C; stage_rc(tid * 16 + i * 8192, R, C); const int Rb = (R & ~31) + perm32(R & 31); Rr[i] = R; Cc[i] = C;
;         voffA[i] = (unsigned)(R * d.lda + C) * 2u; voffA1[i] = voffA[i] + (unsigned)hstepA; voffB[i] = (unsigned)(Rb * d.ldb + C) * 2u; }
;     ...
;     PG8_STAGE(PG8_SB(0, 0), cB, voffB); PG8_STAGE(PG8_SB(0, 1), cB + hstepB, voffB); PG8_STAGE(PG8_SA(0, 0), cA, voffA); PG8_STAGE(PG8_SA(0, 1), cA, voffA1);
;     if (wr == 1) PG8_BAR;
;     PG8_WAIT_V(2); PG8_BAR;
;     PG8_STAGE(PG8_SB(1, 0), cB + kstep, voffB); PG8_STAGE(PG8_SA(1, 0), cA + kstep, voffA); PG8_STAGE(PG8_SB(1, 1), cB + hstepB + kstep, voffB);
;     PG8_WAIT_V(6); PG8_BAR;
.LBB0_1065:
	s_andn2_b64 vcc, exec, s[0:1]
	s_cbranch_vccnz .LBB0_1148
	v_readlane_b32 s0, v254, 1
	v_readlane_b32 s1, v254, 2
	s_load_dwordx2 s[20:21], s[0:1], 0xc0
	v_readlane_b32 s0, v254, 5
	s_mov_b32 s1, s27
	v_readlane_b32 s23, v254, 0
	s_waitcnt lgkmcnt(0)
	s_load_dword s22, s[18:19], 0x0
	v_mbcnt_lo_u32_b32 v0, -1, s1
	v_mbcnt_hi_u32_b32 v0, -1, v0
	v_lshl_add_u32 v1, s0, 6, v0
	s_cmpk_gt_u32 s23, 0x1ff
	v_readfirstlane_b32 s1, v1
	s_waitcnt lgkmcnt(0)
	s_mov_b32 s24, s22
	s_cbranch_scc1 .LBB0_1098
	v_ashrrev_i32_e32 v3, 31, v1
	v_lshrrev_b32_e32 v3, 26, v3
	v_lshlrev_b32_e32 v2, 4, v1
	v_add_u32_e32 v3, v1, v3
	v_bfe_i32 v1, v1, 27, 1
	v_lshrrev_b32_e32 v1, 22, v1
	v_add_u32_e32 v1, v2, v1
	v_and_b32_e32 v1, 0xfffffc00, v1
	v_sub_u32_e32 v1, v2, v1
	v_lshrrev_b32_e32 v4, 4, v1
	v_bitop3_b32 v1, v4, v1, 32 bitop3:0x6c
	v_ashrrev_i32_e32 v5, 31, v1
	s_add_u32 s25, s20, 0x51400000
	v_readlane_b32 s2, v254, 57
	v_ashrrev_i32_e32 v3, 6, v3
	v_lshrrev_b32_e32 v5, 26, v5
	s_addc_u32 s56, s21, 0
	s_lshl_b32 s0, s2, 21
	v_lshlrev_b32_e32 v4, 3, v3
	v_add_u32_e32 v5, v1, v5
	s_add_u32 s0, s20, s0
	v_and_b32_e32 v4, -16, v4
	v_ashrrev_i32_e32 v6, 6, v5
	v_and_b32_e32 v5, 0xc0, v5
	s_addc_u32 s2, s21, 0
	v_add_u32_e32 v4, v6, v4
	v_sub_u32_e32 v1, v1, v5
	s_add_u32 s57, s0, 0xe00000
	v_lshlrev_b32_e32 v3, 5, v3
	v_ashrrev_i16_sdwa v1, v216, sext(v1) dst_sel:DWORD dst_unused:UNUSED_PAD src0_sel:DWORD src1_sel:BYTE_0
	v_lshlrev_b32_e32 v5, 1, v4
	v_lshrrev_b32_e32 v7, 2, v4
	v_and_b32_e32 v6, 3, v6
	s_mov_b32 s0, 0x1fffe0
	v_and_b32_e32 v3, 32, v3
	v_bfe_i32 v1, v1, 0, 16
	v_and_b32_e32 v5, 24, v5
	v_and_b32_e32 v7, 4, v7
	v_and_or_b32 v6, v4, s0, v6
	v_or3_b32 v5, v6, v7, v5
	v_add_lshl_u32 v1, v3, v1, 1
	v_lshl_add_u32 v219, v4, 11, v1
	v_lshl_add_u32 v221, v5, 11, v1
	v_add_u32_e32 v1, 0x2000, v2
	v_ashrrev_i32_e32 v2, 31, v1
	v_lshrrev_b32_e32 v2, 22, v2
	v_add_u32_e32 v2, v1, v2
	v_ashrrev_i32_e32 v2, 10, v2
	v_mul_i32_i24_e32 v3, 0x400, v2
	v_sub_u32_e32 v1, v1, v3
	v_lshrrev_b32_e32 v3, 4, v1
	v_bitop3_b32 v1, v3, v1, 32 bitop3:0x6c
	v_ashrrev_i32_e32 v4, 31, v1
	v_lshrrev_b32_e32 v4, 26, v4
	v_lshlrev_b32_e32 v3, 3, v2
	v_add_u32_e32 v4, v1, v4
	v_and_b32_e32 v3, -16, v3
	v_ashrrev_i32_e32 v5, 6, v4
	v_readlane_b32 s3, v254, 58
	s_addc_u32 s58, s2, 0
	v_add_u32_e32 v3, v5, v3
	v_and_b32_e32 v4, 0xc0, v4
	v_and_b32_e32 v5, 3, v5
	s_lshl_b32 s2, s23, 5
	v_sub_u32_e32 v1, v1, v4
	v_and_or_b32 v5, v3, s0, v5
	s_and_b32 s0, s23, 0x100
	s_and_b32 s2, s2, 0xe0
	s_lshr_b32 s3, s23, 3
	s_ashr_i32 s26, s1, 6
	v_lshlrev_b32_e32 v2, 5, v2
	v_ashrrev_i16_sdwa v1, v216, sext(v1) dst_sel:DWORD dst_unused:UNUSED_PAD src0_sel:DWORD src1_sel:BYTE_0
	v_lshlrev_b32_e32 v4, 1, v3
	v_lshrrev_b32_e32 v6, 2, v3
	s_and_b32 s3, s3, 28
	s_or_b32 s0, s2, s0
	s_bfe_u32 s61, s23, 0x20003
	v_and_b32_e32 v2, 32, v2
	v_bfe_i32 v1, v1, 0, 16
	v_and_b32_e32 v4, 24, v4
	v_and_b32_e32 v6, 4, v6
	s_ashr_i32 s29, s1, 8
	s_lshl_b32 s59, s26, 10
	s_or_b32 s0, s0, s3
	s_lshl_b32 s2, s61, 19
	v_or3_b32 v4, v5, v6, v4
	v_add_lshl_u32 v1, v2, v1, 1
	s_add_u32 s4, s57, s2
	v_lshl_add_u32 v222, v3, 11, v1
	v_lshl_add_u32 v224, v4, 11, v1
	s_addc_u32 s5, s58, 0
	s_add_i32 s60, s59, 0
	s_add_i32 m0, s60, 0x10000
	v_add_u32_e32 v220, 0x40000, v219
	global_load_lds_dwordx4 v221, s[4:5]
	s_add_i32 m0, s60, 0x12000
	s_add_u32 s2, s4, 0x40000
	global_load_lds_dwordx4 v224, s[4:5]
	s_addc_u32 s3, s5, 0
	s_add_i32 m0, s60, 0x14000
	v_add_u32_e32 v223, 0x40000, v222
	global_load_lds_dwordx4 v221, s[2:3]
	s_add_i32 m0, s60, 0x16000
	s_nop 0
	global_load_lds_dwordx4 v224, s[2:3]
	s_lshl_b32 s2, s0, 17
	s_add_u32 s2, s25, s2
	s_addc_u32 s3, s56, 0
	s_mov_b32 m0, s60
	s_add_i32 s62, s60, 0x2000
	global_load_lds_dwordx4 v219, s[2:3]
	s_mov_b32 m0, s62
	s_add_i32 s63, s60, 0x4000
	global_load_lds_dwordx4 v222, s[2:3]
	s_mov_b32 m0, s63
	s_add_i32 s64, s60, 0x6000
	global_load_lds_dwordx4 v220, s[2:3]
	v_mov_b32_e32 v1, v223
	s_mov_b32 m0, s64
	s_cmp_eq_u32 s29, 1
	global_load_lds_dwordx4 v1, s[2:3]
	s_cselect_b64 s[38:39], -1, 0
	s_cmp_lg_u32 s29, 1
	s_cbranch_scc1 .LBB0_1069
	s_barrier
.LBB0_1069:
	s_lshr_b32 s0, s0, 2
	s_add_u32 s40, s20, 0x33600000
	s_addc_u32 s41, s21, 0
	v_bfe_u32 v2, v0, 4, 2
	s_add_u32 s42, s20, 0x37800000
	v_and_b32_e32 v1, 15, v0
	v_lshlrev_b32_e32 v4, 4, v2
	v_lshlrev_b32_e32 v0, 2, v0
	s_addc_u32 s43, s21, 0
	s_and_b32 s65, s26, 3
	v_lshl_or_b32 v225, s29, 6, v1
	v_lshl_or_b32 v1, v1, 6, v4
	s_lshl_b32 s20, s29, 13
	v_and_b32_e32 v0, 32, v0
	v_bitop3_b32 v4, v1, s20, v0 bitop3:0xde
	s_lshl_b32 s20, s65, 12
	v_mov_b32_e32 v96, v221
	v_bitop3_b32 v226, v1, s20, v0 bitop3:0xde
	s_waitcnt vmcnt(2)
	s_barrier
	s_add_i32 m0, s60, 0x18000
	v_lshl_add_u64 v[0:1], s[4:5], 0, v[96:97]
	v_lshl_add_u64 v[0:1], v[0:1], 0, s[30:31]
	v_mov_b32_e32 v96, v224
	global_load_lds_dwordx4 v[0:1], off
	s_add_i32 m0, s60, 0x1a000
	v_lshl_add_u64 v[0:1], s[4:5], 0, v[96:97]
	v_lshl_add_u64 v[0:1], v[0:1], 0, s[30:31]
	v_mov_b32_e32 v96, v219
	global_load_lds_dwordx4 v[0:1], off
	s_add_i32 s66, s60, 0x8000
	v_lshl_add_u64 v[0:1], s[2:3], 0, v[96:97]
	v_lshl_add_u64 v[0:1], v[0:1], 0, s[30:31]
	s_mov_b32 m0, s66
	v_mov_b32_e32 v96, v222
	global_load_lds_dwordx4 v[0:1], off
	s_add_i32 s67, s60, 0xa000
	v_lshl_add_u64 v[0:1], s[2:3], 0, v[96:97]
	v_lshl_add_u64 v[0:1], v[0:1], 0, s[30:31]
	s_mov_b32 m0, s67
	s_add_u32 s20, s4, 0x40080
	global_load_lds_dwordx4 v[0:1], off
	s_addc_u32 s21, s5, 0
	s_add_i32 m0, s60, 0x1c000
	v_lshlrev_b32_e32 v3, 3, v2
	global_load_lds_dwordx4 v221, s[20:21]
	v_mov_b32_e32 v0, v224
	s_add_i32 m0, s60, 0x1e000
	s_cmpk_lt_u32 s1, 0x100
	global_load_lds_dwordx4 v0, s[20:21]
	s_waitcnt vmcnt(6)
	s_cselect_b64 s[44:45], -1, 0
	v_lshl_or_b32 v227, s65, 5, v3
	s_mov_b32 s68, 0
	v_cmp_eq_u32_e64 s[36:37], 0, v2
	v_or_b32_e32 v228, 16, v225
	v_or_b32_e32 v229, 32, v225
	v_or_b32_e32 v230, 48, v225
	v_add_u32_e32 v231, 0, v4
	s_mov_b64 s[52:53], s[4:5]
	s_mov_b64 s[50:51], s[2:3]
	s_barrier
	s_waitcnt vmcnt(0)
	s_branch .LBB0_1072

; #define PG8_STAGE(bufoff, gbase, voff) do { _Pragma("unroll") for (int _i = 0; _i < 2; ++_i) \
;         __builtin_amdgcn_global_load_lds((const __attribute__((address_space(1))) unsigned*)((const __attribute__((address_space(1))) char*)(gbase) + (unsigned)lnd_v((int)(voff)[_i])), (LAS unsigned*)(lds + (bufoff) + ldsw + _i * 8192), 16, 0, 0); } while (0)
; #define PG8_LDA(dst, b, h) do { _Pragma("unroll") for (int m = 0; m < 4; ++m) _Pragma("unroll") for (int k = 0; k < 2; ++k) dst[m][k] = *(const LAS bf16x8*)(lds + PG8_SA(b, h) + aoff + m * 2048 + k * 1024); } while (0)
; #define PG8_LDB(dst, b, h) do { _Pragma("unroll") for (int n = 0; n < 2; ++n) _Pragma("unroll") for (int k = 0; k < 2; ++k) dst[n][k] = *(const LAS bf16x8*)(lds + PG8_SB(b, h) + boff + n * 2048 + k * 1024); } while (0)
; #define PG8_WAIT_V(n) asm volatile("s_waitcnt vmcnt(" #n ")" ::: "memory")
; #define PG8_WAIT_L(n) asm volatile("s_waitcnt lgkmcnt(" #n ")" ::: "memory")
; #define PG8_BAR __builtin_amdgcn_s_barrier()
; template <class Desc, class Epi>
; __device__ __forceinline__ void gemm_phase(const int wv_, LAS unsigned char* lds, const Desc& d, const Epi& E) {
;     ...
;         for (int t = 0; t < nt; t += 2) {
;             const bool last = (t == nt - 2);
;             unsigned sA0[2], sA1[2];
;             if constexpr (Desc::GATHER) { sA0[0] = last ? voffAn[0] : voffA[0]; sA0[1] = last ? voffAn[1] : voffA[1]; sA1[0] = last ? voffAn1[0] : voffA1[0]; sA1[1] = last ? voffAn1[1] : voffA1[1]; }
;             else { sA0[0] = voffA[0]; sA0[1] = voffA[1]; sA1[0] = voffA1[0]; sA1[1] = voffA1[1]; }
;             const char* a1 = cA + (size_t)(t + 1) * kstep;
;             const char* a2 = last ? nA : cA + (size_t)(t + 2) * kstep; const char* b2 = last ? nB : cB + (size_t)(t + 2) * kstep;
;             const char* a3 = a2 + kstep; const char* b3 = b2 + kstep;
;             PG8_LDB(B0, 0, 0); PG8_LDB(B1, 0, 1); PG8_SCHED; PG8_LDA(At, 0, 0); PG8_STAGE(PG8_SA(1, 1), a1, voffA1);
;             PG8_WAIT_V(8); PG8_WAIT_L(0); PG8_BAR; PG8_MMA(0, 0, At, B0); PG8_MMA(0, 1, At, B1); PG8_BAR; PG8_SCHED;
;             PG8_LDA(At, 0, 1); PG8_STAGE(PG8_SB(0, 0), b2, voffB); PG8_STAGE(PG8_SB(0, 1), b2 + hstepB, voffB); PG8_STAGE(PG8_SA(0, 0), a2, sA0);
;             PG8_WAIT_V(8); PG8_WAIT_L(0); PG8_BAR; PG8_MMA(1, 0, At, B0); PG8_MMA(1, 1, At, B1); PG8_BAR; PG8_SCHED;
.LBB0_1075:
	s_add_u32 s4, s2, 0x80
	s_addc_u32 s5, s3, 0
	s_add_i32 s47, 0, 0x10000
	s_cmp_eq_u32 s29, 12
	s_cselect_b32 s5, s51, s5
	s_cselect_b32 s4, s50, s4
	v_add_u32_e32 v96, s47, v226
	s_cselect_b32 s21, s53, s26
	s_cselect_b32 s20, s52, s1
	s_add_i32 s49, 0, 0x14000
	ds_read_b128 v[118:121], v96
	ds_read_b128 v[126:129], v96 offset:1024
	ds_read_b128 v[130:133], v96 offset:2048
	ds_read_b128 v[134:137], v96 offset:3072
	v_add_u32_e32 v96, s49, v226
	ds_read_b128 v[142:145], v96
	ds_read_b128 v[150:153], v96 offset:1024
	ds_read_b128 v[154:157], v96 offset:2048
	ds_read_b128 v[158:161], v96 offset:3072
	ds_read_b128 v[162:165], v231
	ds_read_b128 v[166:169], v231 offset:1024
	ds_read_b128 v[170:173], v231 offset:2048
	ds_read_b128 v[174:177], v231 offset:3072
	ds_read_b128 v[178:181], v231 offset:4096
	ds_read_b128 v[182:185], v231 offset:5120
	ds_read_b128 v[186:189], v231 offset:6144
	ds_read_b128 v[190:193], v231 offset:7168
	s_add_i32 m0, s60, 0xc000
	s_nop 0
	global_load_lds_dwordx4 v220, s[2:3]
	s_add_i32 m0, s60, 0xe000
	s_nop 0
	global_load_lds_dwordx4 v223, s[2:3]
	s_waitcnt vmcnt(8)
	s_waitcnt lgkmcnt(0)
	s_barrier
	s_waitcnt lgkmcnt(0)
	v_mfma_f32_16x16x32_bf16 v[146:149], v[118:121], v[162:165], v[146:149]
	v_mfma_f32_16x16x32_bf16 v[138:141], v[130:133], v[162:165], v[138:141]
	v_mfma_f32_16x16x32_bf16 v[110:113], v[118:121], v[170:173], v[110:113]
	v_mfma_f32_16x16x32_bf16 v[106:109], v[130:133], v[170:173], v[106:109]
	v_mfma_f32_16x16x32_bf16 v[92:95], v[118:121], v[178:181], v[92:95]
	v_mfma_f32_16x16x32_bf16 v[88:91], v[130:133], v[178:181], v[88:91]
	v_mfma_f32_16x16x32_bf16 v[76:79], v[118:121], v[186:189], v[76:79]
	v_mfma_f32_16x16x32_bf16 v[72:75], v[130:133], v[186:189], v[72:75]
	v_mfma_f32_16x16x32_bf16 v[146:149], v[126:129], v[166:169], v[146:149]
	v_mfma_f32_16x16x32_bf16 v[138:141], v[134:137], v[166:169], v[138:141]
	v_mfma_f32_16x16x32_bf16 v[110:113], v[126:129], v[174:177], v[110:113]
	v_mfma_f32_16x16x32_bf16 v[106:109], v[134:137], v[174:177], v[106:109]
	v_mfma_f32_16x16x32_bf16 v[92:95], v[126:129], v[182:185], v[92:95]
	v_mfma_f32_16x16x32_bf16 v[88:91], v[134:137], v[182:185], v[88:91]
	v_mfma_f32_16x16x32_bf16 v[76:79], v[126:129], v[190:193], v[76:79]
	v_mfma_f32_16x16x32_bf16 v[72:75], v[134:137], v[190:193], v[72:75]
	v_mfma_f32_16x16x32_bf16 v[122:125], v[142:145], v[162:165], v[122:125]
	v_mfma_f32_16x16x32_bf16 v[114:117], v[154:157], v[162:165], v[114:117]
	v_mfma_f32_16x16x32_bf16 v[102:105], v[142:145], v[170:173], v[102:105]
	v_mfma_f32_16x16x32_bf16 v[98:101], v[154:157], v[170:173], v[98:101]
	v_mfma_f32_16x16x32_bf16 v[84:87], v[142:145], v[178:181], v[84:87]
	v_mfma_f32_16x16x32_bf16 v[80:83], v[154:157], v[178:181], v[80:83]
	v_mfma_f32_16x16x32_bf16 v[68:71], v[142:145], v[186:189], v[68:71]
	v_mfma_f32_16x16x32_bf16 v[64:67], v[154:157], v[186:189], v[64:67]
	v_mfma_f32_16x16x32_bf16 v[122:125], v[150:153], v[166:169], v[122:125]
	v_mfma_f32_16x16x32_bf16 v[114:117], v[158:161], v[166:169], v[114:117]
	v_mfma_f32_16x16x32_bf16 v[102:105], v[150:153], v[174:177], v[102:105]
	v_mfma_f32_16x16x32_bf16 v[98:101], v[158:161], v[174:177], v[98:101]
	v_mfma_f32_16x16x32_bf16 v[84:87], v[150:153], v[182:185], v[84:87]
	v_mfma_f32_16x16x32_bf16 v[80:83], v[158:161], v[182:185], v[80:83]
	v_mfma_f32_16x16x32_bf16 v[68:71], v[150:153], v[190:193], v[68:71]
	v_mfma_f32_16x16x32_bf16 v[64:67], v[158:161], v[190:193], v[64:67]
	s_barrier
	s_add_i32 s47, s47, s59
	ds_read_b128 v[162:165], v231 offset:16384
	ds_read_b128 v[166:169], v231 offset:17408
	ds_read_b128 v[170:173], v231 offset:18432
	ds_read_b128 v[174:177], v231 offset:19456
	ds_read_b128 v[178:181], v231 offset:20480
	ds_read_b128 v[182:185], v231 offset:21504
	ds_read_b128 v[186:189], v231 offset:22528
	ds_read_b128 v[190:193], v231 offset:23552
	s_mov_b32 m0, s47
	s_nop 0
	global_load_lds_dwordx4 v221, s[20:21]
	s_add_i32 m0, s47, 0x2000
	s_add_u32 s70, s20, 0x40000
	global_load_lds_dwordx4 v224, s[20:21]
	s_addc_u32 s71, s21, 0
	s_add_i32 s47, s49, s59
	s_mov_b32 m0, s47
	s_nop 0
	global_load_lds_dwordx4 v221, s[70:71]
	s_add_i32 m0, s47, 0x2000
	s_nop 0
	global_load_lds_dwordx4 v224, s[70:71]
	s_mov_b32 m0, s60
	s_nop 0
	global_load_lds_dwordx4 v219, s[4:5]
	s_mov_b32 m0, s62
	s_nop 0
	global_load_lds_dwordx4 v222, s[4:5]
	s_waitcnt vmcnt(8)
	s_waitcnt lgkmcnt(0)
	s_barrier
	s_waitcnt lgkmcnt(0)
	v_mfma_f32_16x16x32_bf16 v[60:63], v[118:121], v[162:165], v[60:63]
	v_mfma_f32_16x16x32_bf16 v[56:59], v[130:133], v[162:165], v[56:59]
	v_mfma_f32_16x16x32_bf16 v[44:47], v[118:121], v[170:173], v[44:47]
	v_mfma_f32_16x16x32_bf16 v[40:43], v[130:133], v[170:173], v[40:43]
	v_mfma_f32_16x16x32_bf16 v[20:23], v[118:121], v[178:181], v[20:23]
	v_mfma_f32_16x16x32_bf16 v[16:19], v[130:133], v[178:181], v[16:19]
	v_mfma_f32_16x16x32_bf16 v[4:7], v[118:121], v[186:189], v[4:7]
	v_mfma_f32_16x16x32_bf16 v[0:3], v[130:133], v[186:189], v[0:3]
	v_mfma_f32_16x16x32_bf16 v[60:63], v[126:129], v[166:169], v[60:63]
	v_mfma_f32_16x16x32_bf16 v[56:59], v[134:137], v[166:169], v[56:59]
	v_mfma_f32_16x16x32_bf16 v[44:47], v[126:129], v[174:177], v[44:47]
	v_mfma_f32_16x16x32_bf16 v[40:43], v[134:137], v[174:177], v[40:43]
	v_mfma_f32_16x16x32_bf16 v[20:23], v[126:129], v[182:185], v[20:23]
	v_mfma_f32_16x16x32_bf16 v[16:19], v[134:137], v[182:185], v[16:19]
	v_mfma_f32_16x16x32_bf16 v[4:7], v[126:129], v[190:193], v[4:7]
	v_mfma_f32_16x16x32_bf16 v[0:3], v[134:137], v[190:193], v[0:3]
	v_mfma_f32_16x16x32_bf16 v[52:55], v[142:145], v[162:165], v[52:55]
	v_mfma_f32_16x16x32_bf16 v[48:51], v[154:157], v[162:165], v[48:51]
	v_mfma_f32_16x16x32_bf16 v[36:39], v[142:145], v[170:173], v[36:39]
	v_mfma_f32_16x16x32_bf16 v[32:35], v[154:157], v[170:173], v[32:35]
	v_mfma_f32_16x16x32_bf16 v[28:31], v[142:145], v[178:181], v[28:31]
	v_mfma_f32_16x16x32_bf16 v[24:27], v[154:157], v[178:181], v[24:27]
	v_mfma_f32_16x16x32_bf16 v[12:15], v[142:145], v[186:189], v[12:15]
	v_mfma_f32_16x16x32_bf16 v[8:11], v[154:157], v[186:189], v[8:11]
	v_mfma_f32_16x16x32_bf16 v[52:55], v[150:153], v[166:169], v[52:55]
	v_mfma_f32_16x16x32_bf16 v[48:51], v[158:161], v[166:169], v[48:51]
	v_mfma_f32_16x16x32_bf16 v[36:39], v[150:153], v[174:177], v[36:39]
	v_mfma_f32_16x16x32_bf16 v[32:35], v[158:161], v[174:177], v[32:35]
	v_mfma_f32_16x16x32_bf16 v[28:31], v[150:153], v[182:185], v[28:31]
	v_mfma_f32_16x16x32_bf16 v[24:27], v[158:161], v[182:185], v[24:27]
	v_mfma_f32_16x16x32_bf16 v[12:15], v[150:153], v[190:193], v[12:15]
	v_mfma_f32_16x16x32_bf16 v[8:11], v[158:161], v[190:193], v[8:11]
	s_barrier
; #define PG8_STAGE(bufoff, gbase, voff) do { _Pragma("unroll") for (int _i = 0; _i < 2; ++_i) \
;         __builtin_amdgcn_global_load_lds((const __attribute__((address_space(1))) unsigned*)((const __attribute__((address_space(1))) char*)(gbase) + (unsigned)lnd_v((int)(voff)[_i])), (LAS unsigned*)(lds + (bufoff) + ldsw + _i * 8192), 16, 0, 0); } while (0)
; #define PG8_LDA(dst, b, h) do { _Pragma("unroll") for (int m = 0; m < 4; ++m) _Pragma("unroll") for (int k = 0; k < 2; ++k) dst[m][k] = *(const LAS bf16x8*)(lds + PG8_SA(b, h) + aoff + m * 2048 + k * 1024); } while (0)
; #define PG8_LDB(dst, b, h) do { _Pragma("unroll") for (int n = 0; n < 2; ++n) _Pragma("unroll") for (int k = 0; k < 2; ++k) dst[n][k] = *(const LAS bf16x8*)(lds + PG8_SB(b, h) + boff + n * 2048 + k * 1024); } while (0)
; #define PG8_MMA(ai, bj, At, Bt) do { __builtin_amdgcn_s_setprio(1); _Pragma("unroll") for (int m = 0; m < 4; ++m) _Pragma("unroll") for (int n = 0; n < 2; ++n) _Pragma("unroll") for (int k = 0; k < 2; ++k) \
;         acc[ai][bj][m][n] = __builtin_amdgcn_mfma_f32_16x16x32_bf16(Bt[n][k], At[m][k], acc[ai][bj][m][n], 0, 0, 0); __builtin_amdgcn_s_setprio(0); } while (0)
; #define PG8_WAIT_V(n) asm volatile("s_waitcnt vmcnt(" #n ")" ::: "memory")
; #define PG8_WAIT_L(n) asm volatile("s_waitcnt lgkmcnt(" #n ")" ::: "memory")
; #define PG8_BAR __builtin_amdgcn_s_barrier()
; #define PG8_SCHED __builtin_amdgcn_sched_barrier(0)
; template <class Desc, class Epi>
; __device__ __forceinline__ void gemm_phase(const int wv_, LAS unsigned char* lds, const Desc& d, const Epi& E) {
;     ...
;             PG8_LDB(B0, 1, 0); PG8_LDB(B1, 1, 1); PG8_SCHED; PG8_LDA(At, 1, 0); PG8_STAGE(PG8_SA(0, 1), a2, sA1);
;             PG8_WAIT_V(8); PG8_WAIT_L(0); PG8_BAR; PG8_MMA(0, 0, At, B0); PG8_MMA(0, 1, At, B1); PG8_BAR; PG8_SCHED;
	s_add_i32 s47, 0, 0x18000
	v_add_u32_e32 v96, s47, v226
	s_add_i32 s49, 0, 0x1c000
	ds_read_b128 v[118:121], v96
	ds_read_b128 v[126:129], v96 offset:1024
	ds_read_b128 v[130:133], v96 offset:2048
	ds_read_b128 v[134:137], v96 offset:3072
	v_add_u32_e32 v96, s49, v226
	ds_read_b128 v[142:145], v96
	ds_read_b128 v[150:153], v96 offset:1024
	ds_read_b128 v[154:157], v96 offset:2048
	ds_read_b128 v[158:161], v96 offset:3072
	s_mov_b32 m0, s63
	ds_read_b128 v[162:165], v231 offset:32768
	ds_read_b128 v[166:169], v231 offset:33792
	ds_read_b128 v[170:173], v231 offset:34816
	ds_read_b128 v[174:177], v231 offset:35840
	ds_read_b128 v[178:181], v231 offset:36864
	ds_read_b128 v[182:185], v231 offset:37888
	ds_read_b128 v[186:189], v231 offset:38912
	ds_read_b128 v[190:193], v231 offset:39936
	s_nop 0
	global_load_lds_dwordx4 v220, s[4:5]
	s_mov_b32 m0, s64
	s_nop 0
	global_load_lds_dwordx4 v223, s[4:5]
	s_waitcnt vmcnt(8)
	s_waitcnt lgkmcnt(0)
	s_barrier
	s_waitcnt lgkmcnt(0)
	v_mfma_f32_16x16x32_bf16 v[146:149], v[118:121], v[162:165], v[146:149]
	v_mfma_f32_16x16x32_bf16 v[138:141], v[130:133], v[162:165], v[138:141]
	v_mfma_f32_16x16x32_bf16 v[110:113], v[118:121], v[170:173], v[110:113]
	v_mfma_f32_16x16x32_bf16 v[106:109], v[130:133], v[170:173], v[106:109]
	v_mfma_f32_16x16x32_bf16 v[92:95], v[118:121], v[178:181], v[92:95]
	v_mfma_f32_16x16x32_bf16 v[88:91], v[130:133], v[178:181], v[88:91]
	v_mfma_f32_16x16x32_bf16 v[76:79], v[118:121], v[186:189], v[76:79]
	v_mfma_f32_16x16x32_bf16 v[72:75], v[130:133], v[186:189], v[72:75]
	v_mfma_f32_16x16x32_bf16 v[146:149], v[126:129], v[166:169], v[146:149]
	v_mfma_f32_16x16x32_bf16 v[138:141], v[134:137], v[166:169], v[138:141]
	v_mfma_f32_16x16x32_bf16 v[110:113], v[126:129], v[174:177], v[110:113]
	v_mfma_f32_16x16x32_bf16 v[106:109], v[134:137], v[174:177], v[106:109]
	v_mfma_f32_16x16x32_bf16 v[92:95], v[126:129], v[182:185], v[92:95]
	v_mfma_f32_16x16x32_bf16 v[88:91], v[134:137], v[182:185], v[88:91]
	v_mfma_f32_16x16x32_bf16 v[76:79], v[126:129], v[190:193], v[76:79]
	v_mfma_f32_16x16x32_bf16 v[72:75], v[134:137], v[190:193], v[72:75]
	v_mfma_f32_16x16x32_bf16 v[122:125], v[142:145], v[162:165], v[122:125]
	v_mfma_f32_16x16x32_bf16 v[114:117], v[154:157], v[162:165], v[114:117]
	v_mfma_f32_16x16x32_bf16 v[102:105], v[142:145], v[170:173], v[102:105]
	v_mfma_f32_16x16x32_bf16 v[98:101], v[154:157], v[170:173], v[98:101]
	v_mfma_f32_16x16x32_bf16 v[84:87], v[142:145], v[178:181], v[84:87]
	v_mfma_f32_16x16x32_bf16 v[80:83], v[154:157], v[178:181], v[80:83]
	v_mfma_f32_16x16x32_bf16 v[68:71], v[142:145], v[186:189], v[68:71]
	v_mfma_f32_16x16x32_bf16 v[64:67], v[154:157], v[186:189], v[64:67]
	v_mfma_f32_16x16x32_bf16 v[122:125], v[150:153], v[166:169], v[122:125]
	v_mfma_f32_16x16x32_bf16 v[114:117], v[158:161], v[166:169], v[114:117]
	v_mfma_f32_16x16x32_bf16 v[102:105], v[150:153], v[174:177], v[102:105]
	v_mfma_f32_16x16x32_bf16 v[98:101], v[158:161], v[174:177], v[98:101]
	v_mfma_f32_16x16x32_bf16 v[84:87], v[150:153], v[182:185], v[84:87]
	v_mfma_f32_16x16x32_bf16 v[80:83], v[158:161], v[182:185], v[80:83]
	v_mfma_f32_16x16x32_bf16 v[68:71], v[150:153], v[190:193], v[68:71]
	v_mfma_f32_16x16x32_bf16 v[64:67], v[158:161], v[190:193], v[64:67]
	s_barrier
; #define PG8_STAGE(bufoff, gbase, voff) do { _Pragma("unroll") for (int _i = 0; _i < 2; ++_i) \
;         __builtin_amdgcn_global_load_lds((const __attribute__((address_space(1))) unsigned*)((const __attribute__((address_space(1))) char*)(gbase) + (unsigned)lnd_v((int)(voff)[_i])), (LAS unsigned*)(lds + (bufoff) + ldsw + _i * 8192), 16, 0, 0); } while (0)
; #define PG8_LDA(dst, b, h) do { _Pragma("unroll") for (int m = 0; m < 4; ++m) _Pragma("unroll") for (int k = 0; k < 2; ++k) dst[m][k] = *(const LAS bf16x8*)(lds + PG8_SA(b, h) + aoff + m * 2048 + k * 1024); } while (0)
; #define PG8_MMA(ai, bj, At, Bt) do { __builtin_amdgcn_s_setprio(1); _Pragma("unroll") for (int m = 0; m < 4; ++m) _Pragma("unroll") for (int n = 0; n < 2; ++n) _Pragma("unroll") for (int k = 0; k < 2; ++k) \
;         acc[ai][bj][m][n] = __builtin_amdgcn_mfma_f32_16x16x32_bf16(Bt[n][k], At[m][k], acc[ai][bj][m][n], 0, 0, 0); __builtin_amdgcn_s_setprio(0); } while (0)
; #define PG8_WAIT_V(n) asm volatile("s_waitcnt vmcnt(" #n ")" ::: "memory")
; #define PG8_WAIT_L(n) asm volatile("s_waitcnt lgkmcnt(" #n ")" ::: "memory")
; #define PG8_BAR __builtin_amdgcn_s_barrier()
; #define PG8_SCHED __builtin_amdgcn_sched_barrier(0)
; template <class Desc, class Epi>
; __device__ __forceinline__ void gemm_phase(const int wv_, LAS unsigned char* lds, const Desc& d, const Epi& E) {
;     ...
;             PG8_LDA(At, 1, 1); PG8_STAGE(PG8_SB(1, 0), b3, voffB); PG8_STAGE(PG8_SB(1, 1), b3 + hstepB, voffB); PG8_STAGE(PG8_SA(1, 0), a3, sA0);
;             PG8_WAIT_V(8); PG8_WAIT_L(0); PG8_BAR; PG8_MMA(1, 0, At, B0); PG8_MMA(1, 1, At, B1); PG8_BAR; PG8_SCHED;
;         }
;         if (wr == 0) PG8_BAR;
	v_mov_b32_e32 v96, v221
	ds_read_b128 v[162:165], v231 offset:49152
	ds_read_b128 v[166:169], v231 offset:50176
	ds_read_b128 v[170:173], v231 offset:51200
	ds_read_b128 v[174:177], v231 offset:52224
	ds_read_b128 v[178:181], v231 offset:53248
	ds_read_b128 v[182:185], v231 offset:54272
	ds_read_b128 v[186:189], v231 offset:55296
	ds_read_b128 v[190:193], v231 offset:56320
	s_add_i32 s47, s47, s59
	v_lshl_add_u64 v[194:195], s[20:21], 0, v[96:97]
	v_lshl_add_u64 v[194:195], v[194:195], 0, s[30:31]
	s_mov_b32 m0, s47
	v_mov_b32_e32 v96, v224
	global_load_lds_dwordx4 v[194:195], off
	s_add_i32 m0, s47, 0x2000
	s_nop 0
	v_lshl_add_u64 v[194:195], s[20:21], 0, v[96:97]
	s_add_u32 s20, s20, 0x40080
	v_lshl_add_u64 v[194:195], v[194:195], 0, s[30:31]
	s_addc_u32 s21, s21, 0
	s_add_i32 s47, s49, s59
	global_load_lds_dwordx4 v[194:195], off
	s_mov_b32 m0, s47
	s_nop 0
	global_load_lds_dwordx4 v221, s[20:21]
	s_add_i32 m0, s47, 0x2000
	s_nop 0
	global_load_lds_dwordx4 v224, s[20:21]
	v_mov_b32_e32 v96, v219
	s_mov_b32 m0, s66
	v_lshl_add_u64 v[194:195], s[4:5], 0, v[96:97]
	v_lshl_add_u64 v[194:195], v[194:195], 0, s[30:31]
	v_mov_b32_e32 v96, v222
	global_load_lds_dwordx4 v[194:195], off
	s_mov_b32 m0, s67
	v_lshl_add_u64 v[194:195], s[4:5], 0, v[96:97]
	v_lshl_add_u64 v[194:195], v[194:195], 0, s[30:31]
	global_load_lds_dwordx4 v[194:195], off
	s_waitcnt vmcnt(8)
	s_waitcnt lgkmcnt(0)
	s_barrier
	s_waitcnt lgkmcnt(0)
	v_mfma_f32_16x16x32_bf16 v[60:63], v[118:121], v[162:165], v[60:63]
	v_mfma_f32_16x16x32_bf16 v[56:59], v[130:133], v[162:165], v[56:59]
	v_mfma_f32_16x16x32_bf16 v[44:47], v[118:121], v[170:173], v[44:47]
	v_mfma_f32_16x16x32_bf16 v[40:43], v[130:133], v[170:173], v[40:43]
	v_mfma_f32_16x16x32_bf16 v[20:23], v[118:121], v[178:181], v[20:23]
	v_mfma_f32_16x16x32_bf16 v[16:19], v[130:133], v[178:181], v[16:19]
	v_mfma_f32_16x16x32_bf16 v[4:7], v[118:121], v[186:189], v[4:7]
	v_mfma_f32_16x16x32_bf16 v[0:3], v[130:133], v[186:189], v[0:3]
	v_mfma_f32_16x16x32_bf16 v[60:63], v[126:129], v[166:169], v[60:63]
	v_mfma_f32_16x16x32_bf16 v[56:59], v[134:137], v[166:169], v[56:59]
	v_mfma_f32_16x16x32_bf16 v[44:47], v[126:129], v[174:177], v[44:47]
	v_mfma_f32_16x16x32_bf16 v[40:43], v[134:137], v[174:177], v[40:43]
	v_mfma_f32_16x16x32_bf16 v[20:23], v[126:129], v[182:185], v[20:23]
	v_mfma_f32_16x16x32_bf16 v[16:19], v[134:137], v[182:185], v[16:19]
	v_mfma_f32_16x16x32_bf16 v[4:7], v[126:129], v[190:193], v[4:7]
	v_mfma_f32_16x16x32_bf16 v[0:3], v[134:137], v[190:193], v[0:3]
	v_mfma_f32_16x16x32_bf16 v[52:55], v[142:145], v[162:165], v[52:55]
	v_mfma_f32_16x16x32_bf16 v[48:51], v[154:157], v[162:165], v[48:51]
	v_mfma_f32_16x16x32_bf16 v[36:39], v[142:145], v[170:173], v[36:39]
	v_mfma_f32_16x16x32_bf16 v[32:35], v[154:157], v[170:173], v[32:35]
	v_mfma_f32_16x16x32_bf16 v[28:31], v[142:145], v[178:181], v[28:31]
	v_mfma_f32_16x16x32_bf16 v[24:27], v[154:157], v[178:181], v[24:27]
	v_mfma_f32_16x16x32_bf16 v[12:15], v[142:145], v[186:189], v[12:15]
	v_mfma_f32_16x16x32_bf16 v[8:11], v[154:157], v[186:189], v[8:11]
	v_mfma_f32_16x16x32_bf16 v[52:55], v[150:153], v[166:169], v[52:55]
	v_mfma_f32_16x16x32_bf16 v[48:51], v[158:161], v[166:169], v[48:51]
	v_mfma_f32_16x16x32_bf16 v[36:39], v[150:153], v[174:177], v[36:39]
	v_mfma_f32_16x16x32_bf16 v[32:35], v[158:161], v[174:177], v[32:35]
	v_mfma_f32_16x16x32_bf16 v[28:31], v[150:153], v[182:185], v[28:31]
	v_mfma_f32_16x16x32_bf16 v[24:27], v[158:161], v[182:185], v[24:27]
	v_mfma_f32_16x16x32_bf16 v[12:15], v[150:153], v[190:193], v[12:15]
	v_mfma_f32_16x16x32_bf16 v[8:11], v[158:161], v[190:193], v[8:11]
	s_barrier
	s_add_i32 s29, s29, 2
	s_add_u32 s2, s2, 0x100
	s_addc_u32 s3, s3, 0
	s_add_u32 s1, s1, 0x100
	s_addc_u32 s26, s26, 0
	s_cmp_gt_u32 s29, 13
	s_cbranch_scc0 .LBB0_1075
	s_and_b64 vcc, exec, s[44:45]
	s_cbranch_vccz .LBB0_1078
	s_barrier

; #define PG8_STAGE(bufoff, gbase, voff) do { _Pragma("unroll") for (int _i = 0; _i < 2; ++_i) \
;         __builtin_amdgcn_global_load_lds((const __attribute__((address_space(1))) unsigned*)((const __attribute__((address_space(1))) char*)(gbase) + (unsigned)lnd_v((int)(voff)[_i])), (LAS unsigned*)(lds + (bufoff) + ldsw + _i * 8192), 16, 0, 0); } while (0)
; #define PG8_WAIT_V(n) asm volatile("s_waitcnt vmcnt(" #n ")" ::: "memory")
; #define PG8_BAR __builtin_amdgcn_s_barrier()
; template <class Desc, class Epi>
; __device__ __forceinline__ void gemm_phase(const int wv_, LAS unsigned char* lds, const Desc& d, const Epi& E) {
;     ...
; #pragma unroll
;     for (int i = 0; i < 2; ++i) { int R, C; stage_rc(tid * 16 + i * 8192, R, C); const int Rb = (R & ~31) + perm32(R & 31); Rr[i] = R; Cc[i] = C;
;         voffA[i] = (unsigned)(R * d.lda + C) * 2u; voffA1[i] = voffA[i] + (unsigned)hstepA; voffB[i] = (unsigned)(Rb * d.ldb + C) * 2u; }
;     ...
;     PG8_STAGE(PG8_SB(0, 0), cB, voffB); PG8_STAGE(PG8_SB(0, 1), cB + hstepB, voffB); PG8_STAGE(PG8_SA(0, 0), cA, voffA); PG8_STAGE(PG8_SA(0, 1), cA, voffA1);
;     if (wr == 1) PG8_BAR;
;     PG8_WAIT_V(2); PG8_BAR;
;     PG8_STAGE(PG8_SB(1, 0), cB + kstep, voffB); PG8_STAGE(PG8_SA(1, 0), cA + kstep, voffA); PG8_STAGE(PG8_SB(1, 1), cB + hstepB + kstep, voffB);
;     PG8_WAIT_V(6); PG8_BAR;
.LBB0_1153:
	s_or_b64 exec, exec, s[4:5]
	v_ashrrev_i32_e32 v3, 31, v1
	v_lshrrev_b32_e32 v3, 26, v3
	v_lshlrev_b32_e32 v2, 4, v1
	v_add_u32_e32 v3, v1, v3
	v_bfe_i32 v1, v1, 27, 1
	v_lshrrev_b32_e32 v1, 22, v1
	v_add_u32_e32 v1, v2, v1
	v_and_b32_e32 v1, 0xfffffc00, v1
	v_sub_u32_e32 v1, v2, v1
	v_lshrrev_b32_e32 v4, 4, v1
	v_bitop3_b32 v1, v4, v1, 32 bitop3:0x6c
	v_ashrrev_i32_e32 v5, 31, v1
	s_add_u32 s22, s2, 0x33600000
	v_readlane_b32 s4, v254, 57
	v_ashrrev_i32_e32 v3, 6, v3
	v_lshrrev_b32_e32 v5, 26, v5
	s_addc_u32 s23, s0, 0
	s_lshl_b32 s3, s4, 24
	v_lshlrev_b32_e32 v4, 3, v3
	v_add_u32_e32 v5, v1, v5
	s_add_u32 s3, s2, s3
	v_and_b32_e32 v4, -16, v4
	v_ashrrev_i32_e32 v6, 6, v5
	v_and_b32_e32 v5, 0xc0, v5
	s_addc_u32 s4, s0, 0
	v_add_u32_e32 v4, v6, v4
	v_sub_u32_e32 v1, v1, v5
	s_add_u32 s52, s3, 0x3b200000
	v_lshlrev_b32_e32 v3, 5, v3
	v_ashrrev_i16_sdwa v1, v216, sext(v1) dst_sel:DWORD dst_unused:UNUSED_PAD src0_sel:DWORD src1_sel:BYTE_0
	v_lshlrev_b32_e32 v5, 1, v4
	v_lshrrev_b32_e32 v7, 2, v4
	v_and_b32_e32 v6, 3, v6
	s_mov_b32 s3, 0x1fffe0
	v_and_b32_e32 v3, 32, v3
	v_bfe_i32 v1, v1, 0, 16
	v_and_b32_e32 v5, 24, v5
	v_and_b32_e32 v7, 4, v7
	v_and_or_b32 v6, v4, s3, v6
	v_or3_b32 v5, v6, v7, v5
	v_add_lshl_u32 v1, v3, v1, 1
	v_lshl_add_u32 v190, v4, 11, v1
	v_lshl_add_u32 v192, v5, 11, v1
	v_add_u32_e32 v1, 0x2000, v2
	v_ashrrev_i32_e32 v2, 31, v1
	v_lshrrev_b32_e32 v2, 22, v2
	v_add_u32_e32 v2, v1, v2
	v_ashrrev_i32_e32 v2, 10, v2
	v_mul_i32_i24_e32 v3, 0x400, v2
	v_sub_u32_e32 v1, v1, v3
	v_lshrrev_b32_e32 v3, 4, v1
	v_readlane_b32 s5, v254, 58
	v_bitop3_b32 v1, v3, v1, 32 bitop3:0x6c
	s_addc_u32 s53, s4, 0
	v_ashrrev_i32_e32 v4, 31, v1
	s_lshl_b32 s5, s25, 5
	v_lshrrev_b32_e32 v4, 26, v4
	s_and_b32 s4, s25, 0x100
	s_and_b32 s5, s5, 0xe0
	s_lshr_b32 s20, s25, 3
	v_lshlrev_b32_e32 v3, 3, v2
	v_add_u32_e32 v4, v1, v4
	s_and_b32 s20, s20, 28
	s_or_b32 s4, s5, s4
	v_and_b32_e32 v3, -16, v3
	v_ashrrev_i32_e32 v5, 6, v4
	v_and_b32_e32 v4, 0xc0, v4
	s_or_b32 s36, s4, s20
	s_lshr_b32 s4, s4, 4
	v_add_u32_e32 v3, v5, v3
	v_sub_u32_e32 v1, v1, v4
	s_bfe_u32 s63, s25, 0x20003
	s_and_b32 s4, s4, 28
	s_ashr_i32 s29, s1, 6
	v_lshlrev_b32_e32 v2, 5, v2
	v_ashrrev_i16_sdwa v1, v216, sext(v1) dst_sel:DWORD dst_unused:UNUSED_PAD src0_sel:DWORD src1_sel:BYTE_0
	v_lshlrev_b32_e32 v4, 1, v3
	v_lshrrev_b32_e32 v6, 2, v3
	v_and_b32_e32 v5, 3, v5
	s_or_b32 s4, s4, s63
	v_and_b32_e32 v2, 32, v2
	v_bfe_i32 v1, v1, 0, 16
	v_and_b32_e32 v4, 24, v4
	v_and_b32_e32 v6, 4, v6
	v_and_or_b32 v5, v3, s3, v5
	s_ashr_i32 s3, s1, 8
	s_lshl_b32 s54, s29, 10
	s_lshl_b32 s37, s36, 17
	s_lshl_b32 s4, s4, 19
	v_or3_b32 v4, v5, v6, v4
	v_add_lshl_u32 v1, v2, v1, 1
	s_add_u32 s4, s52, s4
	v_lshl_add_u32 v193, v3, 11, v1
	v_lshl_add_u32 v195, v4, 11, v1
	s_addc_u32 s5, s53, 0
	s_add_i32 s55, s54, 0
	s_waitcnt vmcnt(0) lgkmcnt(0)
	s_barrier
	s_add_i32 m0, s55, 0x10000
	v_add_u32_e32 v191, 0x40000, v190
	global_load_lds_dwordx4 v192, s[4:5]
	s_add_i32 m0, s55, 0x12000
	s_add_u32 s20, s4, 0x40000
	global_load_lds_dwordx4 v195, s[4:5]
	s_addc_u32 s21, s5, 0
	s_add_i32 m0, s55, 0x14000
	v_add_u32_e32 v194, 0x40000, v193
	global_load_lds_dwordx4 v192, s[20:21]
	s_add_i32 m0, s55, 0x16000
	s_nop 0
	global_load_lds_dwordx4 v195, s[20:21]
	s_add_u32 s20, s22, s37
	s_addc_u32 s21, s23, 0
	s_mov_b32 m0, s55
	s_add_i32 s56, s55, 0x2000
	global_load_lds_dwordx4 v190, s[20:21]
	s_mov_b32 m0, s56
	s_add_i32 s57, s55, 0x4000
	global_load_lds_dwordx4 v193, s[20:21]
	s_mov_b32 m0, s57
	s_add_i32 s58, s55, 0x6000
	global_load_lds_dwordx4 v191, s[20:21]
	v_mov_b32_e32 v1, v194
	s_mov_b32 m0, s58
	s_cmp_eq_u32 s3, 1
	global_load_lds_dwordx4 v1, s[20:21]
	s_cselect_b64 s[38:39], -1, 0
	s_and_b64 vcc, exec, s[38:39]
	s_cbranch_vccz .LBB0_1155
	s_barrier
.LBB0_1155:
	s_lshr_b32 s64, s36, 2
	v_mov_b32_e32 v96, v192
	s_add_u32 s40, s2, 0x61400000
	s_waitcnt vmcnt(2)
	s_barrier
	s_addc_u32 s41, s0, 0
	v_lshl_add_u64 v[2:3], s[4:5], 0, v[96:97]
	s_add_i32 m0, s55, 0x18000
	v_lshl_add_u64 v[2:3], v[2:3], 0, s[30:31]
	v_mov_b32_e32 v96, v195
	global_load_lds_dwordx4 v[2:3], off
	s_add_i32 m0, s55, 0x1a000
	v_lshl_add_u64 v[2:3], s[4:5], 0, v[96:97]
	v_lshl_add_u64 v[2:3], v[2:3], 0, s[30:31]
	v_mov_b32_e32 v96, v190
	global_load_lds_dwordx4 v[2:3], off
	s_add_i32 s59, s55, 0x8000
	v_lshl_add_u64 v[2:3], s[20:21], 0, v[96:97]
	s_and_b32 s2, s29, 3
	v_lshl_add_u64 v[2:3], v[2:3], 0, s[30:31]
	s_mov_b32 m0, s59
	v_mov_b32_e32 v96, v193
	s_lshl_b32 s0, s3, 13
	s_lshl_b32 s29, s2, 12
	global_load_lds_dwordx4 v[2:3], off
	s_add_i32 s60, s55, 0xa000
	v_lshl_add_u64 v[2:3], s[20:21], 0, v[96:97]
	v_lshl_add_u64 v[2:3], v[2:3], 0, s[30:31]
	s_mov_b32 m0, s60
	s_add_u32 s36, s4, 0x40080
	global_load_lds_dwordx4 v[2:3], off
	s_addc_u32 s37, s5, 0
	s_add_i32 m0, s55, 0x1c000
	v_bfe_u32 v2, v0, 4, 2
	global_load_lds_dwordx4 v192, s[36:37]
	s_add_i32 m0, s55, 0x1e000
	v_lshlrev_b32_e32 v4, 4, v2
	global_load_lds_dwordx4 v195, s[36:37]
	v_and_b32_e32 v1, 15, v0
	v_lshlrev_b32_e32 v0, 2, v0
	s_cmpk_lt_u32 s1, 0x100
	v_lshl_or_b32 v196, s3, 6, v1
	v_lshl_or_b32 v4, v1, 6, v4
	v_and_b32_e32 v0, 32, v0
	s_cselect_b64 s[42:43], -1, 0
	s_and_b32 s1, s1, 0x3fffff00
	v_lshlrev_b32_e32 v3, 3, v2
	v_lshlrev_b32_e32 v5, 2, v196
	v_bitop3_b32 v197, v4, s29, v0 bitop3:0xde
	v_readlane_b32 s29, v254, 54
	s_lshl_b32 s1, s1, 2
	v_and_b32_e32 v6, 32, v5
	s_waitcnt vmcnt(6)
	v_lshl_or_b32 v198, s2, 5, v3
	v_or_b32_e32 v200, 16, v196
	v_or_b32_e32 v202, 32, v196
	v_or_b32_e32 v204, 48, v196
	v_add_u32_e32 v206, 0x80, v196
	v_add_u32_e32 v208, 0x90, v196
	v_add_u32_e32 v210, 0xa0, v196
	v_add_u32_e32 v212, 0xb0, v196
	s_lshl_b32 s2, s2, 2
	s_add_i32 s1, s29, s1
	v_bitop3_b32 v6, v4, s0, v6 bitop3:0xde
	v_lshlrev_b32_e32 v199, 4, v196
	v_lshlrev_b32_e32 v201, 4, v200
	v_lshlrev_b32_e32 v203, 4, v202
	v_lshlrev_b32_e32 v205, 4, v204
	v_lshlrev_b32_e32 v207, 4, v206
	v_lshlrev_b32_e32 v209, 4, v208
	v_lshlrev_b32_e32 v211, 4, v210
	v_lshlrev_b32_e32 v213, 4, v212
	s_add_i32 s3, s2, s29
	v_lshl_add_u32 v225, v1, 4, s1
	s_add_i32 s1, 0, 0x20000
	s_mov_b32 s0, 0
	v_cmp_eq_u32_e64 s[36:37], 0, v2
	v_add_u32_e32 v214, s3, v199
	v_add_u32_e32 v215, s3, v201
	v_add_u32_e32 v219, s3, v203
	v_add_u32_e32 v220, s3, v205
	v_add_u32_e32 v221, s3, v207
	v_add_u32_e32 v222, s3, v209
	v_add_u32_e32 v223, s3, v211
	v_add_u32_e32 v224, s3, v213
	v_add_u32_e32 v226, s2, v225
	v_add_u32_e32 v227, s1, v5
	v_add_u32_e32 v228, 0, v6
	s_mov_b64 s[48:49], s[4:5]
	s_mov_b64 s[46:47], s[20:21]
	s_barrier
	s_waitcnt vmcnt(0)
	s_branch .LBB0_1158

; #define PG8_STAGE(bufoff, gbase, voff) do { _Pragma("unroll") for (int _i = 0; _i < 2; ++_i) \
;         __builtin_amdgcn_global_load_lds((const __attribute__((address_space(1))) unsigned*)((const __attribute__((address_space(1))) char*)(gbase) + (unsigned)lnd_v((int)(voff)[_i])), (LAS unsigned*)(lds + (bufoff) + ldsw + _i * 8192), 16, 0, 0); } while (0)
; #define PG8_LDA(dst, b, h) do { _Pragma("unroll") for (int m = 0; m < 4; ++m) _Pragma("unroll") for (int k = 0; k < 2; ++k) dst[m][k] = *(const LAS bf16x8*)(lds + PG8_SA(b, h) + aoff + m * 2048 + k * 1024); } while (0)
; #define PG8_LDB(dst, b, h) do { _Pragma("unroll") for (int n = 0; n < 2; ++n) _Pragma("unroll") for (int k = 0; k < 2; ++k) dst[n][k] = *(const LAS bf16x8*)(lds + PG8_SB(b, h) + boff + n * 2048 + k * 1024); } while (0)
; #define PG8_WAIT_V(n) asm volatile("s_waitcnt vmcnt(" #n ")" ::: "memory")
; #define PG8_WAIT_L(n) asm volatile("s_waitcnt lgkmcnt(" #n ")" ::: "memory")
; #define PG8_BAR __builtin_amdgcn_s_barrier()
; template <class Desc, class Epi>
; __device__ __forceinline__ void gemm_phase(const int wv_, LAS unsigned char* lds, const Desc& d, const Epi& E) {
;     ...
;         for (int t = 0; t < nt; t += 2) {
;             const bool last = (t == nt - 2);
;             unsigned sA0[2], sA1[2];
;             if constexpr (Desc::GATHER) { sA0[0] = last ? voffAn[0] : voffA[0]; sA0[1] = last ? voffAn[1] : voffA[1]; sA1[0] = last ? voffAn1[0] : voffA1[0]; sA1[1] = last ? voffAn1[1] : voffA1[1]; }
;             else { sA0[0] = voffA[0]; sA0[1] = voffA[1]; sA1[0] = voffA1[0]; sA1[1] = voffA1[1]; }
;             const char* a1 = cA + (size_t)(t + 1) * kstep;
;             const char* a2 = last ? nA : cA + (size_t)(t + 2) * kstep; const char* b2 = last ? nB : cB + (size_t)(t + 2) * kstep;
;             const char* a3 = a2 + kstep; const char* b3 = b2 + kstep;
;             PG8_LDB(B0, 0, 0); PG8_LDB(B1, 0, 1); PG8_SCHED; PG8_LDA(At, 0, 0); PG8_STAGE(PG8_SA(1, 1), a1, voffA1);
;             PG8_WAIT_V(8); PG8_WAIT_L(0); PG8_BAR; PG8_MMA(0, 0, At, B0); PG8_MMA(0, 1, At, B1); PG8_BAR; PG8_SCHED;
;             PG8_LDA(At, 0, 1); PG8_STAGE(PG8_SB(0, 0), b2, voffB); PG8_STAGE(PG8_SB(0, 1), b2 + hstepB, voffB); PG8_STAGE(PG8_SA(0, 0), a2, sA0);
;             PG8_WAIT_V(8); PG8_WAIT_L(0); PG8_BAR; PG8_MMA(1, 0, At, B0); PG8_MMA(1, 1, At, B1); PG8_BAR; PG8_SCHED;
.LBB0_1161:
	s_add_u32 s4, s2, 0x80
	s_addc_u32 s5, s3, 0
	s_add_i32 s65, 0, 0x10000
	s_cmp_eq_u32 s45, 12
	s_cselect_b32 s5, s47, s5
	s_cselect_b32 s4, s46, s4
	v_add_u32_e32 v96, s65, v197
	s_cselect_b32 s21, s49, s29
	s_cselect_b32 s20, s48, s1
	s_add_i32 s68, 0, 0x14000
	ds_read_b128 v[130:133], v96
	ds_read_b128 v[134:137], v96 offset:1024
	ds_read_b128 v[138:141], v96 offset:2048
	ds_read_b128 v[142:145], v96 offset:3072
	v_add_u32_e32 v96, s68, v197
	ds_read_b128 v[146:149], v96
	ds_read_b128 v[150:153], v96 offset:1024
	ds_read_b128 v[154:157], v96 offset:2048
	ds_read_b128 v[158:161], v96 offset:3072
	ds_read_b128 v[162:165], v228
	ds_read_b128 v[166:169], v228 offset:1024
	ds_read_b128 v[170:173], v228 offset:2048
	ds_read_b128 v[174:177], v228 offset:3072
	ds_read_b128 v[178:181], v228 offset:4096
	ds_read_b128 v[182:185], v228 offset:5120
	ds_read_b128 v[186:189], v228 offset:6144
	ds_read_b128 v[230:233], v228 offset:7168
	s_add_i32 m0, s55, 0xc000
	s_nop 0
	global_load_lds_dwordx4 v191, s[2:3]
	s_add_i32 m0, s55, 0xe000
	s_nop 0
	global_load_lds_dwordx4 v194, s[2:3]
	s_waitcnt vmcnt(8)
	s_waitcnt lgkmcnt(0)
	s_barrier
	s_waitcnt lgkmcnt(0)
	v_mfma_f32_16x16x32_bf16 v[126:129], v[130:133], v[162:165], v[126:129]
	v_mfma_f32_16x16x32_bf16 v[122:125], v[138:141], v[162:165], v[122:125]
	v_mfma_f32_16x16x32_bf16 v[114:117], v[130:133], v[170:173], v[114:117]
	v_mfma_f32_16x16x32_bf16 v[106:109], v[138:141], v[170:173], v[106:109]
	v_mfma_f32_16x16x32_bf16 v[98:101], v[130:133], v[178:181], v[98:101]
	v_mfma_f32_16x16x32_bf16 v[88:91], v[138:141], v[178:181], v[88:91]
	v_mfma_f32_16x16x32_bf16 v[80:83], v[130:133], v[186:189], v[80:83]
	v_mfma_f32_16x16x32_bf16 v[72:75], v[138:141], v[186:189], v[72:75]
	v_mfma_f32_16x16x32_bf16 v[126:129], v[134:137], v[166:169], v[126:129]
	v_mfma_f32_16x16x32_bf16 v[122:125], v[142:145], v[166:169], v[122:125]
	v_mfma_f32_16x16x32_bf16 v[114:117], v[134:137], v[174:177], v[114:117]
	v_mfma_f32_16x16x32_bf16 v[106:109], v[142:145], v[174:177], v[106:109]
	v_mfma_f32_16x16x32_bf16 v[98:101], v[134:137], v[182:185], v[98:101]
	v_mfma_f32_16x16x32_bf16 v[88:91], v[142:145], v[182:185], v[88:91]
	v_mfma_f32_16x16x32_bf16 v[80:83], v[134:137], v[230:233], v[80:83]
	v_mfma_f32_16x16x32_bf16 v[72:75], v[142:145], v[230:233], v[72:75]
	v_mfma_f32_16x16x32_bf16 v[118:121], v[146:149], v[162:165], v[118:121]
	v_mfma_f32_16x16x32_bf16 v[110:113], v[154:157], v[162:165], v[110:113]
	v_mfma_f32_16x16x32_bf16 v[102:105], v[146:149], v[170:173], v[102:105]
	v_mfma_f32_16x16x32_bf16 v[92:95], v[154:157], v[170:173], v[92:95]
	v_mfma_f32_16x16x32_bf16 v[84:87], v[146:149], v[178:181], v[84:87]
	v_mfma_f32_16x16x32_bf16 v[76:79], v[154:157], v[178:181], v[76:79]
	v_mfma_f32_16x16x32_bf16 v[68:71], v[146:149], v[186:189], v[68:71]
	v_mfma_f32_16x16x32_bf16 v[64:67], v[154:157], v[186:189], v[64:67]
	v_mfma_f32_16x16x32_bf16 v[118:121], v[150:153], v[166:169], v[118:121]
	v_mfma_f32_16x16x32_bf16 v[110:113], v[158:161], v[166:169], v[110:113]
	v_mfma_f32_16x16x32_bf16 v[102:105], v[150:153], v[174:177], v[102:105]
	v_mfma_f32_16x16x32_bf16 v[92:95], v[158:161], v[174:177], v[92:95]
	v_mfma_f32_16x16x32_bf16 v[84:87], v[150:153], v[182:185], v[84:87]
	v_mfma_f32_16x16x32_bf16 v[76:79], v[158:161], v[182:185], v[76:79]
	v_mfma_f32_16x16x32_bf16 v[68:71], v[150:153], v[230:233], v[68:71]
	v_mfma_f32_16x16x32_bf16 v[64:67], v[158:161], v[230:233], v[64:67]
	s_barrier
	s_add_i32 s65, s65, s54
	ds_read_b128 v[162:165], v228 offset:16384
	ds_read_b128 v[166:169], v228 offset:17408
	ds_read_b128 v[170:173], v228 offset:18432
	ds_read_b128 v[174:177], v228 offset:19456
	ds_read_b128 v[178:181], v228 offset:20480
	ds_read_b128 v[182:185], v228 offset:21504
	ds_read_b128 v[186:189], v228 offset:22528
	ds_read_b128 v[230:233], v228 offset:23552
	s_mov_b32 m0, s65
	s_nop 0
	global_load_lds_dwordx4 v192, s[20:21]
	s_add_i32 m0, s65, 0x2000
	s_add_u32 s66, s20, 0x40000
	global_load_lds_dwordx4 v195, s[20:21]
	s_addc_u32 s67, s21, 0
	s_add_i32 s65, s68, s54
	s_mov_b32 m0, s65
	s_nop 0
	global_load_lds_dwordx4 v192, s[66:67]
	s_add_i32 m0, s65, 0x2000
	s_nop 0
	global_load_lds_dwordx4 v195, s[66:67]
	s_mov_b32 m0, s55
	s_nop 0
	global_load_lds_dwordx4 v190, s[4:5]
	s_mov_b32 m0, s56
	s_nop 0
	global_load_lds_dwordx4 v193, s[4:5]
	s_waitcnt vmcnt(8)
	s_waitcnt lgkmcnt(0)
	s_barrier
	s_waitcnt lgkmcnt(0)
	v_mfma_f32_16x16x32_bf16 v[60:63], v[130:133], v[162:165], v[60:63]
	v_mfma_f32_16x16x32_bf16 v[56:59], v[138:141], v[162:165], v[56:59]
	v_mfma_f32_16x16x32_bf16 v[40:43], v[130:133], v[170:173], v[40:43]
	v_mfma_f32_16x16x32_bf16 v[32:35], v[138:141], v[170:173], v[32:35]
	v_mfma_f32_16x16x32_bf16 v[16:19], v[130:133], v[178:181], v[16:19]
	v_mfma_f32_16x16x32_bf16 v[8:11], v[138:141], v[178:181], v[8:11]
	v_mfma_f32_16x16x32_bf16 v[4:7], v[130:133], v[186:189], v[4:7]
	v_mfma_f32_16x16x32_bf16 v[0:3], v[138:141], v[186:189], v[0:3]
	v_mfma_f32_16x16x32_bf16 v[60:63], v[134:137], v[166:169], v[60:63]
	v_mfma_f32_16x16x32_bf16 v[56:59], v[142:145], v[166:169], v[56:59]
	v_mfma_f32_16x16x32_bf16 v[40:43], v[134:137], v[174:177], v[40:43]
	v_mfma_f32_16x16x32_bf16 v[32:35], v[142:145], v[174:177], v[32:35]
	v_mfma_f32_16x16x32_bf16 v[16:19], v[134:137], v[182:185], v[16:19]
	v_mfma_f32_16x16x32_bf16 v[8:11], v[142:145], v[182:185], v[8:11]
	v_mfma_f32_16x16x32_bf16 v[4:7], v[134:137], v[230:233], v[4:7]
	v_mfma_f32_16x16x32_bf16 v[0:3], v[142:145], v[230:233], v[0:3]
	v_mfma_f32_16x16x32_bf16 v[44:47], v[146:149], v[162:165], v[44:47]
	v_mfma_f32_16x16x32_bf16 v[36:39], v[154:157], v[162:165], v[36:39]
	v_mfma_f32_16x16x32_bf16 v[20:23], v[146:149], v[170:173], v[20:23]
	v_mfma_f32_16x16x32_bf16 v[12:15], v[154:157], v[170:173], v[12:15]
	v_mfma_f32_16x16x32_bf16 v[52:55], v[146:149], v[178:181], v[52:55]
	v_mfma_f32_16x16x32_bf16 v[48:51], v[154:157], v[178:181], v[48:51]
	v_mfma_f32_16x16x32_bf16 v[28:31], v[146:149], v[186:189], v[28:31]
	v_mfma_f32_16x16x32_bf16 v[24:27], v[154:157], v[186:189], v[24:27]
	v_mfma_f32_16x16x32_bf16 v[44:47], v[150:153], v[166:169], v[44:47]
	v_mfma_f32_16x16x32_bf16 v[36:39], v[158:161], v[166:169], v[36:39]
	v_mfma_f32_16x16x32_bf16 v[20:23], v[150:153], v[174:177], v[20:23]
	v_mfma_f32_16x16x32_bf16 v[12:15], v[158:161], v[174:177], v[12:15]
	v_mfma_f32_16x16x32_bf16 v[52:55], v[150:153], v[182:185], v[52:55]
	v_mfma_f32_16x16x32_bf16 v[48:51], v[158:161], v[182:185], v[48:51]
	v_mfma_f32_16x16x32_bf16 v[28:31], v[150:153], v[230:233], v[28:31]
	v_mfma_f32_16x16x32_bf16 v[24:27], v[158:161], v[230:233], v[24:27]
	s_barrier
; #define PG8_STAGE(bufoff, gbase, voff) do { _Pragma("unroll") for (int _i = 0; _i < 2; ++_i) \
;         __builtin_amdgcn_global_load_lds((const __attribute__((address_space(1))) unsigned*)((const __attribute__((address_space(1))) char*)(gbase) + (unsigned)lnd_v((int)(voff)[_i])), (LAS unsigned*)(lds + (bufoff) + ldsw + _i * 8192), 16, 0, 0); } while (0)
; #define PG8_LDA(dst, b, h) do { _Pragma("unroll") for (int m = 0; m < 4; ++m) _Pragma("unroll") for (int k = 0; k < 2; ++k) dst[m][k] = *(const LAS bf16x8*)(lds + PG8_SA(b, h) + aoff + m * 2048 + k * 1024); } while (0)
; #define PG8_LDB(dst, b, h) do { _Pragma("unroll") for (int n = 0; n < 2; ++n) _Pragma("unroll") for (int k = 0; k < 2; ++k) dst[n][k] = *(const LAS bf16x8*)(lds + PG8_SB(b, h) + boff + n * 2048 + k * 1024); } while (0)
; #define PG8_MMA(ai, bj, At, Bt) do { __builtin_amdgcn_s_setprio(1); _Pragma("unroll") for (int m = 0; m < 4; ++m) _Pragma("unroll") for (int n = 0; n < 2; ++n) _Pragma("unroll") for (int k = 0; k < 2; ++k) \
;         acc[ai][bj][m][n] = __builtin_amdgcn_mfma_f32_16x16x32_bf16(Bt[n][k], At[m][k], acc[ai][bj][m][n], 0, 0, 0); __builtin_amdgcn_s_setprio(0); } while (0)
; #define PG8_WAIT_V(n) asm volatile("s_waitcnt vmcnt(" #n ")" ::: "memory")
; #define PG8_WAIT_L(n) asm volatile("s_waitcnt lgkmcnt(" #n ")" ::: "memory")
; #define PG8_BAR __builtin_amdgcn_s_barrier()
; #define PG8_SCHED __builtin_amdgcn_sched_barrier(0)
; template <class Desc, class Epi>
; __device__ __forceinline__ void gemm_phase(const int wv_, LAS unsigned char* lds, const Desc& d, const Epi& E) {
;     ...
;             PG8_LDB(B0, 1, 0); PG8_LDB(B1, 1, 1); PG8_SCHED; PG8_LDA(At, 1, 0); PG8_STAGE(PG8_SA(0, 1), a2, sA1);
;             PG8_WAIT_V(8); PG8_WAIT_L(0); PG8_BAR; PG8_MMA(0, 0, At, B0); PG8_MMA(0, 1, At, B1); PG8_BAR; PG8_SCHED;
	s_add_i32 s65, 0, 0x18000
	v_add_u32_e32 v96, s65, v197
	s_add_i32 s66, 0, 0x1c000
	ds_read_b128 v[130:133], v96
	ds_read_b128 v[134:137], v96 offset:1024
	ds_read_b128 v[138:141], v96 offset:2048
	ds_read_b128 v[142:145], v96 offset:3072
	v_add_u32_e32 v96, s66, v197
	ds_read_b128 v[146:149], v96
	ds_read_b128 v[150:153], v96 offset:1024
	ds_read_b128 v[154:157], v96 offset:2048
	ds_read_b128 v[158:161], v96 offset:3072
	s_mov_b32 m0, s57
	ds_read_b128 v[162:165], v228 offset:32768
	ds_read_b128 v[166:169], v228 offset:33792
	ds_read_b128 v[170:173], v228 offset:34816
	ds_read_b128 v[174:177], v228 offset:35840
	ds_read_b128 v[178:181], v228 offset:36864
	ds_read_b128 v[182:185], v228 offset:37888
	ds_read_b128 v[186:189], v228 offset:38912
	ds_read_b128 v[230:233], v228 offset:39936
	s_nop 0
	global_load_lds_dwordx4 v191, s[4:5]
	s_mov_b32 m0, s58
	s_nop 0
	global_load_lds_dwordx4 v194, s[4:5]
	s_waitcnt vmcnt(8)
	s_waitcnt lgkmcnt(0)
	s_barrier
	s_waitcnt lgkmcnt(0)
	v_mfma_f32_16x16x32_bf16 v[126:129], v[130:133], v[162:165], v[126:129]
	v_mfma_f32_16x16x32_bf16 v[122:125], v[138:141], v[162:165], v[122:125]
	v_mfma_f32_16x16x32_bf16 v[114:117], v[130:133], v[170:173], v[114:117]
	v_mfma_f32_16x16x32_bf16 v[106:109], v[138:141], v[170:173], v[106:109]
	v_mfma_f32_16x16x32_bf16 v[98:101], v[130:133], v[178:181], v[98:101]
	v_mfma_f32_16x16x32_bf16 v[88:91], v[138:141], v[178:181], v[88:91]
	v_mfma_f32_16x16x32_bf16 v[80:83], v[130:133], v[186:189], v[80:83]
	v_mfma_f32_16x16x32_bf16 v[72:75], v[138:141], v[186:189], v[72:75]
	v_mfma_f32_16x16x32_bf16 v[126:129], v[134:137], v[166:169], v[126:129]
	v_mfma_f32_16x16x32_bf16 v[122:125], v[142:145], v[166:169], v[122:125]
	v_mfma_f32_16x16x32_bf16 v[114:117], v[134:137], v[174:177], v[114:117]
	v_mfma_f32_16x16x32_bf16 v[106:109], v[142:145], v[174:177], v[106:109]
	v_mfma_f32_16x16x32_bf16 v[98:101], v[134:137], v[182:185], v[98:101]
	v_mfma_f32_16x16x32_bf16 v[88:91], v[142:145], v[182:185], v[88:91]
	v_mfma_f32_16x16x32_bf16 v[80:83], v[134:137], v[230:233], v[80:83]
	v_mfma_f32_16x16x32_bf16 v[72:75], v[142:145], v[230:233], v[72:75]
	v_mfma_f32_16x16x32_bf16 v[118:121], v[146:149], v[162:165], v[118:121]
	v_mfma_f32_16x16x32_bf16 v[110:113], v[154:157], v[162:165], v[110:113]
	v_mfma_f32_16x16x32_bf16 v[102:105], v[146:149], v[170:173], v[102:105]
	v_mfma_f32_16x16x32_bf16 v[92:95], v[154:157], v[170:173], v[92:95]
	v_mfma_f32_16x16x32_bf16 v[84:87], v[146:149], v[178:181], v[84:87]
	v_mfma_f32_16x16x32_bf16 v[76:79], v[154:157], v[178:181], v[76:79]
	v_mfma_f32_16x16x32_bf16 v[68:71], v[146:149], v[186:189], v[68:71]
	v_mfma_f32_16x16x32_bf16 v[64:67], v[154:157], v[186:189], v[64:67]
	v_mfma_f32_16x16x32_bf16 v[118:121], v[150:153], v[166:169], v[118:121]
	v_mfma_f32_16x16x32_bf16 v[110:113], v[158:161], v[166:169], v[110:113]
	v_mfma_f32_16x16x32_bf16 v[102:105], v[150:153], v[174:177], v[102:105]
	v_mfma_f32_16x16x32_bf16 v[92:95], v[158:161], v[174:177], v[92:95]
	v_mfma_f32_16x16x32_bf16 v[84:87], v[150:153], v[182:185], v[84:87]
	v_mfma_f32_16x16x32_bf16 v[76:79], v[158:161], v[182:185], v[76:79]
	v_mfma_f32_16x16x32_bf16 v[68:71], v[150:153], v[230:233], v[68:71]
	v_mfma_f32_16x16x32_bf16 v[64:67], v[158:161], v[230:233], v[64:67]
	s_barrier
; #define PG8_STAGE(bufoff, gbase, voff) do { _Pragma("unroll") for (int _i = 0; _i < 2; ++_i) \
;         __builtin_amdgcn_global_load_lds((const __attribute__((address_space(1))) unsigned*)((const __attribute__((address_space(1))) char*)(gbase) + (unsigned)lnd_v((int)(voff)[_i])), (LAS unsigned*)(lds + (bufoff) + ldsw + _i * 8192), 16, 0, 0); } while (0)
; #define PG8_LDA(dst, b, h) do { _Pragma("unroll") for (int m = 0; m < 4; ++m) _Pragma("unroll") for (int k = 0; k < 2; ++k) dst[m][k] = *(const LAS bf16x8*)(lds + PG8_SA(b, h) + aoff + m * 2048 + k * 1024); } while (0)
; #define PG8_MMA(ai, bj, At, Bt) do { __builtin_amdgcn_s_setprio(1); _Pragma("unroll") for (int m = 0; m < 4; ++m) _Pragma("unroll") for (int n = 0; n < 2; ++n) _Pragma("unroll") for (int k = 0; k < 2; ++k) \
;         acc[ai][bj][m][n] = __builtin_amdgcn_mfma_f32_16x16x32_bf16(Bt[n][k], At[m][k], acc[ai][bj][m][n], 0, 0, 0); __builtin_amdgcn_s_setprio(0); } while (0)
; #define PG8_WAIT_V(n) asm volatile("s_waitcnt vmcnt(" #n ")" ::: "memory")
; #define PG8_WAIT_L(n) asm volatile("s_waitcnt lgkmcnt(" #n ")" ::: "memory")
; #define PG8_BAR __builtin_amdgcn_s_barrier()
; #define PG8_SCHED __builtin_amdgcn_sched_barrier(0)
; template <class Desc, class Epi>
; __device__ __forceinline__ void gemm_phase(const int wv_, LAS unsigned char* lds, const Desc& d, const Epi& E) {
;     ...
;             PG8_LDA(At, 1, 1); PG8_STAGE(PG8_SB(1, 0), b3, voffB); PG8_STAGE(PG8_SB(1, 1), b3 + hstepB, voffB); PG8_STAGE(PG8_SA(1, 0), a3, sA0);
;             PG8_WAIT_V(8); PG8_WAIT_L(0); PG8_BAR; PG8_MMA(1, 0, At, B0); PG8_MMA(1, 1, At, B1); PG8_BAR; PG8_SCHED;
;         }
;         if (wr == 0) PG8_BAR;
	v_mov_b32_e32 v96, v192
	ds_read_b128 v[162:165], v228 offset:49152
	ds_read_b128 v[166:169], v228 offset:50176
	ds_read_b128 v[170:173], v228 offset:51200
	ds_read_b128 v[174:177], v228 offset:52224
	ds_read_b128 v[178:181], v228 offset:53248
	ds_read_b128 v[182:185], v228 offset:54272
	ds_read_b128 v[186:189], v228 offset:55296
	ds_read_b128 v[230:233], v228 offset:56320
	s_add_i32 s65, s65, s54
	v_lshl_add_u64 v[234:235], s[20:21], 0, v[96:97]
	v_lshl_add_u64 v[234:235], v[234:235], 0, s[30:31]
	s_mov_b32 m0, s65
	v_mov_b32_e32 v96, v195
	global_load_lds_dwordx4 v[234:235], off
	s_add_i32 m0, s65, 0x2000
	s_nop 0
	v_lshl_add_u64 v[234:235], s[20:21], 0, v[96:97]
	s_add_u32 s20, s20, 0x40080
	v_lshl_add_u64 v[234:235], v[234:235], 0, s[30:31]
	s_addc_u32 s21, s21, 0
	s_add_i32 s65, s66, s54
	global_load_lds_dwordx4 v[234:235], off
	s_mov_b32 m0, s65
	s_nop 0
	global_load_lds_dwordx4 v192, s[20:21]
	s_add_i32 m0, s65, 0x2000
	s_nop 0
	global_load_lds_dwordx4 v195, s[20:21]
	v_mov_b32_e32 v96, v190
	s_mov_b32 m0, s59
	v_lshl_add_u64 v[234:235], s[4:5], 0, v[96:97]
	v_lshl_add_u64 v[234:235], v[234:235], 0, s[30:31]
	v_mov_b32_e32 v96, v193
	global_load_lds_dwordx4 v[234:235], off
	s_mov_b32 m0, s60
	v_lshl_add_u64 v[234:235], s[4:5], 0, v[96:97]
	v_lshl_add_u64 v[234:235], v[234:235], 0, s[30:31]
	global_load_lds_dwordx4 v[234:235], off
	s_waitcnt vmcnt(8)
	s_waitcnt lgkmcnt(0)
	s_barrier
	s_waitcnt lgkmcnt(0)
	v_mfma_f32_16x16x32_bf16 v[60:63], v[130:133], v[162:165], v[60:63]
	v_mfma_f32_16x16x32_bf16 v[56:59], v[138:141], v[162:165], v[56:59]
	v_mfma_f32_16x16x32_bf16 v[40:43], v[130:133], v[170:173], v[40:43]
	v_mfma_f32_16x16x32_bf16 v[32:35], v[138:141], v[170:173], v[32:35]
	v_mfma_f32_16x16x32_bf16 v[16:19], v[130:133], v[178:181], v[16:19]
	v_mfma_f32_16x16x32_bf16 v[8:11], v[138:141], v[178:181], v[8:11]
	v_mfma_f32_16x16x32_bf16 v[4:7], v[130:133], v[186:189], v[4:7]
	v_mfma_f32_16x16x32_bf16 v[0:3], v[138:141], v[186:189], v[0:3]
	v_mfma_f32_16x16x32_bf16 v[60:63], v[134:137], v[166:169], v[60:63]
	v_mfma_f32_16x16x32_bf16 v[56:59], v[142:145], v[166:169], v[56:59]
	v_mfma_f32_16x16x32_bf16 v[40:43], v[134:137], v[174:177], v[40:43]
	v_mfma_f32_16x16x32_bf16 v[32:35], v[142:145], v[174:177], v[32:35]
	v_mfma_f32_16x16x32_bf16 v[16:19], v[134:137], v[182:185], v[16:19]
	v_mfma_f32_16x16x32_bf16 v[8:11], v[142:145], v[182:185], v[8:11]
	v_mfma_f32_16x16x32_bf16 v[4:7], v[134:137], v[230:233], v[4:7]
	v_mfma_f32_16x16x32_bf16 v[0:3], v[142:145], v[230:233], v[0:3]
	v_mfma_f32_16x16x32_bf16 v[44:47], v[146:149], v[162:165], v[44:47]
	v_mfma_f32_16x16x32_bf16 v[36:39], v[154:157], v[162:165], v[36:39]
	v_mfma_f32_16x16x32_bf16 v[20:23], v[146:149], v[170:173], v[20:23]
	v_mfma_f32_16x16x32_bf16 v[12:15], v[154:157], v[170:173], v[12:15]
	v_mfma_f32_16x16x32_bf16 v[52:55], v[146:149], v[178:181], v[52:55]
	v_mfma_f32_16x16x32_bf16 v[48:51], v[154:157], v[178:181], v[48:51]
	v_mfma_f32_16x16x32_bf16 v[28:31], v[146:149], v[186:189], v[28:31]
	v_mfma_f32_16x16x32_bf16 v[24:27], v[154:157], v[186:189], v[24:27]
	v_mfma_f32_16x16x32_bf16 v[44:47], v[150:153], v[166:169], v[44:47]
	v_mfma_f32_16x16x32_bf16 v[36:39], v[158:161], v[166:169], v[36:39]
	v_mfma_f32_16x16x32_bf16 v[20:23], v[150:153], v[174:177], v[20:23]
	v_mfma_f32_16x16x32_bf16 v[12:15], v[158:161], v[174:177], v[12:15]
	v_mfma_f32_16x16x32_bf16 v[52:55], v[150:153], v[182:185], v[52:55]
	v_mfma_f32_16x16x32_bf16 v[48:51], v[158:161], v[182:185], v[48:51]
	v_mfma_f32_16x16x32_bf16 v[28:31], v[150:153], v[230:233], v[28:31]
	v_mfma_f32_16x16x32_bf16 v[24:27], v[158:161], v[230:233], v[24:27]
	s_barrier
	s_add_i32 s45, s45, 2
	s_add_u32 s2, s2, 0x100
	s_addc_u32 s3, s3, 0
	s_add_u32 s1, s1, 0x100
	s_addc_u32 s29, s29, 0
	s_cmp_gt_u32 s45, 13
	s_cbranch_scc0 .LBB0_1161
	s_and_b64 vcc, exec, s[42:43]
	s_cbranch_vccz .LBB0_1164
	s_barrier

; #define PG8_STAGE(bufoff, gbase, voff) do { _Pragma("unroll") for (int _i = 0; _i < 2; ++_i) \
;         __builtin_amdgcn_global_load_lds((const __attribute__((address_space(1))) unsigned*)((const __attribute__((address_space(1))) char*)(gbase) + (unsigned)lnd_v((int)(voff)[_i])), (LAS unsigned*)(lds + (bufoff) + ldsw + _i * 8192), 16, 0, 0); } while (0)
; #define PG8_WAIT_V(n) asm volatile("s_waitcnt vmcnt(" #n ")" ::: "memory")
; #define PG8_BAR __builtin_amdgcn_s_barrier()
; template <class Desc, class Epi>
; __device__ __forceinline__ void gemm_phase(const int wv_, LAS unsigned char* lds, const Desc& d, const Epi& E) {
;     ...
; #pragma unroll
;     for (int i = 0; i < 2; ++i) { int R, C; stage_rc(tid * 16 + i * 8192, R, C); const int Rb = (R & ~31) + perm32(R & 31); Rr[i] = R; Cc[i] = C;
;         voffA[i] = (unsigned)(R * d.lda + C) * 2u; voffA1[i] = voffA[i] + (unsigned)hstepA; voffB[i] = (unsigned)(Rb * d.ldb + C) * 2u; }
;     ...
;     PG8_STAGE(PG8_SB(0, 0), cB, voffB); PG8_STAGE(PG8_SB(0, 1), cB + hstepB, voffB); PG8_STAGE(PG8_SA(0, 0), cA, voffA); PG8_STAGE(PG8_SA(0, 1), cA, voffA1);
;     if (wr == 1) PG8_BAR;
;     PG8_WAIT_V(2); PG8_BAR;
;     PG8_STAGE(PG8_SB(1, 0), cB + kstep, voffB); PG8_STAGE(PG8_SA(1, 0), cA + kstep, voffA); PG8_STAGE(PG8_SB(1, 1), cB + hstepB + kstep, voffB);
;     PG8_WAIT_V(6); PG8_BAR;
.LBB0_1252:
	s_andn2_b64 vcc, exec, s[0:1]
	s_cbranch_vccnz .LBB0_1319
	v_readlane_b32 s0, v254, 1
	v_readlane_b32 s1, v254, 2
	s_load_dwordx2 s[20:21], s[0:1], 0xc0
	v_readlane_b32 s0, v254, 5
	s_mov_b32 s1, s27
	v_readlane_b32 s23, v254, 0
	s_waitcnt lgkmcnt(0)
	s_load_dword s22, s[18:19], 0x0
	v_mbcnt_lo_u32_b32 v0, -1, s1
	v_mbcnt_hi_u32_b32 v0, -1, v0
	v_lshl_add_u32 v1, s0, 6, v0
	s_cmpk_gt_u32 s23, 0x1ff
	v_readfirstlane_b32 s29, v1
	s_waitcnt lgkmcnt(0)
	s_mov_b32 s24, s22
	s_cbranch_scc1 .LBB0_1269
	v_ashrrev_i32_e32 v3, 31, v1
	v_lshrrev_b32_e32 v3, 26, v3
	v_lshlrev_b32_e32 v2, 4, v1
	v_add_u32_e32 v3, v1, v3
	v_bfe_i32 v1, v1, 27, 1
	v_lshrrev_b32_e32 v1, 22, v1
	v_add_u32_e32 v1, v2, v1
	v_and_b32_e32 v1, 0xfffffc00, v1
	v_sub_u32_e32 v1, v2, v1
	v_lshrrev_b32_e32 v4, 4, v1
	v_bitop3_b32 v1, v4, v1, 32 bitop3:0x6c
	v_ashrrev_i32_e32 v5, 31, v1
	s_add_u32 s25, s20, 0x61400000
	v_readlane_b32 s0, v254, 57
	v_ashrrev_i32_e32 v3, 6, v3
	v_lshrrev_b32_e32 v5, 26, v5
	s_addc_u32 s26, s21, 0
	s_lshl_b32 s0, s0, 24
	v_lshlrev_b32_e32 v4, 3, v3
	v_add_u32_e32 v5, v1, v5
	v_readlane_b32 s1, v254, 58
	s_add_u32 s0, s20, s0
	v_and_b32_e32 v4, -16, v4
	v_ashrrev_i32_e32 v6, 6, v5
	v_and_b32_e32 v5, 0xc0, v5
	s_addc_u32 s1, s21, 0
	v_add_u32_e32 v4, v6, v4
	v_sub_u32_e32 v1, v1, v5
	s_add_u32 s50, s0, 0x3f200000
	v_lshlrev_b32_e32 v3, 5, v3
	v_ashrrev_i16_sdwa v1, v216, sext(v1) dst_sel:DWORD dst_unused:UNUSED_PAD src0_sel:DWORD src1_sel:BYTE_0
	v_lshlrev_b32_e32 v5, 1, v4
	v_lshrrev_b32_e32 v7, 2, v4
	v_and_b32_e32 v6, 3, v6
	s_mov_b32 s0, 0x1fffe0
	v_and_b32_e32 v3, 32, v3
	v_bfe_i32 v1, v1, 0, 16
	v_and_b32_e32 v5, 24, v5
	v_and_b32_e32 v7, 4, v7
	v_and_or_b32 v6, v4, s0, v6
	v_or3_b32 v5, v6, v7, v5
	v_add_lshl_u32 v1, v3, v1, 1
	v_lshl_add_u32 v206, v4, 11, v1
	v_lshl_add_u32 v208, v5, 11, v1
	v_add_u32_e32 v1, 0x2000, v2
	v_ashrrev_i32_e32 v2, 31, v1
	v_lshrrev_b32_e32 v2, 22, v2
	v_add_u32_e32 v2, v1, v2
	v_ashrrev_i32_e32 v2, 10, v2
	v_mul_i32_i24_e32 v3, 0x400, v2
	v_sub_u32_e32 v1, v1, v3
	v_lshrrev_b32_e32 v3, 4, v1
	v_bitop3_b32 v1, v3, v1, 32 bitop3:0x6c
	v_ashrrev_i32_e32 v4, 31, v1
	v_lshrrev_b32_e32 v4, 26, v4
	v_lshlrev_b32_e32 v3, 3, v2
	v_add_u32_e32 v4, v1, v4
	v_and_b32_e32 v3, -16, v3
	v_ashrrev_i32_e32 v5, 6, v4
	s_addc_u32 s51, s1, 0
	v_add_u32_e32 v3, v5, v3
	v_and_b32_e32 v5, 3, v5
	s_lshl_b32 s1, s23, 5
	v_and_or_b32 v5, v3, s0, v5
	s_and_b32 s0, s23, 0x100
	s_and_b32 s1, s1, 0xe0
	s_lshr_b32 s2, s23, 3
	s_and_b32 s2, s2, 28
	s_or_b32 s3, s1, s0
	v_and_b32_e32 v4, 0xc0, v4
	s_or_b32 s1, s3, s2
	s_lshr_b32 s2, s3, 4
	v_sub_u32_e32 v1, v1, v4
	s_bfe_u32 s0, s23, 0x20003
	s_and_b32 s2, s2, 28
	s_ashr_i32 s41, s29, 6
	v_lshlrev_b32_e32 v2, 5, v2
	v_ashrrev_i16_sdwa v1, v216, sext(v1) dst_sel:DWORD dst_unused:UNUSED_PAD src0_sel:DWORD src1_sel:BYTE_0
	v_lshlrev_b32_e32 v4, 1, v3
	v_lshrrev_b32_e32 v6, 2, v3
	s_or_b32 s2, s2, s0
	v_and_b32_e32 v2, 32, v2
	v_bfe_i32 v1, v1, 0, 16
	v_and_b32_e32 v4, 24, v4
	v_and_b32_e32 v6, 4, v6
	s_ashr_i32 s40, s29, 8
	s_lshl_b32 s52, s41, 10
	s_lshl_b32 s36, s1, 17
	s_lshl_b32 s2, s2, 19
	v_or3_b32 v4, v5, v6, v4
	v_add_lshl_u32 v1, v2, v1, 1
	s_add_u32 s4, s50, s2
	v_lshl_add_u32 v209, v3, 11, v1
	v_lshl_add_u32 v211, v4, 11, v1
	s_addc_u32 s5, s51, 0
	s_add_i32 s53, s52, 0
	s_add_i32 m0, s53, 0x10000
	v_add_u32_e32 v207, 0x40000, v206
	global_load_lds_dwordx4 v208, s[4:5]
	s_add_i32 m0, s53, 0x12000
	s_add_u32 s2, s4, 0x40000
	global_load_lds_dwordx4 v211, s[4:5]
	s_addc_u32 s3, s5, 0
	s_add_i32 m0, s53, 0x14000
	v_add_u32_e32 v210, 0x40000, v209
	global_load_lds_dwordx4 v208, s[2:3]
	s_add_i32 m0, s53, 0x16000
	s_nop 0
	global_load_lds_dwordx4 v211, s[2:3]
	s_add_u32 s2, s25, s36
	s_addc_u32 s3, s26, 0
	s_mov_b32 m0, s53
	s_add_i32 s54, s53, 0x2000
	global_load_lds_dwordx4 v206, s[2:3]
	s_mov_b32 m0, s54
	s_add_i32 s55, s53, 0x4000
	global_load_lds_dwordx4 v209, s[2:3]
	s_mov_b32 m0, s55
	s_add_i32 s56, s53, 0x6000
	global_load_lds_dwordx4 v207, s[2:3]
	v_mov_b32_e32 v1, v210
	s_mov_b32 m0, s56
	s_cmp_eq_u32 s40, 1
	global_load_lds_dwordx4 v1, s[2:3]
	s_cselect_b64 s[36:37], -1, 0
	s_cmp_lg_u32 s40, 1
	s_cbranch_scc1 .LBB0_1256
	s_barrier
.LBB0_1256:
	s_lshr_b32 s1, s1, 2
	v_mov_b32_e32 v96, v208
	s_add_u32 s38, s20, 0x33600000
	s_waitcnt vmcnt(2)
	s_barrier
	s_addc_u32 s39, s21, 0
	v_lshl_add_u64 v[2:3], s[4:5], 0, v[96:97]
	s_add_i32 m0, s53, 0x18000
	v_lshl_add_u64 v[2:3], v[2:3], 0, s[30:31]
	v_mov_b32_e32 v96, v211
	global_load_lds_dwordx4 v[2:3], off
	s_add_i32 m0, s53, 0x1a000
	v_lshl_add_u64 v[2:3], s[4:5], 0, v[96:97]
	v_lshl_add_u64 v[2:3], v[2:3], 0, s[30:31]
	v_mov_b32_e32 v96, v206
	global_load_lds_dwordx4 v[2:3], off
	s_add_i32 s57, s53, 0x8000
	v_lshl_add_u64 v[2:3], s[2:3], 0, v[96:97]
	s_and_b32 s42, s41, 3
	v_lshl_add_u64 v[2:3], v[2:3], 0, s[30:31]
	s_mov_b32 m0, s57
	v_mov_b32_e32 v96, v209
	s_lshl_b32 s41, s40, 13
	s_lshl_b32 s43, s42, 12
	global_load_lds_dwordx4 v[2:3], off
	s_add_i32 s58, s53, 0xa000
	v_lshl_add_u64 v[2:3], s[2:3], 0, v[96:97]
	v_lshl_add_u64 v[2:3], v[2:3], 0, s[30:31]
	s_mov_b32 m0, s58
	s_add_u32 s20, s4, 0x40080
	global_load_lds_dwordx4 v[2:3], off
	s_addc_u32 s21, s5, 0
	s_add_i32 m0, s53, 0x1c000
	v_bfe_u32 v2, v0, 4, 2
	global_load_lds_dwordx4 v208, s[20:21]
	s_add_i32 m0, s53, 0x1e000
	v_lshlrev_b32_e32 v3, 3, v2
	global_load_lds_dwordx4 v211, s[20:21]
	v_and_b32_e32 v1, 15, v0
	v_lshlrev_b32_e32 v2, 4, v2
	v_lshlrev_b32_e32 v0, 2, v0
	v_lshl_or_b32 v212, s40, 6, v1
	v_lshl_or_b32 v1, v1, 6, v2
	v_and_b32_e32 v0, 32, v0
	s_waitcnt vmcnt(6)
	v_bitop3_b32 v2, v1, s41, v0 bitop3:0xde
	s_cmpk_lt_u32 s29, 0x100
	v_bitop3_b32 v213, v1, s43, v0 bitop3:0xde
	s_cselect_b64 s[40:41], -1, 0
	v_lshl_or_b32 v214, s42, 5, v3
	v_or_b32_e32 v215, 16, v212
	v_or_b32_e32 v219, 32, v212
	v_or_b32_e32 v220, 48, v212
	s_mov_b32 s59, 0
	v_add_u32_e32 v221, 0, v2
	s_mov_b64 s[46:47], s[4:5]
	s_mov_b64 s[44:45], s[2:3]
	s_barrier
	s_waitcnt vmcnt(0)
	s_branch .LBB0_1259

; #define PG8_STAGE(bufoff, gbase, voff) do { _Pragma("unroll") for (int _i = 0; _i < 2; ++_i) \
;         __builtin_amdgcn_global_load_lds((const __attribute__((address_space(1))) unsigned*)((const __attribute__((address_space(1))) char*)(gbase) + (unsigned)lnd_v((int)(voff)[_i])), (LAS unsigned*)(lds + (bufoff) + ldsw + _i * 8192), 16, 0, 0); } while (0)
; #define PG8_LDA(dst, b, h) do { _Pragma("unroll") for (int m = 0; m < 4; ++m) _Pragma("unroll") for (int k = 0; k < 2; ++k) dst[m][k] = *(const LAS bf16x8*)(lds + PG8_SA(b, h) + aoff + m * 2048 + k * 1024); } while (0)
; #define PG8_LDB(dst, b, h) do { _Pragma("unroll") for (int n = 0; n < 2; ++n) _Pragma("unroll") for (int k = 0; k < 2; ++k) dst[n][k] = *(const LAS bf16x8*)(lds + PG8_SB(b, h) + boff + n * 2048 + k * 1024); } while (0)
; #define PG8_WAIT_V(n) asm volatile("s_waitcnt vmcnt(" #n ")" ::: "memory")
; #define PG8_WAIT_L(n) asm volatile("s_waitcnt lgkmcnt(" #n ")" ::: "memory")
; #define PG8_BAR __builtin_amdgcn_s_barrier()
; template <class Desc, class Epi>
; __device__ __forceinline__ void gemm_phase(const int wv_, LAS unsigned char* lds, const Desc& d, const Epi& E) {
;     ...
;         for (int t = 0; t < nt; t += 2) {
;             const bool last = (t == nt - 2);
;             unsigned sA0[2], sA1[2];
;             if constexpr (Desc::GATHER) { sA0[0] = last ? voffAn[0] : voffA[0]; sA0[1] = last ? voffAn[1] : voffA[1]; sA1[0] = last ? voffAn1[0] : voffA1[0]; sA1[1] = last ? voffAn1[1] : voffA1[1]; }
;             else { sA0[0] = voffA[0]; sA0[1] = voffA[1]; sA1[0] = voffA1[0]; sA1[1] = voffA1[1]; }
;             const char* a1 = cA + (size_t)(t + 1) * kstep;
;             const char* a2 = last ? nA : cA + (size_t)(t + 2) * kstep; const char* b2 = last ? nB : cB + (size_t)(t + 2) * kstep;
;             const char* a3 = a2 + kstep; const char* b3 = b2 + kstep;
;             PG8_LDB(B0, 0, 0); PG8_LDB(B1, 0, 1); PG8_SCHED; PG8_LDA(At, 0, 0); PG8_STAGE(PG8_SA(1, 1), a1, voffA1);
;             PG8_WAIT_V(8); PG8_WAIT_L(0); PG8_BAR; PG8_MMA(0, 0, At, B0); PG8_MMA(0, 1, At, B1); PG8_BAR; PG8_SCHED;
;             PG8_LDA(At, 0, 1); PG8_STAGE(PG8_SB(0, 0), b2, voffB); PG8_STAGE(PG8_SB(0, 1), b2 + hstepB, voffB); PG8_STAGE(PG8_SA(0, 0), a2, sA0);
;             PG8_WAIT_V(8); PG8_WAIT_L(0); PG8_BAR; PG8_MMA(1, 0, At, B0); PG8_MMA(1, 1, At, B1); PG8_BAR; PG8_SCHED;
.LBB0_1262:
	s_add_u32 s4, s2, 0x80
	s_addc_u32 s5, s3, 0
	s_add_i32 s62, 0, 0x10000
	s_cmp_eq_u32 s61, 12
	s_cselect_b32 s5, s45, s5
	s_cselect_b32 s4, s44, s4
	v_add_u32_e32 v96, s62, v213
	s_cselect_b32 s21, s47, s43
	s_cselect_b32 s20, s46, s29
	s_add_i32 s64, 0, 0x14000
	ds_read_b128 v[130:133], v96
	ds_read_b128 v[134:137], v96 offset:1024
	ds_read_b128 v[138:141], v96 offset:2048
	ds_read_b128 v[142:145], v96 offset:3072
	v_add_u32_e32 v96, s64, v213
	ds_read_b128 v[146:149], v96
	ds_read_b128 v[150:153], v96 offset:1024
	ds_read_b128 v[154:157], v96 offset:2048
	ds_read_b128 v[158:161], v96 offset:3072
	ds_read_b128 v[162:165], v221
	ds_read_b128 v[166:169], v221 offset:1024
	ds_read_b128 v[170:173], v221 offset:2048
	ds_read_b128 v[174:177], v221 offset:3072
	ds_read_b128 v[178:181], v221 offset:4096
	ds_read_b128 v[182:185], v221 offset:5120
	ds_read_b128 v[186:189], v221 offset:6144
	ds_read_b128 v[190:193], v221 offset:7168
	s_add_i32 m0, s53, 0xc000
	s_nop 0
	global_load_lds_dwordx4 v207, s[2:3]
	s_add_i32 m0, s53, 0xe000
	s_nop 0
	global_load_lds_dwordx4 v210, s[2:3]
	s_waitcnt vmcnt(8)
	s_waitcnt lgkmcnt(0)
	s_barrier
	s_waitcnt lgkmcnt(0)
	v_mfma_f32_16x16x32_bf16 v[126:129], v[130:133], v[162:165], v[126:129]
	v_mfma_f32_16x16x32_bf16 v[122:125], v[138:141], v[162:165], v[122:125]
	v_mfma_f32_16x16x32_bf16 v[110:113], v[130:133], v[170:173], v[110:113]
	v_mfma_f32_16x16x32_bf16 v[106:109], v[138:141], v[170:173], v[106:109]
	v_mfma_f32_16x16x32_bf16 v[92:95], v[130:133], v[178:181], v[92:95]
	v_mfma_f32_16x16x32_bf16 v[88:91], v[138:141], v[178:181], v[88:91]
	v_mfma_f32_16x16x32_bf16 v[76:79], v[130:133], v[186:189], v[76:79]
	v_mfma_f32_16x16x32_bf16 v[72:75], v[138:141], v[186:189], v[72:75]
	v_mfma_f32_16x16x32_bf16 v[126:129], v[134:137], v[166:169], v[126:129]
	v_mfma_f32_16x16x32_bf16 v[122:125], v[142:145], v[166:169], v[122:125]
	v_mfma_f32_16x16x32_bf16 v[110:113], v[134:137], v[174:177], v[110:113]
	v_mfma_f32_16x16x32_bf16 v[106:109], v[142:145], v[174:177], v[106:109]
	v_mfma_f32_16x16x32_bf16 v[92:95], v[134:137], v[182:185], v[92:95]
	v_mfma_f32_16x16x32_bf16 v[88:91], v[142:145], v[182:185], v[88:91]
	v_mfma_f32_16x16x32_bf16 v[76:79], v[134:137], v[190:193], v[76:79]
	v_mfma_f32_16x16x32_bf16 v[72:75], v[142:145], v[190:193], v[72:75]
	v_mfma_f32_16x16x32_bf16 v[118:121], v[146:149], v[162:165], v[118:121]
	v_mfma_f32_16x16x32_bf16 v[114:117], v[154:157], v[162:165], v[114:117]
	v_mfma_f32_16x16x32_bf16 v[102:105], v[146:149], v[170:173], v[102:105]
	v_mfma_f32_16x16x32_bf16 v[98:101], v[154:157], v[170:173], v[98:101]
	v_mfma_f32_16x16x32_bf16 v[84:87], v[146:149], v[178:181], v[84:87]
	v_mfma_f32_16x16x32_bf16 v[80:83], v[154:157], v[178:181], v[80:83]
	v_mfma_f32_16x16x32_bf16 v[68:71], v[146:149], v[186:189], v[68:71]
	v_mfma_f32_16x16x32_bf16 v[64:67], v[154:157], v[186:189], v[64:67]
	v_mfma_f32_16x16x32_bf16 v[118:121], v[150:153], v[166:169], v[118:121]
	v_mfma_f32_16x16x32_bf16 v[114:117], v[158:161], v[166:169], v[114:117]
	v_mfma_f32_16x16x32_bf16 v[102:105], v[150:153], v[174:177], v[102:105]
	v_mfma_f32_16x16x32_bf16 v[98:101], v[158:161], v[174:177], v[98:101]
	v_mfma_f32_16x16x32_bf16 v[84:87], v[150:153], v[182:185], v[84:87]
	v_mfma_f32_16x16x32_bf16 v[80:83], v[158:161], v[182:185], v[80:83]
	v_mfma_f32_16x16x32_bf16 v[68:71], v[150:153], v[190:193], v[68:71]
	v_mfma_f32_16x16x32_bf16 v[64:67], v[158:161], v[190:193], v[64:67]
	s_barrier
	s_add_i32 s62, s62, s52
	ds_read_b128 v[162:165], v221 offset:16384
	ds_read_b128 v[166:169], v221 offset:17408
	ds_read_b128 v[170:173], v221 offset:18432
	ds_read_b128 v[174:177], v221 offset:19456
	ds_read_b128 v[178:181], v221 offset:20480
	ds_read_b128 v[182:185], v221 offset:21504
	ds_read_b128 v[186:189], v221 offset:22528
	ds_read_b128 v[190:193], v221 offset:23552
	s_mov_b32 m0, s62
	s_nop 0
	global_load_lds_dwordx4 v208, s[20:21]
	s_add_i32 m0, s62, 0x2000
	s_add_u32 s62, s20, 0x40000
	global_load_lds_dwordx4 v211, s[20:21]
	s_addc_u32 s63, s21, 0
	s_add_i32 s64, s64, s52
	s_mov_b32 m0, s64
	s_nop 0
	global_load_lds_dwordx4 v208, s[62:63]
	s_add_i32 m0, s64, 0x2000
	s_nop 0
	global_load_lds_dwordx4 v211, s[62:63]
	s_mov_b32 m0, s53
	s_nop 0
	global_load_lds_dwordx4 v206, s[4:5]
	s_mov_b32 m0, s54
	s_nop 0
	global_load_lds_dwordx4 v209, s[4:5]
	s_waitcnt vmcnt(8)
	s_waitcnt lgkmcnt(0)
	s_barrier
	s_waitcnt lgkmcnt(0)
	v_mfma_f32_16x16x32_bf16 v[60:63], v[130:133], v[162:165], v[60:63]
	v_mfma_f32_16x16x32_bf16 v[56:59], v[138:141], v[162:165], v[56:59]
	v_mfma_f32_16x16x32_bf16 v[44:47], v[130:133], v[170:173], v[44:47]
	v_mfma_f32_16x16x32_bf16 v[40:43], v[138:141], v[170:173], v[40:43]
	v_mfma_f32_16x16x32_bf16 v[24:27], v[130:133], v[178:181], v[24:27]
	v_mfma_f32_16x16x32_bf16 v[16:19], v[138:141], v[178:181], v[16:19]
	v_mfma_f32_16x16x32_bf16 v[4:7], v[130:133], v[186:189], v[4:7]
	v_mfma_f32_16x16x32_bf16 v[0:3], v[138:141], v[186:189], v[0:3]
	v_mfma_f32_16x16x32_bf16 v[60:63], v[134:137], v[166:169], v[60:63]
	v_mfma_f32_16x16x32_bf16 v[56:59], v[142:145], v[166:169], v[56:59]
	v_mfma_f32_16x16x32_bf16 v[44:47], v[134:137], v[174:177], v[44:47]
	v_mfma_f32_16x16x32_bf16 v[40:43], v[142:145], v[174:177], v[40:43]
	v_mfma_f32_16x16x32_bf16 v[24:27], v[134:137], v[182:185], v[24:27]
	v_mfma_f32_16x16x32_bf16 v[16:19], v[142:145], v[182:185], v[16:19]
	v_mfma_f32_16x16x32_bf16 v[4:7], v[134:137], v[190:193], v[4:7]
	v_mfma_f32_16x16x32_bf16 v[0:3], v[142:145], v[190:193], v[0:3]
	v_mfma_f32_16x16x32_bf16 v[52:55], v[146:149], v[162:165], v[52:55]
	v_mfma_f32_16x16x32_bf16 v[48:51], v[154:157], v[162:165], v[48:51]
	v_mfma_f32_16x16x32_bf16 v[28:31], v[146:149], v[170:173], v[28:31]
	v_mfma_f32_16x16x32_bf16 v[20:23], v[154:157], v[170:173], v[20:23]
	v_mfma_f32_16x16x32_bf16 v[36:39], v[146:149], v[178:181], v[36:39]
	v_mfma_f32_16x16x32_bf16 v[32:35], v[154:157], v[178:181], v[32:35]
	v_mfma_f32_16x16x32_bf16 v[12:15], v[146:149], v[186:189], v[12:15]
	v_mfma_f32_16x16x32_bf16 v[8:11], v[154:157], v[186:189], v[8:11]
	v_mfma_f32_16x16x32_bf16 v[52:55], v[150:153], v[166:169], v[52:55]
	v_mfma_f32_16x16x32_bf16 v[48:51], v[158:161], v[166:169], v[48:51]
	v_mfma_f32_16x16x32_bf16 v[28:31], v[150:153], v[174:177], v[28:31]
	v_mfma_f32_16x16x32_bf16 v[20:23], v[158:161], v[174:177], v[20:23]
	v_mfma_f32_16x16x32_bf16 v[36:39], v[150:153], v[182:185], v[36:39]
	v_mfma_f32_16x16x32_bf16 v[32:35], v[158:161], v[182:185], v[32:35]
	v_mfma_f32_16x16x32_bf16 v[12:15], v[150:153], v[190:193], v[12:15]
	v_mfma_f32_16x16x32_bf16 v[8:11], v[158:161], v[190:193], v[8:11]
	s_barrier
; #define PG8_STAGE(bufoff, gbase, voff) do { _Pragma("unroll") for (int _i = 0; _i < 2; ++_i) \
;         __builtin_amdgcn_global_load_lds((const __attribute__((address_space(1))) unsigned*)((const __attribute__((address_space(1))) char*)(gbase) + (unsigned)lnd_v((int)(voff)[_i])), (LAS unsigned*)(lds + (bufoff) + ldsw + _i * 8192), 16, 0, 0); } while (0)
; #define PG8_LDA(dst, b, h) do { _Pragma("unroll") for (int m = 0; m < 4; ++m) _Pragma("unroll") for (int k = 0; k < 2; ++k) dst[m][k] = *(const LAS bf16x8*)(lds + PG8_SA(b, h) + aoff + m * 2048 + k * 1024); } while (0)
; #define PG8_LDB(dst, b, h) do { _Pragma("unroll") for (int n = 0; n < 2; ++n) _Pragma("unroll") for (int k = 0; k < 2; ++k) dst[n][k] = *(const LAS bf16x8*)(lds + PG8_SB(b, h) + boff + n * 2048 + k * 1024); } while (0)
; #define PG8_MMA(ai, bj, At, Bt) do { __builtin_amdgcn_s_setprio(1); _Pragma("unroll") for (int m = 0; m < 4; ++m) _Pragma("unroll") for (int n = 0; n < 2; ++n) _Pragma("unroll") for (int k = 0; k < 2; ++k) \
;         acc[ai][bj][m][n] = __builtin_amdgcn_mfma_f32_16x16x32_bf16(Bt[n][k], At[m][k], acc[ai][bj][m][n], 0, 0, 0); __builtin_amdgcn_s_setprio(0); } while (0)
; #define PG8_WAIT_V(n) asm volatile("s_waitcnt vmcnt(" #n ")" ::: "memory")
; #define PG8_WAIT_L(n) asm volatile("s_waitcnt lgkmcnt(" #n ")" ::: "memory")
; #define PG8_BAR __builtin_amdgcn_s_barrier()
; #define PG8_SCHED __builtin_amdgcn_sched_barrier(0)
; template <class Desc, class Epi>
; __device__ __forceinline__ void gemm_phase(const int wv_, LAS unsigned char* lds, const Desc& d, const Epi& E) {
;     ...
;             PG8_LDB(B0, 1, 0); PG8_LDB(B1, 1, 1); PG8_SCHED; PG8_LDA(At, 1, 0); PG8_STAGE(PG8_SA(0, 1), a2, sA1);
;             PG8_WAIT_V(8); PG8_WAIT_L(0); PG8_BAR; PG8_MMA(0, 0, At, B0); PG8_MMA(0, 1, At, B1); PG8_BAR; PG8_SCHED;
	s_add_i32 s62, 0, 0x18000
	v_add_u32_e32 v96, s62, v213
	s_add_i32 s63, 0, 0x1c000
	ds_read_b128 v[130:133], v96
	ds_read_b128 v[134:137], v96 offset:1024
	ds_read_b128 v[138:141], v96 offset:2048
	ds_read_b128 v[142:145], v96 offset:3072
	v_add_u32_e32 v96, s63, v213
	ds_read_b128 v[146:149], v96
	ds_read_b128 v[150:153], v96 offset:1024
	ds_read_b128 v[154:157], v96 offset:2048
	ds_read_b128 v[158:161], v96 offset:3072
	s_mov_b32 m0, s55
	ds_read_b128 v[162:165], v221 offset:32768
	ds_read_b128 v[166:169], v221 offset:33792
	ds_read_b128 v[170:173], v221 offset:34816
	ds_read_b128 v[174:177], v221 offset:35840
	ds_read_b128 v[178:181], v221 offset:36864
	ds_read_b128 v[182:185], v221 offset:37888
	ds_read_b128 v[186:189], v221 offset:38912
	ds_read_b128 v[190:193], v221 offset:39936
	s_nop 0
	global_load_lds_dwordx4 v207, s[4:5]
	s_mov_b32 m0, s56
	s_nop 0
	global_load_lds_dwordx4 v210, s[4:5]
	s_waitcnt vmcnt(8)
	s_waitcnt lgkmcnt(0)
	s_barrier
	s_waitcnt lgkmcnt(0)
	v_mfma_f32_16x16x32_bf16 v[126:129], v[130:133], v[162:165], v[126:129]
	v_mfma_f32_16x16x32_bf16 v[122:125], v[138:141], v[162:165], v[122:125]
	v_mfma_f32_16x16x32_bf16 v[110:113], v[130:133], v[170:173], v[110:113]
	v_mfma_f32_16x16x32_bf16 v[106:109], v[138:141], v[170:173], v[106:109]
	v_mfma_f32_16x16x32_bf16 v[92:95], v[130:133], v[178:181], v[92:95]
	v_mfma_f32_16x16x32_bf16 v[88:91], v[138:141], v[178:181], v[88:91]
	v_mfma_f32_16x16x32_bf16 v[76:79], v[130:133], v[186:189], v[76:79]
	v_mfma_f32_16x16x32_bf16 v[72:75], v[138:141], v[186:189], v[72:75]
	v_mfma_f32_16x16x32_bf16 v[126:129], v[134:137], v[166:169], v[126:129]
	v_mfma_f32_16x16x32_bf16 v[122:125], v[142:145], v[166:169], v[122:125]
	v_mfma_f32_16x16x32_bf16 v[110:113], v[134:137], v[174:177], v[110:113]
	v_mfma_f32_16x16x32_bf16 v[106:109], v[142:145], v[174:177], v[106:109]
	v_mfma_f32_16x16x32_bf16 v[92:95], v[134:137], v[182:185], v[92:95]
	v_mfma_f32_16x16x32_bf16 v[88:91], v[142:145], v[182:185], v[88:91]
	v_mfma_f32_16x16x32_bf16 v[76:79], v[134:137], v[190:193], v[76:79]
	v_mfma_f32_16x16x32_bf16 v[72:75], v[142:145], v[190:193], v[72:75]
	v_mfma_f32_16x16x32_bf16 v[118:121], v[146:149], v[162:165], v[118:121]
	v_mfma_f32_16x16x32_bf16 v[114:117], v[154:157], v[162:165], v[114:117]
	v_mfma_f32_16x16x32_bf16 v[102:105], v[146:149], v[170:173], v[102:105]
	v_mfma_f32_16x16x32_bf16 v[98:101], v[154:157], v[170:173], v[98:101]
	v_mfma_f32_16x16x32_bf16 v[84:87], v[146:149], v[178:181], v[84:87]
	v_mfma_f32_16x16x32_bf16 v[80:83], v[154:157], v[178:181], v[80:83]
	v_mfma_f32_16x16x32_bf16 v[68:71], v[146:149], v[186:189], v[68:71]
	v_mfma_f32_16x16x32_bf16 v[64:67], v[154:157], v[186:189], v[64:67]
	v_mfma_f32_16x16x32_bf16 v[118:121], v[150:153], v[166:169], v[118:121]
	v_mfma_f32_16x16x32_bf16 v[114:117], v[158:161], v[166:169], v[114:117]
	v_mfma_f32_16x16x32_bf16 v[102:105], v[150:153], v[174:177], v[102:105]
	v_mfma_f32_16x16x32_bf16 v[98:101], v[158:161], v[174:177], v[98:101]
	v_mfma_f32_16x16x32_bf16 v[84:87], v[150:153], v[182:185], v[84:87]
	v_mfma_f32_16x16x32_bf16 v[80:83], v[158:161], v[182:185], v[80:83]
	v_mfma_f32_16x16x32_bf16 v[68:71], v[150:153], v[190:193], v[68:71]
	v_mfma_f32_16x16x32_bf16 v[64:67], v[158:161], v[190:193], v[64:67]
	s_barrier
; #define PG8_STAGE(bufoff, gbase, voff) do { _Pragma("unroll") for (int _i = 0; _i < 2; ++_i) \
;         __builtin_amdgcn_global_load_lds((const __attribute__((address_space(1))) unsigned*)((const __attribute__((address_space(1))) char*)(gbase) + (unsigned)lnd_v((int)(voff)[_i])), (LAS unsigned*)(lds + (bufoff) + ldsw + _i * 8192), 16, 0, 0); } while (0)
; #define PG8_LDA(dst, b, h) do { _Pragma("unroll") for (int m = 0; m < 4; ++m) _Pragma("unroll") for (int k = 0; k < 2; ++k) dst[m][k] = *(const LAS bf16x8*)(lds + PG8_SA(b, h) + aoff + m * 2048 + k * 1024); } while (0)
; #define PG8_MMA(ai, bj, At, Bt) do { __builtin_amdgcn_s_setprio(1); _Pragma("unroll") for (int m = 0; m < 4; ++m) _Pragma("unroll") for (int n = 0; n < 2; ++n) _Pragma("unroll") for (int k = 0; k < 2; ++k) \
;         acc[ai][bj][m][n] = __builtin_amdgcn_mfma_f32_16x16x32_bf16(Bt[n][k], At[m][k], acc[ai][bj][m][n], 0, 0, 0); __builtin_amdgcn_s_setprio(0); } while (0)
; #define PG8_WAIT_V(n) asm volatile("s_waitcnt vmcnt(" #n ")" ::: "memory")
; #define PG8_WAIT_L(n) asm volatile("s_waitcnt lgkmcnt(" #n ")" ::: "memory")
; #define PG8_BAR __builtin_amdgcn_s_barrier()
; #define PG8_SCHED __builtin_amdgcn_sched_barrier(0)
; template <class Desc, class Epi>
; __device__ __forceinline__ void gemm_phase(const int wv_, LAS unsigned char* lds, const Desc& d, const Epi& E) {
;     ...
;             PG8_LDA(At, 1, 1); PG8_STAGE(PG8_SB(1, 0), b3, voffB); PG8_STAGE(PG8_SB(1, 1), b3 + hstepB, voffB); PG8_STAGE(PG8_SA(1, 0), a3, sA0);
;             PG8_WAIT_V(8); PG8_WAIT_L(0); PG8_BAR; PG8_MMA(1, 0, At, B0); PG8_MMA(1, 1, At, B1); PG8_BAR; PG8_SCHED;
;         }
;         if (wr == 0) PG8_BAR;
	v_mov_b32_e32 v96, v208
	ds_read_b128 v[162:165], v221 offset:49152
	ds_read_b128 v[166:169], v221 offset:50176
	ds_read_b128 v[170:173], v221 offset:51200
	ds_read_b128 v[174:177], v221 offset:52224
	ds_read_b128 v[178:181], v221 offset:53248
	ds_read_b128 v[182:185], v221 offset:54272
	ds_read_b128 v[186:189], v221 offset:55296
	ds_read_b128 v[190:193], v221 offset:56320
	s_add_i32 s62, s62, s52
	v_lshl_add_u64 v[194:195], s[20:21], 0, v[96:97]
	v_lshl_add_u64 v[194:195], v[194:195], 0, s[30:31]
	s_mov_b32 m0, s62
	v_mov_b32_e32 v96, v211
	global_load_lds_dwordx4 v[194:195], off
	s_add_i32 m0, s62, 0x2000
	s_nop 0
	v_lshl_add_u64 v[194:195], s[20:21], 0, v[96:97]
	s_add_u32 s20, s20, 0x40080
	v_lshl_add_u64 v[194:195], v[194:195], 0, s[30:31]
	s_addc_u32 s21, s21, 0
	s_add_i32 s62, s63, s52
	global_load_lds_dwordx4 v[194:195], off
	s_mov_b32 m0, s62
	s_nop 0
	global_load_lds_dwordx4 v208, s[20:21]
	s_add_i32 m0, s62, 0x2000
	s_nop 0
	global_load_lds_dwordx4 v211, s[20:21]
	v_mov_b32_e32 v96, v206
	s_mov_b32 m0, s57
	v_lshl_add_u64 v[194:195], s[4:5], 0, v[96:97]
	v_lshl_add_u64 v[194:195], v[194:195], 0, s[30:31]
	v_mov_b32_e32 v96, v209
	global_load_lds_dwordx4 v[194:195], off
	s_mov_b32 m0, s58
	v_lshl_add_u64 v[194:195], s[4:5], 0, v[96:97]
	v_lshl_add_u64 v[194:195], v[194:195], 0, s[30:31]
	global_load_lds_dwordx4 v[194:195], off
	s_waitcnt vmcnt(8)
	s_waitcnt lgkmcnt(0)
	s_barrier
	s_waitcnt lgkmcnt(0)
	v_mfma_f32_16x16x32_bf16 v[60:63], v[130:133], v[162:165], v[60:63]
	v_mfma_f32_16x16x32_bf16 v[56:59], v[138:141], v[162:165], v[56:59]
	v_mfma_f32_16x16x32_bf16 v[44:47], v[130:133], v[170:173], v[44:47]
	v_mfma_f32_16x16x32_bf16 v[40:43], v[138:141], v[170:173], v[40:43]
	v_mfma_f32_16x16x32_bf16 v[24:27], v[130:133], v[178:181], v[24:27]
	v_mfma_f32_16x16x32_bf16 v[16:19], v[138:141], v[178:181], v[16:19]
	v_mfma_f32_16x16x32_bf16 v[4:7], v[130:133], v[186:189], v[4:7]
	v_mfma_f32_16x16x32_bf16 v[0:3], v[138:141], v[186:189], v[0:3]
	v_mfma_f32_16x16x32_bf16 v[60:63], v[134:137], v[166:169], v[60:63]
	v_mfma_f32_16x16x32_bf16 v[56:59], v[142:145], v[166:169], v[56:59]
	v_mfma_f32_16x16x32_bf16 v[44:47], v[134:137], v[174:177], v[44:47]
	v_mfma_f32_16x16x32_bf16 v[40:43], v[142:145], v[174:177], v[40:43]
	v_mfma_f32_16x16x32_bf16 v[24:27], v[134:137], v[182:185], v[24:27]
	v_mfma_f32_16x16x32_bf16 v[16:19], v[142:145], v[182:185], v[16:19]
	v_mfma_f32_16x16x32_bf16 v[4:7], v[134:137], v[190:193], v[4:7]
	v_mfma_f32_16x16x32_bf16 v[0:3], v[142:145], v[190:193], v[0:3]
	v_mfma_f32_16x16x32_bf16 v[52:55], v[146:149], v[162:165], v[52:55]
	v_mfma_f32_16x16x32_bf16 v[48:51], v[154:157], v[162:165], v[48:51]
	v_mfma_f32_16x16x32_bf16 v[28:31], v[146:149], v[170:173], v[28:31]
	v_mfma_f32_16x16x32_bf16 v[20:23], v[154:157], v[170:173], v[20:23]
	v_mfma_f32_16x16x32_bf16 v[36:39], v[146:149], v[178:181], v[36:39]
	v_mfma_f32_16x16x32_bf16 v[32:35], v[154:157], v[178:181], v[32:35]
	v_mfma_f32_16x16x32_bf16 v[12:15], v[146:149], v[186:189], v[12:15]
	v_mfma_f32_16x16x32_bf16 v[8:11], v[154:157], v[186:189], v[8:11]
	v_mfma_f32_16x16x32_bf16 v[52:55], v[150:153], v[166:169], v[52:55]
	v_mfma_f32_16x16x32_bf16 v[48:51], v[158:161], v[166:169], v[48:51]
	v_mfma_f32_16x16x32_bf16 v[28:31], v[150:153], v[174:177], v[28:31]
	v_mfma_f32_16x16x32_bf16 v[20:23], v[158:161], v[174:177], v[20:23]
	v_mfma_f32_16x16x32_bf16 v[36:39], v[150:153], v[182:185], v[36:39]
	v_mfma_f32_16x16x32_bf16 v[32:35], v[158:161], v[182:185], v[32:35]
	v_mfma_f32_16x16x32_bf16 v[12:15], v[150:153], v[190:193], v[12:15]
	v_mfma_f32_16x16x32_bf16 v[8:11], v[158:161], v[190:193], v[8:11]
	s_barrier
	s_add_i32 s61, s61, 2
	s_add_u32 s2, s2, 0x100
	s_addc_u32 s3, s3, 0
	s_add_u32 s29, s29, 0x100
	s_addc_u32 s43, s43, 0
	s_cmp_gt_u32 s61, 13
	s_cbranch_scc0 .LBB0_1262
	s_and_b64 vcc, exec, s[40:41]
	s_cbranch_vccz .LBB0_1265
	s_barrier

; #define PG8_STAGE(bufoff, gbase, voff) do { _Pragma("unroll") for (int _i = 0; _i < 2; ++_i) \
;         __builtin_amdgcn_global_load_lds((const __attribute__((address_space(1))) unsigned*)((const __attribute__((address_space(1))) char*)(gbase) + (unsigned)lnd_v((int)(voff)[_i])), (LAS unsigned*)(lds + (bufoff) + ldsw + _i * 8192), 16, 0, 0); } while (0)
; #define PG8_WAIT_V(n) asm volatile("s_waitcnt vmcnt(" #n ")" ::: "memory")
; #define PG8_BAR __builtin_amdgcn_s_barrier()
; template <class Desc, class Epi>
; __device__ __forceinline__ void gemm_phase(const int wv_, LAS unsigned char* lds, const Desc& d, const Epi& E) {
;     ...
; #pragma unroll
;     for (int i = 0; i < 2; ++i) { int R, C; stage_rc(tid * 16 + i * 8192, R, C); const int Rb = (R & ~31) + perm32(R & 31); Rr[i] = R; Cc[i] = C;
;         voffA[i] = (unsigned)(R * d.lda + C) * 2u; voffA1[i] = voffA[i] + (unsigned)hstepA; voffB[i] = (unsigned)(Rb * d.ldb + C) * 2u; }
;     ...
;     PG8_STAGE(PG8_SB(0, 0), cB, voffB); PG8_STAGE(PG8_SB(0, 1), cB + hstepB, voffB); PG8_STAGE(PG8_SA(0, 0), cA, voffA); PG8_STAGE(PG8_SA(0, 1), cA, voffA1);
;     if (wr == 1) PG8_BAR;
;     PG8_WAIT_V(2); PG8_BAR;
;     PG8_STAGE(PG8_SB(1, 0), cB + kstep, voffB); PG8_STAGE(PG8_SA(1, 0), cA + kstep, voffA); PG8_STAGE(PG8_SB(1, 1), cB + hstepB + kstep, voffB);
;     PG8_WAIT_V(6); PG8_BAR;
.LBB0_1473:
	s_or_b64 exec, exec, s[4:5]
	v_ashrrev_i32_e32 v3, 31, v1
	v_lshrrev_b32_e32 v3, 26, v3
	v_lshlrev_b32_e32 v2, 4, v1
	v_add_u32_e32 v3, v1, v3
	v_bfe_i32 v1, v1, 27, 1
	v_lshrrev_b32_e32 v1, 22, v1
	v_add_u32_e32 v1, v2, v1
	v_and_b32_e32 v1, 0xfffffc00, v1
	v_sub_u32_e32 v1, v2, v1
	v_lshrrev_b32_e32 v4, 4, v1
	v_bitop3_b32 v1, v4, v1, 32 bitop3:0x6c
	v_ashrrev_i32_e32 v5, 31, v1
	v_ashrrev_i32_e32 v3, 6, v3
	v_lshrrev_b32_e32 v5, 26, v5
	v_lshlrev_b32_e32 v4, 3, v3
	v_add_u32_e32 v5, v1, v5
	v_and_b32_e32 v4, -16, v4
	v_ashrrev_i32_e32 v6, 6, v5
	v_and_b32_e32 v5, 0xc0, v5
	v_add_u32_e32 v4, v6, v4
	v_sub_u32_e32 v1, v1, v5
	v_lshlrev_b32_e32 v3, 5, v3
	v_ashrrev_i16_sdwa v1, v216, sext(v1) dst_sel:DWORD dst_unused:UNUSED_PAD src0_sel:DWORD src1_sel:BYTE_0
	v_lshlrev_b32_e32 v5, 1, v4
	v_lshrrev_b32_e32 v7, 2, v4
	v_and_b32_e32 v6, 3, v6
	s_mov_b32 s0, 0x1fffe0
	v_and_b32_e32 v3, 32, v3
	v_bfe_i32 v1, v1, 0, 16
	v_and_b32_e32 v5, 24, v5
	v_and_b32_e32 v7, 4, v7
	v_and_or_b32 v6, v4, s0, v6
	v_or3_b32 v5, v6, v7, v5
	v_add_lshl_u32 v1, v3, v1, 1
	v_lshl_add_u32 v132, v4, 11, v1
	v_lshl_add_u32 v134, v5, 11, v1
	v_add_u32_e32 v1, 0x2000, v2
	v_ashrrev_i32_e32 v2, 31, v1
	v_lshrrev_b32_e32 v2, 22, v2
	v_add_u32_e32 v2, v1, v2
	v_ashrrev_i32_e32 v2, 10, v2
	v_mul_i32_i24_e32 v3, 0x400, v2
	v_sub_u32_e32 v1, v1, v3
	v_lshrrev_b32_e32 v3, 4, v1
	v_bitop3_b32 v1, v3, v1, 32 bitop3:0x6c
	v_ashrrev_i32_e32 v4, 31, v1
	v_lshrrev_b32_e32 v4, 26, v4
	v_lshlrev_b32_e32 v3, 3, v2
	v_add_u32_e32 v4, v1, v4
	s_add_u32 s55, s2, 0x2e00000
	v_and_b32_e32 v3, -16, v3
	v_ashrrev_i32_e32 v5, 6, v4
	s_addc_u32 s56, s3, 0
	v_add_u32_e32 v3, v5, v3
	v_and_b32_e32 v5, 3, v5
	s_add_u32 s57, s2, 0x3a200000
	v_and_or_b32 v5, v3, s0, v5
	v_readlane_b32 s0, v254, 57
	s_addc_u32 s58, s3, 0
	s_ashr_i32 s5, s20, 6
	v_readlane_b32 s1, v254, 58
	s_add_i32 s26, s0, 1
	s_ashr_i32 s4, s20, 8
	s_lshl_b32 s59, s5, 10
	s_lshl_b64 s[24:25], s[26:27], 21
	s_lshl_b64 s[36:37], s[26:27], 22
	s_bfe_u32 s1, s21, 0x30004
	s_bfe_u32 s0, s21, 0x20002
	s_and_b32 s22, s21, 3
	s_add_u32 s23, s55, s24
	s_addc_u32 s24, s56, s25
	s_add_u32 s25, s57, s36
	s_addc_u32 s29, s58, s37
	s_lshl_b32 s36, s1, 19
	v_and_b32_e32 v4, 0xc0, v4
	s_add_u32 s25, s25, s36
	v_sub_u32_e32 v1, v1, v4
	s_addc_u32 s29, s29, 0
	s_lshl_b32 s36, s22, 19
	v_lshlrev_b32_e32 v2, 5, v2
	v_ashrrev_i16_sdwa v1, v216, sext(v1) dst_sel:DWORD dst_unused:UNUSED_PAD src0_sel:DWORD src1_sel:BYTE_0
	v_lshlrev_b32_e32 v4, 1, v3
	v_lshrrev_b32_e32 v6, 2, v3
	s_add_u32 s23, s23, s36
	v_and_b32_e32 v2, 32, v2
	v_bfe_i32 v1, v1, 0, 16
	v_and_b32_e32 v4, 24, v4
	v_and_b32_e32 v6, 4, v6
	s_addc_u32 s36, s24, 0
	s_lshl_b32 s37, s0, 9
	v_or3_b32 v4, v5, v6, v4
	v_add_lshl_u32 v1, v2, v1, 1
	s_add_u32 s48, s25, s37
	v_lshl_add_u32 v135, v3, 11, v1
	v_lshl_add_u32 v137, v4, 11, v1
	s_addc_u32 s49, s29, 0
	s_add_i32 s60, s59, 0
	s_waitcnt vmcnt(0) lgkmcnt(0)
	s_barrier
	s_add_i32 m0, s60, 0x10000
	v_add_u32_e32 v133, 0x40000, v132
	global_load_lds_dwordx4 v134, s[48:49]
	s_add_i32 m0, s60, 0x12000
	s_add_u32 s24, s48, 0x40000
	global_load_lds_dwordx4 v137, s[48:49]
	s_addc_u32 s25, s49, 0
	s_add_i32 m0, s60, 0x14000
	v_add_u32_e32 v136, 0x40000, v135
	global_load_lds_dwordx4 v134, s[24:25]
	s_add_i32 m0, s60, 0x16000
	s_add_u32 s50, s23, s37
	global_load_lds_dwordx4 v137, s[24:25]
	s_addc_u32 s51, s36, 0
	s_mov_b32 m0, s60
	s_add_i32 s61, s60, 0x2000
	global_load_lds_dwordx4 v132, s[50:51]
	s_mov_b32 m0, s61
	s_add_i32 s62, s60, 0x4000
	global_load_lds_dwordx4 v135, s[50:51]
	s_mov_b32 m0, s62
	s_add_i32 s63, s60, 0x6000
	global_load_lds_dwordx4 v133, s[50:51]
	v_mov_b32_e32 v1, v136
	s_mov_b32 m0, s63
	s_cmp_eq_u32 s4, 1
	global_load_lds_dwordx4 v1, s[50:51]
	s_cselect_b64 s[36:37], -1, 0
	s_and_b64 vcc, exec, s[36:37]
	s_cbranch_vccz .LBB0_1475
	s_barrier
.LBB0_1475:
	s_lshl_b32 s23, s26, 5
	s_lshl_b32 s1, s1, 2
	s_or_b32 s1, s1, s23
	s_or_b32 s1, s1, s22
	v_mov_b32_e32 v96, v134
	s_add_u32 s38, s2, 0x3f200000
	s_waitcnt vmcnt(2)
	s_barrier
	s_addc_u32 s39, s3, 0
	v_lshl_add_u64 v[2:3], s[48:49], 0, v[96:97]
	s_add_i32 m0, s60, 0x18000
	v_lshl_add_u64 v[2:3], v[2:3], 0, s[30:31]
	v_mov_b32_e32 v96, v137
	global_load_lds_dwordx4 v[2:3], off
	s_lshl_b32 s2, s5, 5
	v_lshl_add_u64 v[2:3], s[48:49], 0, v[96:97]
	v_lshl_add_u64 v[2:3], v[2:3], 0, s[30:31]
	s_add_i32 m0, s60, 0x1a000
	v_mov_b32_e32 v96, v132
	s_and_b32 s5, s2, 0x60
	v_readlane_b32 s2, v254, 57
	global_load_lds_dwordx4 v[2:3], off
	s_add_i32 s65, s60, 0x8000
	v_lshl_add_u64 v[2:3], s[50:51], 0, v[96:97]
	s_lshl_b32 s64, s2, 7
	v_lshl_add_u64 v[2:3], v[2:3], 0, s[30:31]
	s_mov_b32 m0, s65
	v_mov_b32_e32 v96, v135
	s_add_i32 s26, s21, 0xffffff80
	s_lshl_b32 s21, s4, 13
	s_lshl_b32 s22, s5, 7
	s_addk_i32 s64, 0x80
	global_load_lds_dwordx4 v[2:3], off
	s_add_i32 s66, s60, 0xa000
	v_lshl_add_u64 v[2:3], s[50:51], 0, v[96:97]
	v_readlane_b32 s3, v254, 58
	v_lshl_add_u64 v[2:3], v[2:3], 0, s[30:31]
	s_mov_b32 m0, s66
	s_add_u32 s2, s48, 0x40080
	global_load_lds_dwordx4 v[2:3], off
	s_addc_u32 s3, s49, 0
	s_add_i32 m0, s60, 0x1c000
	v_lshrrev_b32_e32 v2, 1, v0
	global_load_lds_dwordx4 v134, s[2:3]
	s_add_i32 m0, s60, 0x1e000
	v_and_b32_e32 v2, 24, v2
	global_load_lds_dwordx4 v137, s[2:3]
	v_and_b32_e32 v1, 15, v0
	v_lshl_or_b32 v138, s4, 6, v1
	v_lshlrev_b32_e32 v3, 1, v2
	v_lshl_or_b32 v1, v1, 6, v3
	v_lshlrev_b32_e32 v3, 2, v138
	v_and_b32_e32 v4, 32, v3
	v_lshlrev_b32_e32 v0, 2, v0
	s_waitcnt vmcnt(6)
	s_cmpk_lt_u32 s20, 0x100
	v_bitop3_b32 v4, v1, s21, v4 bitop3:0xde
	v_and_b32_e32 v0, 32, v0
	s_cselect_b64 s[40:41], -1, 0
	s_add_i32 s2, 0, 0x20000
	v_bitop3_b32 v139, v1, s22, v0 bitop3:0xde
	v_or_b32_e32 v140, 16, v138
	v_or_b32_e32 v141, 32, v138
	v_or_b32_e32 v142, 48, v138
	v_add_u32_e32 v143, 0x80, v138
	v_add_u32_e32 v144, 0x90, v138
	v_add_u32_e32 v145, 0xa0, v138
	v_add_u32_e32 v146, 0xb0, v138
	v_or_b32_e32 v147, s5, v2
	v_add_u32_e32 v148, s2, v3
	s_mov_b32 s70, 0
	v_add_u32_e32 v149, 0, v4
	s_mov_b64 s[44:45], s[48:49]
	s_mov_b64 s[42:43], s[50:51]
	s_barrier
	s_waitcnt vmcnt(0)
	s_branch .LBB0_1478

; #define PG8_STAGE(bufoff, gbase, voff) do { _Pragma("unroll") for (int _i = 0; _i < 2; ++_i) \
;         __builtin_amdgcn_global_load_lds((const __attribute__((address_space(1))) unsigned*)((const __attribute__((address_space(1))) char*)(gbase) + (unsigned)lnd_v((int)(voff)[_i])), (LAS unsigned*)(lds + (bufoff) + ldsw + _i * 8192), 16, 0, 0); } while (0)
; #define PG8_LDA(dst, b, h) do { _Pragma("unroll") for (int m = 0; m < 4; ++m) _Pragma("unroll") for (int k = 0; k < 2; ++k) dst[m][k] = *(const LAS bf16x8*)(lds + PG8_SA(b, h) + aoff + m * 2048 + k * 1024); } while (0)
; #define PG8_LDB(dst, b, h) do { _Pragma("unroll") for (int n = 0; n < 2; ++n) _Pragma("unroll") for (int k = 0; k < 2; ++k) dst[n][k] = *(const LAS bf16x8*)(lds + PG8_SB(b, h) + boff + n * 2048 + k * 1024); } while (0)
; #define PG8_WAIT_V(n) asm volatile("s_waitcnt vmcnt(" #n ")" ::: "memory")
; #define PG8_WAIT_L(n) asm volatile("s_waitcnt lgkmcnt(" #n ")" ::: "memory")
; #define PG8_BAR __builtin_amdgcn_s_barrier()
; template <class Desc, class Epi>
; __device__ __forceinline__ void gemm_phase(const int wv_, LAS unsigned char* lds, const Desc& d, const Epi& E) {
;     ...
;         const char* nA = has_next ? (const char*)nxt.a : cA; const char* nB = has_next ? (const char*)nxt.b : cB;
;         for (int t = 0; t < nt; t += 2) {
;             const bool last = (t == nt - 2);
;             unsigned sA0[2], sA1[2];
;             if constexpr (Desc::GATHER) { sA0[0] = last ? voffAn[0] : voffA[0]; sA0[1] = last ? voffAn[1] : voffA[1]; sA1[0] = last ? voffAn1[0] : voffA1[0]; sA1[1] = last ? voffAn1[1] : voffA1[1]; }
;             else { sA0[0] = voffA[0]; sA0[1] = voffA[1]; sA1[0] = voffA1[0]; sA1[1] = voffA1[1]; }
;             const char* a1 = cA + (size_t)(t + 1) * kstep;
;             const char* a2 = last ? nA : cA + (size_t)(t + 2) * kstep; const char* b2 = last ? nB : cB + (size_t)(t + 2) * kstep;
;             const char* a3 = a2 + kstep; const char* b3 = b2 + kstep;
;             PG8_LDB(B0, 0, 0); PG8_LDB(B1, 0, 1); PG8_SCHED; PG8_LDA(At, 0, 0); PG8_STAGE(PG8_SA(1, 1), a1, voffA1);
;             PG8_WAIT_V(8); PG8_WAIT_L(0); PG8_BAR; PG8_MMA(0, 0, At, B0); PG8_MMA(0, 1, At, B1); PG8_BAR; PG8_SCHED;
;             PG8_LDA(At, 0, 1); PG8_STAGE(PG8_SB(0, 0), b2, voffB); PG8_STAGE(PG8_SB(0, 1), b2 + hstepB, voffB); PG8_STAGE(PG8_SA(0, 0), a2, sA0);
.LBB0_1481:
	s_add_u32 s52, s50, s22
	s_addc_u32 s53, s51, 0
	s_add_u32 s23, s52, 0x100
	s_addc_u32 s24, s53, 0
	s_and_b64 s[4:5], s[20:21], exec
	s_cselect_b32 s4, s42, s23
	s_cselect_b32 s5, s43, s24
	s_add_u32 s22, s48, s22
	s_addc_u32 s23, s49, 0
	s_add_u32 s22, s22, 0x100
	s_addc_u32 s23, s23, 0
	s_add_i32 s77, 0, 0x10000
	s_and_b64 s[20:21], s[20:21], exec
	s_cselect_b32 s21, s45, s23
	s_cselect_b32 s20, s44, s22
	s_add_i32 s23, 0, 0x14000
	v_add_u32_e32 v96, s77, v139
	s_add_i32 s79, s77, s59
	ds_read_b128 v[150:153], v96
	ds_read_b128 v[154:157], v96 offset:1024
	ds_read_b128 v[158:161], v96 offset:2048
	ds_read_b128 v[162:165], v96 offset:3072
	v_add_u32_e32 v96, s23, v139
	s_add_i32 m0, s60, 0xc000
	s_add_i32 s80, s60, 0xe000
	s_add_i32 s75, s79, 0x2000
	ds_read_b128 v[166:169], v96
	ds_read_b128 v[170:173], v96 offset:1024
	ds_read_b128 v[174:177], v96 offset:2048
	ds_read_b128 v[178:181], v96 offset:3072
	s_add_u32 s24, s20, 0x40000
	s_addc_u32 s25, s21, 0
	s_add_i32 s73, 0, 0x18000
	s_add_i32 s76, s23, s59
	s_add_i32 s71, s73, s59
	s_add_i32 s74, s76, 0x2000
	s_add_i32 s72, 0, 0x1c000
	s_add_i32 s29, s71, 0x2000
	s_add_u32 s22, s20, 0x40080
	s_addc_u32 s23, s21, 0
	s_add_i32 s78, s72, s59
	s_add_i32 s77, s78, 0x2000
	v_mov_b32_e32 v96, v133
	ds_read_b128 v[182:185], v149
	ds_read_b128 v[186:189], v149 offset:1024
	ds_read_b128 v[190:193], v149 offset:2048
	ds_read_b128 v[194:197], v149 offset:3072
	ds_read_b128 v[198:201], v149 offset:4096
	ds_read_b128 v[202:205], v149 offset:5120
	ds_read_b128 v[206:209], v149 offset:6144
	ds_read_b128 v[210:213], v149 offset:7168
	s_nop 0
	v_lshl_add_u64 v[130:131], s[52:53], 0, v[96:97]
	v_lshl_add_u64 v[130:131], v[130:131], 0, s[30:31]
	v_mov_b32_e32 v96, v136
	global_load_lds_dwordx4 v[130:131], off
	s_mov_b32 m0, s80
	v_lshl_add_u64 v[130:131], s[52:53], 0, v[96:97]
	v_lshl_add_u64 v[130:131], v[130:131], 0, s[30:31]
	global_load_lds_dwordx4 v[130:131], off
	s_waitcnt vmcnt(8)
	s_waitcnt lgkmcnt(0)
	s_barrier
	s_waitcnt lgkmcnt(0)
	v_mfma_f32_16x16x32_bf16 v[126:129], v[150:153], v[182:185], v[126:129]
	v_mfma_f32_16x16x32_bf16 v[122:125], v[158:161], v[182:185], v[122:125]
	v_mfma_f32_16x16x32_bf16 v[110:113], v[150:153], v[190:193], v[110:113]
	v_mfma_f32_16x16x32_bf16 v[106:109], v[158:161], v[190:193], v[106:109]
	v_mfma_f32_16x16x32_bf16 v[92:95], v[150:153], v[198:201], v[92:95]
	v_mfma_f32_16x16x32_bf16 v[88:91], v[158:161], v[198:201], v[88:91]
	v_mfma_f32_16x16x32_bf16 v[76:79], v[150:153], v[206:209], v[76:79]
	v_mfma_f32_16x16x32_bf16 v[72:75], v[158:161], v[206:209], v[72:75]
	v_mfma_f32_16x16x32_bf16 v[126:129], v[154:157], v[186:189], v[126:129]
	v_mfma_f32_16x16x32_bf16 v[122:125], v[162:165], v[186:189], v[122:125]
	v_mfma_f32_16x16x32_bf16 v[110:113], v[154:157], v[194:197], v[110:113]
	v_mfma_f32_16x16x32_bf16 v[106:109], v[162:165], v[194:197], v[106:109]
	v_mfma_f32_16x16x32_bf16 v[92:95], v[154:157], v[202:205], v[92:95]
	v_mfma_f32_16x16x32_bf16 v[88:91], v[162:165], v[202:205], v[88:91]
	v_mfma_f32_16x16x32_bf16 v[76:79], v[154:157], v[210:213], v[76:79]
	v_mfma_f32_16x16x32_bf16 v[72:75], v[162:165], v[210:213], v[72:75]
	v_mfma_f32_16x16x32_bf16 v[118:121], v[166:169], v[182:185], v[118:121]
	v_mfma_f32_16x16x32_bf16 v[114:117], v[174:177], v[182:185], v[114:117]
	v_mfma_f32_16x16x32_bf16 v[102:105], v[166:169], v[190:193], v[102:105]
	v_mfma_f32_16x16x32_bf16 v[98:101], v[174:177], v[190:193], v[98:101]
	v_mfma_f32_16x16x32_bf16 v[84:87], v[166:169], v[198:201], v[84:87]
	v_mfma_f32_16x16x32_bf16 v[80:83], v[174:177], v[198:201], v[80:83]
	v_mfma_f32_16x16x32_bf16 v[68:71], v[166:169], v[206:209], v[68:71]
	v_mfma_f32_16x16x32_bf16 v[64:67], v[174:177], v[206:209], v[64:67]
	v_mfma_f32_16x16x32_bf16 v[118:121], v[170:173], v[186:189], v[118:121]
	v_mfma_f32_16x16x32_bf16 v[114:117], v[178:181], v[186:189], v[114:117]
	v_mfma_f32_16x16x32_bf16 v[102:105], v[170:173], v[194:197], v[102:105]
	v_mfma_f32_16x16x32_bf16 v[98:101], v[178:181], v[194:197], v[98:101]
	v_mfma_f32_16x16x32_bf16 v[84:87], v[170:173], v[202:205], v[84:87]
	v_mfma_f32_16x16x32_bf16 v[80:83], v[178:181], v[202:205], v[80:83]
	v_mfma_f32_16x16x32_bf16 v[68:71], v[170:173], v[210:213], v[68:71]
	v_mfma_f32_16x16x32_bf16 v[64:67], v[178:181], v[210:213], v[64:67]
	s_barrier
	s_mov_b32 m0, s79
	ds_read_b128 v[182:185], v149 offset:16384
	ds_read_b128 v[186:189], v149 offset:17408
	ds_read_b128 v[190:193], v149 offset:18432
	ds_read_b128 v[194:197], v149 offset:19456
	ds_read_b128 v[198:201], v149 offset:20480
	ds_read_b128 v[202:205], v149 offset:21504
	ds_read_b128 v[206:209], v149 offset:22528
	ds_read_b128 v[210:213], v149 offset:23552
	s_nop 0
	global_load_lds_dwordx4 v134, s[20:21]
	s_mov_b32 m0, s75
	s_nop 0
	global_load_lds_dwordx4 v137, s[20:21]
	s_mov_b32 m0, s76
	s_nop 0
	global_load_lds_dwordx4 v134, s[24:25]
	s_mov_b32 m0, s74
	s_nop 0
	global_load_lds_dwordx4 v137, s[24:25]
	s_mov_b32 m0, s60
	s_nop 0
	global_load_lds_dwordx4 v132, s[4:5]
	s_mov_b32 m0, s61
	s_nop 0
	global_load_lds_dwordx4 v135, s[4:5]
	s_waitcnt vmcnt(8)
	s_waitcnt lgkmcnt(0)
	s_barrier
; #define PG8_STAGE(bufoff, gbase, voff) do { _Pragma("unroll") for (int _i = 0; _i < 2; ++_i) \
;         __builtin_amdgcn_global_load_lds((const __attribute__((address_space(1))) unsigned*)((const __attribute__((address_space(1))) char*)(gbase) + (unsigned)lnd_v((int)(voff)[_i])), (LAS unsigned*)(lds + (bufoff) + ldsw + _i * 8192), 16, 0, 0); } while (0)
; #define PG8_LDA(dst, b, h) do { _Pragma("unroll") for (int m = 0; m < 4; ++m) _Pragma("unroll") for (int k = 0; k < 2; ++k) dst[m][k] = *(const LAS bf16x8*)(lds + PG8_SA(b, h) + aoff + m * 2048 + k * 1024); } while (0)
; #define PG8_LDB(dst, b, h) do { _Pragma("unroll") for (int n = 0; n < 2; ++n) _Pragma("unroll") for (int k = 0; k < 2; ++k) dst[n][k] = *(const LAS bf16x8*)(lds + PG8_SB(b, h) + boff + n * 2048 + k * 1024); } while (0)
; #define PG8_MMA(ai, bj, At, Bt) do { __builtin_amdgcn_s_setprio(1); _Pragma("unroll") for (int m = 0; m < 4; ++m) _Pragma("unroll") for (int n = 0; n < 2; ++n) _Pragma("unroll") for (int k = 0; k < 2; ++k) \
;         acc[ai][bj][m][n] = __builtin_amdgcn_mfma_f32_16x16x32_bf16(Bt[n][k], At[m][k], acc[ai][bj][m][n], 0, 0, 0); __builtin_amdgcn_s_setprio(0); } while (0)
; #define PG8_WAIT_V(n) asm volatile("s_waitcnt vmcnt(" #n ")" ::: "memory")
; #define PG8_WAIT_L(n) asm volatile("s_waitcnt lgkmcnt(" #n ")" ::: "memory")
; #define PG8_BAR __builtin_amdgcn_s_barrier()
; #define PG8_SCHED __builtin_amdgcn_sched_barrier(0)
; template <class Desc, class Epi>
; __device__ __forceinline__ void gemm_phase(const int wv_, LAS unsigned char* lds, const Desc& d, const Epi& E) {
;     ...
;             PG8_WAIT_V(8); PG8_WAIT_L(0); PG8_BAR; PG8_MMA(1, 0, At, B0); PG8_MMA(1, 1, At, B1); PG8_BAR; PG8_SCHED;
;             PG8_LDB(B0, 1, 0); PG8_LDB(B1, 1, 1); PG8_SCHED; PG8_LDA(At, 1, 0); PG8_STAGE(PG8_SA(0, 1), a2, sA1);
;             PG8_WAIT_V(8); PG8_WAIT_L(0); PG8_BAR; PG8_MMA(0, 0, At, B0); PG8_MMA(0, 1, At, B1); PG8_BAR; PG8_SCHED;
	s_waitcnt lgkmcnt(0)
	v_mfma_f32_16x16x32_bf16 v[60:63], v[150:153], v[182:185], v[60:63]
	v_mfma_f32_16x16x32_bf16 v[56:59], v[158:161], v[182:185], v[56:59]
	v_mfma_f32_16x16x32_bf16 v[44:47], v[150:153], v[190:193], v[44:47]
	v_mfma_f32_16x16x32_bf16 v[32:35], v[158:161], v[190:193], v[32:35]
	v_mfma_f32_16x16x32_bf16 v[16:19], v[150:153], v[198:201], v[16:19]
	v_mfma_f32_16x16x32_bf16 v[8:11], v[158:161], v[198:201], v[8:11]
	v_mfma_f32_16x16x32_bf16 v[4:7], v[150:153], v[206:209], v[4:7]
	v_mfma_f32_16x16x32_bf16 v[0:3], v[158:161], v[206:209], v[0:3]
	v_mfma_f32_16x16x32_bf16 v[60:63], v[154:157], v[186:189], v[60:63]
	v_mfma_f32_16x16x32_bf16 v[56:59], v[162:165], v[186:189], v[56:59]
	v_mfma_f32_16x16x32_bf16 v[44:47], v[154:157], v[194:197], v[44:47]
	v_mfma_f32_16x16x32_bf16 v[32:35], v[162:165], v[194:197], v[32:35]
	v_mfma_f32_16x16x32_bf16 v[16:19], v[154:157], v[202:205], v[16:19]
	v_mfma_f32_16x16x32_bf16 v[8:11], v[162:165], v[202:205], v[8:11]
	v_mfma_f32_16x16x32_bf16 v[4:7], v[154:157], v[210:213], v[4:7]
	v_mfma_f32_16x16x32_bf16 v[0:3], v[162:165], v[210:213], v[0:3]
	v_mfma_f32_16x16x32_bf16 v[52:55], v[166:169], v[182:185], v[52:55]
	v_mfma_f32_16x16x32_bf16 v[48:51], v[174:177], v[182:185], v[48:51]
	v_mfma_f32_16x16x32_bf16 v[28:31], v[166:169], v[190:193], v[28:31]
	v_mfma_f32_16x16x32_bf16 v[12:15], v[174:177], v[190:193], v[12:15]
	v_mfma_f32_16x16x32_bf16 v[36:39], v[166:169], v[198:201], v[36:39]
	v_mfma_f32_16x16x32_bf16 v[40:43], v[174:177], v[198:201], v[40:43]
	v_mfma_f32_16x16x32_bf16 v[20:23], v[166:169], v[206:209], v[20:23]
	v_mfma_f32_16x16x32_bf16 v[24:27], v[174:177], v[206:209], v[24:27]
	v_mfma_f32_16x16x32_bf16 v[52:55], v[170:173], v[186:189], v[52:55]
	v_mfma_f32_16x16x32_bf16 v[48:51], v[178:181], v[186:189], v[48:51]
	v_mfma_f32_16x16x32_bf16 v[28:31], v[170:173], v[194:197], v[28:31]
	v_mfma_f32_16x16x32_bf16 v[12:15], v[178:181], v[194:197], v[12:15]
	v_mfma_f32_16x16x32_bf16 v[36:39], v[170:173], v[202:205], v[36:39]
	v_mfma_f32_16x16x32_bf16 v[40:43], v[178:181], v[202:205], v[40:43]
	v_mfma_f32_16x16x32_bf16 v[20:23], v[170:173], v[210:213], v[20:23]
	v_mfma_f32_16x16x32_bf16 v[24:27], v[178:181], v[210:213], v[24:27]
	s_barrier
	v_add_u32_e32 v96, s73, v139
	ds_read_b128 v[150:153], v96
	ds_read_b128 v[154:157], v96 offset:1024
	ds_read_b128 v[158:161], v96 offset:2048
	ds_read_b128 v[162:165], v96 offset:3072
	v_add_u32_e32 v96, s72, v139
	ds_read_b128 v[166:169], v96
	ds_read_b128 v[170:173], v96 offset:1024
	ds_read_b128 v[174:177], v96 offset:2048
	ds_read_b128 v[178:181], v96 offset:3072
	s_mov_b32 m0, s62
	ds_read_b128 v[182:185], v149 offset:32768
	ds_read_b128 v[186:189], v149 offset:33792
	ds_read_b128 v[190:193], v149 offset:34816
	ds_read_b128 v[194:197], v149 offset:35840
	ds_read_b128 v[198:201], v149 offset:36864
	ds_read_b128 v[202:205], v149 offset:37888
	ds_read_b128 v[206:209], v149 offset:38912
	ds_read_b128 v[210:213], v149 offset:39936
	s_nop 0
	global_load_lds_dwordx4 v133, s[4:5]
	s_mov_b32 m0, s63
	s_nop 0
	global_load_lds_dwordx4 v136, s[4:5]
	s_waitcnt vmcnt(8)
	s_waitcnt lgkmcnt(0)
	s_barrier
	s_waitcnt lgkmcnt(0)
	v_mfma_f32_16x16x32_bf16 v[126:129], v[150:153], v[182:185], v[126:129]
	v_mfma_f32_16x16x32_bf16 v[122:125], v[158:161], v[182:185], v[122:125]
	v_mfma_f32_16x16x32_bf16 v[110:113], v[150:153], v[190:193], v[110:113]
	v_mfma_f32_16x16x32_bf16 v[106:109], v[158:161], v[190:193], v[106:109]
	v_mfma_f32_16x16x32_bf16 v[92:95], v[150:153], v[198:201], v[92:95]
	v_mfma_f32_16x16x32_bf16 v[88:91], v[158:161], v[198:201], v[88:91]
	v_mfma_f32_16x16x32_bf16 v[76:79], v[150:153], v[206:209], v[76:79]
	v_mfma_f32_16x16x32_bf16 v[72:75], v[158:161], v[206:209], v[72:75]
	v_mfma_f32_16x16x32_bf16 v[126:129], v[154:157], v[186:189], v[126:129]
	v_mfma_f32_16x16x32_bf16 v[122:125], v[162:165], v[186:189], v[122:125]
	v_mfma_f32_16x16x32_bf16 v[110:113], v[154:157], v[194:197], v[110:113]
	v_mfma_f32_16x16x32_bf16 v[106:109], v[162:165], v[194:197], v[106:109]
	v_mfma_f32_16x16x32_bf16 v[92:95], v[154:157], v[202:205], v[92:95]
	v_mfma_f32_16x16x32_bf16 v[88:91], v[162:165], v[202:205], v[88:91]
	v_mfma_f32_16x16x32_bf16 v[76:79], v[154:157], v[210:213], v[76:79]
	v_mfma_f32_16x16x32_bf16 v[72:75], v[162:165], v[210:213], v[72:75]
	v_mfma_f32_16x16x32_bf16 v[118:121], v[166:169], v[182:185], v[118:121]
	v_mfma_f32_16x16x32_bf16 v[114:117], v[174:177], v[182:185], v[114:117]
	v_mfma_f32_16x16x32_bf16 v[102:105], v[166:169], v[190:193], v[102:105]
	v_mfma_f32_16x16x32_bf16 v[98:101], v[174:177], v[190:193], v[98:101]
	v_mfma_f32_16x16x32_bf16 v[84:87], v[166:169], v[198:201], v[84:87]
	v_mfma_f32_16x16x32_bf16 v[80:83], v[174:177], v[198:201], v[80:83]
	v_mfma_f32_16x16x32_bf16 v[68:71], v[166:169], v[206:209], v[68:71]
	v_mfma_f32_16x16x32_bf16 v[64:67], v[174:177], v[206:209], v[64:67]
	v_mfma_f32_16x16x32_bf16 v[118:121], v[170:173], v[186:189], v[118:121]
	v_mfma_f32_16x16x32_bf16 v[114:117], v[178:181], v[186:189], v[114:117]
	v_mfma_f32_16x16x32_bf16 v[102:105], v[170:173], v[194:197], v[102:105]
	v_mfma_f32_16x16x32_bf16 v[98:101], v[178:181], v[194:197], v[98:101]
	v_mfma_f32_16x16x32_bf16 v[84:87], v[170:173], v[202:205], v[84:87]
	v_mfma_f32_16x16x32_bf16 v[80:83], v[178:181], v[202:205], v[80:83]
	v_mfma_f32_16x16x32_bf16 v[68:71], v[170:173], v[210:213], v[68:71]
	v_mfma_f32_16x16x32_bf16 v[64:67], v[178:181], v[210:213], v[64:67]
	s_barrier
; #define PG8_STAGE(bufoff, gbase, voff) do { _Pragma("unroll") for (int _i = 0; _i < 2; ++_i) \
;         __builtin_amdgcn_global_load_lds((const __attribute__((address_space(1))) unsigned*)((const __attribute__((address_space(1))) char*)(gbase) + (unsigned)lnd_v((int)(voff)[_i])), (LAS unsigned*)(lds + (bufoff) + ldsw + _i * 8192), 16, 0, 0); } while (0)
; #define PG8_LDA(dst, b, h) do { _Pragma("unroll") for (int m = 0; m < 4; ++m) _Pragma("unroll") for (int k = 0; k < 2; ++k) dst[m][k] = *(const LAS bf16x8*)(lds + PG8_SA(b, h) + aoff + m * 2048 + k * 1024); } while (0)
; #define PG8_MMA(ai, bj, At, Bt) do { __builtin_amdgcn_s_setprio(1); _Pragma("unroll") for (int m = 0; m < 4; ++m) _Pragma("unroll") for (int n = 0; n < 2; ++n) _Pragma("unroll") for (int k = 0; k < 2; ++k) \
;         acc[ai][bj][m][n] = __builtin_amdgcn_mfma_f32_16x16x32_bf16(Bt[n][k], At[m][k], acc[ai][bj][m][n], 0, 0, 0); __builtin_amdgcn_s_setprio(0); } while (0)
; #define PG8_WAIT_V(n) asm volatile("s_waitcnt vmcnt(" #n ")" ::: "memory")
; #define PG8_WAIT_L(n) asm volatile("s_waitcnt lgkmcnt(" #n ")" ::: "memory")
; #define PG8_BAR __builtin_amdgcn_s_barrier()
; #define PG8_SCHED __builtin_amdgcn_sched_barrier(0)
; template <class Desc, class Epi>
; __device__ __forceinline__ void gemm_phase(const int wv_, LAS unsigned char* lds, const Desc& d, const Epi& E) {
;     ...
;             PG8_LDA(At, 1, 1); PG8_STAGE(PG8_SB(1, 0), b3, voffB); PG8_STAGE(PG8_SB(1, 1), b3 + hstepB, voffB); PG8_STAGE(PG8_SA(1, 0), a3, sA0);
;             PG8_WAIT_V(8); PG8_WAIT_L(0); PG8_BAR; PG8_MMA(1, 0, At, B0); PG8_MMA(1, 1, At, B1); PG8_BAR; PG8_SCHED;
;         }
;         if (wr == 0) PG8_BAR;
	v_mov_b32_e32 v96, v134
	ds_read_b128 v[182:185], v149 offset:49152
	ds_read_b128 v[186:189], v149 offset:50176
	ds_read_b128 v[190:193], v149 offset:51200
	ds_read_b128 v[194:197], v149 offset:52224
	ds_read_b128 v[198:201], v149 offset:53248
	ds_read_b128 v[202:205], v149 offset:54272
	ds_read_b128 v[206:209], v149 offset:55296
	ds_read_b128 v[210:213], v149 offset:56320
	s_mov_b32 m0, s71
	v_lshl_add_u64 v[130:131], s[20:21], 0, v[96:97]
	v_lshl_add_u64 v[130:131], v[130:131], 0, s[30:31]
	v_mov_b32_e32 v96, v137
	global_load_lds_dwordx4 v[130:131], off
	s_mov_b32 m0, s29
	v_lshl_add_u64 v[130:131], s[20:21], 0, v[96:97]
	v_lshl_add_u64 v[130:131], v[130:131], 0, s[30:31]
	global_load_lds_dwordx4 v[130:131], off
	s_mov_b32 m0, s78
	s_nop 0
	global_load_lds_dwordx4 v134, s[22:23]
	s_mov_b32 m0, s77
	s_nop 0
	global_load_lds_dwordx4 v137, s[22:23]
	v_mov_b32_e32 v96, v132
	s_mov_b32 m0, s65
	v_lshl_add_u64 v[130:131], s[4:5], 0, v[96:97]
	v_lshl_add_u64 v[130:131], v[130:131], 0, s[30:31]
	v_mov_b32_e32 v96, v135
	global_load_lds_dwordx4 v[130:131], off
	s_mov_b32 m0, s66
	v_lshl_add_u64 v[130:131], s[4:5], 0, v[96:97]
	v_lshl_add_u64 v[130:131], v[130:131], 0, s[30:31]
	global_load_lds_dwordx4 v[130:131], off
	s_waitcnt vmcnt(8)
	s_waitcnt lgkmcnt(0)
	s_barrier
	s_waitcnt lgkmcnt(0)
	v_mfma_f32_16x16x32_bf16 v[60:63], v[150:153], v[182:185], v[60:63]
	v_mfma_f32_16x16x32_bf16 v[56:59], v[158:161], v[182:185], v[56:59]
	v_mfma_f32_16x16x32_bf16 v[44:47], v[150:153], v[190:193], v[44:47]
	v_mfma_f32_16x16x32_bf16 v[32:35], v[158:161], v[190:193], v[32:35]
	v_mfma_f32_16x16x32_bf16 v[16:19], v[150:153], v[198:201], v[16:19]
	v_mfma_f32_16x16x32_bf16 v[8:11], v[158:161], v[198:201], v[8:11]
	v_mfma_f32_16x16x32_bf16 v[4:7], v[150:153], v[206:209], v[4:7]
	v_mfma_f32_16x16x32_bf16 v[0:3], v[158:161], v[206:209], v[0:3]
	v_mfma_f32_16x16x32_bf16 v[60:63], v[154:157], v[186:189], v[60:63]
	v_mfma_f32_16x16x32_bf16 v[56:59], v[162:165], v[186:189], v[56:59]
	v_mfma_f32_16x16x32_bf16 v[44:47], v[154:157], v[194:197], v[44:47]
	v_mfma_f32_16x16x32_bf16 v[32:35], v[162:165], v[194:197], v[32:35]
	v_mfma_f32_16x16x32_bf16 v[16:19], v[154:157], v[202:205], v[16:19]
	v_mfma_f32_16x16x32_bf16 v[8:11], v[162:165], v[202:205], v[8:11]
	v_mfma_f32_16x16x32_bf16 v[4:7], v[154:157], v[210:213], v[4:7]
	v_mfma_f32_16x16x32_bf16 v[0:3], v[162:165], v[210:213], v[0:3]
	v_mfma_f32_16x16x32_bf16 v[52:55], v[166:169], v[182:185], v[52:55]
	v_mfma_f32_16x16x32_bf16 v[48:51], v[174:177], v[182:185], v[48:51]
	v_mfma_f32_16x16x32_bf16 v[28:31], v[166:169], v[190:193], v[28:31]
	v_mfma_f32_16x16x32_bf16 v[12:15], v[174:177], v[190:193], v[12:15]
	v_mfma_f32_16x16x32_bf16 v[36:39], v[166:169], v[198:201], v[36:39]
	v_mfma_f32_16x16x32_bf16 v[40:43], v[174:177], v[198:201], v[40:43]
	v_mfma_f32_16x16x32_bf16 v[20:23], v[166:169], v[206:209], v[20:23]
	v_mfma_f32_16x16x32_bf16 v[24:27], v[174:177], v[206:209], v[24:27]
	v_mfma_f32_16x16x32_bf16 v[52:55], v[170:173], v[186:189], v[52:55]
	v_mfma_f32_16x16x32_bf16 v[48:51], v[178:181], v[186:189], v[48:51]
	v_mfma_f32_16x16x32_bf16 v[28:31], v[170:173], v[194:197], v[28:31]
	v_mfma_f32_16x16x32_bf16 v[12:15], v[178:181], v[194:197], v[12:15]
	v_mfma_f32_16x16x32_bf16 v[36:39], v[170:173], v[202:205], v[36:39]
	v_mfma_f32_16x16x32_bf16 v[40:43], v[178:181], v[202:205], v[40:43]
	v_mfma_f32_16x16x32_bf16 v[20:23], v[170:173], v[210:213], v[20:23]
	v_mfma_f32_16x16x32_bf16 v[24:27], v[178:181], v[210:213], v[24:27]
	s_barrier
	s_movk_i32 s22, 0x100
	s_andn2_b64 vcc, exec, s[2:3]
	s_mov_b64 s[20:21], -1
	s_mov_b64 s[2:3], 0
	s_cbranch_vccz .LBB0_1481
	s_and_b64 vcc, exec, s[40:41]
	s_cbranch_vccz .LBB0_1484
	s_barrier

; #define LAS __attribute__((address_space(3)))
; template <class Desc, class Epi>
; __device__ __forceinline__ void gemm_phase(const int wv_, LAS unsigned char* lds, const Desc& d, const Epi& E) {
;     ...
; #pragma unroll
;     for (int i = 0; i < 2; ++i) { int R, C; stage_rc(tid * 16 + i * 8192, R, C); const int Rb = (R & ~31) + perm32(R & 31); Rr[i] = R; Cc[i] = C;
;         voffA[i] = (unsigned)(R * d.lda + C) * 2u; voffA1[i] = voffA[i] + (unsigned)hstepA; voffB[i] = (unsigned)(Rb * d.ldb + C) * 2u; }
;     unsigned voffAn[2] = {0u, 0u}, voffAn1[2] = {0u, 0u};
;     LAS unsigned short* const tix = (LAS unsigned short*)(lds + STAGE_BYTES + 16384);
;     ...
;     const unsigned ldsw = (unsigned)wid * 1024u;
;     const int aoff = lds_byte(wr * 64 + fr, fq * 8), boff = lds_byte(wc * 32 + fr, fq * 8);
;     ...
;     GU cur, nxt; int ui = 0;
;     if (bid < 0 || bid >= d.nunits) return;
;     LAS float* const rsc = (LAS float*)(lds + STAGE_BYTES);
;     if constexpr (Epi::STAGED || Desc::GATHER) {
;         const int nmy = (d.nunits - bid + nblk - 1) / nblk;
;         for (int idx = tid; idx < nmy * 256; idx += NTHREADS) { GU su; d.unit(bid + (idx >> 8) * nblk, su);
;             if constexpr (Epi::STAGED) rsc[idx] = E.rowscale(su, idx & 255);
;             if constexpr (Desc::GATHER) tix[idx] = (unsigned short)d.tokidx(su, idx & 255); }
;         asm volatile("s_waitcnt vmcnt(0) lgkmcnt(0)" ::: "memory"); __builtin_amdgcn_s_barrier(); asm volatile("" ::: "memory");
;     }
;     d.unit(bid, cur);
;     if constexpr (Desc::GATHER) PG8_AOFF(0, cur, voffA, voffA1);
;     f32x4 acc[2][2][4][2];
; #pragma unroll
;     for (int a = 0; a < 2; ++a)
; #pragma unroll
;         for (int b = 0; b < 2; ++b)
; #pragma unroll
;             for (int m = 0; m < 4; ++m)
; #pragma unroll
;                 for (int n = 0; n < 2; ++n) acc[a][b][m][n] = (f32x4){0.f, 0.f, 0.f, 0.f};
;     bf16x8 At[4][2], B0[2][2], B1[2][2];
;     const char* cA = (const char*)cur.a; const char* cB = (const char*)cur.b;
;     PG8_STAGE(PG8_SB(0, 0), cB, voffB); PG8_STAGE(PG8_SB(0, 1), cB + hstepB, voffB); PG8_STAGE(PG8_SA(0, 0), cA, voffA); PG8_STAGE(PG8_SA(0, 1), cA, voffA1);
;     if (wr == 1) PG8_BAR;
;     PG8_WAIT_V(2); PG8_BAR;
;     PG8_STAGE(PG8_SB(1, 0), cB + kstep, voffB); PG8_STAGE(PG8_SA(1, 0), cA + kstep, voffA); PG8_STAGE(PG8_SB(1, 1), cB + hstepB + kstep, voffB);
;     PG8_WAIT_V(6); PG8_BAR;
.LBB0_1557:
	s_or_b64 exec, exec, s[2:3]
	v_ashrrev_i32_e32 v2, 31, v0
	v_lshrrev_b32_e32 v2, 26, v2
	v_lshlrev_b32_e32 v1, 4, v0
	v_add_u32_e32 v2, v0, v2
	v_bfe_i32 v0, v0, 27, 1
	v_lshrrev_b32_e32 v0, 22, v0
	v_add_u32_e32 v0, v1, v0
	v_and_b32_e32 v0, 0xfffffc00, v0
	v_sub_u32_e32 v0, v1, v0
	v_lshrrev_b32_e32 v3, 4, v0
	v_bitop3_b32 v0, v3, v0, 32 bitop3:0x6c
	v_ashrrev_i32_e32 v5, 31, v0
	v_ashrrev_i32_e32 v2, 6, v2
	v_lshrrev_b32_e32 v5, 26, v5
	v_lshlrev_b32_e32 v3, 3, v2
	v_add_u32_e32 v5, v0, v5
	v_and_b32_e32 v3, -16, v3
	v_ashrrev_i32_e32 v6, 6, v5
	v_add_u32_e32 v136, v6, v3
	v_and_b32_e32 v3, 0xc0, v5
	v_sub_u32_e32 v0, v0, v3
	v_lshlrev_b32_e32 v2, 5, v2
	v_ashrrev_i16_sdwa v0, v216, sext(v0) dst_sel:DWORD dst_unused:UNUSED_PAD src0_sel:DWORD src1_sel:BYTE_0
	v_and_b32_e32 v2, 32, v2
	v_bfe_i32 v0, v0, 0, 16
	v_add_lshl_u32 v137, v2, v0, 1
	v_add_u32_e32 v0, 0x2000, v1
	v_ashrrev_i32_e32 v1, 31, v0
	v_lshrrev_b32_e32 v1, 22, v1
	s_lshl_b32 s0, s66, 1
	v_add_u32_e32 v1, v0, v1
	s_add_u32 s0, s46, s0
	v_ashrrev_i32_e32 v1, 10, v1
	s_addc_u32 s1, s47, 0
	v_mul_i32_i24_e32 v2, 0x400, v1
	s_add_u32 s24, s0, 0x3600000
	v_lshlrev_b32_e32 v3, 1, v136
	v_lshrrev_b32_e32 v7, 2, v136
	v_and_b32_e32 v6, 3, v6
	s_mov_b32 s0, 0x1fffe0
	v_sub_u32_e32 v0, v0, v2
	v_and_b32_e32 v5, 24, v3
	v_and_b32_e32 v7, 4, v7
	v_and_or_b32 v6, v136, s0, v6
	v_lshrrev_b32_e32 v2, 4, v0
	v_or3_b32 v5, v6, v7, v5
	v_bitop3_b32 v0, v2, v0, 32 bitop3:0x6c
	v_lshl_add_u32 v138, v5, 11, v137
	v_ashrrev_i32_e32 v5, 31, v0
	v_lshrrev_b32_e32 v5, 26, v5
	v_lshlrev_b32_e32 v2, 3, v1
	v_add_u32_e32 v5, v0, v5
	v_and_b32_e32 v2, -16, v2
	v_ashrrev_i32_e32 v6, 6, v5
	v_add_u32_e32 v139, v6, v2
	v_and_b32_e32 v6, 3, v6
	s_addc_u32 s25, s1, 0
	v_and_b32_e32 v2, 0xc0, v5
	v_and_or_b32 v6, v139, s0, v6
	s_lshl_b32 s0, s61, 1
	v_sub_u32_e32 v0, v0, v2
	s_and_b32 s1, s0, 12
	s_lshr_b32 s0, s61, 6
	v_lshlrev_b32_e32 v1, 5, v1
	v_ashrrev_i16_sdwa v0, v216, sext(v0) dst_sel:DWORD dst_unused:UNUSED_PAD src0_sel:DWORD src1_sel:BYTE_0
	s_and_b32 s2, s0, 2
	v_and_b32_e32 v1, 32, v1
	v_bfe_i32 v0, v0, 0, 16
	v_lshlrev_b32_e32 v2, 1, v139
	s_lshr_b32 s26, s61, 8
	s_or_b32 s2, s1, s2
	v_readlane_b32 s23, v254, 54
	v_and_b32_e32 v5, 24, v2
	v_add_lshl_u32 v140, v1, v0, 1
	s_waitcnt vmcnt(0) lgkmcnt(0)
	s_barrier
	s_lshl_b32 s1, s61, 3
	s_lshl_b32 s20, s2, 4
	s_lshl_b32 s2, s26, 1
	v_add_u32_e32 v0, s23, v3
	v_add_u32_e32 v2, s23, v2
	s_and_b32 s1, s1, 8
	s_bfe_u32 s3, s61, 0x30003
	s_add_i32 s20, s20, s2
	ds_read_u16 v1, v0
	ds_read_u16 v0, v0 offset:256
	ds_read_u16 v3, v2
	ds_read_u16 v2, v2 offset:256
	s_ashr_i32 s5, s52, 6
	s_or_b32 s1, s1, s3
	s_lshl_b32 s22, s20, 7
	s_ashr_i32 s4, s52, 8
	s_lshl_b32 s63, s5, 10
	s_lshl_b32 s21, s1, 19
	s_lshl_b64 s[2:3], s[26:27], 23
	s_and_b32 s22, s22, 0x7ffff000
	s_waitcnt lgkmcnt(0)
	v_add_u32_e32 v0, s22, v0
	s_add_u32 s2, s24, s2
	v_lshrrev_b32_e32 v7, 2, v139
	v_lshl_add_u32 v131, v0, 11, v137
	v_add_u32_e32 v0, s22, v3
	s_addc_u32 s3, s25, s3
	v_and_b32_e32 v7, 4, v7
	v_lshl_add_u32 v159, v0, 11, v140
	v_add_u32_e32 v0, s22, v2
	s_add_u32 s2, s2, s21
	v_or3_b32 v5, v6, v7, v5
	v_lshl_add_u32 v158, v0, 11, v140
	s_addc_u32 s3, s3, 0
	s_add_i32 s64, s63, 0
	v_lshl_add_u32 v141, v5, 11, v140
	s_add_i32 m0, s64, 0x10000
	v_add_u32_e32 v1, s22, v1
	global_load_lds_dwordx4 v138, s[2:3]
	s_add_i32 m0, s64, 0x12000
	s_add_u32 s22, s2, 0x40000
	global_load_lds_dwordx4 v141, s[2:3]
	s_addc_u32 s23, s3, 0
	s_add_i32 m0, s64, 0x14000
	v_lshl_add_u32 v157, v1, 11, v137
	global_load_lds_dwordx4 v138, s[22:23]
	s_add_i32 m0, s64, 0x16000
	s_add_i32 s65, s64, 0x2000
	global_load_lds_dwordx4 v141, s[22:23]
	s_mov_b32 m0, s64
	s_add_i32 s68, s64, 0x4000
	global_load_lds_dwordx4 v157, s[42:43]
	s_mov_b32 m0, s65
	s_add_i32 s69, s64, 0x6000
	global_load_lds_dwordx4 v159, s[42:43]
	s_mov_b32 m0, s68
	s_cmp_eq_u32 s4, 1
	global_load_lds_dwordx4 v131, s[42:43]
	v_mov_b32_e32 v0, v158
	s_mov_b32 m0, s69
	s_cselect_b64 s[38:39], -1, 0
	global_load_lds_dwordx4 v0, s[42:43]
	s_and_b64 vcc, exec, s[38:39]
	s_cbranch_vccz .LBB0_1559
	s_barrier
.LBB0_1559:
	v_mov_b32_e32 v96, v138
	s_lshl_b32 s5, s5, 5
	s_waitcnt vmcnt(2)
	s_barrier
	s_and_b32 s0, s0, 1
	v_lshl_add_u64 v[0:1], s[2:3], 0, v[96:97]
	s_and_b32 s5, s5, 0x60
	s_add_i32 m0, s64, 0x18000
	v_lshl_add_u64 v[0:1], v[0:1], 0, s[30:31]
	v_mov_b32_e32 v96, v141
	s_or_b32 s0, s20, s0
	s_lshl_b32 s22, s4, 13
	s_lshl_b32 s23, s5, 7
	global_load_lds_dwordx4 v[0:1], off
	s_add_i32 m0, s64, 0x1a000
	v_lshl_add_u64 v[0:1], s[2:3], 0, v[96:97]
	v_lshl_add_u64 v[0:1], v[0:1], 0, s[30:31]
	s_add_u32 s40, s46, 0x33600080
	global_load_lds_dwordx4 v[0:1], off
	s_addc_u32 s41, s47, 0
	s_add_i32 s70, s64, 0x8000
	s_mov_b32 m0, s70
	s_add_i32 s71, s64, 0xa000
	global_load_lds_dwordx4 v157, s[40:41]
	s_mov_b32 m0, s71
	s_add_u32 s20, s2, 0x40080
	global_load_lds_dwordx4 v159, s[40:41]
	s_addc_u32 s21, s3, 0
	s_add_i32 m0, s64, 0x1c000
	v_and_b32_e32 v1, 15, v4
	global_load_lds_dwordx4 v138, s[20:21]
	s_add_i32 m0, s64, 0x1e000
	v_lshl_or_b32 v142, s4, 6, v1
	global_load_lds_dwordx4 v141, s[20:21]
	v_lshrrev_b32_e32 v0, 1, v4
	v_and_b32_e32 v0, 24, v0
	v_lshlrev_b32_e32 v2, 1, v0
	v_lshl_or_b32 v1, v1, 6, v2
	v_lshlrev_b32_e32 v2, 2, v142
	v_and_b32_e32 v3, 32, v2
	v_lshlrev_b32_e32 v4, 2, v4
	s_waitcnt vmcnt(6)
	s_cmpk_lt_u32 s52, 0x100
	v_bitop3_b32 v3, v1, s22, v3 bitop3:0xde
	v_and_b32_e32 v4, 32, v4
	s_cselect_b64 s[52:53], -1, 0
	s_add_i32 s4, 0, 0x20000
	v_bitop3_b32 v143, v1, s23, v4 bitop3:0xde
	v_or_b32_e32 v144, 16, v142
	v_or_b32_e32 v145, 32, v142
	v_or_b32_e32 v146, 48, v142
	v_add_u32_e32 v147, 0x80, v142
	v_add_u32_e32 v148, 0x90, v142
	v_add_u32_e32 v149, 0xa0, v142
	v_add_u32_e32 v150, 0xb0, v142
	v_add_u32_e32 v151, s4, v2
	s_mov_b32 s58, 0
	v_add_u32_e32 v152, 0, v3
	s_lshl_b32 s26, s5, 1
	v_lshlrev_b32_e32 v130, 1, v0
	v_mov_b32_e32 v154, v159
	v_mov_b32_e32 v153, v157
	v_mov_b32_e32 v156, v158
	v_mov_b32_e32 v155, v131
	s_mov_b64 s[54:55], s[2:3]
	s_barrier
	s_waitcnt vmcnt(0)
	s_branch .LBB0_1562

; #define PG8_STAGE(bufoff, gbase, voff) do { _Pragma("unroll") for (int _i = 0; _i < 2; ++_i) \
;         __builtin_amdgcn_global_load_lds((const __attribute__((address_space(1))) unsigned*)((const __attribute__((address_space(1))) char*)(gbase) + (unsigned)lnd_v((int)(voff)[_i])), (LAS unsigned*)(lds + (bufoff) + ldsw + _i * 8192), 16, 0, 0); } while (0)
; #define PG8_LDA(dst, b, h) do { _Pragma("unroll") for (int m = 0; m < 4; ++m) _Pragma("unroll") for (int k = 0; k < 2; ++k) dst[m][k] = *(const LAS bf16x8*)(lds + PG8_SA(b, h) + aoff + m * 2048 + k * 1024); } while (0)
; #define PG8_LDB(dst, b, h) do { _Pragma("unroll") for (int n = 0; n < 2; ++n) _Pragma("unroll") for (int k = 0; k < 2; ++k) dst[n][k] = *(const LAS bf16x8*)(lds + PG8_SB(b, h) + boff + n * 2048 + k * 1024); } while (0)
; #define PG8_WAIT_V(n) asm volatile("s_waitcnt vmcnt(" #n ")" ::: "memory")
; #define PG8_WAIT_L(n) asm volatile("s_waitcnt lgkmcnt(" #n ")" ::: "memory")
; #define PG8_BAR __builtin_amdgcn_s_barrier()
; template <class Desc, class Epi>
; __device__ __forceinline__ void gemm_phase(const int wv_, LAS unsigned char* lds, const Desc& d, const Epi& E) {
;     ...
;         const char* nA = has_next ? (const char*)nxt.a : cA; const char* nB = has_next ? (const char*)nxt.b : cB;
;         for (int t = 0; t < nt; t += 2) {
;             const bool last = (t == nt - 2);
;             unsigned sA0[2], sA1[2];
;             if constexpr (Desc::GATHER) { sA0[0] = last ? voffAn[0] : voffA[0]; sA0[1] = last ? voffAn[1] : voffA[1]; sA1[0] = last ? voffAn1[0] : voffA1[0]; sA1[1] = last ? voffAn1[1] : voffA1[1]; }
;             else { sA0[0] = voffA[0]; sA0[1] = voffA[1]; sA1[0] = voffA1[0]; sA1[1] = voffA1[1]; }
;             const char* a1 = cA + (size_t)(t + 1) * kstep;
;             const char* a2 = last ? nA : cA + (size_t)(t + 2) * kstep; const char* b2 = last ? nB : cB + (size_t)(t + 2) * kstep;
;             const char* a3 = a2 + kstep; const char* b3 = b2 + kstep;
;             PG8_LDB(B0, 0, 0); PG8_LDB(B1, 0, 1); PG8_SCHED; PG8_LDA(At, 0, 0); PG8_STAGE(PG8_SA(1, 1), a1, voffA1);
;             PG8_WAIT_V(8); PG8_WAIT_L(0); PG8_BAR; PG8_MMA(0, 0, At, B0); PG8_MMA(0, 1, At, B1); PG8_BAR; PG8_SCHED;
;             PG8_LDA(At, 0, 1); PG8_STAGE(PG8_SB(0, 0), b2, voffB); PG8_STAGE(PG8_SB(0, 1), b2 + hstepB, voffB); PG8_STAGE(PG8_SA(0, 0), a2, sA0);
.LBB0_1565:
	s_add_u32 s4, s2, 0x100
	s_addc_u32 s5, s3, 0
	s_add_u32 s22, s29, s2
	s_addc_u32 s23, s59, s3
	s_cmp_eq_u32 s75, 12
	s_cselect_b64 vcc, -1, 0
	s_and_b64 s[20:21], vcc, exec
	s_cselect_b32 s20, 0, s4
	s_cselect_b32 s21, 0, s5
	s_cselect_b32 s22, s54, s22
	s_cselect_b32 s23, s55, s23
	s_add_u32 s20, s42, s20
	s_addc_u32 s21, s43, s21
	s_add_i32 s76, 0, 0x10000
	v_add_u32_e32 v135, s76, v143
	s_add_i32 s77, 0, 0x14000
	ds_read_b128 v[160:163], v135
	ds_read_b128 v[164:167], v135 offset:1024
	ds_read_b128 v[168:171], v135 offset:2048
	ds_read_b128 v[172:175], v135 offset:3072
	v_add_u32_e32 v135, s77, v143
	ds_read_b128 v[176:179], v135
	ds_read_b128 v[180:183], v135 offset:1024
	ds_read_b128 v[184:187], v135 offset:2048
	ds_read_b128 v[188:191], v135 offset:3072
	v_cndmask_b32_e32 v134, v157, v153, vcc
	v_cndmask_b32_e32 v132, v159, v154, vcc
	v_cndmask_b32_e32 v96, v131, v155, vcc
	v_cndmask_b32_e32 v133, v158, v156, vcc
	s_add_i32 m0, s64, 0xc000
	s_add_u32 s2, s40, s2
	ds_read_b128 v[192:195], v152
	ds_read_b128 v[196:199], v152 offset:1024
	ds_read_b128 v[200:203], v152 offset:2048
	ds_read_b128 v[204:207], v152 offset:3072
	ds_read_b128 v[208:211], v152 offset:4096
	ds_read_b128 v[212:215], v152 offset:5120
	ds_read_b128 v[220:223], v152 offset:6144
	ds_read_b128 v[224:227], v152 offset:7168
	s_addc_u32 s3, s41, s3
	global_load_lds_dwordx4 v131, s[2:3]
	s_add_i32 m0, s64, 0xe000
	s_nop 0
	global_load_lds_dwordx4 v158, s[2:3]
	s_waitcnt vmcnt(8)
	s_waitcnt lgkmcnt(0)
	s_barrier
	s_waitcnt lgkmcnt(0)
	v_mfma_f32_16x16x32_bf16 v[122:125], v[160:163], v[192:195], v[122:125]
	v_mfma_f32_16x16x32_bf16 v[114:117], v[168:171], v[192:195], v[114:117]
	v_mfma_f32_16x16x32_bf16 v[106:109], v[160:163], v[200:203], v[106:109]
	v_mfma_f32_16x16x32_bf16 v[98:101], v[168:171], v[200:203], v[98:101]
	v_mfma_f32_16x16x32_bf16 v[88:91], v[160:163], v[208:211], v[88:91]
	v_mfma_f32_16x16x32_bf16 v[80:83], v[168:171], v[208:211], v[80:83]
	v_mfma_f32_16x16x32_bf16 v[72:75], v[160:163], v[220:223], v[72:75]
	v_mfma_f32_16x16x32_bf16 v[64:67], v[168:171], v[220:223], v[64:67]
	v_mfma_f32_16x16x32_bf16 v[122:125], v[164:167], v[196:199], v[122:125]
	v_mfma_f32_16x16x32_bf16 v[114:117], v[172:175], v[196:199], v[114:117]
	v_mfma_f32_16x16x32_bf16 v[106:109], v[164:167], v[204:207], v[106:109]
	v_mfma_f32_16x16x32_bf16 v[98:101], v[172:175], v[204:207], v[98:101]
	v_mfma_f32_16x16x32_bf16 v[88:91], v[164:167], v[212:215], v[88:91]
	v_mfma_f32_16x16x32_bf16 v[80:83], v[172:175], v[212:215], v[80:83]
	v_mfma_f32_16x16x32_bf16 v[72:75], v[164:167], v[224:227], v[72:75]
	v_mfma_f32_16x16x32_bf16 v[64:67], v[172:175], v[224:227], v[64:67]
	v_mfma_f32_16x16x32_bf16 v[126:129], v[176:179], v[192:195], v[126:129]
	v_mfma_f32_16x16x32_bf16 v[118:121], v[184:187], v[192:195], v[118:121]
	v_mfma_f32_16x16x32_bf16 v[110:113], v[176:179], v[200:203], v[110:113]
	v_mfma_f32_16x16x32_bf16 v[102:105], v[184:187], v[200:203], v[102:105]
	v_mfma_f32_16x16x32_bf16 v[92:95], v[176:179], v[208:211], v[92:95]
	v_mfma_f32_16x16x32_bf16 v[84:87], v[184:187], v[208:211], v[84:87]
	v_mfma_f32_16x16x32_bf16 v[76:79], v[176:179], v[220:223], v[76:79]
	v_mfma_f32_16x16x32_bf16 v[68:71], v[184:187], v[220:223], v[68:71]
	v_mfma_f32_16x16x32_bf16 v[126:129], v[180:183], v[196:199], v[126:129]
	v_mfma_f32_16x16x32_bf16 v[118:121], v[188:191], v[196:199], v[118:121]
	v_mfma_f32_16x16x32_bf16 v[110:113], v[180:183], v[204:207], v[110:113]
	v_mfma_f32_16x16x32_bf16 v[102:105], v[188:191], v[204:207], v[102:105]
	v_mfma_f32_16x16x32_bf16 v[92:95], v[180:183], v[212:215], v[92:95]
	v_mfma_f32_16x16x32_bf16 v[84:87], v[188:191], v[212:215], v[84:87]
	v_mfma_f32_16x16x32_bf16 v[76:79], v[180:183], v[224:227], v[76:79]
	v_mfma_f32_16x16x32_bf16 v[68:71], v[188:191], v[224:227], v[68:71]
	s_barrier
	s_add_i32 s2, s76, s63
	ds_read_b128 v[192:195], v152 offset:16384
	ds_read_b128 v[196:199], v152 offset:17408
	ds_read_b128 v[200:203], v152 offset:18432
	ds_read_b128 v[204:207], v152 offset:19456
	ds_read_b128 v[208:211], v152 offset:20480
	ds_read_b128 v[212:215], v152 offset:21504
	ds_read_b128 v[220:223], v152 offset:22528
	ds_read_b128 v[224:227], v152 offset:23552
	s_mov_b32 m0, s2
	s_nop 0
	global_load_lds_dwordx4 v138, s[22:23]
	s_add_i32 m0, s2, 0x2000
	s_add_u32 s2, s22, 0x40000
	global_load_lds_dwordx4 v141, s[22:23]
	s_addc_u32 s3, s23, 0
	s_add_i32 s76, s77, s63
	s_mov_b32 m0, s76
	s_nop 0
	global_load_lds_dwordx4 v138, s[2:3]
	s_add_i32 m0, s76, 0x2000
	s_nop 0
	global_load_lds_dwordx4 v141, s[2:3]
	s_mov_b32 m0, s64
	s_nop 0
	global_load_lds_dwordx4 v134, s[20:21]
	s_mov_b32 m0, s65
	s_nop 0
	global_load_lds_dwordx4 v132, s[20:21]
	s_waitcnt vmcnt(8)
	s_waitcnt lgkmcnt(0)
	s_barrier
; #define PG8_STAGE(bufoff, gbase, voff) do { _Pragma("unroll") for (int _i = 0; _i < 2; ++_i) \
;         __builtin_amdgcn_global_load_lds((const __attribute__((address_space(1))) unsigned*)((const __attribute__((address_space(1))) char*)(gbase) + (unsigned)lnd_v((int)(voff)[_i])), (LAS unsigned*)(lds + (bufoff) + ldsw + _i * 8192), 16, 0, 0); } while (0)
; #define PG8_LDA(dst, b, h) do { _Pragma("unroll") for (int m = 0; m < 4; ++m) _Pragma("unroll") for (int k = 0; k < 2; ++k) dst[m][k] = *(const LAS bf16x8*)(lds + PG8_SA(b, h) + aoff + m * 2048 + k * 1024); } while (0)
; #define PG8_LDB(dst, b, h) do { _Pragma("unroll") for (int n = 0; n < 2; ++n) _Pragma("unroll") for (int k = 0; k < 2; ++k) dst[n][k] = *(const LAS bf16x8*)(lds + PG8_SB(b, h) + boff + n * 2048 + k * 1024); } while (0)
; #define PG8_MMA(ai, bj, At, Bt) do { __builtin_amdgcn_s_setprio(1); _Pragma("unroll") for (int m = 0; m < 4; ++m) _Pragma("unroll") for (int n = 0; n < 2; ++n) _Pragma("unroll") for (int k = 0; k < 2; ++k) \
;         acc[ai][bj][m][n] = __builtin_amdgcn_mfma_f32_16x16x32_bf16(Bt[n][k], At[m][k], acc[ai][bj][m][n], 0, 0, 0); __builtin_amdgcn_s_setprio(0); } while (0)
; #define PG8_WAIT_V(n) asm volatile("s_waitcnt vmcnt(" #n ")" ::: "memory")
; #define PG8_WAIT_L(n) asm volatile("s_waitcnt lgkmcnt(" #n ")" ::: "memory")
; #define PG8_BAR __builtin_amdgcn_s_barrier()
; #define PG8_SCHED __builtin_amdgcn_sched_barrier(0)
; template <class Desc, class Epi>
; __device__ __forceinline__ void gemm_phase(const int wv_, LAS unsigned char* lds, const Desc& d, const Epi& E) {
;     ...
;             PG8_WAIT_V(8); PG8_WAIT_L(0); PG8_BAR; PG8_MMA(1, 0, At, B0); PG8_MMA(1, 1, At, B1); PG8_BAR; PG8_SCHED;
;             PG8_LDB(B0, 1, 0); PG8_LDB(B1, 1, 1); PG8_SCHED; PG8_LDA(At, 1, 0); PG8_STAGE(PG8_SA(0, 1), a2, sA1);
;             PG8_WAIT_V(8); PG8_WAIT_L(0); PG8_BAR; PG8_MMA(0, 0, At, B0); PG8_MMA(0, 1, At, B1); PG8_BAR; PG8_SCHED;
	s_waitcnt lgkmcnt(0)
	v_mfma_f32_16x16x32_bf16 v[56:59], v[160:163], v[192:195], v[56:59]
	v_mfma_f32_16x16x32_bf16 v[48:51], v[168:171], v[192:195], v[48:51]
	v_mfma_f32_16x16x32_bf16 v[40:43], v[160:163], v[200:203], v[40:43]
	v_mfma_f32_16x16x32_bf16 v[32:35], v[168:171], v[200:203], v[32:35]
	v_mfma_f32_16x16x32_bf16 v[24:27], v[160:163], v[208:211], v[24:27]
	v_mfma_f32_16x16x32_bf16 v[16:19], v[168:171], v[208:211], v[16:19]
	v_mfma_f32_16x16x32_bf16 v[8:11], v[160:163], v[220:223], v[8:11]
	v_mfma_f32_16x16x32_bf16 v[4:7], v[168:171], v[220:223], v[4:7]
	v_mfma_f32_16x16x32_bf16 v[56:59], v[164:167], v[196:199], v[56:59]
	v_mfma_f32_16x16x32_bf16 v[48:51], v[172:175], v[196:199], v[48:51]
	v_mfma_f32_16x16x32_bf16 v[40:43], v[164:167], v[204:207], v[40:43]
	v_mfma_f32_16x16x32_bf16 v[32:35], v[172:175], v[204:207], v[32:35]
	v_mfma_f32_16x16x32_bf16 v[24:27], v[164:167], v[212:215], v[24:27]
	v_mfma_f32_16x16x32_bf16 v[16:19], v[172:175], v[212:215], v[16:19]
	v_mfma_f32_16x16x32_bf16 v[8:11], v[164:167], v[224:227], v[8:11]
	v_mfma_f32_16x16x32_bf16 v[4:7], v[172:175], v[224:227], v[4:7]
	v_mfma_f32_16x16x32_bf16 v[60:63], v[176:179], v[192:195], v[60:63]
	v_mfma_f32_16x16x32_bf16 v[52:55], v[184:187], v[192:195], v[52:55]
	v_mfma_f32_16x16x32_bf16 v[44:47], v[176:179], v[200:203], v[44:47]
	v_mfma_f32_16x16x32_bf16 v[36:39], v[184:187], v[200:203], v[36:39]
	v_mfma_f32_16x16x32_bf16 v[28:31], v[176:179], v[208:211], v[28:31]
	v_mfma_f32_16x16x32_bf16 v[20:23], v[184:187], v[208:211], v[20:23]
	v_mfma_f32_16x16x32_bf16 v[12:15], v[176:179], v[220:223], v[12:15]
	v_mfma_f32_16x16x32_bf16 v[0:3], v[184:187], v[220:223], v[0:3]
	v_mfma_f32_16x16x32_bf16 v[60:63], v[180:183], v[196:199], v[60:63]
	v_mfma_f32_16x16x32_bf16 v[52:55], v[188:191], v[196:199], v[52:55]
	v_mfma_f32_16x16x32_bf16 v[44:47], v[180:183], v[204:207], v[44:47]
	v_mfma_f32_16x16x32_bf16 v[36:39], v[188:191], v[204:207], v[36:39]
	v_mfma_f32_16x16x32_bf16 v[28:31], v[180:183], v[212:215], v[28:31]
	v_mfma_f32_16x16x32_bf16 v[20:23], v[188:191], v[212:215], v[20:23]
	v_mfma_f32_16x16x32_bf16 v[12:15], v[180:183], v[224:227], v[12:15]
	v_mfma_f32_16x16x32_bf16 v[0:3], v[188:191], v[224:227], v[0:3]
	s_barrier
	s_add_i32 s2, 0, 0x18000
	v_add_u32_e32 v135, s2, v143
	s_add_i32 s76, 0, 0x1c000
	ds_read_b128 v[160:163], v135
	ds_read_b128 v[164:167], v135 offset:1024
	ds_read_b128 v[168:171], v135 offset:2048
	ds_read_b128 v[172:175], v135 offset:3072
	v_add_u32_e32 v135, s76, v143
	ds_read_b128 v[176:179], v135
	ds_read_b128 v[180:183], v135 offset:1024
	ds_read_b128 v[184:187], v135 offset:2048
	ds_read_b128 v[188:191], v135 offset:3072
	s_mov_b32 m0, s68
	ds_read_b128 v[192:195], v152 offset:32768
	ds_read_b128 v[196:199], v152 offset:33792
	ds_read_b128 v[200:203], v152 offset:34816
	ds_read_b128 v[204:207], v152 offset:35840
	ds_read_b128 v[208:211], v152 offset:36864
	ds_read_b128 v[212:215], v152 offset:37888
	ds_read_b128 v[220:223], v152 offset:38912
	ds_read_b128 v[224:227], v152 offset:39936
	s_nop 0
	global_load_lds_dwordx4 v96, s[20:21]
	s_mov_b32 m0, s69
	s_nop 0
	global_load_lds_dwordx4 v133, s[20:21]
	s_waitcnt vmcnt(8)
	s_waitcnt lgkmcnt(0)
	s_barrier
	s_waitcnt lgkmcnt(0)
	v_mfma_f32_16x16x32_bf16 v[122:125], v[160:163], v[192:195], v[122:125]
	v_mfma_f32_16x16x32_bf16 v[114:117], v[168:171], v[192:195], v[114:117]
	v_mfma_f32_16x16x32_bf16 v[106:109], v[160:163], v[200:203], v[106:109]
	v_mfma_f32_16x16x32_bf16 v[98:101], v[168:171], v[200:203], v[98:101]
	v_mfma_f32_16x16x32_bf16 v[88:91], v[160:163], v[208:211], v[88:91]
	v_mfma_f32_16x16x32_bf16 v[80:83], v[168:171], v[208:211], v[80:83]
	v_mfma_f32_16x16x32_bf16 v[72:75], v[160:163], v[220:223], v[72:75]
	v_mfma_f32_16x16x32_bf16 v[64:67], v[168:171], v[220:223], v[64:67]
	v_mfma_f32_16x16x32_bf16 v[122:125], v[164:167], v[196:199], v[122:125]
	v_mfma_f32_16x16x32_bf16 v[114:117], v[172:175], v[196:199], v[114:117]
	v_mfma_f32_16x16x32_bf16 v[106:109], v[164:167], v[204:207], v[106:109]
	v_mfma_f32_16x16x32_bf16 v[98:101], v[172:175], v[204:207], v[98:101]
	v_mfma_f32_16x16x32_bf16 v[88:91], v[164:167], v[212:215], v[88:91]
	v_mfma_f32_16x16x32_bf16 v[80:83], v[172:175], v[212:215], v[80:83]
	v_mfma_f32_16x16x32_bf16 v[72:75], v[164:167], v[224:227], v[72:75]
	v_mfma_f32_16x16x32_bf16 v[64:67], v[172:175], v[224:227], v[64:67]
	v_mfma_f32_16x16x32_bf16 v[126:129], v[176:179], v[192:195], v[126:129]
	v_mfma_f32_16x16x32_bf16 v[118:121], v[184:187], v[192:195], v[118:121]
	v_mfma_f32_16x16x32_bf16 v[110:113], v[176:179], v[200:203], v[110:113]
	v_mfma_f32_16x16x32_bf16 v[102:105], v[184:187], v[200:203], v[102:105]
	v_mfma_f32_16x16x32_bf16 v[92:95], v[176:179], v[208:211], v[92:95]
	v_mfma_f32_16x16x32_bf16 v[84:87], v[184:187], v[208:211], v[84:87]
	v_mfma_f32_16x16x32_bf16 v[76:79], v[176:179], v[220:223], v[76:79]
	v_mfma_f32_16x16x32_bf16 v[68:71], v[184:187], v[220:223], v[68:71]
	v_mfma_f32_16x16x32_bf16 v[126:129], v[180:183], v[196:199], v[126:129]
	v_mfma_f32_16x16x32_bf16 v[118:121], v[188:191], v[196:199], v[118:121]
	v_mfma_f32_16x16x32_bf16 v[110:113], v[180:183], v[204:207], v[110:113]
	v_mfma_f32_16x16x32_bf16 v[102:105], v[188:191], v[204:207], v[102:105]
	v_mfma_f32_16x16x32_bf16 v[92:95], v[180:183], v[212:215], v[92:95]
	v_mfma_f32_16x16x32_bf16 v[84:87], v[188:191], v[212:215], v[84:87]
	v_mfma_f32_16x16x32_bf16 v[76:79], v[180:183], v[224:227], v[76:79]
	v_mfma_f32_16x16x32_bf16 v[68:71], v[188:191], v[224:227], v[68:71]
	s_barrier
; #define PG8_STAGE(bufoff, gbase, voff) do { _Pragma("unroll") for (int _i = 0; _i < 2; ++_i) \
;         __builtin_amdgcn_global_load_lds((const __attribute__((address_space(1))) unsigned*)((const __attribute__((address_space(1))) char*)(gbase) + (unsigned)lnd_v((int)(voff)[_i])), (LAS unsigned*)(lds + (bufoff) + ldsw + _i * 8192), 16, 0, 0); } while (0)
; #define PG8_LDA(dst, b, h) do { _Pragma("unroll") for (int m = 0; m < 4; ++m) _Pragma("unroll") for (int k = 0; k < 2; ++k) dst[m][k] = *(const LAS bf16x8*)(lds + PG8_SA(b, h) + aoff + m * 2048 + k * 1024); } while (0)
; #define PG8_MMA(ai, bj, At, Bt) do { __builtin_amdgcn_s_setprio(1); _Pragma("unroll") for (int m = 0; m < 4; ++m) _Pragma("unroll") for (int n = 0; n < 2; ++n) _Pragma("unroll") for (int k = 0; k < 2; ++k) \
;         acc[ai][bj][m][n] = __builtin_amdgcn_mfma_f32_16x16x32_bf16(Bt[n][k], At[m][k], acc[ai][bj][m][n], 0, 0, 0); __builtin_amdgcn_s_setprio(0); } while (0)
; #define PG8_WAIT_V(n) asm volatile("s_waitcnt vmcnt(" #n ")" ::: "memory")
; #define PG8_WAIT_L(n) asm volatile("s_waitcnt lgkmcnt(" #n ")" ::: "memory")
; #define PG8_BAR __builtin_amdgcn_s_barrier()
; #define PG8_SCHED __builtin_amdgcn_sched_barrier(0)
; template <class Desc, class Epi>
; __device__ __forceinline__ void gemm_phase(const int wv_, LAS unsigned char* lds, const Desc& d, const Epi& E) {
;     ...
;             PG8_LDA(At, 1, 1); PG8_STAGE(PG8_SB(1, 0), b3, voffB); PG8_STAGE(PG8_SB(1, 1), b3 + hstepB, voffB); PG8_STAGE(PG8_SA(1, 0), a3, sA0);
;             PG8_WAIT_V(8); PG8_WAIT_L(0); PG8_BAR; PG8_MMA(1, 0, At, B0); PG8_MMA(1, 1, At, B1); PG8_BAR; PG8_SCHED;
;         }
	v_mov_b32_e32 v96, v138
	ds_read_b128 v[192:195], v152 offset:49152
	ds_read_b128 v[196:199], v152 offset:50176
	ds_read_b128 v[200:203], v152 offset:51200
	ds_read_b128 v[204:207], v152 offset:52224
	ds_read_b128 v[208:211], v152 offset:53248
	ds_read_b128 v[212:215], v152 offset:54272
	ds_read_b128 v[220:223], v152 offset:55296
	ds_read_b128 v[224:227], v152 offset:56320
	s_add_i32 s2, s2, s63
	v_lshl_add_u64 v[228:229], s[22:23], 0, v[96:97]
	v_lshl_add_u64 v[228:229], v[228:229], 0, s[30:31]
	s_mov_b32 m0, s2
	v_mov_b32_e32 v96, v141
	global_load_lds_dwordx4 v[228:229], off
	s_add_i32 m0, s2, 0x2000
	s_add_u32 s2, s22, 0x40080
	v_lshl_add_u64 v[228:229], s[22:23], 0, v[96:97]
	v_lshl_add_u64 v[228:229], v[228:229], 0, s[30:31]
	s_addc_u32 s3, s23, 0
	s_add_i32 s22, s76, s63
	global_load_lds_dwordx4 v[228:229], off
	s_mov_b32 m0, s22
	v_mov_b32_e32 v135, v97
	global_load_lds_dwordx4 v138, s[2:3]
	v_mov_b32_e32 v96, v141
	s_add_i32 m0, s22, 0x2000
	v_mov_b32_e32 v133, v97
	global_load_lds_dwordx4 v96, s[2:3]
	s_mov_b32 m0, s70
	v_lshl_add_u64 v[134:135], s[20:21], 0, v[134:135]
	v_lshl_add_u64 v[134:135], v[134:135], 0, s[30:31]
	global_load_lds_dwordx4 v[134:135], off
	s_mov_b32 m0, s71
	v_lshl_add_u64 v[132:133], s[20:21], 0, v[132:133]
	v_lshl_add_u64 v[132:133], v[132:133], 0, s[30:31]
	global_load_lds_dwordx4 v[132:133], off
	s_waitcnt vmcnt(8)
	s_waitcnt lgkmcnt(0)
	s_barrier
	s_waitcnt lgkmcnt(0)
	v_mfma_f32_16x16x32_bf16 v[56:59], v[160:163], v[192:195], v[56:59]
	v_mfma_f32_16x16x32_bf16 v[48:51], v[168:171], v[192:195], v[48:51]
	v_mfma_f32_16x16x32_bf16 v[40:43], v[160:163], v[200:203], v[40:43]
	v_mfma_f32_16x16x32_bf16 v[32:35], v[168:171], v[200:203], v[32:35]
	v_mfma_f32_16x16x32_bf16 v[24:27], v[160:163], v[208:211], v[24:27]
	v_mfma_f32_16x16x32_bf16 v[16:19], v[168:171], v[208:211], v[16:19]
	v_mfma_f32_16x16x32_bf16 v[8:11], v[160:163], v[220:223], v[8:11]
	v_mfma_f32_16x16x32_bf16 v[4:7], v[168:171], v[220:223], v[4:7]
	v_mfma_f32_16x16x32_bf16 v[56:59], v[164:167], v[196:199], v[56:59]
	v_mfma_f32_16x16x32_bf16 v[48:51], v[172:175], v[196:199], v[48:51]
	v_mfma_f32_16x16x32_bf16 v[40:43], v[164:167], v[204:207], v[40:43]
	v_mfma_f32_16x16x32_bf16 v[32:35], v[172:175], v[204:207], v[32:35]
	v_mfma_f32_16x16x32_bf16 v[24:27], v[164:167], v[212:215], v[24:27]
	v_mfma_f32_16x16x32_bf16 v[16:19], v[172:175], v[212:215], v[16:19]
	v_mfma_f32_16x16x32_bf16 v[8:11], v[164:167], v[224:227], v[8:11]
	v_mfma_f32_16x16x32_bf16 v[4:7], v[172:175], v[224:227], v[4:7]
	v_mfma_f32_16x16x32_bf16 v[60:63], v[176:179], v[192:195], v[60:63]
	v_mfma_f32_16x16x32_bf16 v[52:55], v[184:187], v[192:195], v[52:55]
	v_mfma_f32_16x16x32_bf16 v[44:47], v[176:179], v[200:203], v[44:47]
	v_mfma_f32_16x16x32_bf16 v[36:39], v[184:187], v[200:203], v[36:39]
	v_mfma_f32_16x16x32_bf16 v[28:31], v[176:179], v[208:211], v[28:31]
	v_mfma_f32_16x16x32_bf16 v[20:23], v[184:187], v[208:211], v[20:23]
	v_mfma_f32_16x16x32_bf16 v[12:15], v[176:179], v[220:223], v[12:15]
	v_mfma_f32_16x16x32_bf16 v[0:3], v[184:187], v[220:223], v[0:3]
	v_mfma_f32_16x16x32_bf16 v[60:63], v[180:183], v[196:199], v[60:63]
	v_mfma_f32_16x16x32_bf16 v[52:55], v[188:191], v[196:199], v[52:55]
	v_mfma_f32_16x16x32_bf16 v[44:47], v[180:183], v[204:207], v[44:47]
	v_mfma_f32_16x16x32_bf16 v[36:39], v[188:191], v[204:207], v[36:39]
	v_mfma_f32_16x16x32_bf16 v[28:31], v[180:183], v[212:215], v[28:31]
	v_mfma_f32_16x16x32_bf16 v[20:23], v[188:191], v[212:215], v[20:23]
	v_mfma_f32_16x16x32_bf16 v[12:15], v[180:183], v[224:227], v[12:15]
	v_mfma_f32_16x16x32_bf16 v[0:3], v[188:191], v[224:227], v[0:3]
	s_barrier
	s_add_i32 s75, s75, 2
	s_cmp_gt_u32 s75, 13
	s_mov_b64 s[2:3], s[4:5]
	s_cbranch_scc0 .LBB0_1565
	s_and_b64 vcc, exec, s[52:53]
	s_cbranch_vccz .LBB0_1568
	s_barrier

; #define LAS __attribute__((address_space(3)))
; template <class Desc, class Epi>
; __device__ __forceinline__ void gemm_phase(const int wv_, LAS unsigned char* lds, const Desc& d, const Epi& E) {
;     ...
; #pragma unroll
;     for (int i = 0; i < 2; ++i) { int R, C; stage_rc(tid * 16 + i * 8192, R, C); const int Rb = (R & ~31) + perm32(R & 31); Rr[i] = R; Cc[i] = C;
;         voffA[i] = (unsigned)(R * d.lda + C) * 2u; voffA1[i] = voffA[i] + (unsigned)hstepA; voffB[i] = (unsigned)(Rb * d.ldb + C) * 2u; }
;     unsigned voffAn[2] = {0u, 0u}, voffAn1[2] = {0u, 0u};
;     LAS unsigned short* const tix = (LAS unsigned short*)(lds + STAGE_BYTES + 16384);
;     ...
;     const unsigned ldsw = (unsigned)wid * 1024u;
;     const int aoff = lds_byte(wr * 64 + fr, fq * 8), boff = lds_byte(wc * 32 + fr, fq * 8);
;     ...
;     GU cur, nxt; int ui = 0;
;     if (bid < 0 || bid >= d.nunits) return;
;     LAS float* const rsc = (LAS float*)(lds + STAGE_BYTES);
;     if constexpr (Epi::STAGED || Desc::GATHER) {
;         const int nmy = (d.nunits - bid + nblk - 1) / nblk;
;         for (int idx = tid; idx < nmy * 256; idx += NTHREADS) { GU su; d.unit(bid + (idx >> 8) * nblk, su);
;             if constexpr (Epi::STAGED) rsc[idx] = E.rowscale(su, idx & 255);
;             if constexpr (Desc::GATHER) tix[idx] = (unsigned short)d.tokidx(su, idx & 255); }
;         asm volatile("s_waitcnt vmcnt(0) lgkmcnt(0)" ::: "memory"); __builtin_amdgcn_s_barrier(); asm volatile("" ::: "memory");
;     }
;     d.unit(bid, cur);
;     if constexpr (Desc::GATHER) PG8_AOFF(0, cur, voffA, voffA1);
;     f32x4 acc[2][2][4][2];
; #pragma unroll
;     for (int a = 0; a < 2; ++a)
; #pragma unroll
;         for (int b = 0; b < 2; ++b)
; #pragma unroll
;             for (int m = 0; m < 4; ++m)
; #pragma unroll
;                 for (int n = 0; n < 2; ++n) acc[a][b][m][n] = (f32x4){0.f, 0.f, 0.f, 0.f};
;     bf16x8 At[4][2], B0[2][2], B1[2][2];
;     const char* cA = (const char*)cur.a; const char* cB = (const char*)cur.b;
;     PG8_STAGE(PG8_SB(0, 0), cB, voffB); PG8_STAGE(PG8_SB(0, 1), cB + hstepB, voffB); PG8_STAGE(PG8_SA(0, 0), cA, voffA); PG8_STAGE(PG8_SA(0, 1), cA, voffA1);
;     if (wr == 1) PG8_BAR;
;     PG8_WAIT_V(2); PG8_BAR;
;     PG8_STAGE(PG8_SB(1, 0), cB + kstep, voffB); PG8_STAGE(PG8_SA(1, 0), cA + kstep, voffA); PG8_STAGE(PG8_SB(1, 1), cB + hstepB + kstep, voffB);
;     PG8_WAIT_V(6); PG8_BAR;
.LBB0_1853:
	s_or_b64 exec, exec, s[2:3]
	v_ashrrev_i32_e32 v2, 31, v0
	v_lshrrev_b32_e32 v2, 26, v2
	v_lshlrev_b32_e32 v1, 4, v0
	v_add_u32_e32 v2, v0, v2
	v_bfe_i32 v0, v0, 27, 1
	v_lshrrev_b32_e32 v0, 22, v0
	v_add_u32_e32 v0, v1, v0
	v_and_b32_e32 v0, 0xfffffc00, v0
	v_sub_u32_e32 v0, v1, v0
	v_lshrrev_b32_e32 v3, 4, v0
	v_bitop3_b32 v0, v3, v0, 32 bitop3:0x6c
	v_ashrrev_i32_e32 v5, 31, v0
	v_ashrrev_i32_e32 v2, 6, v2
	v_lshrrev_b32_e32 v5, 26, v5
	v_lshlrev_b32_e32 v3, 3, v2
	v_add_u32_e32 v5, v0, v5
	v_and_b32_e32 v3, -16, v3
	v_ashrrev_i32_e32 v6, 6, v5
	v_add_u32_e32 v136, v6, v3
	v_and_b32_e32 v3, 0xc0, v5
	v_sub_u32_e32 v0, v0, v3
	v_lshlrev_b32_e32 v2, 5, v2
	v_ashrrev_i16_sdwa v0, v216, sext(v0) dst_sel:DWORD dst_unused:UNUSED_PAD src0_sel:DWORD src1_sel:BYTE_0
	v_and_b32_e32 v2, 32, v2
	v_bfe_i32 v0, v0, 0, 16
	v_add_lshl_u32 v137, v2, v0, 1
	v_add_u32_e32 v0, 0x2000, v1
	v_ashrrev_i32_e32 v1, 31, v0
	v_lshrrev_b32_e32 v1, 22, v1
	s_lshl_b32 s0, s66, 1
	v_add_u32_e32 v1, v0, v1
	s_add_u32 s0, s46, s0
	v_ashrrev_i32_e32 v1, 10, v1
	s_addc_u32 s1, s47, 0
	v_mul_i32_i24_e32 v2, 0x400, v1
	s_add_u32 s24, s0, 0x3600000
	v_lshlrev_b32_e32 v3, 1, v136
	v_lshrrev_b32_e32 v7, 2, v136
	v_and_b32_e32 v6, 3, v6
	s_mov_b32 s0, 0x1fffe0
	v_sub_u32_e32 v0, v0, v2
	v_and_b32_e32 v5, 24, v3
	v_and_b32_e32 v7, 4, v7
	v_and_or_b32 v6, v136, s0, v6
	v_lshrrev_b32_e32 v2, 4, v0
	v_or3_b32 v5, v6, v7, v5
	v_bitop3_b32 v0, v2, v0, 32 bitop3:0x6c
	v_lshl_add_u32 v138, v5, 11, v137
	v_ashrrev_i32_e32 v5, 31, v0
	v_lshrrev_b32_e32 v5, 26, v5
	v_lshlrev_b32_e32 v2, 3, v1
	v_add_u32_e32 v5, v0, v5
	v_and_b32_e32 v2, -16, v2
	v_ashrrev_i32_e32 v6, 6, v5
	v_add_u32_e32 v139, v6, v2
	v_and_b32_e32 v6, 3, v6
	s_addc_u32 s25, s1, 0
	v_and_b32_e32 v2, 0xc0, v5
	v_and_or_b32 v6, v139, s0, v6
	s_lshl_b32 s0, s36, 1
	v_sub_u32_e32 v0, v0, v2
	s_and_b32 s1, s0, 12
	s_lshr_b32 s0, s36, 6
	v_lshlrev_b32_e32 v1, 5, v1
	v_ashrrev_i16_sdwa v0, v216, sext(v0) dst_sel:DWORD dst_unused:UNUSED_PAD src0_sel:DWORD src1_sel:BYTE_0
	s_and_b32 s2, s0, 2
	v_and_b32_e32 v1, 32, v1
	v_bfe_i32 v0, v0, 0, 16
	v_lshlrev_b32_e32 v2, 1, v139
	s_lshr_b32 s26, s36, 8
	s_or_b32 s2, s1, s2
	v_readlane_b32 s23, v254, 54
	v_and_b32_e32 v5, 24, v2
	v_add_lshl_u32 v140, v1, v0, 1
	s_waitcnt vmcnt(0) lgkmcnt(0)
	s_barrier
	s_lshl_b32 s1, s36, 3
	s_lshl_b32 s20, s2, 4
	s_lshl_b32 s2, s26, 1
	v_add_u32_e32 v0, s23, v3
	v_add_u32_e32 v2, s23, v2
	s_and_b32 s1, s1, 8
	s_bfe_u32 s3, s54, 0x30003
	s_add_i32 s20, s20, s2
	ds_read_u16 v1, v0
	ds_read_u16 v0, v0 offset:256
	ds_read_u16 v3, v2
	ds_read_u16 v2, v2 offset:256
	s_ashr_i32 s5, s40, 6
	s_or_b32 s1, s1, s3
	s_lshl_b32 s22, s20, 7
	s_ashr_i32 s4, s40, 8
	s_lshl_b32 s56, s5, 10
	s_lshl_b32 s21, s1, 19
	s_lshl_b64 s[2:3], s[26:27], 23
	s_and_b32 s22, s22, 0x7ffff000
	s_waitcnt lgkmcnt(0)
	v_add_u32_e32 v0, s22, v0
	s_add_u32 s2, s24, s2
	v_lshrrev_b32_e32 v7, 2, v139
	v_lshl_add_u32 v131, v0, 11, v137
	v_add_u32_e32 v0, s22, v3
	s_addc_u32 s3, s25, s3
	v_and_b32_e32 v7, 4, v7
	v_lshl_add_u32 v159, v0, 11, v140
	v_add_u32_e32 v0, s22, v2
	s_add_u32 s2, s2, s21
	v_or3_b32 v5, v6, v7, v5
	v_lshl_add_u32 v158, v0, 11, v140
	s_addc_u32 s3, s3, 0
	s_add_i32 s57, s56, 0
	v_lshl_add_u32 v141, v5, 11, v140
	s_add_i32 m0, s57, 0x10000
	v_add_u32_e32 v1, s22, v1
	global_load_lds_dwordx4 v138, s[2:3]
	s_add_i32 m0, s57, 0x12000
	s_add_u32 s22, s2, 0x40000
	global_load_lds_dwordx4 v141, s[2:3]
	s_addc_u32 s23, s3, 0
	s_add_i32 m0, s57, 0x14000
	v_lshl_add_u32 v157, v1, 11, v137
	global_load_lds_dwordx4 v138, s[22:23]
	s_add_i32 m0, s57, 0x16000
	s_add_i32 s58, s57, 0x2000
	global_load_lds_dwordx4 v141, s[22:23]
	s_mov_b32 m0, s57
	s_add_i32 s59, s57, 0x4000
	global_load_lds_dwordx4 v157, s[42:43]
	s_mov_b32 m0, s58
	s_add_i32 s60, s57, 0x6000
	global_load_lds_dwordx4 v159, s[42:43]
	s_mov_b32 m0, s59
	s_cmp_eq_u32 s4, 1
	global_load_lds_dwordx4 v131, s[42:43]
	v_mov_b32_e32 v0, v158
	s_mov_b32 m0, s60
	s_cselect_b64 s[36:37], -1, 0
	global_load_lds_dwordx4 v0, s[42:43]
	s_and_b64 vcc, exec, s[36:37]
	s_cbranch_vccz .LBB0_1855
	s_barrier
.LBB0_1855:
	v_mov_b32_e32 v96, v138
	s_lshl_b32 s5, s5, 5
	s_waitcnt vmcnt(2)
	s_barrier
	s_and_b32 s0, s0, 1
	v_lshl_add_u64 v[0:1], s[2:3], 0, v[96:97]
	s_and_b32 s5, s5, 0x60
	s_add_i32 m0, s57, 0x18000
	v_lshl_add_u64 v[0:1], v[0:1], 0, s[30:31]
	v_mov_b32_e32 v96, v141
	s_or_b32 s0, s20, s0
	s_lshl_b32 s22, s4, 13
	s_lshl_b32 s23, s5, 7
	global_load_lds_dwordx4 v[0:1], off
	s_add_i32 m0, s57, 0x1a000
	v_lshl_add_u64 v[0:1], s[2:3], 0, v[96:97]
	v_lshl_add_u64 v[0:1], v[0:1], 0, s[30:31]
	s_add_u32 s38, s46, 0x33600080
	global_load_lds_dwordx4 v[0:1], off
	s_addc_u32 s39, s47, 0
	s_add_i32 s61, s57, 0x8000
	s_mov_b32 m0, s61
	s_add_i32 s62, s57, 0xa000
	global_load_lds_dwordx4 v157, s[38:39]
	s_mov_b32 m0, s62
	s_add_u32 s20, s2, 0x40080
	global_load_lds_dwordx4 v159, s[38:39]
	s_addc_u32 s21, s3, 0
	s_add_i32 m0, s57, 0x1c000
	v_and_b32_e32 v1, 15, v4
	global_load_lds_dwordx4 v138, s[20:21]
	s_add_i32 m0, s57, 0x1e000
	v_lshl_or_b32 v142, s4, 6, v1
	global_load_lds_dwordx4 v141, s[20:21]
	v_lshrrev_b32_e32 v0, 1, v4
	v_and_b32_e32 v0, 24, v0
	v_lshlrev_b32_e32 v2, 1, v0
	v_lshl_or_b32 v1, v1, 6, v2
	v_lshlrev_b32_e32 v2, 2, v142
	v_and_b32_e32 v3, 32, v2
	v_lshlrev_b32_e32 v4, 2, v4
	s_waitcnt vmcnt(6)
	s_cmpk_lt_u32 s40, 0x100
	v_bitop3_b32 v3, v1, s22, v3 bitop3:0xde
	v_and_b32_e32 v4, 32, v4
	s_cselect_b64 s[40:41], -1, 0
	s_add_i32 s4, 0, 0x20000
	v_bitop3_b32 v143, v1, s23, v4 bitop3:0xde
	v_or_b32_e32 v144, 16, v142
	v_or_b32_e32 v145, 32, v142
	v_or_b32_e32 v146, 48, v142
	v_add_u32_e32 v147, 0x80, v142
	v_add_u32_e32 v148, 0x90, v142
	v_add_u32_e32 v149, 0xa0, v142
	v_add_u32_e32 v150, 0xb0, v142
	v_add_u32_e32 v151, s4, v2
	s_mov_b32 s50, 0
	v_add_u32_e32 v152, 0, v3
	s_lshl_b32 s26, s5, 1
	v_lshlrev_b32_e32 v130, 1, v0
	v_mov_b32_e32 v154, v159
	v_mov_b32_e32 v153, v157
	v_mov_b32_e32 v156, v158
	v_mov_b32_e32 v155, v131
	s_mov_b64 s[46:47], s[2:3]
	s_barrier
	s_waitcnt vmcnt(0)
	s_branch .LBB0_1858

; #define PG8_STAGE(bufoff, gbase, voff) do { _Pragma("unroll") for (int _i = 0; _i < 2; ++_i) \
;         __builtin_amdgcn_global_load_lds((const __attribute__((address_space(1))) unsigned*)((const __attribute__((address_space(1))) char*)(gbase) + (unsigned)lnd_v((int)(voff)[_i])), (LAS unsigned*)(lds + (bufoff) + ldsw + _i * 8192), 16, 0, 0); } while (0)
; #define PG8_LDA(dst, b, h) do { _Pragma("unroll") for (int m = 0; m < 4; ++m) _Pragma("unroll") for (int k = 0; k < 2; ++k) dst[m][k] = *(const LAS bf16x8*)(lds + PG8_SA(b, h) + aoff + m * 2048 + k * 1024); } while (0)
; #define PG8_LDB(dst, b, h) do { _Pragma("unroll") for (int n = 0; n < 2; ++n) _Pragma("unroll") for (int k = 0; k < 2; ++k) dst[n][k] = *(const LAS bf16x8*)(lds + PG8_SB(b, h) + boff + n * 2048 + k * 1024); } while (0)
; #define PG8_WAIT_V(n) asm volatile("s_waitcnt vmcnt(" #n ")" ::: "memory")
; #define PG8_WAIT_L(n) asm volatile("s_waitcnt lgkmcnt(" #n ")" ::: "memory")
; #define PG8_BAR __builtin_amdgcn_s_barrier()
; template <class Desc, class Epi>
; __device__ __forceinline__ void gemm_phase(const int wv_, LAS unsigned char* lds, const Desc& d, const Epi& E) {
;     ...
;         const char* nA = has_next ? (const char*)nxt.a : cA; const char* nB = has_next ? (const char*)nxt.b : cB;
;         for (int t = 0; t < nt; t += 2) {
;             const bool last = (t == nt - 2);
;             unsigned sA0[2], sA1[2];
;             if constexpr (Desc::GATHER) { sA0[0] = last ? voffAn[0] : voffA[0]; sA0[1] = last ? voffAn[1] : voffA[1]; sA1[0] = last ? voffAn1[0] : voffA1[0]; sA1[1] = last ? voffAn1[1] : voffA1[1]; }
;             else { sA0[0] = voffA[0]; sA0[1] = voffA[1]; sA1[0] = voffA1[0]; sA1[1] = voffA1[1]; }
;             const char* a1 = cA + (size_t)(t + 1) * kstep;
;             const char* a2 = last ? nA : cA + (size_t)(t + 2) * kstep; const char* b2 = last ? nB : cB + (size_t)(t + 2) * kstep;
;             const char* a3 = a2 + kstep; const char* b3 = b2 + kstep;
;             PG8_LDB(B0, 0, 0); PG8_LDB(B1, 0, 1); PG8_SCHED; PG8_LDA(At, 0, 0); PG8_STAGE(PG8_SA(1, 1), a1, voffA1);
;             PG8_WAIT_V(8); PG8_WAIT_L(0); PG8_BAR; PG8_MMA(0, 0, At, B0); PG8_MMA(0, 1, At, B1); PG8_BAR; PG8_SCHED;
;             PG8_LDA(At, 0, 1); PG8_STAGE(PG8_SB(0, 0), b2, voffB); PG8_STAGE(PG8_SB(0, 1), b2 + hstepB, voffB); PG8_STAGE(PG8_SA(0, 0), a2, sA0);
.LBB0_1861:
	s_add_u32 s4, s2, 0x100
	s_addc_u32 s5, s3, 0
	s_add_u32 s22, s29, s2
	s_addc_u32 s23, s51, s3
	s_cmp_eq_u32 s66, 12
	s_cselect_b64 vcc, -1, 0
	s_and_b64 s[20:21], vcc, exec
	s_cselect_b32 s20, 0, s4
	s_cselect_b32 s21, 0, s5
	s_cselect_b32 s22, s46, s22
	s_cselect_b32 s23, s47, s23
	s_add_u32 s20, s42, s20
	s_addc_u32 s21, s43, s21
	s_add_i32 s67, 0, 0x10000
	v_add_u32_e32 v135, s67, v143
	s_add_i32 s68, 0, 0x14000
	ds_read_b128 v[160:163], v135
	ds_read_b128 v[164:167], v135 offset:1024
	ds_read_b128 v[168:171], v135 offset:2048
	ds_read_b128 v[172:175], v135 offset:3072
	v_add_u32_e32 v135, s68, v143
	ds_read_b128 v[176:179], v135
	ds_read_b128 v[180:183], v135 offset:1024
	ds_read_b128 v[184:187], v135 offset:2048
	ds_read_b128 v[188:191], v135 offset:3072
	v_cndmask_b32_e32 v134, v157, v153, vcc
	v_cndmask_b32_e32 v132, v159, v154, vcc
	v_cndmask_b32_e32 v96, v131, v155, vcc
	v_cndmask_b32_e32 v133, v158, v156, vcc
	s_add_i32 m0, s57, 0xc000
	s_add_u32 s2, s38, s2
	ds_read_b128 v[192:195], v152
	ds_read_b128 v[196:199], v152 offset:1024
	ds_read_b128 v[200:203], v152 offset:2048
	ds_read_b128 v[204:207], v152 offset:3072
	ds_read_b128 v[208:211], v152 offset:4096
	ds_read_b128 v[212:215], v152 offset:5120
	ds_read_b128 v[220:223], v152 offset:6144
	ds_read_b128 v[224:227], v152 offset:7168
	s_addc_u32 s3, s39, s3
	global_load_lds_dwordx4 v131, s[2:3]
	s_add_i32 m0, s57, 0xe000
	s_nop 0
	global_load_lds_dwordx4 v158, s[2:3]
	s_waitcnt vmcnt(8)
	s_waitcnt lgkmcnt(0)
	s_barrier
	s_waitcnt lgkmcnt(0)
	v_mfma_f32_16x16x32_bf16 v[122:125], v[160:163], v[192:195], v[122:125]
	v_mfma_f32_16x16x32_bf16 v[114:117], v[168:171], v[192:195], v[114:117]
	v_mfma_f32_16x16x32_bf16 v[106:109], v[160:163], v[200:203], v[106:109]
	v_mfma_f32_16x16x32_bf16 v[98:101], v[168:171], v[200:203], v[98:101]
	v_mfma_f32_16x16x32_bf16 v[88:91], v[160:163], v[208:211], v[88:91]
	v_mfma_f32_16x16x32_bf16 v[80:83], v[168:171], v[208:211], v[80:83]
	v_mfma_f32_16x16x32_bf16 v[72:75], v[160:163], v[220:223], v[72:75]
	v_mfma_f32_16x16x32_bf16 v[64:67], v[168:171], v[220:223], v[64:67]
	v_mfma_f32_16x16x32_bf16 v[122:125], v[164:167], v[196:199], v[122:125]
	v_mfma_f32_16x16x32_bf16 v[114:117], v[172:175], v[196:199], v[114:117]
	v_mfma_f32_16x16x32_bf16 v[106:109], v[164:167], v[204:207], v[106:109]
	v_mfma_f32_16x16x32_bf16 v[98:101], v[172:175], v[204:207], v[98:101]
	v_mfma_f32_16x16x32_bf16 v[88:91], v[164:167], v[212:215], v[88:91]
	v_mfma_f32_16x16x32_bf16 v[80:83], v[172:175], v[212:215], v[80:83]
	v_mfma_f32_16x16x32_bf16 v[72:75], v[164:167], v[224:227], v[72:75]
	v_mfma_f32_16x16x32_bf16 v[64:67], v[172:175], v[224:227], v[64:67]
	v_mfma_f32_16x16x32_bf16 v[126:129], v[176:179], v[192:195], v[126:129]
	v_mfma_f32_16x16x32_bf16 v[118:121], v[184:187], v[192:195], v[118:121]
	v_mfma_f32_16x16x32_bf16 v[110:113], v[176:179], v[200:203], v[110:113]
	v_mfma_f32_16x16x32_bf16 v[102:105], v[184:187], v[200:203], v[102:105]
	v_mfma_f32_16x16x32_bf16 v[92:95], v[176:179], v[208:211], v[92:95]
	v_mfma_f32_16x16x32_bf16 v[84:87], v[184:187], v[208:211], v[84:87]
	v_mfma_f32_16x16x32_bf16 v[76:79], v[176:179], v[220:223], v[76:79]
	v_mfma_f32_16x16x32_bf16 v[68:71], v[184:187], v[220:223], v[68:71]
	v_mfma_f32_16x16x32_bf16 v[126:129], v[180:183], v[196:199], v[126:129]
	v_mfma_f32_16x16x32_bf16 v[118:121], v[188:191], v[196:199], v[118:121]
	v_mfma_f32_16x16x32_bf16 v[110:113], v[180:183], v[204:207], v[110:113]
	v_mfma_f32_16x16x32_bf16 v[102:105], v[188:191], v[204:207], v[102:105]
	v_mfma_f32_16x16x32_bf16 v[92:95], v[180:183], v[212:215], v[92:95]
	v_mfma_f32_16x16x32_bf16 v[84:87], v[188:191], v[212:215], v[84:87]
	v_mfma_f32_16x16x32_bf16 v[76:79], v[180:183], v[224:227], v[76:79]
	v_mfma_f32_16x16x32_bf16 v[68:71], v[188:191], v[224:227], v[68:71]
	s_barrier
	s_add_i32 s2, s67, s56
	ds_read_b128 v[192:195], v152 offset:16384
	ds_read_b128 v[196:199], v152 offset:17408
	ds_read_b128 v[200:203], v152 offset:18432
	ds_read_b128 v[204:207], v152 offset:19456
	ds_read_b128 v[208:211], v152 offset:20480
	ds_read_b128 v[212:215], v152 offset:21504
	ds_read_b128 v[220:223], v152 offset:22528
	ds_read_b128 v[224:227], v152 offset:23552
	s_mov_b32 m0, s2
	s_nop 0
	global_load_lds_dwordx4 v138, s[22:23]
	s_add_i32 m0, s2, 0x2000
	s_add_u32 s2, s22, 0x40000
	global_load_lds_dwordx4 v141, s[22:23]
	s_addc_u32 s3, s23, 0
	s_add_i32 s67, s68, s56
	s_mov_b32 m0, s67
	s_nop 0
	global_load_lds_dwordx4 v138, s[2:3]
	s_add_i32 m0, s67, 0x2000
	s_nop 0
	global_load_lds_dwordx4 v141, s[2:3]
	s_mov_b32 m0, s57
	s_nop 0
	global_load_lds_dwordx4 v134, s[20:21]
	s_mov_b32 m0, s58
	s_nop 0
	global_load_lds_dwordx4 v132, s[20:21]
	s_waitcnt vmcnt(8)
	s_waitcnt lgkmcnt(0)
	s_barrier
; #define PG8_STAGE(bufoff, gbase, voff) do { _Pragma("unroll") for (int _i = 0; _i < 2; ++_i) \
;         __builtin_amdgcn_global_load_lds((const __attribute__((address_space(1))) unsigned*)((const __attribute__((address_space(1))) char*)(gbase) + (unsigned)lnd_v((int)(voff)[_i])), (LAS unsigned*)(lds + (bufoff) + ldsw + _i * 8192), 16, 0, 0); } while (0)
; #define PG8_LDA(dst, b, h) do { _Pragma("unroll") for (int m = 0; m < 4; ++m) _Pragma("unroll") for (int k = 0; k < 2; ++k) dst[m][k] = *(const LAS bf16x8*)(lds + PG8_SA(b, h) + aoff + m * 2048 + k * 1024); } while (0)
; #define PG8_LDB(dst, b, h) do { _Pragma("unroll") for (int n = 0; n < 2; ++n) _Pragma("unroll") for (int k = 0; k < 2; ++k) dst[n][k] = *(const LAS bf16x8*)(lds + PG8_SB(b, h) + boff + n * 2048 + k * 1024); } while (0)
; #define PG8_MMA(ai, bj, At, Bt) do { __builtin_amdgcn_s_setprio(1); _Pragma("unroll") for (int m = 0; m < 4; ++m) _Pragma("unroll") for (int n = 0; n < 2; ++n) _Pragma("unroll") for (int k = 0; k < 2; ++k) \
;         acc[ai][bj][m][n] = __builtin_amdgcn_mfma_f32_16x16x32_bf16(Bt[n][k], At[m][k], acc[ai][bj][m][n], 0, 0, 0); __builtin_amdgcn_s_setprio(0); } while (0)
; #define PG8_WAIT_V(n) asm volatile("s_waitcnt vmcnt(" #n ")" ::: "memory")
; #define PG8_WAIT_L(n) asm volatile("s_waitcnt lgkmcnt(" #n ")" ::: "memory")
; #define PG8_BAR __builtin_amdgcn_s_barrier()
; #define PG8_SCHED __builtin_amdgcn_sched_barrier(0)
; template <class Desc, class Epi>
; __device__ __forceinline__ void gemm_phase(const int wv_, LAS unsigned char* lds, const Desc& d, const Epi& E) {
;     ...
;             PG8_WAIT_V(8); PG8_WAIT_L(0); PG8_BAR; PG8_MMA(1, 0, At, B0); PG8_MMA(1, 1, At, B1); PG8_BAR; PG8_SCHED;
;             PG8_LDB(B0, 1, 0); PG8_LDB(B1, 1, 1); PG8_SCHED; PG8_LDA(At, 1, 0); PG8_STAGE(PG8_SA(0, 1), a2, sA1);
;             PG8_WAIT_V(8); PG8_WAIT_L(0); PG8_BAR; PG8_MMA(0, 0, At, B0); PG8_MMA(0, 1, At, B1); PG8_BAR; PG8_SCHED;
	s_waitcnt lgkmcnt(0)
	v_mfma_f32_16x16x32_bf16 v[56:59], v[160:163], v[192:195], v[56:59]
	v_mfma_f32_16x16x32_bf16 v[48:51], v[168:171], v[192:195], v[48:51]
	v_mfma_f32_16x16x32_bf16 v[40:43], v[160:163], v[200:203], v[40:43]
	v_mfma_f32_16x16x32_bf16 v[32:35], v[168:171], v[200:203], v[32:35]
	v_mfma_f32_16x16x32_bf16 v[24:27], v[160:163], v[208:211], v[24:27]
	v_mfma_f32_16x16x32_bf16 v[16:19], v[168:171], v[208:211], v[16:19]
	v_mfma_f32_16x16x32_bf16 v[8:11], v[160:163], v[220:223], v[8:11]
	v_mfma_f32_16x16x32_bf16 v[4:7], v[168:171], v[220:223], v[4:7]
	v_mfma_f32_16x16x32_bf16 v[56:59], v[164:167], v[196:199], v[56:59]
	v_mfma_f32_16x16x32_bf16 v[48:51], v[172:175], v[196:199], v[48:51]
	v_mfma_f32_16x16x32_bf16 v[40:43], v[164:167], v[204:207], v[40:43]
	v_mfma_f32_16x16x32_bf16 v[32:35], v[172:175], v[204:207], v[32:35]
	v_mfma_f32_16x16x32_bf16 v[24:27], v[164:167], v[212:215], v[24:27]
	v_mfma_f32_16x16x32_bf16 v[16:19], v[172:175], v[212:215], v[16:19]
	v_mfma_f32_16x16x32_bf16 v[8:11], v[164:167], v[224:227], v[8:11]
	v_mfma_f32_16x16x32_bf16 v[4:7], v[172:175], v[224:227], v[4:7]
	v_mfma_f32_16x16x32_bf16 v[60:63], v[176:179], v[192:195], v[60:63]
	v_mfma_f32_16x16x32_bf16 v[52:55], v[184:187], v[192:195], v[52:55]
	v_mfma_f32_16x16x32_bf16 v[44:47], v[176:179], v[200:203], v[44:47]
	v_mfma_f32_16x16x32_bf16 v[36:39], v[184:187], v[200:203], v[36:39]
	v_mfma_f32_16x16x32_bf16 v[28:31], v[176:179], v[208:211], v[28:31]
	v_mfma_f32_16x16x32_bf16 v[20:23], v[184:187], v[208:211], v[20:23]
	v_mfma_f32_16x16x32_bf16 v[12:15], v[176:179], v[220:223], v[12:15]
	v_mfma_f32_16x16x32_bf16 v[0:3], v[184:187], v[220:223], v[0:3]
	v_mfma_f32_16x16x32_bf16 v[60:63], v[180:183], v[196:199], v[60:63]
	v_mfma_f32_16x16x32_bf16 v[52:55], v[188:191], v[196:199], v[52:55]
	v_mfma_f32_16x16x32_bf16 v[44:47], v[180:183], v[204:207], v[44:47]
	v_mfma_f32_16x16x32_bf16 v[36:39], v[188:191], v[204:207], v[36:39]
	v_mfma_f32_16x16x32_bf16 v[28:31], v[180:183], v[212:215], v[28:31]
	v_mfma_f32_16x16x32_bf16 v[20:23], v[188:191], v[212:215], v[20:23]
	v_mfma_f32_16x16x32_bf16 v[12:15], v[180:183], v[224:227], v[12:15]
	v_mfma_f32_16x16x32_bf16 v[0:3], v[188:191], v[224:227], v[0:3]
	s_barrier
	s_add_i32 s2, 0, 0x18000
	v_add_u32_e32 v135, s2, v143
	s_add_i32 s67, 0, 0x1c000
	ds_read_b128 v[160:163], v135
	ds_read_b128 v[164:167], v135 offset:1024
	ds_read_b128 v[168:171], v135 offset:2048
	ds_read_b128 v[172:175], v135 offset:3072
	v_add_u32_e32 v135, s67, v143
	ds_read_b128 v[176:179], v135
	ds_read_b128 v[180:183], v135 offset:1024
	ds_read_b128 v[184:187], v135 offset:2048
	ds_read_b128 v[188:191], v135 offset:3072
	s_mov_b32 m0, s59
	ds_read_b128 v[192:195], v152 offset:32768
	ds_read_b128 v[196:199], v152 offset:33792
	ds_read_b128 v[200:203], v152 offset:34816
	ds_read_b128 v[204:207], v152 offset:35840
	ds_read_b128 v[208:211], v152 offset:36864
	ds_read_b128 v[212:215], v152 offset:37888
	ds_read_b128 v[220:223], v152 offset:38912
	ds_read_b128 v[224:227], v152 offset:39936
	s_nop 0
	global_load_lds_dwordx4 v96, s[20:21]
	s_mov_b32 m0, s60
	s_nop 0
	global_load_lds_dwordx4 v133, s[20:21]
	s_waitcnt vmcnt(8)
	s_waitcnt lgkmcnt(0)
	s_barrier
	s_waitcnt lgkmcnt(0)
	v_mfma_f32_16x16x32_bf16 v[122:125], v[160:163], v[192:195], v[122:125]
	v_mfma_f32_16x16x32_bf16 v[114:117], v[168:171], v[192:195], v[114:117]
	v_mfma_f32_16x16x32_bf16 v[106:109], v[160:163], v[200:203], v[106:109]
	v_mfma_f32_16x16x32_bf16 v[98:101], v[168:171], v[200:203], v[98:101]
	v_mfma_f32_16x16x32_bf16 v[88:91], v[160:163], v[208:211], v[88:91]
	v_mfma_f32_16x16x32_bf16 v[80:83], v[168:171], v[208:211], v[80:83]
	v_mfma_f32_16x16x32_bf16 v[72:75], v[160:163], v[220:223], v[72:75]
	v_mfma_f32_16x16x32_bf16 v[64:67], v[168:171], v[220:223], v[64:67]
	v_mfma_f32_16x16x32_bf16 v[122:125], v[164:167], v[196:199], v[122:125]
	v_mfma_f32_16x16x32_bf16 v[114:117], v[172:175], v[196:199], v[114:117]
	v_mfma_f32_16x16x32_bf16 v[106:109], v[164:167], v[204:207], v[106:109]
	v_mfma_f32_16x16x32_bf16 v[98:101], v[172:175], v[204:207], v[98:101]
	v_mfma_f32_16x16x32_bf16 v[88:91], v[164:167], v[212:215], v[88:91]
	v_mfma_f32_16x16x32_bf16 v[80:83], v[172:175], v[212:215], v[80:83]
	v_mfma_f32_16x16x32_bf16 v[72:75], v[164:167], v[224:227], v[72:75]
	v_mfma_f32_16x16x32_bf16 v[64:67], v[172:175], v[224:227], v[64:67]
	v_mfma_f32_16x16x32_bf16 v[126:129], v[176:179], v[192:195], v[126:129]
	v_mfma_f32_16x16x32_bf16 v[118:121], v[184:187], v[192:195], v[118:121]
	v_mfma_f32_16x16x32_bf16 v[110:113], v[176:179], v[200:203], v[110:113]
	v_mfma_f32_16x16x32_bf16 v[102:105], v[184:187], v[200:203], v[102:105]
	v_mfma_f32_16x16x32_bf16 v[92:95], v[176:179], v[208:211], v[92:95]
	v_mfma_f32_16x16x32_bf16 v[84:87], v[184:187], v[208:211], v[84:87]
	v_mfma_f32_16x16x32_bf16 v[76:79], v[176:179], v[220:223], v[76:79]
	v_mfma_f32_16x16x32_bf16 v[68:71], v[184:187], v[220:223], v[68:71]
	v_mfma_f32_16x16x32_bf16 v[126:129], v[180:183], v[196:199], v[126:129]
	v_mfma_f32_16x16x32_bf16 v[118:121], v[188:191], v[196:199], v[118:121]
	v_mfma_f32_16x16x32_bf16 v[110:113], v[180:183], v[204:207], v[110:113]
	v_mfma_f32_16x16x32_bf16 v[102:105], v[188:191], v[204:207], v[102:105]
	v_mfma_f32_16x16x32_bf16 v[92:95], v[180:183], v[212:215], v[92:95]
	v_mfma_f32_16x16x32_bf16 v[84:87], v[188:191], v[212:215], v[84:87]
	v_mfma_f32_16x16x32_bf16 v[76:79], v[180:183], v[224:227], v[76:79]
	v_mfma_f32_16x16x32_bf16 v[68:71], v[188:191], v[224:227], v[68:71]
	s_barrier
; #define PG8_STAGE(bufoff, gbase, voff) do { _Pragma("unroll") for (int _i = 0; _i < 2; ++_i) \
;         __builtin_amdgcn_global_load_lds((const __attribute__((address_space(1))) unsigned*)((const __attribute__((address_space(1))) char*)(gbase) + (unsigned)lnd_v((int)(voff)[_i])), (LAS unsigned*)(lds + (bufoff) + ldsw + _i * 8192), 16, 0, 0); } while (0)
; #define PG8_LDA(dst, b, h) do { _Pragma("unroll") for (int m = 0; m < 4; ++m) _Pragma("unroll") for (int k = 0; k < 2; ++k) dst[m][k] = *(const LAS bf16x8*)(lds + PG8_SA(b, h) + aoff + m * 2048 + k * 1024); } while (0)
; #define PG8_MMA(ai, bj, At, Bt) do { __builtin_amdgcn_s_setprio(1); _Pragma("unroll") for (int m = 0; m < 4; ++m) _Pragma("unroll") for (int n = 0; n < 2; ++n) _Pragma("unroll") for (int k = 0; k < 2; ++k) \
;         acc[ai][bj][m][n] = __builtin_amdgcn_mfma_f32_16x16x32_bf16(Bt[n][k], At[m][k], acc[ai][bj][m][n], 0, 0, 0); __builtin_amdgcn_s_setprio(0); } while (0)
; #define PG8_WAIT_V(n) asm volatile("s_waitcnt vmcnt(" #n ")" ::: "memory")
; #define PG8_WAIT_L(n) asm volatile("s_waitcnt lgkmcnt(" #n ")" ::: "memory")
; #define PG8_BAR __builtin_amdgcn_s_barrier()
; #define PG8_SCHED __builtin_amdgcn_sched_barrier(0)
; template <class Desc, class Epi>
; __device__ __forceinline__ void gemm_phase(const int wv_, LAS unsigned char* lds, const Desc& d, const Epi& E) {
;     ...
;             PG8_LDA(At, 1, 1); PG8_STAGE(PG8_SB(1, 0), b3, voffB); PG8_STAGE(PG8_SB(1, 1), b3 + hstepB, voffB); PG8_STAGE(PG8_SA(1, 0), a3, sA0);
;             PG8_WAIT_V(8); PG8_WAIT_L(0); PG8_BAR; PG8_MMA(1, 0, At, B0); PG8_MMA(1, 1, At, B1); PG8_BAR; PG8_SCHED;
;         }
	v_mov_b32_e32 v96, v138
	ds_read_b128 v[192:195], v152 offset:49152
	ds_read_b128 v[196:199], v152 offset:50176
	ds_read_b128 v[200:203], v152 offset:51200
	ds_read_b128 v[204:207], v152 offset:52224
	ds_read_b128 v[208:211], v152 offset:53248
	ds_read_b128 v[212:215], v152 offset:54272
	ds_read_b128 v[220:223], v152 offset:55296
	ds_read_b128 v[224:227], v152 offset:56320
	s_add_i32 s2, s2, s56
	v_lshl_add_u64 v[228:229], s[22:23], 0, v[96:97]
	v_lshl_add_u64 v[228:229], v[228:229], 0, s[30:31]
	s_mov_b32 m0, s2
	v_mov_b32_e32 v96, v141
	global_load_lds_dwordx4 v[228:229], off
	s_add_i32 m0, s2, 0x2000
	s_add_u32 s2, s22, 0x40080
	v_lshl_add_u64 v[228:229], s[22:23], 0, v[96:97]
	v_lshl_add_u64 v[228:229], v[228:229], 0, s[30:31]
	s_addc_u32 s3, s23, 0
	s_add_i32 s22, s67, s56
	global_load_lds_dwordx4 v[228:229], off
	s_mov_b32 m0, s22
	v_mov_b32_e32 v135, v97
	global_load_lds_dwordx4 v138, s[2:3]
	v_mov_b32_e32 v96, v141
	s_add_i32 m0, s22, 0x2000
	v_mov_b32_e32 v133, v97
	global_load_lds_dwordx4 v96, s[2:3]
	s_mov_b32 m0, s61
	v_lshl_add_u64 v[134:135], s[20:21], 0, v[134:135]
	v_lshl_add_u64 v[134:135], v[134:135], 0, s[30:31]
	global_load_lds_dwordx4 v[134:135], off
	s_mov_b32 m0, s62
	v_lshl_add_u64 v[132:133], s[20:21], 0, v[132:133]
	v_lshl_add_u64 v[132:133], v[132:133], 0, s[30:31]
	global_load_lds_dwordx4 v[132:133], off
	s_waitcnt vmcnt(8)
	s_waitcnt lgkmcnt(0)
	s_barrier
	s_waitcnt lgkmcnt(0)
	v_mfma_f32_16x16x32_bf16 v[56:59], v[160:163], v[192:195], v[56:59]
	v_mfma_f32_16x16x32_bf16 v[48:51], v[168:171], v[192:195], v[48:51]
	v_mfma_f32_16x16x32_bf16 v[40:43], v[160:163], v[200:203], v[40:43]
	v_mfma_f32_16x16x32_bf16 v[32:35], v[168:171], v[200:203], v[32:35]
	v_mfma_f32_16x16x32_bf16 v[24:27], v[160:163], v[208:211], v[24:27]
	v_mfma_f32_16x16x32_bf16 v[16:19], v[168:171], v[208:211], v[16:19]
	v_mfma_f32_16x16x32_bf16 v[8:11], v[160:163], v[220:223], v[8:11]
	v_mfma_f32_16x16x32_bf16 v[4:7], v[168:171], v[220:223], v[4:7]
	v_mfma_f32_16x16x32_bf16 v[56:59], v[164:167], v[196:199], v[56:59]
	v_mfma_f32_16x16x32_bf16 v[48:51], v[172:175], v[196:199], v[48:51]
	v_mfma_f32_16x16x32_bf16 v[40:43], v[164:167], v[204:207], v[40:43]
	v_mfma_f32_16x16x32_bf16 v[32:35], v[172:175], v[204:207], v[32:35]
	v_mfma_f32_16x16x32_bf16 v[24:27], v[164:167], v[212:215], v[24:27]
	v_mfma_f32_16x16x32_bf16 v[16:19], v[172:175], v[212:215], v[16:19]
	v_mfma_f32_16x16x32_bf16 v[8:11], v[164:167], v[224:227], v[8:11]
	v_mfma_f32_16x16x32_bf16 v[4:7], v[172:175], v[224:227], v[4:7]
	v_mfma_f32_16x16x32_bf16 v[60:63], v[176:179], v[192:195], v[60:63]
	v_mfma_f32_16x16x32_bf16 v[52:55], v[184:187], v[192:195], v[52:55]
	v_mfma_f32_16x16x32_bf16 v[44:47], v[176:179], v[200:203], v[44:47]
	v_mfma_f32_16x16x32_bf16 v[36:39], v[184:187], v[200:203], v[36:39]
	v_mfma_f32_16x16x32_bf16 v[28:31], v[176:179], v[208:211], v[28:31]
	v_mfma_f32_16x16x32_bf16 v[20:23], v[184:187], v[208:211], v[20:23]
	v_mfma_f32_16x16x32_bf16 v[12:15], v[176:179], v[220:223], v[12:15]
	v_mfma_f32_16x16x32_bf16 v[0:3], v[184:187], v[220:223], v[0:3]
	v_mfma_f32_16x16x32_bf16 v[60:63], v[180:183], v[196:199], v[60:63]
	v_mfma_f32_16x16x32_bf16 v[52:55], v[188:191], v[196:199], v[52:55]
	v_mfma_f32_16x16x32_bf16 v[44:47], v[180:183], v[204:207], v[44:47]
	v_mfma_f32_16x16x32_bf16 v[36:39], v[188:191], v[204:207], v[36:39]
	v_mfma_f32_16x16x32_bf16 v[28:31], v[180:183], v[212:215], v[28:31]
	v_mfma_f32_16x16x32_bf16 v[20:23], v[188:191], v[212:215], v[20:23]
	v_mfma_f32_16x16x32_bf16 v[12:15], v[180:183], v[224:227], v[12:15]
	v_mfma_f32_16x16x32_bf16 v[0:3], v[188:191], v[224:227], v[0:3]
	s_barrier
	s_add_i32 s66, s66, 2
	s_cmp_gt_u32 s66, 13
	s_mov_b64 s[2:3], s[4:5]
	s_cbranch_scc0 .LBB0_1861
	s_and_b64 vcc, exec, s[40:41]
	s_cbranch_vccz .LBB0_1864
	s_barrier

; #define LAS __attribute__((address_space(3)))
; template <class Desc, class Epi>
; __device__ __forceinline__ void gemm_phase(const int wv_, LAS unsigned char* lds, const Desc& d, const Epi& E) {
;     ...
; #pragma unroll
;     for (int i = 0; i < 2; ++i) { int R, C; stage_rc(tid * 16 + i * 8192, R, C); const int Rb = (R & ~31) + perm32(R & 31); Rr[i] = R; Cc[i] = C;
;         voffA[i] = (unsigned)(R * d.lda + C) * 2u; voffA1[i] = voffA[i] + (unsigned)hstepA; voffB[i] = (unsigned)(Rb * d.ldb + C) * 2u; }
;     unsigned voffAn[2] = {0u, 0u}, voffAn1[2] = {0u, 0u};
;     LAS unsigned short* const tix = (LAS unsigned short*)(lds + STAGE_BYTES + 16384);
;     ...
;     const unsigned ldsw = (unsigned)wid * 1024u;
;     const int aoff = lds_byte(wr * 64 + fr, fq * 8), boff = lds_byte(wc * 32 + fr, fq * 8);
;     ...
;     GU cur, nxt; int ui = 0;
;     if (bid < 0 || bid >= d.nunits) return;
;     LAS float* const rsc = (LAS float*)(lds + STAGE_BYTES);
;     if constexpr (Epi::STAGED || Desc::GATHER) {
;         const int nmy = (d.nunits - bid + nblk - 1) / nblk;
;         for (int idx = tid; idx < nmy * 256; idx += NTHREADS) { GU su; d.unit(bid + (idx >> 8) * nblk, su);
;             if constexpr (Epi::STAGED) rsc[idx] = E.rowscale(su, idx & 255);
;             if constexpr (Desc::GATHER) tix[idx] = (unsigned short)d.tokidx(su, idx & 255); }
;         asm volatile("s_waitcnt vmcnt(0) lgkmcnt(0)" ::: "memory"); __builtin_amdgcn_s_barrier(); asm volatile("" ::: "memory");
;     }
;     d.unit(bid, cur);
;     if constexpr (Desc::GATHER) PG8_AOFF(0, cur, voffA, voffA1);
;     f32x4 acc[2][2][4][2];
; #pragma unroll
;     for (int a = 0; a < 2; ++a)
; #pragma unroll
;         for (int b = 0; b < 2; ++b)
; #pragma unroll
;             for (int m = 0; m < 4; ++m)
; #pragma unroll
;                 for (int n = 0; n < 2; ++n) acc[a][b][m][n] = (f32x4){0.f, 0.f, 0.f, 0.f};
;     bf16x8 At[4][2], B0[2][2], B1[2][2];
;     const char* cA = (const char*)cur.a; const char* cB = (const char*)cur.b;
;     PG8_STAGE(PG8_SB(0, 0), cB, voffB); PG8_STAGE(PG8_SB(0, 1), cB + hstepB, voffB); PG8_STAGE(PG8_SA(0, 0), cA, voffA); PG8_STAGE(PG8_SA(0, 1), cA, voffA1);
;     if (wr == 1) PG8_BAR;
;     PG8_WAIT_V(2); PG8_BAR;
;     PG8_STAGE(PG8_SB(1, 0), cB + kstep, voffB); PG8_STAGE(PG8_SA(1, 0), cA + kstep, voffA); PG8_STAGE(PG8_SB(1, 1), cB + hstepB + kstep, voffB);
;     PG8_WAIT_V(6); PG8_BAR;
.LBB0_1934:
	s_or_b64 exec, exec, s[4:5]
	v_ashrrev_i32_e32 v2, 31, v0
	v_lshrrev_b32_e32 v2, 26, v2
	v_lshlrev_b32_e32 v1, 4, v0
	v_add_u32_e32 v2, v0, v2
	v_bfe_i32 v0, v0, 27, 1
	v_lshrrev_b32_e32 v0, 22, v0
	v_add_u32_e32 v0, v1, v0
	v_and_b32_e32 v0, 0xfffffc00, v0
	v_sub_u32_e32 v0, v1, v0
	v_lshrrev_b32_e32 v3, 4, v0
	v_bitop3_b32 v0, v3, v0, 32 bitop3:0x6c
	v_ashrrev_i32_e32 v5, 31, v0
	s_add_u32 s22, s2, 0x4b800000
	v_readlane_b32 s0, v254, 57
	v_ashrrev_i32_e32 v2, 6, v2
	v_lshrrev_b32_e32 v5, 26, v5
	s_addc_u32 s23, s29, 0
	s_lshl_b32 s0, s0, 26
	v_lshlrev_b32_e32 v3, 3, v2
	v_add_u32_e32 v5, v0, v5
	v_readlane_b32 s1, v254, 58
	s_add_u32 s0, s2, s0
	v_and_b32_e32 v3, -16, v3
	v_ashrrev_i32_e32 v6, 6, v5
	v_and_b32_e32 v5, 0xc0, v5
	s_addc_u32 s1, s29, 0
	v_add_u32_e32 v3, v6, v3
	v_sub_u32_e32 v0, v0, v5
	s_add_u32 s24, s0, 0x23600000
	v_lshlrev_b32_e32 v2, 5, v2
	v_ashrrev_i16_sdwa v0, v216, sext(v0) dst_sel:DWORD dst_unused:UNUSED_PAD src0_sel:DWORD src1_sel:BYTE_0
	v_lshlrev_b32_e32 v5, 1, v3
	v_lshrrev_b32_e32 v7, 2, v3
	v_and_b32_e32 v6, 3, v6
	s_mov_b32 s0, 0xfffe0
	v_and_b32_e32 v2, 32, v2
	v_bfe_i32 v0, v0, 0, 16
	v_and_b32_e32 v5, 24, v5
	v_and_b32_e32 v7, 4, v7
	v_and_or_b32 v6, v3, s0, v6
	v_or3_b32 v5, v6, v7, v5
	v_add_lshl_u32 v0, v2, v0, 1
	v_lshl_add_u32 v132, v3, 12, v0
	v_lshl_add_u32 v134, v5, 12, v0
	v_add_u32_e32 v0, 0x2000, v1
	v_ashrrev_i32_e32 v1, 31, v0
	v_lshrrev_b32_e32 v1, 22, v1
	v_add_u32_e32 v1, v0, v1
	v_ashrrev_i32_e32 v1, 10, v1
	v_mul_i32_i24_e32 v2, 0x400, v1
	v_sub_u32_e32 v0, v0, v2
	v_lshrrev_b32_e32 v2, 4, v0
	v_bitop3_b32 v0, v2, v0, 32 bitop3:0x6c
	v_ashrrev_i32_e32 v3, 31, v0
	v_lshrrev_b32_e32 v3, 26, v3
	v_lshlrev_b32_e32 v2, 3, v1
	v_add_u32_e32 v3, v0, v3
	v_and_b32_e32 v2, -16, v2
	v_ashrrev_i32_e32 v5, 6, v3
	v_add_u32_e32 v2, v5, v2
	v_and_b32_e32 v5, 3, v5
	s_addc_u32 s25, s1, 0
	v_and_or_b32 v5, v2, s0, v5
	s_lshr_b32 s0, s50, 6
	s_and_b32 s0, s0, 12
	s_bfe_u32 s1, s50, 0x20001
	s_or_b32 s0, s0, s1
	s_xor_b32 s4, s0, 15
	s_lshl_b32 s0, s50, 3
	s_lshr_b32 s1, s50, 5
	s_and_b32 s0, s0, 8
	s_and_b32 s1, s1, 6
	s_or_b32 s1, s0, s1
	s_lshl_b32 s1, s1, 4
	s_lshl_b32 s5, s4, 1
	s_or_b32 s1, s5, s1
	s_bfe_u32 s5, s50, 0x10005
	v_and_b32_e32 v3, 0xc0, v3
	s_ashr_i32 s41, s3, 6
	s_bfe_u32 s0, s50, 0x20003
	s_or_b32 s1, s1, s5
	s_ashr_i32 s40, s3, 8
	v_sub_u32_e32 v0, v0, v3
	s_lshl_b32 s52, s41, 10
	s_lshl_b32 s36, s1, 20
	s_lshl_b32 s5, s0, 20
	s_lshl_b32 s4, s4, 22
	v_lshlrev_b32_e32 v1, 5, v1
	v_ashrrev_i16_sdwa v0, v216, sext(v0) dst_sel:DWORD dst_unused:UNUSED_PAD src0_sel:DWORD src1_sel:BYTE_0
	v_lshlrev_b32_e32 v3, 1, v2
	v_lshrrev_b32_e32 v6, 2, v2
	s_add_u32 s4, s24, s4
	v_and_b32_e32 v1, 32, v1
	v_bfe_i32 v0, v0, 0, 16
	v_and_b32_e32 v3, 24, v3
	v_and_b32_e32 v6, 4, v6
	s_addc_u32 s20, s25, 0
	v_or3_b32 v3, v5, v6, v3
	v_add_lshl_u32 v0, v1, v0, 1
	s_add_u32 s4, s4, s5
	v_lshl_add_u32 v135, v2, 12, v0
	v_lshl_add_u32 v137, v3, 12, v0
	s_addc_u32 s5, s20, 0
	s_add_i32 s53, s52, 0
	s_waitcnt vmcnt(0) lgkmcnt(0)
	s_barrier
	s_add_i32 m0, s53, 0x10000
	v_add_u32_e32 v133, 0x80000, v132
	global_load_lds_dwordx4 v134, s[4:5]
	s_add_i32 m0, s53, 0x12000
	s_add_u32 s20, s4, 0x80000
	global_load_lds_dwordx4 v137, s[4:5]
	s_addc_u32 s21, s5, 0
	s_add_i32 m0, s53, 0x14000
	v_add_u32_e32 v136, 0x80000, v135
	global_load_lds_dwordx4 v134, s[20:21]
	s_add_i32 m0, s53, 0x16000
	s_nop 0
	global_load_lds_dwordx4 v137, s[20:21]
	s_add_u32 s20, s22, s36
	s_addc_u32 s21, s23, 0
	s_mov_b32 m0, s53
	s_add_i32 s54, s53, 0x2000
	global_load_lds_dwordx4 v132, s[20:21]
	s_mov_b32 m0, s54
	s_add_i32 s55, s53, 0x4000
	global_load_lds_dwordx4 v135, s[20:21]
	s_mov_b32 m0, s55
	s_add_i32 s56, s53, 0x6000
	global_load_lds_dwordx4 v133, s[20:21]
	v_mov_b32_e32 v0, v136
	s_mov_b32 m0, s56
	s_cmp_eq_u32 s40, 1
	global_load_lds_dwordx4 v0, s[20:21]
	s_cselect_b64 s[36:37], -1, 0
	s_and_b64 vcc, exec, s[36:37]
	s_cbranch_vccz .LBB0_1936
	s_barrier
.LBB0_1936:
	v_mov_b32_e32 v96, v134
	s_add_u32 s38, s2, 0x5b800000
	s_waitcnt vmcnt(2)
	s_barrier
	s_addc_u32 s39, s29, 0
	v_lshl_add_u64 v[0:1], s[4:5], 0, v[96:97]
	s_add_i32 m0, s53, 0x18000
	v_lshl_add_u64 v[0:1], v[0:1], 0, s[30:31]
	v_mov_b32_e32 v96, v137
	global_load_lds_dwordx4 v[0:1], off
	s_add_i32 m0, s53, 0x1a000
	v_lshl_add_u64 v[0:1], s[4:5], 0, v[96:97]
	v_lshl_add_u64 v[0:1], v[0:1], 0, s[30:31]
	v_mov_b32_e32 v96, v132
	global_load_lds_dwordx4 v[0:1], off
	s_add_i32 s57, s53, 0x8000
	v_lshl_add_u64 v[0:1], s[20:21], 0, v[96:97]
	s_lshl_b32 s29, s41, 5
	v_lshl_add_u64 v[0:1], v[0:1], 0, s[30:31]
	s_mov_b32 m0, s57
	v_mov_b32_e32 v96, v135
	s_and_b32 s29, s29, 0x60
	global_load_lds_dwordx4 v[0:1], off
	s_add_i32 s58, s53, 0xa000
	v_lshl_add_u64 v[0:1], s[20:21], 0, v[96:97]
	s_lshl_b32 s2, s40, 13
	s_lshl_b32 s41, s29, 7
	v_lshl_add_u64 v[0:1], v[0:1], 0, s[30:31]
	s_mov_b32 m0, s58
	s_add_u32 s42, s4, 0x80080
	global_load_lds_dwordx4 v[0:1], off
	s_addc_u32 s43, s5, 0
	s_add_i32 m0, s53, 0x1c000
	v_lshrrev_b32_e32 v1, 1, v4
	global_load_lds_dwordx4 v134, s[42:43]
	s_add_i32 m0, s53, 0x1e000
	v_and_b32_e32 v1, 24, v1
	global_load_lds_dwordx4 v137, s[42:43]
	v_and_b32_e32 v0, 15, v4
	v_lshl_or_b32 v138, s40, 6, v0
	v_lshlrev_b32_e32 v2, 1, v1
	v_lshl_or_b32 v0, v0, 6, v2
	v_lshlrev_b32_e32 v2, 2, v138
	v_lshlrev_b32_e32 v4, 2, v4
	v_and_b32_e32 v3, 32, v2
	v_and_b32_e32 v4, 32, v4
	s_waitcnt vmcnt(6)
	s_cmpk_lt_u32 s3, 0x100
	v_bitop3_b32 v3, v0, s2, v3 bitop3:0xde
	v_bitop3_b32 v139, v0, s41, v4 bitop3:0xde
	s_cselect_b64 s[40:41], -1, 0
	s_add_i32 s2, 0, 0x20000
	v_or_b32_e32 v140, 16, v138
	v_or_b32_e32 v141, 32, v138
	v_or_b32_e32 v142, 48, v138
	v_add_u32_e32 v143, 0x80, v138
	v_add_u32_e32 v144, 0x90, v138
	v_add_u32_e32 v145, 0xa0, v138
	v_add_u32_e32 v146, 0xb0, v138
	v_or_b32_e32 v147, s29, v1
	v_add_u32_e32 v148, s2, v2
	s_mov_b32 s61, 0
	v_add_u32_e32 v149, 0, v3
	s_mov_b64 s[44:45], s[4:5]
	s_mov_b64 s[46:47], s[20:21]
	s_barrier
	s_waitcnt vmcnt(0)
	s_branch .LBB0_1939

; #define PG8_STAGE(bufoff, gbase, voff) do { _Pragma("unroll") for (int _i = 0; _i < 2; ++_i) \
;         __builtin_amdgcn_global_load_lds((const __attribute__((address_space(1))) unsigned*)((const __attribute__((address_space(1))) char*)(gbase) + (unsigned)lnd_v((int)(voff)[_i])), (LAS unsigned*)(lds + (bufoff) + ldsw + _i * 8192), 16, 0, 0); } while (0)
; #define PG8_LDA(dst, b, h) do { _Pragma("unroll") for (int m = 0; m < 4; ++m) _Pragma("unroll") for (int k = 0; k < 2; ++k) dst[m][k] = *(const LAS bf16x8*)(lds + PG8_SA(b, h) + aoff + m * 2048 + k * 1024); } while (0)
; #define PG8_LDB(dst, b, h) do { _Pragma("unroll") for (int n = 0; n < 2; ++n) _Pragma("unroll") for (int k = 0; k < 2; ++k) dst[n][k] = *(const LAS bf16x8*)(lds + PG8_SB(b, h) + boff + n * 2048 + k * 1024); } while (0)
; #define PG8_WAIT_V(n) asm volatile("s_waitcnt vmcnt(" #n ")" ::: "memory")
; #define PG8_BAR __builtin_amdgcn_s_barrier()
; template <class Desc, class Epi>
; __device__ __forceinline__ void gemm_phase(const int wv_, LAS unsigned char* lds, const Desc& d, const Epi& E) {
;     ...
;         const char* nA = has_next ? (const char*)nxt.a : cA; const char* nB = has_next ? (const char*)nxt.b : cB;
;         for (int t = 0; t < nt; t += 2) {
;             const bool last = (t == nt - 2);
;             unsigned sA0[2], sA1[2];
;             if constexpr (Desc::GATHER) { sA0[0] = last ? voffAn[0] : voffA[0]; sA0[1] = last ? voffAn[1] : voffA[1]; sA1[0] = last ? voffAn1[0] : voffA1[0]; sA1[1] = last ? voffAn1[1] : voffA1[1]; }
;             else { sA0[0] = voffA[0]; sA0[1] = voffA[1]; sA1[0] = voffA1[0]; sA1[1] = voffA1[1]; }
;             const char* a1 = cA + (size_t)(t + 1) * kstep;
;             const char* a2 = last ? nA : cA + (size_t)(t + 2) * kstep; const char* b2 = last ? nB : cB + (size_t)(t + 2) * kstep;
;             const char* a3 = a2 + kstep; const char* b3 = b2 + kstep;
;             PG8_LDB(B0, 0, 0); PG8_LDB(B1, 0, 1); PG8_SCHED; PG8_LDA(At, 0, 0); PG8_STAGE(PG8_SA(1, 1), a1, voffA1);
;             PG8_WAIT_V(8); PG8_WAIT_L(0); PG8_BAR; PG8_MMA(0, 0, At, B0); PG8_MMA(0, 1, At, B1); PG8_BAR; PG8_SCHED;
;             PG8_LDA(At, 0, 1); PG8_STAGE(PG8_SB(0, 0), b2, voffB); PG8_STAGE(PG8_SB(0, 1), b2 + hstepB, voffB); PG8_STAGE(PG8_SA(0, 0), a2, sA0);
;             PG8_WAIT_V(8); PG8_WAIT_L(0); PG8_BAR; PG8_MMA(1, 0, At, B0); PG8_MMA(1, 1, At, B1); PG8_BAR; PG8_SCHED;
.LBB0_1942:
	s_add_u32 s4, s2, 0x80
	s_addc_u32 s5, s3, 0
	s_add_i32 s63, 0, 0x10000
	s_cmp_eq_u32 s62, 28
	s_cselect_b32 s5, s47, s5
	s_cselect_b32 s4, s46, s4
	v_add_u32_e32 v96, s63, v139
	s_cselect_b32 s21, s45, s43
	s_cselect_b32 s20, s44, s29
	s_add_i32 s66, 0, 0x14000
	ds_read_b128 v[150:153], v96
	ds_read_b128 v[154:157], v96 offset:1024
	ds_read_b128 v[158:161], v96 offset:2048
	ds_read_b128 v[162:165], v96 offset:3072
	v_add_u32_e32 v96, s66, v139
	ds_read_b128 v[166:169], v96
	ds_read_b128 v[170:173], v96 offset:1024
	ds_read_b128 v[174:177], v96 offset:2048
	ds_read_b128 v[178:181], v96 offset:3072
	ds_read_b128 v[182:185], v149
	ds_read_b128 v[186:189], v149 offset:1024
	ds_read_b128 v[190:193], v149 offset:2048
	ds_read_b128 v[194:197], v149 offset:3072
	ds_read_b128 v[198:201], v149 offset:4096
	ds_read_b128 v[202:205], v149 offset:5120
	ds_read_b128 v[206:209], v149 offset:6144
	ds_read_b128 v[210:213], v149 offset:7168
	s_add_i32 m0, s53, 0xc000
	s_nop 0
	global_load_lds_dwordx4 v133, s[2:3]
	s_add_i32 m0, s53, 0xe000
	s_nop 0
	global_load_lds_dwordx4 v136, s[2:3]
	s_waitcnt vmcnt(8)
	s_waitcnt lgkmcnt(0)
	s_barrier
	s_waitcnt lgkmcnt(0)
	v_mfma_f32_16x16x32_bf16 v[126:129], v[150:153], v[182:185], v[126:129]
	v_mfma_f32_16x16x32_bf16 v[122:125], v[158:161], v[182:185], v[122:125]
	v_mfma_f32_16x16x32_bf16 v[110:113], v[150:153], v[190:193], v[110:113]
	v_mfma_f32_16x16x32_bf16 v[106:109], v[158:161], v[190:193], v[106:109]
	v_mfma_f32_16x16x32_bf16 v[92:95], v[150:153], v[198:201], v[92:95]
	v_mfma_f32_16x16x32_bf16 v[88:91], v[158:161], v[198:201], v[88:91]
	v_mfma_f32_16x16x32_bf16 v[76:79], v[150:153], v[206:209], v[76:79]
	v_mfma_f32_16x16x32_bf16 v[72:75], v[158:161], v[206:209], v[72:75]
	v_mfma_f32_16x16x32_bf16 v[126:129], v[154:157], v[186:189], v[126:129]
	v_mfma_f32_16x16x32_bf16 v[122:125], v[162:165], v[186:189], v[122:125]
	v_mfma_f32_16x16x32_bf16 v[110:113], v[154:157], v[194:197], v[110:113]
	v_mfma_f32_16x16x32_bf16 v[106:109], v[162:165], v[194:197], v[106:109]
	v_mfma_f32_16x16x32_bf16 v[92:95], v[154:157], v[202:205], v[92:95]
	v_mfma_f32_16x16x32_bf16 v[88:91], v[162:165], v[202:205], v[88:91]
	v_mfma_f32_16x16x32_bf16 v[76:79], v[154:157], v[210:213], v[76:79]
	v_mfma_f32_16x16x32_bf16 v[72:75], v[162:165], v[210:213], v[72:75]
	v_mfma_f32_16x16x32_bf16 v[118:121], v[166:169], v[182:185], v[118:121]
	v_mfma_f32_16x16x32_bf16 v[114:117], v[174:177], v[182:185], v[114:117]
	v_mfma_f32_16x16x32_bf16 v[102:105], v[166:169], v[190:193], v[102:105]
	v_mfma_f32_16x16x32_bf16 v[98:101], v[174:177], v[190:193], v[98:101]
	v_mfma_f32_16x16x32_bf16 v[84:87], v[166:169], v[198:201], v[84:87]
	v_mfma_f32_16x16x32_bf16 v[80:83], v[174:177], v[198:201], v[80:83]
	v_mfma_f32_16x16x32_bf16 v[68:71], v[166:169], v[206:209], v[68:71]
	v_mfma_f32_16x16x32_bf16 v[64:67], v[174:177], v[206:209], v[64:67]
	v_mfma_f32_16x16x32_bf16 v[118:121], v[170:173], v[186:189], v[118:121]
	v_mfma_f32_16x16x32_bf16 v[114:117], v[178:181], v[186:189], v[114:117]
	v_mfma_f32_16x16x32_bf16 v[102:105], v[170:173], v[194:197], v[102:105]
	v_mfma_f32_16x16x32_bf16 v[98:101], v[178:181], v[194:197], v[98:101]
	v_mfma_f32_16x16x32_bf16 v[84:87], v[170:173], v[202:205], v[84:87]
	v_mfma_f32_16x16x32_bf16 v[80:83], v[178:181], v[202:205], v[80:83]
	v_mfma_f32_16x16x32_bf16 v[68:71], v[170:173], v[210:213], v[68:71]
	v_mfma_f32_16x16x32_bf16 v[64:67], v[178:181], v[210:213], v[64:67]
	s_barrier
	s_add_i32 s63, s63, s52
	ds_read_b128 v[182:185], v149 offset:16384
	ds_read_b128 v[186:189], v149 offset:17408
	ds_read_b128 v[190:193], v149 offset:18432
	ds_read_b128 v[194:197], v149 offset:19456
	ds_read_b128 v[198:201], v149 offset:20480
	ds_read_b128 v[202:205], v149 offset:21504
	ds_read_b128 v[206:209], v149 offset:22528
	ds_read_b128 v[210:213], v149 offset:23552
	s_mov_b32 m0, s63
	s_nop 0
	global_load_lds_dwordx4 v134, s[20:21]
	s_add_i32 m0, s63, 0x2000
	s_add_u32 s64, s20, 0x80000
	global_load_lds_dwordx4 v137, s[20:21]
	s_addc_u32 s65, s21, 0
	s_add_i32 s63, s66, s52
	s_mov_b32 m0, s63
	s_nop 0
	global_load_lds_dwordx4 v134, s[64:65]
	s_add_i32 m0, s63, 0x2000
	s_nop 0
	global_load_lds_dwordx4 v137, s[64:65]
	s_mov_b32 m0, s53
	s_nop 0
	global_load_lds_dwordx4 v132, s[4:5]
	s_mov_b32 m0, s54
	s_nop 0
	global_load_lds_dwordx4 v135, s[4:5]
	s_waitcnt vmcnt(8)
	s_waitcnt lgkmcnt(0)
	s_barrier
	s_waitcnt lgkmcnt(0)
	v_mfma_f32_16x16x32_bf16 v[60:63], v[150:153], v[182:185], v[60:63]
	v_mfma_f32_16x16x32_bf16 v[56:59], v[158:161], v[182:185], v[56:59]
	v_mfma_f32_16x16x32_bf16 v[44:47], v[150:153], v[190:193], v[44:47]
	v_mfma_f32_16x16x32_bf16 v[32:35], v[158:161], v[190:193], v[32:35]
	v_mfma_f32_16x16x32_bf16 v[16:19], v[150:153], v[198:201], v[16:19]
	v_mfma_f32_16x16x32_bf16 v[8:11], v[158:161], v[198:201], v[8:11]
	v_mfma_f32_16x16x32_bf16 v[4:7], v[150:153], v[206:209], v[4:7]
	v_mfma_f32_16x16x32_bf16 v[0:3], v[158:161], v[206:209], v[0:3]
	v_mfma_f32_16x16x32_bf16 v[60:63], v[154:157], v[186:189], v[60:63]
	v_mfma_f32_16x16x32_bf16 v[56:59], v[162:165], v[186:189], v[56:59]
	v_mfma_f32_16x16x32_bf16 v[44:47], v[154:157], v[194:197], v[44:47]
	v_mfma_f32_16x16x32_bf16 v[32:35], v[162:165], v[194:197], v[32:35]
	v_mfma_f32_16x16x32_bf16 v[16:19], v[154:157], v[202:205], v[16:19]
	v_mfma_f32_16x16x32_bf16 v[8:11], v[162:165], v[202:205], v[8:11]
	v_mfma_f32_16x16x32_bf16 v[4:7], v[154:157], v[210:213], v[4:7]
	v_mfma_f32_16x16x32_bf16 v[0:3], v[162:165], v[210:213], v[0:3]
	v_mfma_f32_16x16x32_bf16 v[52:55], v[166:169], v[182:185], v[52:55]
	v_mfma_f32_16x16x32_bf16 v[48:51], v[174:177], v[182:185], v[48:51]
	v_mfma_f32_16x16x32_bf16 v[28:31], v[166:169], v[190:193], v[28:31]
	v_mfma_f32_16x16x32_bf16 v[12:15], v[174:177], v[190:193], v[12:15]
	v_mfma_f32_16x16x32_bf16 v[36:39], v[166:169], v[198:201], v[36:39]
	v_mfma_f32_16x16x32_bf16 v[40:43], v[174:177], v[198:201], v[40:43]
	v_mfma_f32_16x16x32_bf16 v[20:23], v[166:169], v[206:209], v[20:23]
	v_mfma_f32_16x16x32_bf16 v[24:27], v[174:177], v[206:209], v[24:27]
	v_mfma_f32_16x16x32_bf16 v[52:55], v[170:173], v[186:189], v[52:55]
	v_mfma_f32_16x16x32_bf16 v[48:51], v[178:181], v[186:189], v[48:51]
	v_mfma_f32_16x16x32_bf16 v[28:31], v[170:173], v[194:197], v[28:31]
	v_mfma_f32_16x16x32_bf16 v[12:15], v[178:181], v[194:197], v[12:15]
	v_mfma_f32_16x16x32_bf16 v[36:39], v[170:173], v[202:205], v[36:39]
	v_mfma_f32_16x16x32_bf16 v[40:43], v[178:181], v[202:205], v[40:43]
	v_mfma_f32_16x16x32_bf16 v[20:23], v[170:173], v[210:213], v[20:23]
	v_mfma_f32_16x16x32_bf16 v[24:27], v[178:181], v[210:213], v[24:27]
	s_barrier
; #define PG8_STAGE(bufoff, gbase, voff) do { _Pragma("unroll") for (int _i = 0; _i < 2; ++_i) \
;         __builtin_amdgcn_global_load_lds((const __attribute__((address_space(1))) unsigned*)((const __attribute__((address_space(1))) char*)(gbase) + (unsigned)lnd_v((int)(voff)[_i])), (LAS unsigned*)(lds + (bufoff) + ldsw + _i * 8192), 16, 0, 0); } while (0)
; #define PG8_LDA(dst, b, h) do { _Pragma("unroll") for (int m = 0; m < 4; ++m) _Pragma("unroll") for (int k = 0; k < 2; ++k) dst[m][k] = *(const LAS bf16x8*)(lds + PG8_SA(b, h) + aoff + m * 2048 + k * 1024); } while (0)
; #define PG8_LDB(dst, b, h) do { _Pragma("unroll") for (int n = 0; n < 2; ++n) _Pragma("unroll") for (int k = 0; k < 2; ++k) dst[n][k] = *(const LAS bf16x8*)(lds + PG8_SB(b, h) + boff + n * 2048 + k * 1024); } while (0)
; #define PG8_MMA(ai, bj, At, Bt) do { __builtin_amdgcn_s_setprio(1); _Pragma("unroll") for (int m = 0; m < 4; ++m) _Pragma("unroll") for (int n = 0; n < 2; ++n) _Pragma("unroll") for (int k = 0; k < 2; ++k) \
;         acc[ai][bj][m][n] = __builtin_amdgcn_mfma_f32_16x16x32_bf16(Bt[n][k], At[m][k], acc[ai][bj][m][n], 0, 0, 0); __builtin_amdgcn_s_setprio(0); } while (0)
; #define PG8_WAIT_V(n) asm volatile("s_waitcnt vmcnt(" #n ")" ::: "memory")
; #define PG8_WAIT_L(n) asm volatile("s_waitcnt lgkmcnt(" #n ")" ::: "memory")
; #define PG8_BAR __builtin_amdgcn_s_barrier()
; #define PG8_SCHED __builtin_amdgcn_sched_barrier(0)
; template <class Desc, class Epi>
; __device__ __forceinline__ void gemm_phase(const int wv_, LAS unsigned char* lds, const Desc& d, const Epi& E) {
;     ...
;             PG8_LDB(B0, 1, 0); PG8_LDB(B1, 1, 1); PG8_SCHED; PG8_LDA(At, 1, 0); PG8_STAGE(PG8_SA(0, 1), a2, sA1);
;             PG8_WAIT_V(8); PG8_WAIT_L(0); PG8_BAR; PG8_MMA(0, 0, At, B0); PG8_MMA(0, 1, At, B1); PG8_BAR; PG8_SCHED;
	s_add_i32 s63, 0, 0x18000
	v_add_u32_e32 v96, s63, v139
	s_add_i32 s64, 0, 0x1c000
	ds_read_b128 v[150:153], v96
	ds_read_b128 v[154:157], v96 offset:1024
	ds_read_b128 v[158:161], v96 offset:2048
	ds_read_b128 v[162:165], v96 offset:3072
	v_add_u32_e32 v96, s64, v139
	ds_read_b128 v[166:169], v96
	ds_read_b128 v[170:173], v96 offset:1024
	ds_read_b128 v[174:177], v96 offset:2048
	ds_read_b128 v[178:181], v96 offset:3072
	s_mov_b32 m0, s55
	ds_read_b128 v[182:185], v149 offset:32768
	ds_read_b128 v[186:189], v149 offset:33792
	ds_read_b128 v[190:193], v149 offset:34816
	ds_read_b128 v[194:197], v149 offset:35840
	ds_read_b128 v[198:201], v149 offset:36864
	ds_read_b128 v[202:205], v149 offset:37888
	ds_read_b128 v[206:209], v149 offset:38912
	ds_read_b128 v[210:213], v149 offset:39936
	s_nop 0
	global_load_lds_dwordx4 v133, s[4:5]
	s_mov_b32 m0, s56
	s_nop 0
	global_load_lds_dwordx4 v136, s[4:5]
	s_waitcnt vmcnt(8)
	s_waitcnt lgkmcnt(0)
	s_barrier
	s_waitcnt lgkmcnt(0)
	v_mfma_f32_16x16x32_bf16 v[126:129], v[150:153], v[182:185], v[126:129]
	v_mfma_f32_16x16x32_bf16 v[122:125], v[158:161], v[182:185], v[122:125]
	v_mfma_f32_16x16x32_bf16 v[110:113], v[150:153], v[190:193], v[110:113]
	v_mfma_f32_16x16x32_bf16 v[106:109], v[158:161], v[190:193], v[106:109]
	v_mfma_f32_16x16x32_bf16 v[92:95], v[150:153], v[198:201], v[92:95]
	v_mfma_f32_16x16x32_bf16 v[88:91], v[158:161], v[198:201], v[88:91]
	v_mfma_f32_16x16x32_bf16 v[76:79], v[150:153], v[206:209], v[76:79]
	v_mfma_f32_16x16x32_bf16 v[72:75], v[158:161], v[206:209], v[72:75]
	v_mfma_f32_16x16x32_bf16 v[126:129], v[154:157], v[186:189], v[126:129]
	v_mfma_f32_16x16x32_bf16 v[122:125], v[162:165], v[186:189], v[122:125]
	v_mfma_f32_16x16x32_bf16 v[110:113], v[154:157], v[194:197], v[110:113]
	v_mfma_f32_16x16x32_bf16 v[106:109], v[162:165], v[194:197], v[106:109]
	v_mfma_f32_16x16x32_bf16 v[92:95], v[154:157], v[202:205], v[92:95]
	v_mfma_f32_16x16x32_bf16 v[88:91], v[162:165], v[202:205], v[88:91]
	v_mfma_f32_16x16x32_bf16 v[76:79], v[154:157], v[210:213], v[76:79]
	v_mfma_f32_16x16x32_bf16 v[72:75], v[162:165], v[210:213], v[72:75]
	v_mfma_f32_16x16x32_bf16 v[118:121], v[166:169], v[182:185], v[118:121]
	v_mfma_f32_16x16x32_bf16 v[114:117], v[174:177], v[182:185], v[114:117]
	v_mfma_f32_16x16x32_bf16 v[102:105], v[166:169], v[190:193], v[102:105]
	v_mfma_f32_16x16x32_bf16 v[98:101], v[174:177], v[190:193], v[98:101]
	v_mfma_f32_16x16x32_bf16 v[84:87], v[166:169], v[198:201], v[84:87]
	v_mfma_f32_16x16x32_bf16 v[80:83], v[174:177], v[198:201], v[80:83]
	v_mfma_f32_16x16x32_bf16 v[68:71], v[166:169], v[206:209], v[68:71]
	v_mfma_f32_16x16x32_bf16 v[64:67], v[174:177], v[206:209], v[64:67]
	v_mfma_f32_16x16x32_bf16 v[118:121], v[170:173], v[186:189], v[118:121]
	v_mfma_f32_16x16x32_bf16 v[114:117], v[178:181], v[186:189], v[114:117]
	v_mfma_f32_16x16x32_bf16 v[102:105], v[170:173], v[194:197], v[102:105]
	v_mfma_f32_16x16x32_bf16 v[98:101], v[178:181], v[194:197], v[98:101]
	v_mfma_f32_16x16x32_bf16 v[84:87], v[170:173], v[202:205], v[84:87]
	v_mfma_f32_16x16x32_bf16 v[80:83], v[178:181], v[202:205], v[80:83]
	v_mfma_f32_16x16x32_bf16 v[68:71], v[170:173], v[210:213], v[68:71]
	v_mfma_f32_16x16x32_bf16 v[64:67], v[178:181], v[210:213], v[64:67]
	s_barrier
; #define PG8_STAGE(bufoff, gbase, voff) do { _Pragma("unroll") for (int _i = 0; _i < 2; ++_i) \
;         __builtin_amdgcn_global_load_lds((const __attribute__((address_space(1))) unsigned*)((const __attribute__((address_space(1))) char*)(gbase) + (unsigned)lnd_v((int)(voff)[_i])), (LAS unsigned*)(lds + (bufoff) + ldsw + _i * 8192), 16, 0, 0); } while (0)
; #define PG8_LDA(dst, b, h) do { _Pragma("unroll") for (int m = 0; m < 4; ++m) _Pragma("unroll") for (int k = 0; k < 2; ++k) dst[m][k] = *(const LAS bf16x8*)(lds + PG8_SA(b, h) + aoff + m * 2048 + k * 1024); } while (0)
; #define PG8_MMA(ai, bj, At, Bt) do { __builtin_amdgcn_s_setprio(1); _Pragma("unroll") for (int m = 0; m < 4; ++m) _Pragma("unroll") for (int n = 0; n < 2; ++n) _Pragma("unroll") for (int k = 0; k < 2; ++k) \
;         acc[ai][bj][m][n] = __builtin_amdgcn_mfma_f32_16x16x32_bf16(Bt[n][k], At[m][k], acc[ai][bj][m][n], 0, 0, 0); __builtin_amdgcn_s_setprio(0); } while (0)
; #define PG8_WAIT_V(n) asm volatile("s_waitcnt vmcnt(" #n ")" ::: "memory")
; #define PG8_WAIT_L(n) asm volatile("s_waitcnt lgkmcnt(" #n ")" ::: "memory")
; #define PG8_BAR __builtin_amdgcn_s_barrier()
; #define PG8_SCHED __builtin_amdgcn_sched_barrier(0)
; template <class Desc, class Epi>
; __device__ __forceinline__ void gemm_phase(const int wv_, LAS unsigned char* lds, const Desc& d, const Epi& E) {
;     ...
;             PG8_LDA(At, 1, 1); PG8_STAGE(PG8_SB(1, 0), b3, voffB); PG8_STAGE(PG8_SB(1, 1), b3 + hstepB, voffB); PG8_STAGE(PG8_SA(1, 0), a3, sA0);
;             PG8_WAIT_V(8); PG8_WAIT_L(0); PG8_BAR; PG8_MMA(1, 0, At, B0); PG8_MMA(1, 1, At, B1); PG8_BAR; PG8_SCHED;
;         }
;         if (wr == 0) PG8_BAR;
	v_mov_b32_e32 v96, v134
	ds_read_b128 v[182:185], v149 offset:49152
	ds_read_b128 v[186:189], v149 offset:50176
	ds_read_b128 v[190:193], v149 offset:51200
	ds_read_b128 v[194:197], v149 offset:52224
	ds_read_b128 v[198:201], v149 offset:53248
	ds_read_b128 v[202:205], v149 offset:54272
	ds_read_b128 v[206:209], v149 offset:55296
	ds_read_b128 v[210:213], v149 offset:56320
	s_add_i32 s63, s63, s52
	v_lshl_add_u64 v[130:131], s[20:21], 0, v[96:97]
	v_lshl_add_u64 v[130:131], v[130:131], 0, s[30:31]
	s_mov_b32 m0, s63
	v_mov_b32_e32 v96, v137
	global_load_lds_dwordx4 v[130:131], off
	s_add_i32 m0, s63, 0x2000
	s_nop 0
	v_lshl_add_u64 v[130:131], s[20:21], 0, v[96:97]
	s_add_u32 s20, s20, 0x80080
	v_lshl_add_u64 v[130:131], v[130:131], 0, s[30:31]
	s_addc_u32 s21, s21, 0
	s_add_i32 s63, s64, s52
	global_load_lds_dwordx4 v[130:131], off
	s_mov_b32 m0, s63
	s_nop 0
	global_load_lds_dwordx4 v134, s[20:21]
	s_add_i32 m0, s63, 0x2000
	s_nop 0
	global_load_lds_dwordx4 v137, s[20:21]
	v_mov_b32_e32 v96, v132
	s_mov_b32 m0, s57
	v_lshl_add_u64 v[130:131], s[4:5], 0, v[96:97]
	v_lshl_add_u64 v[130:131], v[130:131], 0, s[30:31]
	v_mov_b32_e32 v96, v135
	global_load_lds_dwordx4 v[130:131], off
	s_mov_b32 m0, s58
	v_lshl_add_u64 v[130:131], s[4:5], 0, v[96:97]
	v_lshl_add_u64 v[130:131], v[130:131], 0, s[30:31]
	global_load_lds_dwordx4 v[130:131], off
	s_waitcnt vmcnt(8)
	s_waitcnt lgkmcnt(0)
	s_barrier
	s_waitcnt lgkmcnt(0)
	v_mfma_f32_16x16x32_bf16 v[60:63], v[150:153], v[182:185], v[60:63]
	v_mfma_f32_16x16x32_bf16 v[56:59], v[158:161], v[182:185], v[56:59]
	v_mfma_f32_16x16x32_bf16 v[44:47], v[150:153], v[190:193], v[44:47]
	v_mfma_f32_16x16x32_bf16 v[32:35], v[158:161], v[190:193], v[32:35]
	v_mfma_f32_16x16x32_bf16 v[16:19], v[150:153], v[198:201], v[16:19]
	v_mfma_f32_16x16x32_bf16 v[8:11], v[158:161], v[198:201], v[8:11]
	v_mfma_f32_16x16x32_bf16 v[4:7], v[150:153], v[206:209], v[4:7]
	v_mfma_f32_16x16x32_bf16 v[0:3], v[158:161], v[206:209], v[0:3]
	v_mfma_f32_16x16x32_bf16 v[60:63], v[154:157], v[186:189], v[60:63]
	v_mfma_f32_16x16x32_bf16 v[56:59], v[162:165], v[186:189], v[56:59]
	v_mfma_f32_16x16x32_bf16 v[44:47], v[154:157], v[194:197], v[44:47]
	v_mfma_f32_16x16x32_bf16 v[32:35], v[162:165], v[194:197], v[32:35]
	v_mfma_f32_16x16x32_bf16 v[16:19], v[154:157], v[202:205], v[16:19]
	v_mfma_f32_16x16x32_bf16 v[8:11], v[162:165], v[202:205], v[8:11]
	v_mfma_f32_16x16x32_bf16 v[4:7], v[154:157], v[210:213], v[4:7]
	v_mfma_f32_16x16x32_bf16 v[0:3], v[162:165], v[210:213], v[0:3]
	v_mfma_f32_16x16x32_bf16 v[52:55], v[166:169], v[182:185], v[52:55]
	v_mfma_f32_16x16x32_bf16 v[48:51], v[174:177], v[182:185], v[48:51]
	v_mfma_f32_16x16x32_bf16 v[28:31], v[166:169], v[190:193], v[28:31]
	v_mfma_f32_16x16x32_bf16 v[12:15], v[174:177], v[190:193], v[12:15]
	v_mfma_f32_16x16x32_bf16 v[36:39], v[166:169], v[198:201], v[36:39]
	v_mfma_f32_16x16x32_bf16 v[40:43], v[174:177], v[198:201], v[40:43]
	v_mfma_f32_16x16x32_bf16 v[20:23], v[166:169], v[206:209], v[20:23]
	v_mfma_f32_16x16x32_bf16 v[24:27], v[174:177], v[206:209], v[24:27]
	v_mfma_f32_16x16x32_bf16 v[52:55], v[170:173], v[186:189], v[52:55]
	v_mfma_f32_16x16x32_bf16 v[48:51], v[178:181], v[186:189], v[48:51]
	v_mfma_f32_16x16x32_bf16 v[28:31], v[170:173], v[194:197], v[28:31]
	v_mfma_f32_16x16x32_bf16 v[12:15], v[178:181], v[194:197], v[12:15]
	v_mfma_f32_16x16x32_bf16 v[36:39], v[170:173], v[202:205], v[36:39]
	v_mfma_f32_16x16x32_bf16 v[40:43], v[178:181], v[202:205], v[40:43]
	v_mfma_f32_16x16x32_bf16 v[20:23], v[170:173], v[210:213], v[20:23]
	v_mfma_f32_16x16x32_bf16 v[24:27], v[178:181], v[210:213], v[24:27]
	s_barrier
	s_add_i32 s62, s62, 2
	s_add_u32 s2, s2, 0x100
	s_addc_u32 s3, s3, 0
	s_add_u32 s29, s29, 0x100
	s_addc_u32 s43, s43, 0
	s_cmp_gt_u32 s62, 29
	s_cbranch_scc0 .LBB0_1942
	s_and_b64 vcc, exec, s[40:41]
	s_cbranch_vccz .LBB0_1945
	s_barrier
